# retention out pass: V piece 1 LDS-DMA issued with piece 0 right after the QK^T barrier (lands under the decay-weight stage)
# baseline (speedup 1.0000x reference)
; #define VM_WAIT() asm volatile("s_waitcnt vmcnt(0)" ::: "memory")
; #define FENCE() do { asm volatile("" ::: "memory"); __builtin_amdgcn_sched_barrier(0); } while (0)
; template <int DK, int DV, bool MLSTM>
; __device__ __forceinline__ void out_unit2(LAS unsigned char* lds, LAS unsigned char* ldstab, const OutArgs a, const int wv) {
;     ...
;     const int l = 32 * rb + r32;
;     float a_fl, a_bl;
;     if (MLSTM) { a_fl = a.af[l]; a_bl = a.ab[l]; } else { a_fl = (float)(l + 1) * a.lgf; a_bl = (float)(128 - l) * a.lgb; }
;     VM_WAIT(); __syncthreads();
;     f32x16 p[4];
; #pragma unroll
;     for (int kb = 0; kb < 4; ++kb) p[kb] = (f32x16){};
;     float qnf = 0.f, qnb = 0.f;
; #pragma unroll
;     for (int ks = 0; ks < NKS; ++ks) {
;         const unsigned po = (ks >> 3) * 32768u + ((ks & 1) ? rb1 : rb0) + 512u * ((ks & 7) >> 1);
;         const bf16x8 qf = lds_r128(QP + po + 8192u * rb);
;         bf16x8 kf[4];
; #pragma unroll
;         for (int kb = 0; kb < 4; ++kb) kf[kb] = lds_r128(KP + po + 8192u * kb);
; #pragma unroll
;         for (int kb = 0; kb < 4; ++kb) p[kb] = __builtin_amdgcn_mfma_f32_32x32x16_bf16(kf[kb], qf, p[kb], 0, 0, 0);
;         FENCE();
;     }
.LBB0_1829:
	s_or_b64 exec, exec, s[4:5]
	s_lshl_b32 s4, s6, 10
	s_add_u32 s39, s7, s4
	s_addc_u32 s16, s12, 0
	s_add_u32 s6, s39, 0x1000
	s_addc_u32 s7, s16, 0
	s_lshl_b32 s12, s11, 1
	s_ashr_i32 s13, s12, 31
	s_lshl_b64 s[4:5], s[12:13], 23
	s_add_u32 s4, s51, s4
	s_addc_u32 s5, s52, s5
	s_lshl_b32 s13, s10, 18
	s_add_u32 s4, s4, s13
	s_addc_u32 s5, s5, 0
	s_or_b32 s10, s12, 1
	v_lshlrev_b32_e32 v1, 6, v171
	s_ashr_i32 s11, s10, 31
	v_lshlrev_b32_e32 v0, 8, v171
	v_and_b32_e32 v1, 0x1c0, v1
	s_lshl_b64 s[10:11], s[10:11], 23
	v_and_or_b32 v71, v0, s64, v1
	v_bitop3_b32 v0, v5, v72, 3 bitop3:0x6c
	s_add_u32 s10, s51, s10
	v_lshlrev_b32_e32 v74, 4, v0
	s_addc_u32 s12, s52, s11
	v_or_b32_e32 v173, v74, v71
	s_add_u32 s11, s10, s13
	v_add_u32_e32 v0, s68, v173
	s_addc_u32 s12, s12, 0
	s_and_b32 s10, s38, 3
	s_lshl_b32 s13, s9, 6
	s_waitcnt vmcnt(0)
	s_waitcnt vmcnt(0) lgkmcnt(0)
	s_barrier
	ds_read_b128 v[0:3], v0
	s_and_b32 s41, s13, 0xffffc000
	v_lshlrev_b32_e32 v8, 11, v72
	s_lshl_b32 s13, s10, 13
	v_lshlrev_b32_e32 v9, 4, v171
	s_add_i32 s13, s13, 0
	v_and_or_b32 v12, v9, s66, v8
	v_add_u32_e32 v8, s70, v173
	v_add_u32_e32 v4, s13, v173
	ds_read_b128 v[8:11], v8
	ds_read_b128 v[4:7], v4
	s_waitcnt lgkmcnt(0)
	v_mfma_f32_32x32x16_bf16 v[48:63], v[0:3], v[4:7], 0
	v_lshrrev_b32_e32 v0, 3, v232
	v_bfe_u32 v1, v232, 1, 1
	v_and_or_b32 v0, v0, 2, v1
	v_lshlrev_b32_e32 v0, 4, v0
	v_bitop3_b32 v13, v0, v232, 32 bitop3:0x78
	v_add_u32_e32 v0, s71, v173
	ds_read_b128 v[0:3], v0
	v_mfma_f32_32x32x16_bf16 v[32:47], v[8:11], v[4:7], 0
	v_lshlrev_b32_e32 v8, 3, v171
	v_and_b32_e32 v8, 8, v8
	v_or3_b32 v68, v13, v12, v8
	v_add_u32_e32 v8, s72, v173
	ds_read_b128 v[8:11], v8
	v_and_b32_e32 v233, 31, v232
	s_lshl_b32 s10, s10, 5
	v_or_b32_e32 v66, s10, v233
	s_waitcnt lgkmcnt(1)
	v_mfma_f32_32x32x16_bf16 v[16:31], v[0:3], v[4:7], 0
	v_add_u32_e32 v0, 1, v66
	v_cvt_f32_ubyte0_e32 v67, v0
	v_sub_u32_e32 v0, 0x80, v66
	v_cvt_f32_ubyte0_e32 v70, v0
	s_mov_b32 s15, 4
	v_or_b32_e32 v175, s41, v68
	s_waitcnt lgkmcnt(0)
	v_mfma_f32_32x32x16_bf16 v[0:15], v[8:11], v[4:7], 0
	s_movk_i32 s14, 0x80
	v_mul_f32_e32 v69, v64, v67
	v_bitop3_b32 v177, v74, 32, v71 bitop3:0x36
	v_add_u32_e32 v71, s68, v177
	ds_read_b128 v[74:77], v71
	v_add_u32_e32 v71, s13, v177
	ds_read_b128 v[78:81], v71
	v_add_u32_e32 v71, s70, v177
	s_waitcnt lgkmcnt(0)
	v_mfma_f32_32x32x16_bf16 v[48:63], v[74:77], v[78:81], v[48:63]
	ds_read_b128 v[74:77], v71
	v_add_u32_e32 v71, s71, v177
	s_waitcnt lgkmcnt(0)
	v_mfma_f32_32x32x16_bf16 v[32:47], v[74:77], v[78:81], v[32:47]
	ds_read_b128 v[74:77], v71
	v_add_u32_e32 v71, s72, v177
	s_waitcnt lgkmcnt(0)
	v_mfma_f32_32x32x16_bf16 v[16:31], v[74:77], v[78:81], v[16:31]
	ds_read_b128 v[74:77], v71
	s_waitcnt lgkmcnt(0)
	v_mfma_f32_32x32x16_bf16 v[0:15], v[74:77], v[78:81], v[0:15]
	v_or_b32_e32 v71, 0x200, v173
	v_add_u32_e32 v74, s68, v71
	ds_read_b128 v[74:77], v74
	v_add_u32_e32 v78, s13, v71
	ds_read_b128 v[78:81], v78
	v_add_u32_e32 v82, s70, v71
	s_waitcnt lgkmcnt(0)
	v_mfma_f32_32x32x16_bf16 v[48:63], v[74:77], v[78:81], v[48:63]
	ds_read_b128 v[74:77], v82
	v_add_u32_e32 v82, s71, v71
	v_add_u32_e32 v71, s72, v71
	s_waitcnt lgkmcnt(0)
	v_mfma_f32_32x32x16_bf16 v[32:47], v[74:77], v[78:81], v[32:47]
	ds_read_b128 v[74:77], v82
	s_waitcnt lgkmcnt(0)
	v_mfma_f32_32x32x16_bf16 v[16:31], v[74:77], v[78:81], v[16:31]
	ds_read_b128 v[74:77], v71
	s_waitcnt lgkmcnt(0)
	v_mfma_f32_32x32x16_bf16 v[0:15], v[74:77], v[78:81], v[0:15]
	v_bitop3_b32 v71, v173, s73, 32 bitop3:0xde
	v_add_u32_e32 v74, s68, v71
	ds_read_b128 v[74:77], v74
	v_add_u32_e32 v78, s13, v71
	ds_read_b128 v[78:81], v78
	v_add_u32_e32 v82, s70, v71
	s_waitcnt lgkmcnt(0)
	v_mfma_f32_32x32x16_bf16 v[48:63], v[74:77], v[78:81], v[48:63]
	ds_read_b128 v[74:77], v82
	v_add_u32_e32 v82, s71, v71
	v_add_u32_e32 v71, s72, v71
	s_waitcnt lgkmcnt(0)
	v_mfma_f32_32x32x16_bf16 v[32:47], v[74:77], v[78:81], v[32:47]
	ds_read_b128 v[74:77], v82
	s_waitcnt lgkmcnt(0)
	v_mfma_f32_32x32x16_bf16 v[16:31], v[74:77], v[78:81], v[16:31]
	ds_read_b128 v[74:77], v71
	s_waitcnt lgkmcnt(0)
	v_mfma_f32_32x32x16_bf16 v[0:15], v[74:77], v[78:81], v[0:15]
	v_or_b32_e32 v71, 0x400, v173
	v_add_u32_e32 v74, s68, v71
	ds_read_b128 v[74:77], v74
	v_add_u32_e32 v78, s13, v71
	ds_read_b128 v[78:81], v78
	v_add_u32_e32 v82, s70, v71
	s_waitcnt lgkmcnt(0)
	v_mfma_f32_32x32x16_bf16 v[48:63], v[74:77], v[78:81], v[48:63]
	ds_read_b128 v[74:77], v82
	v_add_u32_e32 v82, s71, v71
	v_add_u32_e32 v71, s72, v71
	s_waitcnt lgkmcnt(0)
	v_mfma_f32_32x32x16_bf16 v[32:47], v[74:77], v[78:81], v[32:47]
	ds_read_b128 v[74:77], v82
	s_waitcnt lgkmcnt(0)
	v_mfma_f32_32x32x16_bf16 v[16:31], v[74:77], v[78:81], v[16:31]
	ds_read_b128 v[74:77], v71
	s_waitcnt lgkmcnt(0)
	v_mfma_f32_32x32x16_bf16 v[0:15], v[74:77], v[78:81], v[0:15]
	v_bitop3_b32 v71, v173, s74, 32 bitop3:0xde
	v_add_u32_e32 v74, s68, v71
	ds_read_b128 v[74:77], v74
	v_add_u32_e32 v78, s13, v71
	ds_read_b128 v[78:81], v78
	v_add_u32_e32 v82, s70, v71
	s_waitcnt lgkmcnt(0)
	v_mfma_f32_32x32x16_bf16 v[48:63], v[74:77], v[78:81], v[48:63]
	ds_read_b128 v[74:77], v82
	v_add_u32_e32 v82, s71, v71
	v_add_u32_e32 v71, s72, v71
	s_waitcnt lgkmcnt(0)
	v_mfma_f32_32x32x16_bf16 v[32:47], v[74:77], v[78:81], v[32:47]
	ds_read_b128 v[74:77], v82
	s_waitcnt lgkmcnt(0)
	v_mfma_f32_32x32x16_bf16 v[16:31], v[74:77], v[78:81], v[16:31]
	ds_read_b128 v[74:77], v71
	s_waitcnt lgkmcnt(0)
	v_mfma_f32_32x32x16_bf16 v[0:15], v[74:77], v[78:81], v[0:15]
	v_or_b32_e32 v71, 0x600, v173
	v_add_u32_e32 v74, s68, v71
	ds_read_b128 v[74:77], v74
	v_add_u32_e32 v78, s13, v71
	ds_read_b128 v[78:81], v78
	v_add_u32_e32 v82, s70, v71
	s_waitcnt lgkmcnt(0)
; #define FENCE() do { asm volatile("" ::: "memory"); __builtin_amdgcn_sched_barrier(0); } while (0)
; template <int DK, int DV, bool MLSTM>
; __device__ __forceinline__ void out_unit2(LAS unsigned char* lds, LAS unsigned char* ldstab, const OutArgs a, const int wv) {
;     ...
; #pragma unroll
;     for (int ks = 0; ks < NKS; ++ks) {
;         const unsigned po = (ks >> 3) * 32768u + ((ks & 1) ? rb1 : rb0) + 512u * ((ks & 7) >> 1);
;         const bf16x8 qf = lds_r128(QP + po + 8192u * rb);
;         bf16x8 kf[4];
; #pragma unroll
;         for (int kb = 0; kb < 4; ++kb) kf[kb] = lds_r128(KP + po + 8192u * kb);
; #pragma unroll
;         for (int kb = 0; kb < 4; ++kb) p[kb] = __builtin_amdgcn_mfma_f32_32x32x16_bf16(kf[kb], qf, p[kb], 0, 0, 0);
;         FENCE();
;     }
	v_mfma_f32_32x32x16_bf16 v[48:63], v[74:77], v[78:81], v[48:63]
	ds_read_b128 v[74:77], v82
	v_add_u32_e32 v82, s71, v71
	v_add_u32_e32 v71, s72, v71
	s_waitcnt lgkmcnt(0)
	v_mfma_f32_32x32x16_bf16 v[32:47], v[74:77], v[78:81], v[32:47]
	ds_read_b128 v[74:77], v82
	s_waitcnt lgkmcnt(0)
	v_mfma_f32_32x32x16_bf16 v[16:31], v[74:77], v[78:81], v[16:31]
	ds_read_b128 v[74:77], v71
	s_waitcnt lgkmcnt(0)
	v_mfma_f32_32x32x16_bf16 v[0:15], v[74:77], v[78:81], v[0:15]
	v_bitop3_b32 v71, v173, s75, 32 bitop3:0xde
	v_add_u32_e32 v74, s68, v71
	ds_read_b128 v[74:77], v74
	v_add_u32_e32 v78, s13, v71
	ds_read_b128 v[78:81], v78
	v_add_u32_e32 v82, s70, v71
	s_waitcnt lgkmcnt(0)
	v_mfma_f32_32x32x16_bf16 v[48:63], v[74:77], v[78:81], v[48:63]
	ds_read_b128 v[74:77], v82
	v_add_u32_e32 v82, s71, v71
	v_add_u32_e32 v71, s72, v71
	s_waitcnt lgkmcnt(0)
	v_mfma_f32_32x32x16_bf16 v[32:47], v[74:77], v[78:81], v[32:47]
	ds_read_b128 v[74:77], v82
	s_waitcnt lgkmcnt(0)
	v_mfma_f32_32x32x16_bf16 v[16:31], v[74:77], v[78:81], v[16:31]
	ds_read_b128 v[74:77], v71
	s_waitcnt lgkmcnt(0)
	v_mfma_f32_32x32x16_bf16 v[0:15], v[74:77], v[78:81], v[0:15]
	v_or_b32_e32 v71, 0x8000, v173
	v_add_u32_e32 v74, s68, v71
	ds_read_b128 v[74:77], v74
	v_add_u32_e32 v78, s13, v71
	ds_read_b128 v[78:81], v78
	v_add_u32_e32 v82, s70, v71
	s_waitcnt lgkmcnt(0)
	v_mfma_f32_32x32x16_bf16 v[48:63], v[74:77], v[78:81], v[48:63]
	ds_read_b128 v[74:77], v82
	v_add_u32_e32 v82, s71, v71
	v_add_u32_e32 v71, s72, v71
	s_waitcnt lgkmcnt(0)
	v_mfma_f32_32x32x16_bf16 v[32:47], v[74:77], v[78:81], v[32:47]
	ds_read_b128 v[74:77], v82
	s_waitcnt lgkmcnt(0)
	v_mfma_f32_32x32x16_bf16 v[16:31], v[74:77], v[78:81], v[16:31]
	ds_read_b128 v[74:77], v71
	s_waitcnt lgkmcnt(0)
	v_mfma_f32_32x32x16_bf16 v[0:15], v[74:77], v[78:81], v[0:15]
	v_bitop3_b32 v71, v173, s76, 32 bitop3:0xde
	v_add_u32_e32 v74, s68, v71
	ds_read_b128 v[74:77], v74
	v_add_u32_e32 v78, s13, v71
	ds_read_b128 v[78:81], v78
	v_add_u32_e32 v82, s70, v71
	s_waitcnt lgkmcnt(0)
	v_mfma_f32_32x32x16_bf16 v[48:63], v[74:77], v[78:81], v[48:63]
	ds_read_b128 v[74:77], v82
	v_add_u32_e32 v82, s71, v71
	v_add_u32_e32 v71, s72, v71
	s_waitcnt lgkmcnt(0)
	v_mfma_f32_32x32x16_bf16 v[32:47], v[74:77], v[78:81], v[32:47]
	ds_read_b128 v[74:77], v82
	s_waitcnt lgkmcnt(0)
	v_mfma_f32_32x32x16_bf16 v[16:31], v[74:77], v[78:81], v[16:31]
	ds_read_b128 v[74:77], v71
	s_waitcnt lgkmcnt(0)
	v_mfma_f32_32x32x16_bf16 v[0:15], v[74:77], v[78:81], v[0:15]
	v_or_b32_e32 v71, 0x8200, v173
	v_add_u32_e32 v74, s68, v71
	ds_read_b128 v[74:77], v74
	v_add_u32_e32 v78, s13, v71
	ds_read_b128 v[78:81], v78
	v_add_u32_e32 v82, s70, v71
	s_waitcnt lgkmcnt(0)
	v_mfma_f32_32x32x16_bf16 v[48:63], v[74:77], v[78:81], v[48:63]
	ds_read_b128 v[74:77], v82
	v_add_u32_e32 v82, s71, v71
	v_add_u32_e32 v71, s72, v71
	s_waitcnt lgkmcnt(0)
	v_mfma_f32_32x32x16_bf16 v[32:47], v[74:77], v[78:81], v[32:47]
	ds_read_b128 v[74:77], v82
	s_waitcnt lgkmcnt(0)
	v_mfma_f32_32x32x16_bf16 v[16:31], v[74:77], v[78:81], v[16:31]
	ds_read_b128 v[74:77], v71
	s_waitcnt lgkmcnt(0)
	v_mfma_f32_32x32x16_bf16 v[0:15], v[74:77], v[78:81], v[0:15]
	v_bitop3_b32 v71, v173, s77, 32 bitop3:0xde
	v_add_u32_e32 v74, s68, v71
	ds_read_b128 v[74:77], v74
	v_add_u32_e32 v78, s13, v71
	ds_read_b128 v[78:81], v78
	v_add_u32_e32 v82, s70, v71
	s_waitcnt lgkmcnt(0)
	v_mfma_f32_32x32x16_bf16 v[48:63], v[74:77], v[78:81], v[48:63]
	ds_read_b128 v[74:77], v82
	v_add_u32_e32 v82, s71, v71
	v_add_u32_e32 v71, s72, v71
	s_waitcnt lgkmcnt(0)
	v_mfma_f32_32x32x16_bf16 v[32:47], v[74:77], v[78:81], v[32:47]
	ds_read_b128 v[74:77], v82
	s_waitcnt lgkmcnt(0)
	v_mfma_f32_32x32x16_bf16 v[16:31], v[74:77], v[78:81], v[16:31]
	ds_read_b128 v[74:77], v71
	s_waitcnt lgkmcnt(0)
	v_mfma_f32_32x32x16_bf16 v[0:15], v[74:77], v[78:81], v[0:15]
	v_or_b32_e32 v71, 0x8400, v173
	v_add_u32_e32 v74, s68, v71
	ds_read_b128 v[74:77], v74
	v_add_u32_e32 v78, s13, v71
	ds_read_b128 v[78:81], v78
	v_add_u32_e32 v82, s70, v71
	s_waitcnt lgkmcnt(0)
	v_mfma_f32_32x32x16_bf16 v[48:63], v[74:77], v[78:81], v[48:63]
	ds_read_b128 v[74:77], v82
	v_add_u32_e32 v82, s71, v71
	v_add_u32_e32 v71, s72, v71
	s_waitcnt lgkmcnt(0)
	v_mfma_f32_32x32x16_bf16 v[32:47], v[74:77], v[78:81], v[32:47]
	ds_read_b128 v[74:77], v82
	s_waitcnt lgkmcnt(0)
	v_mfma_f32_32x32x16_bf16 v[16:31], v[74:77], v[78:81], v[16:31]
	ds_read_b128 v[74:77], v71
	s_waitcnt lgkmcnt(0)
	v_mfma_f32_32x32x16_bf16 v[0:15], v[74:77], v[78:81], v[0:15]
	v_bitop3_b32 v71, v173, s78, 32 bitop3:0xde
	v_add_u32_e32 v74, s68, v71
	ds_read_b128 v[74:77], v74
	v_add_u32_e32 v78, s13, v71
	ds_read_b128 v[78:81], v78
	v_add_u32_e32 v82, s70, v71
	s_waitcnt lgkmcnt(0)
	v_mfma_f32_32x32x16_bf16 v[48:63], v[74:77], v[78:81], v[48:63]
	ds_read_b128 v[74:77], v82
	v_add_u32_e32 v82, s71, v71
	v_add_u32_e32 v71, s72, v71
	s_waitcnt lgkmcnt(0)
	v_mfma_f32_32x32x16_bf16 v[32:47], v[74:77], v[78:81], v[32:47]
	ds_read_b128 v[74:77], v82
	s_waitcnt lgkmcnt(0)
	v_mfma_f32_32x32x16_bf16 v[16:31], v[74:77], v[78:81], v[16:31]
	ds_read_b128 v[74:77], v71
	s_waitcnt lgkmcnt(0)
	v_mfma_f32_32x32x16_bf16 v[0:15], v[74:77], v[78:81], v[0:15]
	v_or_b32_e32 v71, 0x8600, v173
	v_add_u32_e32 v74, s68, v71
	ds_read_b128 v[74:77], v74
	v_add_u32_e32 v78, s13, v71
	ds_read_b128 v[78:81], v78
	v_add_u32_e32 v82, s70, v71
	s_waitcnt lgkmcnt(0)
	v_mfma_f32_32x32x16_bf16 v[48:63], v[74:77], v[78:81], v[48:63]
	ds_read_b128 v[74:77], v82
	v_add_u32_e32 v82, s71, v71
	v_add_u32_e32 v71, s72, v71
	s_waitcnt lgkmcnt(0)
	v_mfma_f32_32x32x16_bf16 v[32:47], v[74:77], v[78:81], v[32:47]
	ds_read_b128 v[74:77], v82
	s_waitcnt lgkmcnt(0)
; #define LAS __attribute__((address_space(3)))
; template <int R, int NP>
; __device__ __forceinline__ void dma_tile(int wid, int lane, unsigned lds_base, const bf16_t* src, int ld) {
;     constexpr int NQ = R * NP / 4, PER = NQ / 8;
;     static_assert(NQ % 8 == 0 && R % 8 == 0, "dma_tile geometry");
;     const int r7 = (lane >> 2) & 7, x = lane & 3, hi = lane >> 5;
; #pragma unroll
;     for (int j = 0; j < PER; ++j) {
;         const int q = wid * PER + j;
;         const int sub = 2 * q + hi, panel = sub / (R / 2), psub = sub % (R / 2), rg = psub >> 2, cblk = psub & 3;
;         const int row = 8 * rg + r7, chlo = x ^ ((row >> 2) & 3);
;         const bf16_t* g = src + (size_t)row * ld + 128 * panel + 32 * cblk + 8 * chlo;
;         __builtin_amdgcn_global_load_lds((const unsigned*)g, (LAS unsigned*)(uintptr_t)(lds_base + q * 1024u), 16, 0, 0);
;     }
; template <int DK, int DV, bool MLSTM>
; __device__ __forceinline__ void out_unit2(LAS unsigned char* lds, LAS unsigned char* ldstab, const OutArgs a, const int wv) {
;     ...
;     __syncthreads();
;     dma_tile<32, NPV>(wid, lane, SB, a.V, a.ldv);
;     float rf = 1.f, rbk = 1.f;
;     if (MLSTM) {
;         float df = 0.f, db = 0.f;
; #pragma unroll
;         for (int kb = 0; kb < 4; ++kb) {
; #pragma unroll
;             for (int r = 0; r < 16; ++r) { const int s = 32 * kb + crow(r, hi);
;                 const float xf = a_fl - akf[s], xb = a_bl - akb[s];
;                 const float wf = __expf((s <= l) ? xf : -1.0e30f), wb = __expf((s >= l) ? xb : -1.0e30f);
;                 df += p[kb][r] * wf; db += p[kb][r] * wb; }
;             FENCE(); }
;         { auto rr = __builtin_amdgcn_permlane32_swap(__float_as_uint(df), __float_as_uint(df), false, false); df = __uint_as_float(rr[0]) + __uint_as_float(rr[1]); }
;         { auto rr = __builtin_amdgcn_permlane32_swap(__float_as_uint(db), __float_as_uint(db), false, false); db = __uint_as_float(rr[0]) + __uint_as_float(rr[1]); }
;         { auto rr = __builtin_amdgcn_permlane32_swap(__float_as_uint(qnf), __float_as_uint(qnf), false, false); qnf = __uint_as_float(rr[0]) + __uint_as_float(rr[1]); }
;         { auto rr = __builtin_amdgcn_permlane32_swap(__float_as_uint(qnb), __float_as_uint(qnb), false, false); qnb = __uint_as_float(rr[0]) + __uint_as_float(rr[1]); }
;         df += __expf(a_fl) * qnf; db += __expf(a_bl) * qnb;
	v_mfma_f32_32x32x16_bf16 v[16:31], v[74:77], v[78:81], v[16:31]
	ds_read_b128 v[74:77], v71
	s_waitcnt lgkmcnt(0)
	v_mfma_f32_32x32x16_bf16 v[0:15], v[74:77], v[78:81], v[0:15]
	v_bitop3_b32 v71, v173, s79, 32 bitop3:0xde
	v_add_u32_e32 v74, s68, v71
	ds_read_b128 v[74:77], v74
	v_add_u32_e32 v78, s13, v71
	ds_read_b128 v[78:81], v78
	v_add_u32_e32 v82, s70, v71
	s_waitcnt lgkmcnt(0)
	v_mfma_f32_32x32x16_bf16 v[48:63], v[74:77], v[78:81], v[48:63]
	ds_read_b128 v[74:77], v82
	v_add_u32_e32 v82, s71, v71
	v_add_u32_e32 v71, s72, v71
	s_waitcnt lgkmcnt(0)
	v_mfma_f32_32x32x16_bf16 v[32:47], v[74:77], v[78:81], v[32:47]
	ds_read_b128 v[74:77], v82
	s_waitcnt lgkmcnt(0)
	v_mfma_f32_32x32x16_bf16 v[16:31], v[74:77], v[78:81], v[16:31]
	ds_read_b128 v[74:77], v71
	s_waitcnt lgkmcnt(0)
	v_mfma_f32_32x32x16_bf16 v[0:15], v[74:77], v[78:81], v[0:15]
	v_or_b32_e32 v74, s40, v72
	v_ashrrev_i32_e32 v75, 31, v74
	v_lshrrev_b32_e32 v75, 28, v75
	v_add_u32_e32 v78, v74, v75
	v_and_b32_e32 v75, -16, v78
	v_sub_u32_e32 v79, v74, v75
	v_lshlrev_b32_e32 v78, 3, v78
	v_lshlrev_b32_e32 v74, 1, v79
	v_and_b32_e32 v158, 0xffffff80, v78
	v_and_or_b32 v182, v74, -16, v73
	v_mov_b64_e32 v[74:75], s[6:7]
	v_ashrrev_i32_e32 v159, 31, v158
	v_lshlrev_b32_e32 v78, 5, v79
	v_mad_i64_i32 v[76:77], s[6:7], v182, s57, v[74:75]
	v_lshlrev_b64 v[184:185], 1, v[158:159]
	v_and_b32_e32 v162, 32, v78
	v_lshl_add_u64 v[76:77], v[76:77], 0, v[184:185]
	v_lshlrev_b32_e32 v160, 1, v162
	s_lshl_b32 s6, s38, 12
	s_lshl_b32 s46, s38, 2
	v_lshl_add_u64 v[76:77], v[76:77], 0, v[160:161]
	s_add_i32 s42, s6, s68
	v_lshl_add_u64 v[76:77], v[76:77], 0, v[156:157]
	s_mov_b32 m0, s42
	s_or_b32 s7, s46, 1
	s_barrier
	s_mov_b32 s98, 0x60000
	s_mov_b32 s99, 0
	global_load_lds_dwordx4 v[76:77], off
	v_lshl_add_u64 v[86:87], v[76:77], 0, s[98:99]
	s_add_i32 m0, m0, 0x8000
	s_nop 0
	global_load_lds_dwordx4 v[86:87], off
	v_lshl_or_b32 v76, s7, 1, v72
	v_ashrrev_i32_e32 v77, 31, v76
	v_lshrrev_b32_e32 v77, 28, v77
	v_add_u32_e32 v78, v76, v77
	v_and_b32_e32 v77, -16, v78
	v_sub_u32_e32 v79, v76, v77
	v_lshlrev_b32_e32 v76, 1, v79
	v_and_or_b32 v186, v76, -8, v73
	v_lshlrev_b32_e32 v78, 3, v78
	v_lshrrev_b32_e32 v76, 2, v186
	v_and_b32_e32 v164, 0xffffff80, v78
	v_xor_b32_e32 v80, v76, v232
	v_ashrrev_i32_e32 v165, 31, v164
	v_lshlrev_b32_e32 v78, 5, v79
	v_mad_i64_i32 v[76:77], s[44:45], v186, s57, v[74:75]
	v_lshlrev_b64 v[188:189], 1, v[164:165]
	v_and_b32_e32 v170, 0x60, v78
	v_lshlrev_b32_e32 v78, 3, v80
	v_lshl_add_u64 v[76:77], v[76:77], 0, v[188:189]
	v_lshlrev_b32_e32 v190, 1, v170
	v_mov_b32_e32 v191, v161
	v_and_b32_e32 v172, 24, v78
	s_lshl_b32 s7, s7, 10
	v_lshl_add_u64 v[76:77], v[76:77], 0, v[190:191]
	v_lshlrev_b32_e32 v192, 1, v172
	v_mov_b32_e32 v193, v161
	s_add_i32 s43, s7, s68
	v_lshl_add_u64 v[76:77], v[76:77], 0, v[192:193]
	s_mov_b32 m0, s43
	s_or_b32 s38, s46, 2
	global_load_lds_dwordx4 v[76:77], off
	v_lshl_add_u64 v[88:89], v[76:77], 0, s[98:99]
	s_add_i32 m0, m0, 0x8000
	s_nop 0
	global_load_lds_dwordx4 v[88:89], off
	v_lshl_or_b32 v76, s38, 1, v72
	v_ashrrev_i32_e32 v77, 31, v76
	v_lshrrev_b32_e32 v77, 28, v77
	v_add_u32_e32 v78, v76, v77
	v_and_b32_e32 v77, -16, v78
	v_sub_u32_e32 v79, v76, v77
	v_lshlrev_b32_e32 v76, 1, v79
	v_and_or_b32 v194, v76, -8, v73
	v_lshlrev_b32_e32 v78, 3, v78
	v_lshrrev_b32_e32 v76, 2, v194
	v_and_b32_e32 v166, 0xffffff80, v78
	v_xor_b32_e32 v80, v76, v232
	v_ashrrev_i32_e32 v167, 31, v166
	v_lshlrev_b32_e32 v78, 5, v79
	v_mad_i64_i32 v[76:77], s[44:45], v194, s57, v[74:75]
	v_lshlrev_b64 v[196:197], 1, v[166:167]
	v_and_b32_e32 v174, 0x60, v78
	v_lshlrev_b32_e32 v78, 3, v80
	v_lshl_add_u64 v[76:77], v[76:77], 0, v[196:197]
	v_lshlrev_b32_e32 v198, 1, v174
	v_mov_b32_e32 v199, v161
	v_and_b32_e32 v176, 24, v78
	s_lshl_b32 s38, s38, 10
	v_lshl_add_u64 v[76:77], v[76:77], 0, v[198:199]
	v_lshlrev_b32_e32 v200, 1, v176
	v_mov_b32_e32 v201, v161
	s_add_i32 s44, s38, s68
	v_lshl_add_u64 v[76:77], v[76:77], 0, v[200:201]
	s_mov_b32 m0, s44
	s_or_b32 s40, s46, 3
	global_load_lds_dwordx4 v[76:77], off
	v_lshl_add_u64 v[90:91], v[76:77], 0, s[98:99]
	s_add_i32 m0, m0, 0x8000
	s_nop 0
	global_load_lds_dwordx4 v[90:91], off
	v_lshl_or_b32 v76, s40, 1, v72
	v_ashrrev_i32_e32 v77, 31, v76
	v_lshrrev_b32_e32 v77, 28, v77
	v_add_u32_e32 v77, v76, v77
	v_and_b32_e32 v78, -16, v77
	v_sub_u32_e32 v76, v76, v78
	v_lshlrev_b32_e32 v78, 1, v76
	v_and_or_b32 v202, v78, -8, v73
	v_lshlrev_b32_e32 v77, 3, v77
	v_lshrrev_b32_e32 v73, 2, v202
	v_and_b32_e32 v168, 0xffffff80, v77
	v_xor_b32_e32 v73, v73, v232
	v_ashrrev_i32_e32 v169, 31, v168
	v_lshlrev_b32_e32 v76, 5, v76
	v_mad_i64_i32 v[74:75], s[46:47], v202, s57, v[74:75]
	v_lshlrev_b64 v[204:205], 1, v[168:169]
	v_and_b32_e32 v178, 0x60, v76
	v_lshlrev_b32_e32 v73, 3, v73
	v_lshl_add_u64 v[74:75], v[74:75], 0, v[204:205]
	v_lshlrev_b32_e32 v206, 1, v178
	v_mov_b32_e32 v207, v161
	v_and_b32_e32 v180, 24, v73
	s_lshl_b32 s40, s40, 10
	v_lshl_add_u64 v[74:75], v[74:75], 0, v[206:207]
	v_lshlrev_b32_e32 v208, 1, v180
	v_mov_b32_e32 v209, v161
	s_add_i32 s45, s40, s68
	v_lshl_add_u64 v[74:75], v[74:75], 0, v[208:209]
	s_mov_b32 m0, s45
	s_add_i32 s46, 0, 0x21500
	v_lshlrev_b32_e32 v73, 4, v72
	global_load_lds_dwordx4 v[74:75], off
	v_lshl_add_u64 v[92:93], v[74:75], 0, s[98:99]
	s_add_i32 m0, m0, 0x8000
	s_nop 0
	global_load_lds_dwordx4 v[92:93], off
	v_add_u32_e32 v74, s46, v73
	s_add_i32 s47, 0, 0x21700
	v_add_u32_e32 v73, s47, v73
	ds_read_b128 v[74:77], v74
	ds_read_b128 v[78:81], v73
	v_lshlrev_b32_e32 v234, 2, v72
	v_cmp_le_i32_e32 vcc, v234, v66
	v_or_b32_e32 v84, 8, v234
	s_waitcnt lgkmcnt(0)
; #define FENCE() do { asm volatile("" ::: "memory"); __builtin_amdgcn_sched_barrier(0); } while (0)
; __device__ __forceinline__ int crow(int r, int hi) { return (r & 3) + 8 * (r >> 2) + 4 * hi; }
; __device__ __forceinline__ int crow(int r, int hi) { return (r & 3) + 8 * (r >> 2) + 4 * hi; }
; template <int DK, int DV, bool MLSTM>
; __device__ __forceinline__ void out_unit2(LAS unsigned char* lds, LAS unsigned char* ldstab, const OutArgs a, const int wv) {
;     ...
;     int l2 = l; asm volatile("" : "+v"(l2));
; #pragma unroll
;     for (int kb = 0; kb < 4; ++kb) {
; #pragma unroll
;         for (int r = 0; r < 16; ++r) { const int s = 32 * kb + crow(r, hi);
;             const float xf = a_fl - akf[s], xb = a_bl - akb[s];
;             const float wf = __expf((s <= l2) ? xf : -1.0e30f), wb = __expf((s >= l2) ? xb : -1.0e30f);
;             p[kb][r] *= (wf * rf + wb * rbk); }
;         FENCE(); }
	v_fma_f32 v72, v64, v67, -v74
	v_fma_f32 v73, v65, v70, -v78
	v_mul_f32_e32 v72, 0x3fb8aa3b, v72
	v_fma_f32 v75, v64, v67, -v75
	v_cndmask_b32_e32 v72, v230, v72, vcc
	v_mul_f32_e32 v73, 0x3fb8aa3b, v73
	v_cmp_lt_i32_e32 vcc, v234, v66
	v_or_b32_e32 v74, 1, v234
	v_fma_f32 v78, v65, v70, -v79
	v_mul_f32_e32 v75, 0x3fb8aa3b, v75
	v_cndmask_b32_e32 v73, v73, v230, vcc
	v_cndmask_b32_e32 v75, v230, v75, vcc
	v_mul_f32_e32 v78, 0x3fb8aa3b, v78
	v_cmp_ge_i32_e32 vcc, v74, v66
	v_exp_f32_e32 v72, v72
	v_exp_f32_e32 v73, v73
	v_cndmask_b32_e32 v74, v230, v78, vcc
	v_exp_f32_e32 v75, v75
	v_exp_f32_e32 v74, v74
	v_add_f32_e32 v72, v72, v73
	v_mul_f32_e32 v48, v48, v72
	v_fma_f32 v73, v64, v67, -v76
	v_add_f32_e32 v72, v75, v74
	v_mul_f32_e32 v49, v49, v72
	v_or_b32_e32 v72, 2, v234
	v_mul_f32_e32 v73, 0x3fb8aa3b, v73
	v_cmp_le_i32_e32 vcc, v72, v66
	v_fma_f32 v74, v65, v70, -v80
	v_mul_f32_e32 v71, v65, v70
	v_cndmask_b32_e32 v73, v230, v73, vcc
	v_exp_f32_e32 v80, v73
	v_mul_f32_e32 v73, 0x3fb8aa3b, v74
	v_cmp_ge_i32_e32 vcc, v72, v66
	v_fma_f32 v74, v65, v70, -v81
	v_ashrrev_i32_e32 v183, 31, v182
	v_cndmask_b32_e32 v72, v230, v73, vcc
	v_exp_f32_e32 v82, v72
	v_or_b32_e32 v72, 3, v234
	v_fma_f32 v73, v64, v67, -v77
	v_mul_f32_e32 v73, 0x3fb8aa3b, v73
	v_cmp_le_i32_e32 vcc, v72, v66
	v_add_f32_e32 v80, v80, v82
	v_mul_f32_e32 v50, v50, v80
	v_cndmask_b32_e32 v73, v230, v73, vcc
	v_exp_f32_e32 v81, v73
	v_mul_f32_e32 v73, 0x3fb8aa3b, v74
	v_cmp_ge_i32_e32 vcc, v72, v66
	v_ashrrev_i32_e32 v187, 31, v186
	v_ashrrev_i32_e32 v195, 31, v194
	v_cndmask_b32_e32 v72, v230, v73, vcc
	v_exp_f32_e32 v83, v72
	v_lshlrev_b32_e32 v72, 2, v84
	v_add_u32_e32 v73, s46, v72
	v_add_u32_e32 v76, s47, v72
	ds_read_b128 v[72:75], v73
	ds_read_b128 v[76:79], v76
	v_cmp_le_i32_e32 vcc, v84, v66
	v_add_f32_e32 v80, v81, v83
	v_or_b32_e32 v81, 9, v234
	s_waitcnt lgkmcnt(0)
	v_fma_f32 v72, v64, v67, -v72
	v_fma_f32 v76, v65, v70, -v76
	v_mul_f32_e32 v72, 0x3fb8aa3b, v72
	v_cndmask_b32_e32 v72, v230, v72, vcc
	v_mul_f32_e32 v76, 0x3fb8aa3b, v76
	v_cmp_ge_i32_e32 vcc, v84, v66
	v_fma_f32 v73, v64, v67, -v73
	v_fma_f32 v77, v65, v70, -v77
	v_cndmask_b32_e32 v76, v230, v76, vcc
	v_mul_f32_e32 v73, 0x3fb8aa3b, v73
	v_cmp_le_i32_e32 vcc, v81, v66
	v_mul_f32_e32 v77, 0x3fb8aa3b, v77
	v_exp_f32_e32 v72, v72
	v_cndmask_b32_e32 v73, v230, v73, vcc
	v_cmp_ge_i32_e32 vcc, v81, v66
	v_exp_f32_e32 v76, v76
	v_exp_f32_e32 v73, v73
	v_cndmask_b32_e32 v77, v230, v77, vcc
	v_exp_f32_e32 v77, v77
	v_add_f32_e32 v72, v72, v76
	v_mul_f32_e32 v52, v52, v72
	v_mul_f32_e32 v51, v51, v80
	v_add_f32_e32 v72, v73, v77
	v_mul_f32_e32 v53, v53, v72
	v_or_b32_e32 v72, 10, v234
	v_fma_f32 v73, v64, v67, -v74
	v_mul_f32_e32 v73, 0x3fb8aa3b, v73
	v_cmp_le_i32_e32 vcc, v72, v66
	v_fma_f32 v74, v65, v70, -v78
	v_or_b32_e32 v84, 16, v234
	v_cndmask_b32_e32 v73, v230, v73, vcc
	v_exp_f32_e32 v80, v73
	v_mul_f32_e32 v73, 0x3fb8aa3b, v74
	v_cmp_ge_i32_e32 vcc, v72, v66
	v_fma_f32 v74, v65, v70, -v79
	v_ashrrev_i32_e32 v203, 31, v202
	v_cndmask_b32_e32 v72, v230, v73, vcc
	v_exp_f32_e32 v81, v72
	v_or_b32_e32 v72, 11, v234
	v_fma_f32 v73, v64, v67, -v75
	v_mul_f32_e32 v73, 0x3fb8aa3b, v73
	v_cmp_le_i32_e32 vcc, v72, v66
	v_add_f32_e32 v80, v80, v81
	v_mul_f32_e32 v54, v54, v80
	v_cndmask_b32_e32 v73, v230, v73, vcc
	v_exp_f32_e32 v82, v73
	v_mul_f32_e32 v73, 0x3fb8aa3b, v74
	v_cmp_ge_i32_e32 vcc, v72, v66
	s_nop 1
	v_cndmask_b32_e32 v72, v230, v73, vcc
	v_exp_f32_e32 v83, v72
	v_lshlrev_b32_e32 v72, 2, v84
	v_add_u32_e32 v73, s46, v72
	v_add_u32_e32 v76, s47, v72
	ds_read_b128 v[72:75], v73
	ds_read_b128 v[76:79], v76
	v_cmp_le_i32_e32 vcc, v84, v66
	v_add_f32_e32 v80, v82, v83
	s_waitcnt lgkmcnt(0)
	v_fma_f32 v72, v64, v67, -v72
	v_mul_f32_e32 v72, 0x3fb8aa3b, v72
	v_fma_f32 v76, v65, v70, -v76
	v_cndmask_b32_e32 v72, v230, v72, vcc
	v_exp_f32_e32 v81, v72
	v_mul_f32_e32 v72, 0x3fb8aa3b, v76
	v_cmp_ge_i32_e32 vcc, v84, v66
	v_fma_f32 v73, v64, v67, -v73
	v_fma_f32 v77, v65, v70, -v77
	v_cndmask_b32_e32 v72, v230, v72, vcc
	v_exp_f32_e32 v76, v72
	v_or_b32_e32 v72, 17, v234
	v_mul_f32_e32 v73, 0x3fb8aa3b, v73
	v_cmp_le_i32_e32 vcc, v72, v66
	v_mul_f32_e32 v77, 0x3fb8aa3b, v77
	v_fma_f32 v75, v64, v67, -v75
	v_cndmask_b32_e32 v73, v230, v73, vcc
	v_cmp_ge_i32_e32 vcc, v72, v66
	v_exp_f32_e32 v73, v73
	v_mul_f32_e32 v75, 0x3fb8aa3b, v75
	v_cndmask_b32_e32 v72, v230, v77, vcc
	v_exp_f32_e32 v77, v72
	v_mul_f32_e32 v72, v55, v80
	v_add_f32_e32 v55, v81, v76
	v_mul_f32_e32 v55, v56, v55
	v_add_f32_e32 v56, v73, v77
	v_mul_f32_e32 v56, v57, v56
	v_or_b32_e32 v57, 18, v234
	v_fma_f32 v73, v64, v67, -v74
	v_fma_f32 v74, v65, v70, -v78
	v_mul_f32_e32 v73, 0x3fb8aa3b, v73
	v_cmp_le_i32_e32 vcc, v57, v66
	v_mul_f32_e32 v74, 0x3fb8aa3b, v74
	v_fma_f32 v76, v65, v70, -v79
	v_cndmask_b32_e32 v73, v230, v73, vcc
	v_cmp_ge_i32_e32 vcc, v57, v66
	v_or_b32_e32 v84, 24, v234
	v_exp_f32_e32 v73, v73
	v_cndmask_b32_e32 v57, v230, v74, vcc
	v_or_b32_e32 v74, 19, v234
	v_cmp_le_i32_e32 vcc, v74, v66
	v_exp_f32_e32 v57, v57
	s_nop 0
	v_cndmask_b32_e32 v75, v230, v75, vcc
	v_exp_f32_e32 v82, v75
	v_mul_f32_e32 v75, 0x3fb8aa3b, v76
	v_cmp_ge_i32_e32 vcc, v74, v66
	v_add_f32_e32 v57, v73, v57
	v_mul_f32_e32 v57, v58, v57
	v_cndmask_b32_e32 v74, v230, v75, vcc
	v_exp_f32_e32 v83, v74
	v_lshlrev_b32_e32 v74, 2, v84
	v_add_u32_e32 v75, s46, v74
	v_add_u32_e32 v78, s47, v74
	ds_read_b128 v[74:77], v75
	ds_read_b128 v[78:81], v78
	v_cmp_le_i32_e32 vcc, v84, v66
	v_add_f32_e32 v58, v82, v83
	v_mul_f32_e32 v58, v59, v58
	s_waitcnt lgkmcnt(0)
; #define FENCE() do { asm volatile("" ::: "memory"); __builtin_amdgcn_sched_barrier(0); } while (0)
; __device__ __forceinline__ int crow(int r, int hi) { return (r & 3) + 8 * (r >> 2) + 4 * hi; }
; __device__ __forceinline__ int crow(int r, int hi) { return (r & 3) + 8 * (r >> 2) + 4 * hi; }
; template <int DK, int DV, bool MLSTM>
; __device__ __forceinline__ void out_unit2(LAS unsigned char* lds, LAS unsigned char* ldstab, const OutArgs a, const int wv) {
;     ...
;     int l2 = l; asm volatile("" : "+v"(l2));
; #pragma unroll
;     for (int kb = 0; kb < 4; ++kb) {
; #pragma unroll
;         for (int r = 0; r < 16; ++r) { const int s = 32 * kb + crow(r, hi);
;             const float xf = a_fl - akf[s], xb = a_bl - akb[s];
;             const float wf = __expf((s <= l2) ? xf : -1.0e30f), wb = __expf((s >= l2) ? xb : -1.0e30f);
;             p[kb][r] *= (wf * rf + wb * rbk); }
;         FENCE(); }
	v_fma_f32 v73, v64, v67, -v74
	v_fma_f32 v74, v65, v70, -v78
	v_mul_f32_e32 v73, 0x3fb8aa3b, v73
	v_cndmask_b32_e32 v73, v230, v73, vcc
	v_mul_f32_e32 v74, 0x3fb8aa3b, v74
	v_cmp_ge_i32_e32 vcc, v84, v66
	v_or_b32_e32 v78, 25, v234
	v_fma_f32 v75, v64, v67, -v75
	v_cndmask_b32_e32 v74, v230, v74, vcc
	v_fma_f32 v79, v65, v70, -v79
	v_mul_f32_e32 v75, 0x3fb8aa3b, v75
	v_cmp_le_i32_e32 vcc, v78, v66
	v_mul_f32_e32 v79, 0x3fb8aa3b, v79
	v_exp_f32_e32 v73, v73
	v_cndmask_b32_e32 v75, v230, v75, vcc
	v_cmp_ge_i32_e32 vcc, v78, v66
	v_exp_f32_e32 v74, v74
	v_exp_f32_e32 v75, v75
	v_cndmask_b32_e32 v78, v230, v79, vcc
	v_exp_f32_e32 v78, v78
	v_add_f32_e32 v59, v73, v74
	v_or_b32_e32 v73, 26, v234
	v_fma_f32 v74, v64, v67, -v76
	v_mul_f32_e32 v59, v60, v59
	v_add_f32_e32 v60, v75, v78
	v_fma_f32 v75, v65, v70, -v80
	v_mul_f32_e32 v74, 0x3fb8aa3b, v74
	v_cmp_le_i32_e32 vcc, v73, v66
	v_mul_f32_e32 v75, 0x3fb8aa3b, v75
	v_fma_f32 v76, v64, v67, -v77
	v_cndmask_b32_e32 v74, v230, v74, vcc
	v_cmp_ge_i32_e32 vcc, v73, v66
	v_fma_f32 v77, v65, v70, -v81
	v_mul_f32_e32 v76, 0x3fb8aa3b, v76
	v_cndmask_b32_e32 v73, v230, v75, vcc
	v_or_b32_e32 v75, 27, v234
	v_cmp_le_i32_e32 vcc, v75, v66
	v_mul_f32_e32 v77, 0x3fb8aa3b, v77
	v_exp_f32_e32 v74, v74
	v_cndmask_b32_e32 v76, v230, v76, vcc
	v_cmp_ge_i32_e32 vcc, v75, v66
	v_exp_f32_e32 v73, v73
	v_exp_f32_e32 v76, v76
	v_cndmask_b32_e32 v75, v230, v77, vcc
	v_exp_f32_e32 v75, v75
	v_mul_f32_e32 v60, v61, v60
	v_add_f32_e32 v61, v74, v73
	v_mul_f32_e32 v61, v62, v61
	v_add_f32_e32 v62, v76, v75
	v_mul_f32_e32 v62, v63, v62
	v_or_b32_e32 v63, 32, v234
	v_lshlrev_b32_e32 v73, 2, v63
	v_add_u32_e32 v74, s46, v73
	v_add_u32_e32 v73, s47, v73
	ds_read_b128 v[74:77], v74
	ds_read_b128 v[78:81], v73
	v_cmp_le_i32_e32 vcc, v63, v66
	v_or_b32_e32 v84, 40, v234
	s_waitcnt lgkmcnt(0)
	v_fma_f32 v73, v64, v67, -v74
	v_fma_f32 v74, v65, v70, -v78
	v_mul_f32_e32 v73, 0x3fb8aa3b, v73
	v_cndmask_b32_e32 v73, v230, v73, vcc
	v_mul_f32_e32 v74, 0x3fb8aa3b, v74
	v_cmp_ge_i32_e32 vcc, v63, v66
	v_fma_f32 v75, v64, v67, -v75
	v_fma_f32 v78, v65, v70, -v79
	v_cndmask_b32_e32 v63, v230, v74, vcc
	v_or_b32_e32 v74, 33, v234
	v_mul_f32_e32 v75, 0x3fb8aa3b, v75
	v_cmp_le_i32_e32 vcc, v74, v66
	v_mul_f32_e32 v78, 0x3fb8aa3b, v78
	v_exp_f32_e32 v73, v73
	v_cndmask_b32_e32 v75, v230, v75, vcc
	v_cmp_ge_i32_e32 vcc, v74, v66
	v_exp_f32_e32 v63, v63
	v_exp_f32_e32 v75, v75
	v_cndmask_b32_e32 v74, v230, v78, vcc
	v_exp_f32_e32 v74, v74
	v_add_f32_e32 v63, v73, v63
	v_mul_f32_e32 v32, v32, v63
	v_fma_f32 v73, v64, v67, -v76
	v_add_f32_e32 v63, v75, v74
	v_mul_f32_e32 v33, v33, v63
	v_or_b32_e32 v63, 34, v234
	v_fma_f32 v74, v65, v70, -v80
	v_mul_f32_e32 v73, 0x3fb8aa3b, v73
	v_cmp_le_i32_e32 vcc, v63, v66
	v_mul_f32_e32 v74, 0x3fb8aa3b, v74
	v_fma_f32 v75, v64, v67, -v77
	v_cndmask_b32_e32 v73, v230, v73, vcc
	v_cmp_ge_i32_e32 vcc, v63, v66
	v_mul_f32_e32 v75, 0x3fb8aa3b, v75
	v_fma_f32 v76, v65, v70, -v81
	v_cndmask_b32_e32 v63, v230, v74, vcc
	v_or_b32_e32 v74, 35, v234
	v_cmp_le_i32_e32 vcc, v74, v66
	v_exp_f32_e32 v73, v73
	v_exp_f32_e32 v63, v63
	v_cndmask_b32_e32 v75, v230, v75, vcc
	v_exp_f32_e32 v82, v75
	v_mul_f32_e32 v75, 0x3fb8aa3b, v76
	v_cmp_ge_i32_e32 vcc, v74, v66
	v_add_f32_e32 v63, v73, v63
	v_mul_f32_e32 v34, v34, v63
	v_cndmask_b32_e32 v74, v230, v75, vcc
	v_exp_f32_e32 v83, v74
	v_lshlrev_b32_e32 v74, 2, v84
	v_add_u32_e32 v75, s46, v74
	v_add_u32_e32 v78, s47, v74
	ds_read_b128 v[74:77], v75
	ds_read_b128 v[78:81], v78
	v_cmp_le_i32_e32 vcc, v84, v66
	v_add_f32_e32 v63, v82, v83
	v_mul_f32_e32 v35, v35, v63
	s_waitcnt lgkmcnt(0)
	v_fma_f32 v73, v64, v67, -v74
	v_fma_f32 v74, v65, v70, -v78
	v_mul_f32_e32 v73, 0x3fb8aa3b, v73
	v_cndmask_b32_e32 v73, v230, v73, vcc
	v_mul_f32_e32 v74, 0x3fb8aa3b, v74
	v_cmp_ge_i32_e32 vcc, v84, v66
	v_or_b32_e32 v78, 41, v234
	v_fma_f32 v75, v64, v67, -v75
	v_cndmask_b32_e32 v74, v230, v74, vcc
	v_fma_f32 v79, v65, v70, -v79
	v_mul_f32_e32 v75, 0x3fb8aa3b, v75
	v_cmp_le_i32_e32 vcc, v78, v66
	v_mul_f32_e32 v79, 0x3fb8aa3b, v79
	v_exp_f32_e32 v73, v73
	v_cndmask_b32_e32 v75, v230, v75, vcc
	v_cmp_ge_i32_e32 vcc, v78, v66
	v_exp_f32_e32 v74, v74
	v_exp_f32_e32 v75, v75
	v_cndmask_b32_e32 v78, v230, v79, vcc
	v_exp_f32_e32 v78, v78
	v_add_f32_e32 v63, v73, v74
	v_mul_f32_e32 v36, v36, v63
	v_fma_f32 v73, v64, v67, -v76
	v_add_f32_e32 v63, v75, v78
	v_mul_f32_e32 v37, v37, v63
	v_or_b32_e32 v63, 42, v234
	v_fma_f32 v74, v65, v70, -v80
	v_mul_f32_e32 v73, 0x3fb8aa3b, v73
	v_cmp_le_i32_e32 vcc, v63, v66
	v_mul_f32_e32 v74, 0x3fb8aa3b, v74
	v_fma_f32 v75, v64, v67, -v77
	v_cndmask_b32_e32 v73, v230, v73, vcc
	v_cmp_ge_i32_e32 vcc, v63, v66
	v_mul_f32_e32 v75, 0x3fb8aa3b, v75
	v_fma_f32 v76, v65, v70, -v81
	v_cndmask_b32_e32 v63, v230, v74, vcc
	v_or_b32_e32 v74, 43, v234
	v_cmp_le_i32_e32 vcc, v74, v66
	v_or_b32_e32 v84, 48, v234
	v_exp_f32_e32 v73, v73
	v_cndmask_b32_e32 v75, v230, v75, vcc
	v_exp_f32_e32 v82, v75
	v_mul_f32_e32 v75, 0x3fb8aa3b, v76
	v_cmp_ge_i32_e32 vcc, v74, v66
	v_exp_f32_e32 v63, v63
	s_nop 0
	v_cndmask_b32_e32 v74, v230, v75, vcc
	v_exp_f32_e32 v83, v74
	v_lshlrev_b32_e32 v74, 2, v84
	v_add_u32_e32 v75, s46, v74
	v_add_u32_e32 v78, s47, v74
	ds_read_b128 v[74:77], v75
	ds_read_b128 v[78:81], v78
	v_add_f32_e32 v63, v73, v63
	v_cmp_le_i32_e32 vcc, v84, v66
	v_mul_f32_e32 v38, v38, v63
	s_waitcnt lgkmcnt(0)
; #define FENCE() do { asm volatile("" ::: "memory"); __builtin_amdgcn_sched_barrier(0); } while (0)
; __device__ __forceinline__ int crow(int r, int hi) { return (r & 3) + 8 * (r >> 2) + 4 * hi; }
; __device__ __forceinline__ int crow(int r, int hi) { return (r & 3) + 8 * (r >> 2) + 4 * hi; }
; template <int DK, int DV, bool MLSTM>
; __device__ __forceinline__ void out_unit2(LAS unsigned char* lds, LAS unsigned char* ldstab, const OutArgs a, const int wv) {
;     ...
;     int l2 = l; asm volatile("" : "+v"(l2));
; #pragma unroll
;     for (int kb = 0; kb < 4; ++kb) {
; #pragma unroll
;         for (int r = 0; r < 16; ++r) { const int s = 32 * kb + crow(r, hi);
;             const float xf = a_fl - akf[s], xb = a_bl - akb[s];
;             const float wf = __expf((s <= l2) ? xf : -1.0e30f), wb = __expf((s >= l2) ? xb : -1.0e30f);
;             p[kb][r] *= (wf * rf + wb * rbk); }
;         FENCE(); }
	v_fma_f32 v73, v64, v67, -v74
	v_fma_f32 v74, v65, v70, -v78
	v_mul_f32_e32 v73, 0x3fb8aa3b, v73
	v_cndmask_b32_e32 v73, v230, v73, vcc
	v_mul_f32_e32 v74, 0x3fb8aa3b, v74
	v_cmp_ge_i32_e32 vcc, v84, v66
	v_or_b32_e32 v78, 49, v234
	v_fma_f32 v75, v64, v67, -v75
	v_cndmask_b32_e32 v74, v230, v74, vcc
	v_fma_f32 v79, v65, v70, -v79
	v_mul_f32_e32 v75, 0x3fb8aa3b, v75
	v_cmp_le_i32_e32 vcc, v78, v66
	v_mul_f32_e32 v79, 0x3fb8aa3b, v79
	v_exp_f32_e32 v73, v73
	v_cndmask_b32_e32 v75, v230, v75, vcc
	v_cmp_ge_i32_e32 vcc, v78, v66
	v_exp_f32_e32 v74, v74
	v_exp_f32_e32 v75, v75
	v_cndmask_b32_e32 v78, v230, v79, vcc
	v_exp_f32_e32 v78, v78
	v_add_f32_e32 v63, v82, v83
	v_mul_f32_e32 v63, v39, v63
	v_add_f32_e32 v39, v73, v74
	v_mul_f32_e32 v39, v40, v39
	v_add_f32_e32 v40, v75, v78
	v_mul_f32_e32 v40, v41, v40
	v_or_b32_e32 v41, 50, v234
	v_fma_f32 v73, v64, v67, -v76
	v_fma_f32 v74, v65, v70, -v80
	v_mul_f32_e32 v73, 0x3fb8aa3b, v73
	v_cmp_le_i32_e32 vcc, v41, v66
	v_mul_f32_e32 v74, 0x3fb8aa3b, v74
	v_fma_f32 v75, v64, v67, -v77
	v_cndmask_b32_e32 v73, v230, v73, vcc
	v_cmp_ge_i32_e32 vcc, v41, v66
	v_mul_f32_e32 v75, 0x3fb8aa3b, v75
	v_fma_f32 v76, v65, v70, -v81
	v_cndmask_b32_e32 v41, v230, v74, vcc
	v_or_b32_e32 v74, 51, v234
	v_cmp_le_i32_e32 vcc, v74, v66
	v_or_b32_e32 v84, 56, v234
	v_exp_f32_e32 v73, v73
	v_cndmask_b32_e32 v75, v230, v75, vcc
	v_exp_f32_e32 v82, v75
	v_mul_f32_e32 v75, 0x3fb8aa3b, v76
	v_cmp_ge_i32_e32 vcc, v74, v66
	v_exp_f32_e32 v41, v41
	s_nop 0
	v_cndmask_b32_e32 v74, v230, v75, vcc
	v_exp_f32_e32 v83, v74
	v_lshlrev_b32_e32 v74, 2, v84
	v_add_u32_e32 v75, s46, v74
	v_add_u32_e32 v78, s47, v74
	ds_read_b128 v[74:77], v75
	ds_read_b128 v[78:81], v78
	v_add_f32_e32 v41, v73, v41
	v_cmp_le_i32_e32 vcc, v84, v66
	v_mul_f32_e32 v41, v42, v41
	s_waitcnt lgkmcnt(0)
	v_fma_f32 v73, v64, v67, -v74
	v_fma_f32 v74, v65, v70, -v78
	v_mul_f32_e32 v73, 0x3fb8aa3b, v73
	v_cndmask_b32_e32 v73, v230, v73, vcc
	v_mul_f32_e32 v74, 0x3fb8aa3b, v74
	v_cmp_ge_i32_e32 vcc, v84, v66
	v_or_b32_e32 v78, 57, v234
	v_fma_f32 v75, v64, v67, -v75
	v_cndmask_b32_e32 v74, v230, v74, vcc
	v_fma_f32 v79, v65, v70, -v79
	v_mul_f32_e32 v75, 0x3fb8aa3b, v75
	v_cmp_le_i32_e32 vcc, v78, v66
	v_mul_f32_e32 v79, 0x3fb8aa3b, v79
	v_exp_f32_e32 v73, v73
	v_cndmask_b32_e32 v75, v230, v75, vcc
	v_cmp_ge_i32_e32 vcc, v78, v66
	v_exp_f32_e32 v74, v74
	v_exp_f32_e32 v75, v75
	v_cndmask_b32_e32 v78, v230, v79, vcc
	v_exp_f32_e32 v78, v78
	v_add_f32_e32 v42, v82, v83
	v_mul_f32_e32 v42, v43, v42
	v_add_f32_e32 v43, v73, v74
	v_or_b32_e32 v73, 58, v234
	v_fma_f32 v74, v64, v67, -v76
	v_mul_f32_e32 v43, v44, v43
	v_add_f32_e32 v44, v75, v78
	v_fma_f32 v75, v65, v70, -v80
	v_mul_f32_e32 v74, 0x3fb8aa3b, v74
	v_cmp_le_i32_e32 vcc, v73, v66
	v_mul_f32_e32 v75, 0x3fb8aa3b, v75
	v_fma_f32 v76, v64, v67, -v77
	v_cndmask_b32_e32 v74, v230, v74, vcc
	v_cmp_ge_i32_e32 vcc, v73, v66
	v_fma_f32 v77, v65, v70, -v81
	v_mul_f32_e32 v76, 0x3fb8aa3b, v76
	v_cndmask_b32_e32 v73, v230, v75, vcc
	v_or_b32_e32 v75, 59, v234
	v_cmp_le_i32_e32 vcc, v75, v66
	v_mul_f32_e32 v77, 0x3fb8aa3b, v77
	v_exp_f32_e32 v74, v74
	v_cndmask_b32_e32 v76, v230, v76, vcc
	v_cmp_ge_i32_e32 vcc, v75, v66
	v_exp_f32_e32 v73, v73
	v_exp_f32_e32 v76, v76
	v_cndmask_b32_e32 v75, v230, v77, vcc
	v_exp_f32_e32 v75, v75
	v_mul_f32_e32 v44, v45, v44
	v_add_f32_e32 v45, v74, v73
	v_mul_f32_e32 v45, v46, v45
	v_add_f32_e32 v46, v76, v75
	v_mul_f32_e32 v46, v47, v46
	v_or_b32_e32 v47, 64, v234
	v_lshlrev_b32_e32 v73, 2, v47
	v_add_u32_e32 v74, s46, v73
	v_add_u32_e32 v73, s47, v73
	ds_read_b128 v[74:77], v74
	ds_read_b128 v[78:81], v73
	v_cmp_le_i32_e32 vcc, v47, v66
	v_or_b32_e32 v84, 0x48, v234
	s_waitcnt lgkmcnt(0)
	v_fma_f32 v73, v64, v67, -v74
	v_fma_f32 v74, v65, v70, -v78
	v_mul_f32_e32 v73, 0x3fb8aa3b, v73
	v_cndmask_b32_e32 v73, v230, v73, vcc
	v_mul_f32_e32 v74, 0x3fb8aa3b, v74
	v_cmp_ge_i32_e32 vcc, v47, v66
	v_fma_f32 v75, v64, v67, -v75
	v_fma_f32 v78, v65, v70, -v79
	v_cndmask_b32_e32 v47, v230, v74, vcc
	v_or_b32_e32 v74, 0x41, v234
	v_mul_f32_e32 v75, 0x3fb8aa3b, v75
	v_cmp_le_i32_e32 vcc, v74, v66
	v_mul_f32_e32 v78, 0x3fb8aa3b, v78
	v_exp_f32_e32 v73, v73
	v_cndmask_b32_e32 v75, v230, v75, vcc
	v_cmp_ge_i32_e32 vcc, v74, v66
	v_exp_f32_e32 v47, v47
	v_exp_f32_e32 v75, v75
	v_cndmask_b32_e32 v74, v230, v78, vcc
	v_exp_f32_e32 v74, v74
	v_add_f32_e32 v47, v73, v47
	v_mul_f32_e32 v16, v16, v47
	v_fma_f32 v73, v64, v67, -v76
	v_add_f32_e32 v47, v75, v74
	v_mul_f32_e32 v17, v17, v47
	v_or_b32_e32 v47, 0x42, v234
	v_fma_f32 v74, v65, v70, -v80
	v_mul_f32_e32 v73, 0x3fb8aa3b, v73
	v_cmp_le_i32_e32 vcc, v47, v66
	v_mul_f32_e32 v74, 0x3fb8aa3b, v74
	v_fma_f32 v75, v64, v67, -v77
	v_cndmask_b32_e32 v73, v230, v73, vcc
	v_cmp_ge_i32_e32 vcc, v47, v66
	v_mul_f32_e32 v75, 0x3fb8aa3b, v75
	v_fma_f32 v76, v65, v70, -v81
	v_cndmask_b32_e32 v47, v230, v74, vcc
	v_or_b32_e32 v74, 0x43, v234
	v_cmp_le_i32_e32 vcc, v74, v66
	v_exp_f32_e32 v73, v73
	v_exp_f32_e32 v47, v47
	v_cndmask_b32_e32 v75, v230, v75, vcc
	v_exp_f32_e32 v82, v75
	v_mul_f32_e32 v75, 0x3fb8aa3b, v76
	v_cmp_ge_i32_e32 vcc, v74, v66
	v_add_f32_e32 v47, v73, v47
	v_mul_f32_e32 v47, v18, v47
	v_cndmask_b32_e32 v74, v230, v75, vcc
	v_exp_f32_e32 v83, v74
	v_lshlrev_b32_e32 v74, 2, v84
	v_add_u32_e32 v75, s46, v74
	v_add_u32_e32 v78, s47, v74
	ds_read_b128 v[74:77], v75
	ds_read_b128 v[78:81], v78
	v_cmp_le_i32_e32 vcc, v84, v66
	v_add_f32_e32 v18, v82, v83
	s_waitcnt lgkmcnt(0)
; #define FENCE() do { asm volatile("" ::: "memory"); __builtin_amdgcn_sched_barrier(0); } while (0)
; __device__ __forceinline__ int crow(int r, int hi) { return (r & 3) + 8 * (r >> 2) + 4 * hi; }
; __device__ __forceinline__ int crow(int r, int hi) { return (r & 3) + 8 * (r >> 2) + 4 * hi; }
; template <int DK, int DV, bool MLSTM>
; __device__ __forceinline__ void out_unit2(LAS unsigned char* lds, LAS unsigned char* ldstab, const OutArgs a, const int wv) {
;     ...
;     int l2 = l; asm volatile("" : "+v"(l2));
; #pragma unroll
;     for (int kb = 0; kb < 4; ++kb) {
; #pragma unroll
;         for (int r = 0; r < 16; ++r) { const int s = 32 * kb + crow(r, hi);
;             const float xf = a_fl - akf[s], xb = a_bl - akb[s];
;             const float wf = __expf((s <= l2) ? xf : -1.0e30f), wb = __expf((s >= l2) ? xb : -1.0e30f);
;             p[kb][r] *= (wf * rf + wb * rbk); }
;         FENCE(); }
	v_fma_f32 v73, v64, v67, -v74
	v_fma_f32 v74, v65, v70, -v78
	v_mul_f32_e32 v73, 0x3fb8aa3b, v73
	v_cndmask_b32_e32 v73, v230, v73, vcc
	v_mul_f32_e32 v74, 0x3fb8aa3b, v74
	v_cmp_ge_i32_e32 vcc, v84, v66
	v_or_b32_e32 v78, 0x49, v234
	v_fma_f32 v75, v64, v67, -v75
	v_cndmask_b32_e32 v74, v230, v74, vcc
	v_fma_f32 v79, v65, v70, -v79
	v_mul_f32_e32 v75, 0x3fb8aa3b, v75
	v_cmp_le_i32_e32 vcc, v78, v66
	v_mul_f32_e32 v79, 0x3fb8aa3b, v79
	v_exp_f32_e32 v73, v73
	v_cndmask_b32_e32 v75, v230, v75, vcc
	v_cmp_ge_i32_e32 vcc, v78, v66
	v_exp_f32_e32 v74, v74
	v_exp_f32_e32 v75, v75
	v_cndmask_b32_e32 v78, v230, v79, vcc
	v_exp_f32_e32 v78, v78
	v_mul_f32_e32 v79, v19, v18
	v_add_f32_e32 v18, v73, v74
	v_mul_f32_e32 v73, v20, v18
	v_add_f32_e32 v18, v75, v78
	v_mul_f32_e32 v78, v21, v18
	v_or_b32_e32 v18, 0x4a, v234
	v_fma_f32 v19, v64, v67, -v76
	v_mul_f32_e32 v19, 0x3fb8aa3b, v19
	v_cmp_le_i32_e32 vcc, v18, v66
	v_fma_f32 v20, v65, v70, -v80
	v_or_b32_e32 v84, 0x50, v234
	v_cndmask_b32_e32 v19, v230, v19, vcc
	v_exp_f32_e32 v80, v19
	v_mul_f32_e32 v19, 0x3fb8aa3b, v20
	v_cmp_ge_i32_e32 vcc, v18, v66
	v_fma_f32 v20, v65, v70, -v81
	s_nop 0
	v_cndmask_b32_e32 v18, v230, v19, vcc
	v_exp_f32_e32 v82, v18
	v_or_b32_e32 v18, 0x4b, v234
	v_fma_f32 v19, v64, v67, -v77
	v_mul_f32_e32 v19, 0x3fb8aa3b, v19
	v_cmp_le_i32_e32 vcc, v18, v66
	v_add_f32_e32 v80, v80, v82
	v_mul_f32_e32 v80, v22, v80
	v_cndmask_b32_e32 v19, v230, v19, vcc
	v_exp_f32_e32 v81, v19
	v_mul_f32_e32 v19, 0x3fb8aa3b, v20
	v_cmp_ge_i32_e32 vcc, v18, v66
	s_nop 1
	v_cndmask_b32_e32 v18, v230, v19, vcc
	v_exp_f32_e32 v83, v18
	v_lshlrev_b32_e32 v18, 2, v84
	v_add_u32_e32 v19, s46, v18
	v_add_u32_e32 v74, s47, v18
	ds_read_b128 v[18:21], v19
	ds_read_b128 v[74:77], v74
	v_cmp_le_i32_e32 vcc, v84, v66
	v_add_f32_e32 v22, v81, v83
	v_or_b32_e32 v81, 0x51, v234
	s_waitcnt lgkmcnt(0)
	v_fma_f32 v18, v64, v67, -v18
	v_fma_f32 v74, v65, v70, -v74
	v_mul_f32_e32 v18, 0x3fb8aa3b, v18
	v_cndmask_b32_e32 v18, v230, v18, vcc
	v_mul_f32_e32 v74, 0x3fb8aa3b, v74
	v_cmp_ge_i32_e32 vcc, v84, v66
	v_fma_f32 v19, v64, v67, -v19
	v_fma_f32 v75, v65, v70, -v75
	v_cndmask_b32_e32 v74, v230, v74, vcc
	v_mul_f32_e32 v19, 0x3fb8aa3b, v19
	v_cmp_le_i32_e32 vcc, v81, v66
	v_mul_f32_e32 v75, 0x3fb8aa3b, v75
	v_exp_f32_e32 v18, v18
	v_cndmask_b32_e32 v19, v230, v19, vcc
	v_cmp_ge_i32_e32 vcc, v81, v66
	v_exp_f32_e32 v74, v74
	v_exp_f32_e32 v19, v19
	v_cndmask_b32_e32 v75, v230, v75, vcc
	v_exp_f32_e32 v75, v75
	v_add_f32_e32 v18, v18, v74
	v_mul_f32_e32 v74, v24, v18
	v_or_b32_e32 v84, 0x58, v234
	v_add_f32_e32 v18, v19, v75
	v_mul_f32_e32 v75, v25, v18
	v_or_b32_e32 v18, 0x52, v234
	v_fma_f32 v19, v64, v67, -v20
	v_mul_f32_e32 v19, 0x3fb8aa3b, v19
	v_cmp_le_i32_e32 vcc, v18, v66
	v_fma_f32 v20, v65, v70, -v76
	v_mul_f32_e32 v81, v23, v22
	v_cndmask_b32_e32 v19, v230, v19, vcc
	v_exp_f32_e32 v76, v19
	v_mul_f32_e32 v19, 0x3fb8aa3b, v20
	v_cmp_ge_i32_e32 vcc, v18, v66
	v_fma_f32 v20, v65, v70, -v77
	s_nop 0
	v_cndmask_b32_e32 v18, v230, v19, vcc
	v_exp_f32_e32 v82, v18
	v_or_b32_e32 v18, 0x53, v234
	v_fma_f32 v19, v64, v67, -v21
	v_mul_f32_e32 v19, 0x3fb8aa3b, v19
	v_cmp_le_i32_e32 vcc, v18, v66
	v_add_f32_e32 v76, v76, v82
	v_mul_f32_e32 v26, v26, v76
	v_cndmask_b32_e32 v19, v230, v19, vcc
	v_exp_f32_e32 v77, v19
	v_mul_f32_e32 v19, 0x3fb8aa3b, v20
	v_cmp_ge_i32_e32 vcc, v18, v66
	s_nop 1
	v_cndmask_b32_e32 v18, v230, v19, vcc
	v_exp_f32_e32 v83, v18
	v_lshlrev_b32_e32 v18, 2, v84
	v_add_u32_e32 v19, s46, v18
	v_add_u32_e32 v22, s47, v18
	ds_read_b128 v[18:21], v19
	ds_read_b128 v[22:25], v22
	v_cmp_le_i32_e32 vcc, v84, v66
	v_add_f32_e32 v76, v77, v83
	v_or_b32_e32 v77, 0x59, v234
	s_waitcnt lgkmcnt(0)
	v_fma_f32 v18, v64, v67, -v18
	v_fma_f32 v22, v65, v70, -v22
	v_mul_f32_e32 v18, 0x3fb8aa3b, v18
	v_cndmask_b32_e32 v18, v230, v18, vcc
	v_mul_f32_e32 v22, 0x3fb8aa3b, v22
	v_cmp_ge_i32_e32 vcc, v84, v66
	v_fma_f32 v19, v64, v67, -v19
	v_fma_f32 v23, v65, v70, -v23
	v_cndmask_b32_e32 v22, v230, v22, vcc
	v_mul_f32_e32 v19, 0x3fb8aa3b, v19
	v_cmp_le_i32_e32 vcc, v77, v66
	v_mul_f32_e32 v23, 0x3fb8aa3b, v23
	v_exp_f32_e32 v18, v18
	v_cndmask_b32_e32 v19, v230, v19, vcc
	v_cmp_ge_i32_e32 vcc, v77, v66
	v_exp_f32_e32 v22, v22
	v_exp_f32_e32 v19, v19
	v_cndmask_b32_e32 v23, v230, v23, vcc
	v_exp_f32_e32 v23, v23
	v_add_f32_e32 v18, v18, v22
	v_mul_f32_e32 v28, v28, v18
	v_fma_f32 v20, v64, v67, -v20
	v_add_f32_e32 v18, v19, v23
	v_or_b32_e32 v19, 0x5a, v234
	v_fma_f32 v22, v65, v70, -v24
	v_mul_f32_e32 v20, 0x3fb8aa3b, v20
	v_cmp_le_i32_e32 vcc, v19, v66
	v_mul_f32_e32 v22, 0x3fb8aa3b, v22
	v_fma_f32 v21, v64, v67, -v21
	v_cndmask_b32_e32 v20, v230, v20, vcc
	v_cmp_ge_i32_e32 vcc, v19, v66
	v_fma_f32 v23, v65, v70, -v25
	v_mul_f32_e32 v21, 0x3fb8aa3b, v21
	v_cndmask_b32_e32 v19, v230, v22, vcc
	v_or_b32_e32 v22, 0x5b, v234
	v_cmp_le_i32_e32 vcc, v22, v66
	v_mul_f32_e32 v23, 0x3fb8aa3b, v23
	v_exp_f32_e32 v20, v20
	v_cndmask_b32_e32 v21, v230, v21, vcc
	v_cmp_ge_i32_e32 vcc, v22, v66
	v_exp_f32_e32 v19, v19
	v_exp_f32_e32 v21, v21
	v_cndmask_b32_e32 v22, v230, v23, vcc
	v_exp_f32_e32 v22, v22
	v_mul_f32_e32 v29, v29, v18
	v_add_f32_e32 v18, v20, v19
	v_mul_f32_e32 v30, v30, v18
	v_add_f32_e32 v18, v21, v22
	v_mul_f32_e32 v27, v27, v76
	v_mul_f32_e32 v31, v31, v18
	v_or_b32_e32 v76, 0x60, v234
	v_lshlrev_b32_e32 v18, 2, v76
	v_add_u32_e32 v19, s46, v18
	v_add_u32_e32 v22, s47, v18
	ds_read_b128 v[18:21], v19
	ds_read_b128 v[22:25], v22
	v_cmp_le_i32_e32 vcc, v76, v66
	v_or_b32_e32 v84, 0x68, v234
	s_waitcnt lgkmcnt(0)
; #define FENCE() do { asm volatile("" ::: "memory"); __builtin_amdgcn_sched_barrier(0); } while (0)
; __device__ __forceinline__ int crow(int r, int hi) { return (r & 3) + 8 * (r >> 2) + 4 * hi; }
; __device__ __forceinline__ int crow(int r, int hi) { return (r & 3) + 8 * (r >> 2) + 4 * hi; }
; template <int DK, int DV, bool MLSTM>
; __device__ __forceinline__ void out_unit2(LAS unsigned char* lds, LAS unsigned char* ldstab, const OutArgs a, const int wv) {
;     ...
;     int l2 = l; asm volatile("" : "+v"(l2));
; #pragma unroll
;     for (int kb = 0; kb < 4; ++kb) {
; #pragma unroll
;         for (int r = 0; r < 16; ++r) { const int s = 32 * kb + crow(r, hi);
;             const float xf = a_fl - akf[s], xb = a_bl - akb[s];
;             const float wf = __expf((s <= l2) ? xf : -1.0e30f), wb = __expf((s >= l2) ? xb : -1.0e30f);
;             p[kb][r] *= (wf * rf + wb * rbk); }
;         FENCE(); }
	v_fma_f32 v18, v64, v67, -v18
	v_fma_f32 v22, v65, v70, -v22
	v_mul_f32_e32 v18, 0x3fb8aa3b, v18
	v_cndmask_b32_e32 v18, v230, v18, vcc
	v_mul_f32_e32 v22, 0x3fb8aa3b, v22
	v_cmp_ge_i32_e32 vcc, v76, v66
	v_or_b32_e32 v76, 0x61, v234
	v_fma_f32 v19, v64, v67, -v19
	v_cndmask_b32_e32 v22, v230, v22, vcc
	v_fma_f32 v23, v65, v70, -v23
	v_mul_f32_e32 v19, 0x3fb8aa3b, v19
	v_cmp_le_i32_e32 vcc, v76, v66
	v_mul_f32_e32 v23, 0x3fb8aa3b, v23
	v_exp_f32_e32 v18, v18
	v_cndmask_b32_e32 v19, v230, v19, vcc
	v_cmp_ge_i32_e32 vcc, v76, v66
	v_exp_f32_e32 v22, v22
	v_exp_f32_e32 v19, v19
	v_cndmask_b32_e32 v23, v230, v23, vcc
	v_exp_f32_e32 v23, v23
	v_add_f32_e32 v18, v18, v22
	v_mul_f32_e32 v76, v0, v18
	v_fma_f32 v18, v65, v70, -v24
	v_add_f32_e32 v0, v19, v23
	v_mul_f32_e32 v77, v1, v0
	v_or_b32_e32 v0, 0x62, v234
	v_fma_f32 v1, v64, v67, -v20
	v_mul_f32_e32 v1, 0x3fb8aa3b, v1
	v_cmp_le_i32_e32 vcc, v0, v66
	v_mul_f32_e32 v18, 0x3fb8aa3b, v18
	v_fma_f32 v19, v64, v67, -v21
	v_cndmask_b32_e32 v1, v230, v1, vcc
	v_cmp_ge_i32_e32 vcc, v0, v66
	v_mul_f32_e32 v19, 0x3fb8aa3b, v19
	v_fma_f32 v20, v65, v70, -v25
	v_cndmask_b32_e32 v0, v230, v18, vcc
	v_or_b32_e32 v18, 0x63, v234
	v_cmp_le_i32_e32 vcc, v18, v66
	v_exp_f32_e32 v1, v1
	v_exp_f32_e32 v0, v0
	v_cndmask_b32_e32 v19, v230, v19, vcc
	v_exp_f32_e32 v82, v19
	v_mul_f32_e32 v19, 0x3fb8aa3b, v20
	v_cmp_ge_i32_e32 vcc, v18, v66
	v_add_f32_e32 v0, v1, v0
	v_mul_f32_e32 v85, v2, v0
	v_cndmask_b32_e32 v18, v230, v19, vcc
	v_exp_f32_e32 v83, v18
	v_lshlrev_b32_e32 v18, 2, v84
	v_add_u32_e32 v19, s46, v18
	v_add_u32_e32 v22, s47, v18
	ds_read_b128 v[18:21], v19
	ds_read_b128 v[22:25], v22
	v_cmp_le_i32_e32 vcc, v84, v66
	v_add_f32_e32 v0, v82, v83
	v_or_b32_e32 v83, 0x70, v234
	s_waitcnt lgkmcnt(0)
	v_fma_f32 v1, v64, v67, -v18
	v_fma_f32 v2, v65, v70, -v22
	v_mul_f32_e32 v1, 0x3fb8aa3b, v1
	v_cndmask_b32_e32 v1, v230, v1, vcc
	v_mul_f32_e32 v2, 0x3fb8aa3b, v2
	v_cmp_ge_i32_e32 vcc, v84, v66
	v_or_b32_e32 v18, 0x69, v234
	v_fma_f32 v19, v64, v67, -v19
	v_cndmask_b32_e32 v2, v230, v2, vcc
	v_fma_f32 v22, v65, v70, -v23
	v_mul_f32_e32 v19, 0x3fb8aa3b, v19
	v_cmp_le_i32_e32 vcc, v18, v66
	v_mul_f32_e32 v22, 0x3fb8aa3b, v22
	v_exp_f32_e32 v1, v1
	v_cndmask_b32_e32 v19, v230, v19, vcc
	v_cmp_ge_i32_e32 vcc, v18, v66
	v_exp_f32_e32 v2, v2
	v_exp_f32_e32 v19, v19
	v_cndmask_b32_e32 v18, v230, v22, vcc
	v_exp_f32_e32 v18, v18
	v_mul_f32_e32 v22, v3, v0
	v_add_f32_e32 v0, v1, v2
	v_mul_f32_e32 v23, v4, v0
	v_add_f32_e32 v0, v19, v18
	v_mul_f32_e32 v82, v5, v0
	v_or_b32_e32 v0, 0x6a, v234
	v_fma_f32 v1, v64, v67, -v20
	v_mul_f32_e32 v1, 0x3fb8aa3b, v1
	v_cmp_le_i32_e32 vcc, v0, v66
	v_fma_f32 v2, v65, v70, -v24
	s_nop 0
	v_cndmask_b32_e32 v1, v230, v1, vcc
	v_exp_f32_e32 v4, v1
	v_mul_f32_e32 v1, 0x3fb8aa3b, v2
	v_cmp_ge_i32_e32 vcc, v0, v66
	v_fma_f32 v2, v65, v70, -v25
	s_nop 0
	v_cndmask_b32_e32 v0, v230, v1, vcc
	v_exp_f32_e32 v5, v0
	v_or_b32_e32 v0, 0x6b, v234
	v_fma_f32 v1, v64, v67, -v21
	v_mul_f32_e32 v1, 0x3fb8aa3b, v1
	v_cmp_le_i32_e32 vcc, v0, v66
	v_add_f32_e32 v4, v4, v5
	v_mul_f32_e32 v84, v6, v4
	v_cndmask_b32_e32 v1, v230, v1, vcc
	v_exp_f32_e32 v24, v1
	v_mul_f32_e32 v1, 0x3fb8aa3b, v2
	v_cmp_ge_i32_e32 vcc, v0, v66
	v_or_b32_e32 v6, 0x71, v234
	s_nop 0
	v_cndmask_b32_e32 v0, v230, v1, vcc
	v_exp_f32_e32 v25, v0
	v_lshlrev_b32_e32 v0, 2, v83
	v_add_u32_e32 v1, s46, v0
	v_add_u32_e32 v18, s47, v0
	ds_read_b128 v[0:3], v1
	ds_read_b128 v[18:21], v18
	v_cmp_le_i32_e32 vcc, v83, v66
	v_add_f32_e32 v4, v24, v25
	v_or_b32_e32 v25, 0x78, v234
	s_waitcnt lgkmcnt(0)
	v_fma_f32 v0, v64, v67, -v0
	v_fma_f32 v5, v65, v70, -v18
	v_mul_f32_e32 v0, 0x3fb8aa3b, v0
	v_cndmask_b32_e32 v0, v230, v0, vcc
	v_mul_f32_e32 v5, 0x3fb8aa3b, v5
	v_cmp_ge_i32_e32 vcc, v83, v66
	v_fma_f32 v1, v64, v67, -v1
	v_fma_f32 v18, v65, v70, -v19
	v_cndmask_b32_e32 v5, v230, v5, vcc
	v_mul_f32_e32 v1, 0x3fb8aa3b, v1
	v_cmp_le_i32_e32 vcc, v6, v66
	v_mul_f32_e32 v18, 0x3fb8aa3b, v18
	v_exp_f32_e32 v0, v0
	v_cndmask_b32_e32 v1, v230, v1, vcc
	v_cmp_ge_i32_e32 vcc, v6, v66
	v_exp_f32_e32 v5, v5
	v_exp_f32_e32 v1, v1
	v_cndmask_b32_e32 v6, v230, v18, vcc
	v_exp_f32_e32 v6, v6
	v_add_f32_e32 v0, v0, v5
	v_mul_f32_e32 v8, v8, v0
	v_mul_f32_e32 v18, v7, v4
	v_add_f32_e32 v0, v1, v6
	v_mul_f32_e32 v9, v9, v0
	v_or_b32_e32 v0, 0x72, v234
	v_fma_f32 v1, v64, v67, -v2
	v_mul_f32_e32 v1, 0x3fb8aa3b, v1
	v_cmp_le_i32_e32 vcc, v0, v66
	v_fma_f32 v2, v65, v70, -v20
	s_nop 0
	v_cndmask_b32_e32 v1, v230, v1, vcc
	v_exp_f32_e32 v19, v1
	v_mul_f32_e32 v1, 0x3fb8aa3b, v2
	v_cmp_ge_i32_e32 vcc, v0, v66
	v_fma_f32 v2, v65, v70, -v21
	s_nop 0
	v_cndmask_b32_e32 v0, v230, v1, vcc
	v_exp_f32_e32 v20, v0
	v_or_b32_e32 v0, 0x73, v234
	v_fma_f32 v1, v64, v67, -v3
	v_mul_f32_e32 v1, 0x3fb8aa3b, v1
	v_cmp_le_i32_e32 vcc, v0, v66
	v_add_f32_e32 v19, v19, v20
	v_or_b32_e32 v20, 0x79, v234
	v_cndmask_b32_e32 v1, v230, v1, vcc
	v_exp_f32_e32 v21, v1
	v_mul_f32_e32 v1, 0x3fb8aa3b, v2
	v_cmp_ge_i32_e32 vcc, v0, v66
	v_mul_f32_e32 v10, v10, v19
	s_nop 0
	v_cndmask_b32_e32 v0, v230, v1, vcc
	v_exp_f32_e32 v24, v0
	v_lshlrev_b32_e32 v0, 2, v25
	v_add_u32_e32 v1, s46, v0
	v_add_u32_e32 v4, s47, v0
	ds_read_b128 v[0:3], v1
	ds_read_b128 v[4:7], v4
	v_cmp_le_i32_e32 vcc, v25, v66
	v_add_f32_e32 v19, v21, v24
	s_waitcnt lgkmcnt(0)
; #define VM_WAIT() asm volatile("s_waitcnt vmcnt(0)" ::: "memory")
; #define FENCE() do { asm volatile("" ::: "memory"); __builtin_amdgcn_sched_barrier(0); } while (0)
; __device__ __forceinline__ int crow(int r, int hi) { return (r & 3) + 8 * (r >> 2) + 4 * hi; }
; __device__ __forceinline__ int crow(int r, int hi) { return (r & 3) + 8 * (r >> 2) + 4 * hi; }
; template <int DK, int DV, bool MLSTM>
; __device__ __forceinline__ void out_unit2(LAS unsigned char* lds, LAS unsigned char* ldstab, const OutArgs a, const int wv) {
;     ...
;     int l2 = l; asm volatile("" : "+v"(l2));
; #pragma unroll
;     for (int kb = 0; kb < 4; ++kb) {
; #pragma unroll
;         for (int r = 0; r < 16; ++r) { const int s = 32 * kb + crow(r, hi);
;             const float xf = a_fl - akf[s], xb = a_bl - akb[s];
;             const float wf = __expf((s <= l2) ? xf : -1.0e30f), wb = __expf((s >= l2) ? xb : -1.0e30f);
;             p[kb][r] *= (wf * rf + wb * rbk); }
;         FENCE(); }
;     const float qsf = __expf(a_fl) * rf, qsb = __expf(a_bl) * rbk;
;     bf16x8 pa[8];
;     ...
; #pragma unroll
;     for (int kb = 0; kb < 4; ++kb) { LA_PK4(p[kb], 0, pa[2 * kb]); LA_PK4(p[kb], 8, pa[2 * kb + 1]); }
;     ...
; #pragma unroll
;     for (int pc = 0; pc < 4; ++pc) {
;         VM_WAIT(); __syncthreads();
;         OUT_DMA(pc + 1);
;         const bf16x8 af0 = pa[2 * pc], af1 = pa[2 * pc + 1];
;         OUT_MMA(pc & 1);
	v_fma_f32 v0, v64, v67, -v0
	v_fma_f32 v4, v65, v70, -v4
	v_mul_f32_e32 v0, 0x3fb8aa3b, v0
	v_cndmask_b32_e32 v0, v230, v0, vcc
	v_mul_f32_e32 v4, 0x3fb8aa3b, v4
	v_cmp_ge_i32_e32 vcc, v25, v66
	v_fma_f32 v1, v64, v67, -v1
	v_fma_f32 v5, v65, v70, -v5
	v_cndmask_b32_e32 v4, v230, v4, vcc
	v_mul_f32_e32 v1, 0x3fb8aa3b, v1
	v_cmp_le_i32_e32 vcc, v20, v66
	v_mul_f32_e32 v5, 0x3fb8aa3b, v5
	v_exp_f32_e32 v0, v0
	v_cndmask_b32_e32 v1, v230, v1, vcc
	v_cmp_ge_i32_e32 vcc, v20, v66
	v_exp_f32_e32 v4, v4
	v_exp_f32_e32 v1, v1
	v_cndmask_b32_e32 v5, v230, v5, vcc
	v_exp_f32_e32 v5, v5
	v_add_f32_e32 v0, v0, v4
	v_or_b32_e32 v4, 0x7a, v234
	v_fma_f32 v2, v64, v67, -v2
	v_add_f32_e32 v1, v1, v5
	v_fma_f32 v5, v65, v70, -v6
	v_mul_f32_e32 v2, 0x3fb8aa3b, v2
	v_cmp_le_i32_e32 vcc, v4, v66
	v_mul_f32_e32 v5, 0x3fb8aa3b, v5
	v_fma_f32 v3, v64, v67, -v3
	v_cndmask_b32_e32 v2, v230, v2, vcc
	v_cmp_ge_i32_e32 vcc, v4, v66
	v_fma_f32 v6, v65, v70, -v7
	v_mul_f32_e32 v3, 0x3fb8aa3b, v3
	v_cndmask_b32_e32 v4, v230, v5, vcc
	v_or_b32_e32 v5, 0x7b, v234
	v_cmp_le_i32_e32 vcc, v5, v66
	v_mul_f32_e32 v6, 0x3fb8aa3b, v6
	v_exp_f32_e32 v2, v2
	v_cndmask_b32_e32 v3, v230, v3, vcc
	v_cmp_ge_i32_e32 vcc, v5, v66
	v_exp_f32_e32 v4, v4
	v_exp_f32_e32 v3, v3
	v_cndmask_b32_e32 v5, v230, v6, vcc
	v_exp_f32_e32 v5, v5
	v_add_f32_e32 v2, v2, v4
	v_mul_f32_e32 v11, v11, v19
	v_mul_f32_e32 v0, v12, v0
	v_add_f32_e32 v3, v3, v5
	v_mul_f32_e32 v1, v13, v1
	v_mul_f32_e32 v2, v14, v2
	v_mul_f32_e32 v3, v15, v3
	s_add_u32 s46, s39, 0x61000
	s_addc_u32 s47, s16, 0
	v_cvt_pk_bf16_f32 v64, v48, v49
	v_cvt_pk_bf16_f32 v65, v50, v51
	v_cvt_pk_bf16_f32 v66, v52, v53
	v_cvt_pk_bf16_f32 v67, v54, v72
	v_cvt_pk_bf16_f32 v152, v55, v56
	v_cvt_pk_bf16_f32 v153, v57, v58
	v_cvt_pk_bf16_f32 v154, v59, v60
	v_cvt_pk_bf16_f32 v155, v61, v62
	v_cvt_pk_bf16_f32 v148, v32, v33
	v_cvt_pk_bf16_f32 v149, v34, v35
	v_cvt_pk_bf16_f32 v150, v36, v37
	v_cvt_pk_bf16_f32 v151, v38, v63
	v_cvt_pk_bf16_f32 v144, v39, v40
	v_cvt_pk_bf16_f32 v145, v41, v42
	v_cvt_pk_bf16_f32 v146, v43, v44
	v_cvt_pk_bf16_f32 v147, v45, v46
	v_cvt_pk_bf16_f32 v140, v16, v17
	v_cvt_pk_bf16_f32 v141, v47, v79
	v_cvt_pk_bf16_f32 v142, v73, v78
	v_cvt_pk_bf16_f32 v143, v80, v81
	v_cvt_pk_bf16_f32 v136, v74, v75
	v_cvt_pk_bf16_f32 v137, v26, v27
	v_cvt_pk_bf16_f32 v138, v28, v29
	v_cvt_pk_bf16_f32 v139, v30, v31
	v_cvt_pk_bf16_f32 v132, v76, v77
	v_cvt_pk_bf16_f32 v133, v85, v22
	v_cvt_pk_bf16_f32 v134, v23, v82
	v_cvt_pk_bf16_f32 v135, v84, v18
	v_cvt_pk_bf16_f32 v128, v8, v9
	v_cvt_pk_bf16_f32 v129, v10, v11
	v_cvt_pk_bf16_f32 v130, v0, v1
	v_mov_b64_e32 v[0:1], s[46:47]
	v_cvt_pk_bf16_f32 v131, v2, v3
	v_mad_i64_i32 v[2:3], s[46:47], v182, s57, v[0:1]
	v_lshl_add_u64 v[2:3], v[2:3], 0, v[184:185]
	v_lshl_add_u64 v[2:3], v[2:3], 0, v[160:161]
	s_add_i32 s94, s6, s80
	v_lshl_add_u64 v[2:3], v[2:3], 0, v[156:157]
	s_mov_b32 m0, s94
	s_waitcnt vmcnt(0)
	s_waitcnt vmcnt(0)
	s_barrier
	v_mad_i64_i32 v[2:3], s[46:47], v186, s57, v[0:1]
	v_lshl_add_u64 v[2:3], v[2:3], 0, v[188:189]
	v_lshl_add_u64 v[2:3], v[2:3], 0, v[190:191]
	s_add_i32 s46, s7, s80
	v_lshl_add_u64 v[2:3], v[2:3], 0, v[192:193]
	s_mov_b32 m0, s46
	s_add_i32 s47, s38, s80
	v_mad_i64_i32 v[2:3], s[96:97], v194, s57, v[0:1]
	v_lshl_add_u64 v[2:3], v[2:3], 0, v[196:197]
	v_mad_i64_i32 v[0:1], s[96:97], v202, s57, v[0:1]
	v_lshl_add_u64 v[2:3], v[2:3], 0, v[198:199]
	v_lshl_add_u64 v[0:1], v[0:1], 0, v[204:205]
	v_lshl_add_u64 v[2:3], v[2:3], 0, v[200:201]
	s_mov_b32 m0, s47
	v_lshl_add_u64 v[0:1], v[0:1], 0, v[206:207]
	s_add_i32 s93, s40, s80
	v_lshl_add_u64 v[0:1], v[0:1], 0, v[208:209]
	s_mov_b32 m0, s93
	v_lshl_add_u64 v[2:3], s[4:5], 0, v[188:189]
	v_mul_f32_e32 v0, 0x3fb8aa3b, v69
	v_exp_f32_e32 v179, v0
	v_lshl_add_u64 v[0:1], s[4:5], 0, v[184:185]
	v_lshl_add_u64 v[0:1], v[0:1], 0, v[160:161]
	v_lshl_add_u64 v[0:1], v[0:1], 0, v[156:157]
	v_lshl_add_u64 v[2:3], v[2:3], 0, v[190:191]
	v_lshl_add_u64 v[4:5], s[4:5], 0, v[196:197]
	v_lshlrev_b64 v[210:211], 10, v[182:183]
	v_lshl_add_u64 v[2:3], v[2:3], 0, v[192:193]
	v_lshl_add_u64 v[4:5], v[4:5], 0, v[198:199]
	v_lshl_add_u64 v[6:7], s[4:5], 0, v[204:205]
	v_lshl_add_u64 v[222:223], v[0:1], 0, v[210:211]
	v_lshlrev_b64 v[212:213], 10, v[186:187]
	v_lshlrev_b64 v[214:215], 10, v[194:195]
	v_bitop3_b32 v183, v68, 16, s41 bitop3:0x36
	v_add_u32_e32 v195, s68, v175
	ds_read_b64_tr_b16 v[0:1], v195 offset:0
	v_lshl_add_u64 v[4:5], v[4:5], 0, v[200:201]
	v_lshl_add_u64 v[6:7], v[6:7], 0, v[206:207]
	v_lshl_add_u64 v[224:225], v[2:3], 0, v[212:213]
	v_lshlrev_b64 v[216:217], 10, v[202:203]
	v_add_u32_e32 v203, s81, v183
	ds_read_b64_tr_b16 v[2:3], v203 offset:0
	v_lshl_add_u64 v[6:7], v[6:7], 0, v[208:209]
	v_lshl_add_u64 v[218:219], v[4:5], 0, v[214:215]
	ds_read_b64_tr_b16 v[4:5], v195 offset:0x200
	v_lshl_add_u64 v[220:221], v[6:7], 0, v[216:217]
	ds_read_b64_tr_b16 v[6:7], v203 offset:0x200
	ds_read_b64_tr_b16 v[32:33], v195 offset:0x400
	ds_read_b64_tr_b16 v[34:35], v203 offset:0x400
	ds_read_b64_tr_b16 v[48:49], v195 offset:0x600
	ds_read_b64_tr_b16 v[50:51], v203 offset:0x600
	s_waitcnt lgkmcnt(0)
; #define VM_WAIT() asm volatile("s_waitcnt vmcnt(0)" ::: "memory")
; template <int DK, int DV, bool MLSTM>
; __device__ __forceinline__ void out_unit2(LAS unsigned char* lds, LAS unsigned char* ldstab, const OutArgs a, const int wv) {
;     ...
; #pragma unroll
;     for (int kb = 0; kb < 4; ++kb) { LA_PK4(p[kb], 0, pa[2 * kb]); LA_PK4(p[kb], 8, pa[2 * kb + 1]); }
;     ...
;     f32x16 o[NB];
; #pragma unroll
;     for (int nb = 0; nb < NB; ++nb) o[nb] = (f32x16){};
;     ...
; #pragma unroll
;     for (int pc = 0; pc < 4; ++pc) {
;         VM_WAIT(); __syncthreads();
;         OUT_DMA(pc + 1);
;         const bf16x8 af0 = pa[2 * pc], af1 = pa[2 * pc + 1];
;         OUT_MMA(pc & 1);
	v_permlane32_swap_b32_e32 v64, v66
	v_permlane32_swap_b32_e32 v65, v67
	v_permlane32_swap_b32_e32 v144, v146
	v_permlane32_swap_b32_e32 v140, v142
	v_permlane32_swap_b32_e32 v136, v138
	v_permlane32_swap_b32_e32 v132, v134
	v_add_u32_e32 v181, 0x100, v183
	v_mul_f32_e32 v235, 0x3fb8aa3b, v71
	v_permlane32_swap_b32_e32 v152, v154
	v_permlane32_swap_b32_e32 v153, v155
	v_permlane32_swap_b32_e32 v148, v150
	v_permlane32_swap_b32_e32 v149, v151
	v_permlane32_swap_b32_e32 v145, v147
	v_permlane32_swap_b32_e32 v141, v143
	v_permlane32_swap_b32_e32 v137, v139
	v_permlane32_swap_b32_e32 v133, v135
	v_permlane32_swap_b32_e32 v128, v130
	v_permlane32_swap_b32_e32 v129, v131
	ds_read_b64_tr_b16 v[68:69], v195 offset:0x1000
	ds_read_b64_tr_b16 v[70:71], v203 offset:0x1000
	ds_read_b64_tr_b16 v[72:73], v195 offset:0x1200
	v_mfma_f32_32x32x16_bf16 v[16:31], v[64:67], v[0:3], 0
	ds_read_b64_tr_b16 v[74:75], v203 offset:0x1200
	ds_read_b64_tr_b16 v[76:77], v195 offset:0x1400
	ds_read_b64_tr_b16 v[78:79], v203 offset:0x1400
	ds_read_b64_tr_b16 v[80:81], v195 offset:0x1600
	ds_read_b64_tr_b16 v[82:83], v203 offset:0x1600
	s_waitcnt lgkmcnt(0)
	v_mfma_f32_32x32x16_bf16 v[0:15], v[64:67], v[4:7], 0
	v_mfma_f32_32x32x16_bf16 v[32:47], v[64:67], v[32:35], 0
	v_mfma_f32_32x32x16_bf16 v[48:63], v[64:67], v[48:51], 0
	v_mfma_f32_32x32x16_bf16 v[16:31], v[152:155], v[68:71], v[16:31]
	v_add_u32_e32 v252, s70, v175
	ds_read_b64_tr_b16 v[68:69], v252 offset:0
	v_add_u32_e32 v253, s82, v183
	ds_read_b64_tr_b16 v[70:71], v253 offset:0
	v_mfma_f32_32x32x16_bf16 v[0:15], v[152:155], v[72:75], v[0:15]
	ds_read_b64_tr_b16 v[72:73], v252 offset:0x200
	ds_read_b64_tr_b16 v[74:75], v253 offset:0x200
	v_mfma_f32_32x32x16_bf16 v[32:47], v[152:155], v[76:79], v[32:47]
	ds_read_b64_tr_b16 v[76:77], v252 offset:0x400
	ds_read_b64_tr_b16 v[78:79], v253 offset:0x400
	ds_read_b64_tr_b16 v[236:237], v252 offset:0x600
	ds_read_b64_tr_b16 v[238:239], v253 offset:0x600
	s_waitcnt lgkmcnt(0)
	v_mfma_f32_32x32x16_bf16 v[48:63], v[152:155], v[80:83], v[48:63]
	v_mfma_f32_32x32x16_bf16 v[96:111], v[64:67], v[68:71], 0
	v_mfma_f32_32x32x16_bf16 v[112:127], v[64:67], v[72:75], 0
	v_mfma_f32_32x32x16_bf16 v[80:95], v[64:67], v[76:79], 0
	v_mfma_f32_32x32x16_bf16 v[64:79], v[64:67], v[236:239], 0
	ds_read_b64_tr_b16 v[236:237], v252 offset:0x1000
	ds_read_b64_tr_b16 v[238:239], v253 offset:0x1000
	ds_read_b64_tr_b16 v[240:241], v252 offset:0x1200
	ds_read_b64_tr_b16 v[242:243], v253 offset:0x1200
	ds_read_b64_tr_b16 v[244:245], v252 offset:0x1400
	ds_read_b64_tr_b16 v[246:247], v253 offset:0x1400
	ds_read_b64_tr_b16 v[248:249], v252 offset:0x1600
	ds_read_b64_tr_b16 v[250:251], v253 offset:0x1600
	s_waitcnt lgkmcnt(0)
	s_add_u32 s96, s39, 0xc1000
	s_addc_u32 s97, s16, 0
	v_mfma_f32_32x32x16_bf16 v[96:111], v[152:155], v[236:239], v[96:111]
	v_mov_b64_e32 v[236:237], s[96:97]
	v_mad_i64_i32 v[238:239], s[96:97], v182, s57, v[236:237]
	v_lshl_add_u64 v[238:239], v[238:239], 0, v[184:185]
	v_lshl_add_u64 v[238:239], v[238:239], 0, v[160:161]
	s_mov_b32 m0, s42
	v_lshl_add_u64 v[238:239], v[238:239], 0, v[156:157]
	s_waitcnt vmcnt(0)
	s_waitcnt vmcnt(0) lgkmcnt(0)
	s_barrier
	global_load_lds_dwordx4 v[238:239], off
	v_mad_i64_i32 v[238:239], s[96:97], v186, s57, v[236:237]
	v_lshl_add_u64 v[238:239], v[238:239], 0, v[188:189]
	v_lshl_add_u64 v[238:239], v[238:239], 0, v[190:191]
	v_lshl_add_u64 v[238:239], v[238:239], 0, v[192:193]
	s_mov_b32 m0, s43
	v_mfma_f32_32x32x16_bf16 v[112:127], v[152:155], v[240:243], v[112:127]
	global_load_lds_dwordx4 v[238:239], off
	v_mad_i64_i32 v[238:239], s[96:97], v194, s57, v[236:237]
	v_lshl_add_u64 v[238:239], v[238:239], 0, v[196:197]
	v_mad_i64_i32 v[236:237], s[96:97], v202, s57, v[236:237]
	v_lshl_add_u64 v[238:239], v[238:239], 0, v[198:199]
	v_lshl_add_u64 v[236:237], v[236:237], 0, v[204:205]
	v_lshl_add_u64 v[238:239], v[238:239], 0, v[200:201]
	s_mov_b32 m0, s44
	v_lshl_add_u64 v[236:237], v[236:237], 0, v[206:207]
	global_load_lds_dwordx4 v[238:239], off
	v_lshl_add_u64 v[236:237], v[236:237], 0, v[208:209]
	s_mov_b32 m0, s45
	v_mfma_f32_32x32x16_bf16 v[80:95], v[152:155], v[244:247], v[80:95]
	global_load_lds_dwordx4 v[236:237], off
	v_add_u32_e32 v254, s80, v175
	v_add_u32_e32 v255, s83, v183
	v_mfma_f32_32x32x16_bf16 v[64:79], v[152:155], v[248:251], v[64:79]
	ds_read_b64_tr_b16 v[152:153], v254 offset:0
	ds_read_b64_tr_b16 v[154:155], v255 offset:0
	ds_read_b64_tr_b16 v[236:237], v254 offset:0x200
	ds_read_b64_tr_b16 v[238:239], v255 offset:0x200
	ds_read_b64_tr_b16 v[240:241], v254 offset:0x400
	ds_read_b64_tr_b16 v[242:243], v255 offset:0x400
	ds_read_b64_tr_b16 v[244:245], v254 offset:0x600
	ds_read_b64_tr_b16 v[246:247], v255 offset:0x600
	s_waitcnt lgkmcnt(0)
	s_nop 0
	v_mfma_f32_32x32x16_bf16 v[16:31], v[148:151], v[152:155], v[16:31]
	ds_read_b64_tr_b16 v[152:153], v254 offset:0x1000
	ds_read_b64_tr_b16 v[154:155], v255 offset:0x1000
	v_mfma_f32_32x32x16_bf16 v[0:15], v[148:151], v[236:239], v[0:15]
	ds_read_b64_tr_b16 v[236:237], v254 offset:0x1200
	ds_read_b64_tr_b16 v[238:239], v255 offset:0x1200
	v_mfma_f32_32x32x16_bf16 v[32:47], v[148:151], v[240:243], v[32:47]
	ds_read_b64_tr_b16 v[240:241], v254 offset:0x1400
	ds_read_b64_tr_b16 v[242:243], v255 offset:0x1400
	ds_read_b64_tr_b16 v[248:249], v254 offset:0x1600
	ds_read_b64_tr_b16 v[250:251], v255 offset:0x1600
	s_waitcnt lgkmcnt(0)
; #define VM_WAIT() asm volatile("s_waitcnt vmcnt(0)" ::: "memory")
; template <int DK, int DV, bool MLSTM>
; __device__ __forceinline__ void out_unit2(LAS unsigned char* lds, LAS unsigned char* ldstab, const OutArgs a, const int wv) {
;     ...
; #pragma unroll
;     for (int pc = 0; pc < 4; ++pc) {
;         VM_WAIT(); __syncthreads();
;         OUT_DMA(pc + 1);
;         const bf16x8 af0 = pa[2 * pc], af1 = pa[2 * pc + 1];
;         OUT_MMA(pc & 1);
	v_mfma_f32_32x32x16_bf16 v[48:63], v[148:151], v[244:247], v[48:63]
	v_mfma_f32_32x32x16_bf16 v[16:31], v[144:147], v[152:155], v[16:31]
	v_add_u32_e32 v226, s84, v175
	ds_read_b64_tr_b16 v[152:153], v226 offset:0
	v_add_u32_e32 v227, s85, v183
	ds_read_b64_tr_b16 v[154:155], v227 offset:0
	v_mfma_f32_32x32x16_bf16 v[0:15], v[144:147], v[236:239], v[0:15]
	ds_read_b64_tr_b16 v[236:237], v226 offset:0x200
	ds_read_b64_tr_b16 v[238:239], v227 offset:0x200
	v_mfma_f32_32x32x16_bf16 v[32:47], v[144:147], v[240:243], v[32:47]
	ds_read_b64_tr_b16 v[240:241], v226 offset:0x400
	ds_read_b64_tr_b16 v[242:243], v227 offset:0x400
	ds_read_b64_tr_b16 v[244:245], v226 offset:0x600
	ds_read_b64_tr_b16 v[246:247], v227 offset:0x600
	s_waitcnt lgkmcnt(0)
	v_mfma_f32_32x32x16_bf16 v[48:63], v[144:147], v[248:251], v[48:63]
	v_mfma_f32_32x32x16_bf16 v[96:111], v[148:151], v[152:155], v[96:111]
	ds_read_b64_tr_b16 v[152:153], v226 offset:0x1000
	ds_read_b64_tr_b16 v[154:155], v227 offset:0x1000
	v_mfma_f32_32x32x16_bf16 v[112:127], v[148:151], v[236:239], v[112:127]
	ds_read_b64_tr_b16 v[236:237], v226 offset:0x1200
	ds_read_b64_tr_b16 v[238:239], v227 offset:0x1200
	v_mfma_f32_32x32x16_bf16 v[80:95], v[148:151], v[240:243], v[80:95]
	ds_read_b64_tr_b16 v[240:241], v226 offset:0x1400
	ds_read_b64_tr_b16 v[242:243], v227 offset:0x1400
	ds_read_b64_tr_b16 v[248:249], v226 offset:0x1600
	ds_read_b64_tr_b16 v[250:251], v227 offset:0x1600
	s_waitcnt lgkmcnt(0)
	v_mfma_f32_32x32x16_bf16 v[64:79], v[148:151], v[244:247], v[64:79]
	s_mov_b32 m0, s94
	s_add_u32 s94, s39, 0x121000
	s_addc_u32 s95, s16, 0
	v_mov_b64_e32 v[148:149], s[94:95]
	v_mad_i64_i32 v[150:151], s[94:95], v182, s57, v[148:149]
	v_lshl_add_u64 v[150:151], v[150:151], 0, v[184:185]
	v_lshl_add_u64 v[150:151], v[150:151], 0, v[160:161]
	v_lshl_add_u64 v[150:151], v[150:151], 0, v[156:157]
	s_waitcnt vmcnt(0)
	s_waitcnt vmcnt(0) lgkmcnt(0)
	s_barrier
	global_load_lds_dwordx4 v[150:151], off
	v_mad_i64_i32 v[150:151], s[94:95], v186, s57, v[148:149]
	v_lshl_add_u64 v[150:151], v[150:151], 0, v[188:189]
	v_lshl_add_u64 v[150:151], v[150:151], 0, v[190:191]
	v_lshl_add_u64 v[150:151], v[150:151], 0, v[192:193]
	s_mov_b32 m0, s46
	v_mfma_f32_32x32x16_bf16 v[96:111], v[144:147], v[152:155], v[96:111]
	global_load_lds_dwordx4 v[150:151], off
	v_mad_i64_i32 v[150:151], s[94:95], v194, s57, v[148:149]
	v_lshl_add_u64 v[150:151], v[150:151], 0, v[196:197]
	s_mov_b32 m0, s47
	v_mad_i64_i32 v[148:149], s[46:47], v202, s57, v[148:149]
	v_lshl_add_u64 v[150:151], v[150:151], 0, v[198:199]
	v_lshl_add_u64 v[148:149], v[148:149], 0, v[204:205]
	v_lshl_add_u64 v[150:151], v[150:151], 0, v[200:201]
	v_lshl_add_u64 v[148:149], v[148:149], 0, v[206:207]
	global_load_lds_dwordx4 v[150:151], off
	v_lshl_add_u64 v[148:149], v[148:149], 0, v[208:209]
	s_mov_b32 m0, s93
	v_mfma_f32_32x32x16_bf16 v[112:127], v[144:147], v[236:239], v[112:127]
	global_load_lds_dwordx4 v[148:149], off
	v_mfma_f32_32x32x16_bf16 v[80:95], v[144:147], v[240:243], v[80:95]
	v_mfma_f32_32x32x16_bf16 v[64:79], v[144:147], v[248:251], v[64:79]
	ds_read_b64_tr_b16 v[144:145], v195 offset:0
	ds_read_b64_tr_b16 v[146:147], v203 offset:0
	ds_read_b64_tr_b16 v[148:149], v195 offset:0x200
	ds_read_b64_tr_b16 v[150:151], v203 offset:0x200
	ds_read_b64_tr_b16 v[152:153], v195 offset:0x400
	ds_read_b64_tr_b16 v[154:155], v203 offset:0x400
	ds_read_b64_tr_b16 v[182:183], v195 offset:0x600
	ds_read_b64_tr_b16 v[184:185], v203 offset:0x600
	s_waitcnt lgkmcnt(0)
	s_nop 0
	v_mfma_f32_32x32x16_bf16 v[16:31], v[140:143], v[144:147], v[16:31]
	ds_read_b64_tr_b16 v[144:145], v195 offset:0x1000
	ds_read_b64_tr_b16 v[146:147], v203 offset:0x1000
	v_mfma_f32_32x32x16_bf16 v[0:15], v[140:143], v[148:151], v[0:15]
	ds_read_b64_tr_b16 v[148:149], v195 offset:0x1200
	ds_read_b64_tr_b16 v[150:151], v203 offset:0x1200
	v_mfma_f32_32x32x16_bf16 v[32:47], v[140:143], v[152:155], v[32:47]
	ds_read_b64_tr_b16 v[152:153], v195 offset:0x1400
	ds_read_b64_tr_b16 v[154:155], v203 offset:0x1400
	ds_read_b64_tr_b16 v[186:187], v195 offset:0x1600
	ds_read_b64_tr_b16 v[188:189], v203 offset:0x1600
	s_waitcnt lgkmcnt(0)
	v_mfma_f32_32x32x16_bf16 v[48:63], v[140:143], v[182:185], v[48:63]
	v_mfma_f32_32x32x16_bf16 v[16:31], v[136:139], v[144:147], v[16:31]
	ds_read_b64_tr_b16 v[144:145], v252 offset:0
	ds_read_b64_tr_b16 v[146:147], v253 offset:0
	v_mfma_f32_32x32x16_bf16 v[0:15], v[136:139], v[148:151], v[0:15]
	ds_read_b64_tr_b16 v[148:149], v252 offset:0x200
	ds_read_b64_tr_b16 v[150:151], v253 offset:0x200
	v_mfma_f32_32x32x16_bf16 v[32:47], v[136:139], v[152:155], v[32:47]
	ds_read_b64_tr_b16 v[152:153], v252 offset:0x400
	ds_read_b64_tr_b16 v[154:155], v253 offset:0x400
	ds_read_b64_tr_b16 v[182:183], v252 offset:0x600
	ds_read_b64_tr_b16 v[184:185], v253 offset:0x600
	s_waitcnt lgkmcnt(0)
	v_mfma_f32_32x32x16_bf16 v[48:63], v[136:139], v[186:189], v[48:63]
	v_mfma_f32_32x32x16_bf16 v[96:111], v[140:143], v[144:147], v[96:111]
	ds_read_b64_tr_b16 v[144:145], v252 offset:0x1000
	ds_read_b64_tr_b16 v[146:147], v253 offset:0x1000
	v_mfma_f32_32x32x16_bf16 v[112:127], v[140:143], v[148:151], v[112:127]
	ds_read_b64_tr_b16 v[148:149], v252 offset:0x1200
	ds_read_b64_tr_b16 v[150:151], v253 offset:0x1200
	v_mfma_f32_32x32x16_bf16 v[80:95], v[140:143], v[152:155], v[80:95]
	ds_read_b64_tr_b16 v[152:153], v252 offset:0x1400
	ds_read_b64_tr_b16 v[154:155], v253 offset:0x1400
	ds_read_b64_tr_b16 v[186:187], v252 offset:0x1600
	ds_read_b64_tr_b16 v[188:189], v253 offset:0x1600
	s_waitcnt lgkmcnt(0)
	v_mfma_f32_32x32x16_bf16 v[64:79], v[140:143], v[182:185], v[64:79]
	s_mov_b32 m0, s42
	s_waitcnt vmcnt(0)
	s_waitcnt vmcnt(0) lgkmcnt(0)
	s_barrier
; #define VM_WAIT() asm volatile("s_waitcnt vmcnt(0)" ::: "memory")
; template <int DK, int DV, bool MLSTM>
; __device__ __forceinline__ void out_unit2(LAS unsigned char* lds, LAS unsigned char* ldstab, const OutArgs a, const int wv) {
;     ...
; #pragma unroll
;     for (int pc = 0; pc < 4; ++pc) {
;         VM_WAIT(); __syncthreads();
;         OUT_DMA(pc + 1);
;         const bf16x8 af0 = pa[2 * pc], af1 = pa[2 * pc + 1];
;         OUT_MMA(pc & 1);
;     }
; #pragma unroll 1
;     for (int pc = 4; pc < 4 + 2 * NCP; ++pc) {
;         VM_WAIT(); __syncthreads();
;         if (pc + 1 < 4 + 2 * NCP) OUT_DMA(pc + 1);
;         const int cq = pc - 4, dirb = cq >= NCP, cp = dirb ? cq - NCP : cq;
;         const float qs = dirb ? qsb : qsf;
;         const unsigned qa = QP + (cp >> 2) * 32768u + 512u * (cp & 3) + 8192u * rb;
;         const bf16x8 af0 = scale_frag(lds_r128(qa + rb0), qs), af1 = scale_frag(lds_r128(qa + rb1), qs);
	global_load_lds_dwordx4 v[222:223], off
	s_mov_b32 m0, s43
	v_mfma_f32_32x32x16_bf16 v[96:111], v[136:139], v[144:147], v[96:111]
	global_load_lds_dwordx4 v[224:225], off
	s_mov_b32 m0, s44
	s_nop 0
	global_load_lds_dwordx4 v[218:219], off
	s_mov_b32 m0, s45
	v_mfma_f32_32x32x16_bf16 v[112:127], v[136:139], v[148:151], v[112:127]
	global_load_lds_dwordx4 v[220:221], off
	ds_read_b64_tr_b16 v[140:141], v254 offset:0
	ds_read_b64_tr_b16 v[142:143], v255 offset:0
	ds_read_b64_tr_b16 v[144:145], v254 offset:0x200
	ds_read_b64_tr_b16 v[146:147], v255 offset:0x200
	ds_read_b64_tr_b16 v[148:149], v254 offset:0x400
	v_mfma_f32_32x32x16_bf16 v[80:95], v[136:139], v[152:155], v[80:95]
	ds_read_b64_tr_b16 v[150:151], v255 offset:0x400
	ds_read_b64_tr_b16 v[152:153], v254 offset:0x600
	ds_read_b64_tr_b16 v[154:155], v255 offset:0x600
	s_waitcnt lgkmcnt(0)
	v_mfma_f32_32x32x16_bf16 v[64:79], v[136:139], v[186:189], v[64:79]
	ds_read_b64_tr_b16 v[136:137], v254 offset:0x1000
	ds_read_b64_tr_b16 v[138:139], v255 offset:0x1000
	v_mfma_f32_32x32x16_bf16 v[16:31], v[132:135], v[140:143], v[16:31]
	ds_read_b64_tr_b16 v[140:141], v254 offset:0x1200
	ds_read_b64_tr_b16 v[142:143], v255 offset:0x1200
	v_mfma_f32_32x32x16_bf16 v[0:15], v[132:135], v[144:147], v[0:15]
	ds_read_b64_tr_b16 v[144:145], v254 offset:0x1400
	ds_read_b64_tr_b16 v[146:147], v255 offset:0x1400
	v_mfma_f32_32x32x16_bf16 v[32:47], v[132:135], v[148:151], v[32:47]
	ds_read_b64_tr_b16 v[148:149], v254 offset:0x1600
	ds_read_b64_tr_b16 v[150:151], v255 offset:0x1600
	s_waitcnt lgkmcnt(0)
	v_mfma_f32_32x32x16_bf16 v[48:63], v[132:135], v[152:155], v[48:63]
	v_mfma_f32_32x32x16_bf16 v[16:31], v[128:131], v[136:139], v[16:31]
	ds_read_b64_tr_b16 v[136:137], v226 offset:0
	ds_read_b64_tr_b16 v[138:139], v227 offset:0
	v_mfma_f32_32x32x16_bf16 v[0:15], v[128:131], v[140:143], v[0:15]
	ds_read_b64_tr_b16 v[140:141], v226 offset:0x200
	ds_read_b64_tr_b16 v[142:143], v227 offset:0x200
	v_mfma_f32_32x32x16_bf16 v[32:47], v[128:131], v[144:147], v[32:47]
	ds_read_b64_tr_b16 v[144:145], v226 offset:0x400
	ds_read_b64_tr_b16 v[146:147], v227 offset:0x400
	ds_read_b64_tr_b16 v[152:153], v226 offset:0x600
	ds_read_b64_tr_b16 v[154:155], v227 offset:0x600
	s_waitcnt lgkmcnt(0)
	v_mfma_f32_32x32x16_bf16 v[48:63], v[128:131], v[148:151], v[48:63]
	v_mfma_f32_32x32x16_bf16 v[96:111], v[132:135], v[136:139], v[96:111]
	ds_read_b64_tr_b16 v[136:137], v226 offset:0x1000
	ds_read_b64_tr_b16 v[138:139], v227 offset:0x1000
	v_mfma_f32_32x32x16_bf16 v[112:127], v[132:135], v[140:143], v[112:127]
	ds_read_b64_tr_b16 v[140:141], v226 offset:0x1200
	ds_read_b64_tr_b16 v[142:143], v227 offset:0x1200
	v_mfma_f32_32x32x16_bf16 v[80:95], v[132:135], v[144:147], v[80:95]
	ds_read_b64_tr_b16 v[146:147], v226 offset:0x1400
	ds_read_b64_tr_b16 v[148:149], v227 offset:0x1400
	ds_read_b64_tr_b16 v[182:183], v226 offset:0x1600
	ds_read_b64_tr_b16 v[184:185], v227 offset:0x1600
	s_waitcnt lgkmcnt(0)
	v_mfma_f32_32x32x16_bf16 v[64:79], v[132:135], v[152:155], v[64:79]
	v_mfma_f32_32x32x16_bf16 v[96:111], v[128:131], v[136:139], v[96:111]
	v_add_u32_e32 v226, s13, v173
	v_add_u32_e32 v227, s13, v177
	ds_read_b128 v[236:239], v226 offset:0
	ds_read_b128 v[240:243], v227 offset:0
	ds_read_b128 v[244:247], v226 offset:512
	ds_read_b128 v[248:251], v227 offset:512
	ds_read_b128 v[252:255], v226 offset:1024
	ds_read_b128 v[218:221], v227 offset:1024
	ds_read_b128 v[222:225], v226 offset:1536
	ds_read_b128 v[206:209], v227 offset:1536
	v_exp_f32_e32 v144, v235
	s_mov_b32 s39, 0x28000
	s_movk_i32 s41, 0x800
	v_lshlrev_b32_e32 v160, 1, v162
	v_lshlrev_b32_e32 v132, 1, v170
	v_lshlrev_b32_e32 v134, 1, v172
	v_lshlrev_b32_e32 v136, 1, v174
	v_mfma_f32_32x32x16_bf16 v[112:127], v[128:131], v[140:143], v[112:127]
	v_lshlrev_b32_e32 v138, 1, v176
	v_lshlrev_b32_e32 v140, 1, v178
	v_lshlrev_b32_e32 v142, 1, v180
	v_mfma_f32_32x32x16_bf16 v[80:95], v[128:131], v[146:149], v[80:95]
	v_mfma_f32_32x32x16_bf16 v[64:79], v[128:131], v[182:185], v[64:79]
	v_lshl_add_u64 v[198:199], v[158:159], 1, v[210:211]
	v_lshl_add_u64 v[198:199], v[198:199], 0, v[160:161]
	v_mov_b32_e32 v157, v161
	v_lshl_add_u64 v[198:199], v[198:199], 0, v[156:157]
	v_mov_b32_e32 v133, v161
	v_mov_b32_e32 v135, v161
	v_lshl_add_u64 v[200:201], v[164:165], 1, v[212:213]
	v_lshl_add_u64 v[200:201], v[200:201], 0, v[132:133]
	v_lshl_add_u64 v[200:201], v[200:201], 0, v[134:135]
	v_mov_b32_e32 v137, v161
	v_mov_b32_e32 v139, v161
	v_lshl_add_u64 v[202:203], v[166:167], 1, v[214:215]
	v_lshl_add_u64 v[202:203], v[202:203], 0, v[136:137]
	v_lshl_add_u64 v[202:203], v[202:203], 0, v[138:139]
	v_mov_b32_e32 v141, v161
	v_mov_b32_e32 v143, v161
	v_lshl_add_u64 v[204:205], v[168:169], 1, v[216:217]
	v_lshl_add_u64 v[204:205], v[204:205], 0, v[140:141]
	v_lshl_add_u64 v[204:205], v[204:205], 0, v[142:143]
	s_waitcnt vmcnt(0) lgkmcnt(0)
	s_barrier
; #define VM_WAIT() asm volatile("s_waitcnt vmcnt(0)" ::: "memory")
; template <int DK, int DV, bool MLSTM>
; __device__ __forceinline__ void out_unit2(LAS unsigned char* lds, LAS unsigned char* ldstab, const OutArgs a, const int wv) {
;     ...
;     for (int pc = 4; pc < 4 + 2 * NCP; ++pc) {
;         VM_WAIT(); __syncthreads();
;         if (pc + 1 < 4 + 2 * NCP) OUT_DMA(pc + 1);
;         const int cq = pc - 4, dirb = cq >= NCP, cp = dirb ? cq - NCP : cq;
;         const float qs = dirb ? qsb : qsf;
;         const unsigned qa = QP + (cp >> 2) * 32768u + 512u * (cp & 3) + 8192u * rb;
;         const bf16x8 af0 = scale_frag(lds_r128(qa + rb0), qs), af1 = scale_frag(lds_r128(qa + rb1), qs);
;         OUT_MMA(pc & 1);
;     }
	s_add_u32 s42, s4, 0x8000
	s_addc_u32 s43, s5, 0
	v_lshl_add_u64 v[128:129], s[42:43], 0, v[198:199]
	v_lshl_add_u64 v[130:131], s[42:43], 0, v[200:201]
	v_lshl_add_u64 v[146:147], s[42:43], 0, v[202:203]
	v_lshl_add_u64 v[148:149], s[42:43], 0, v[204:205]
	s_add_i32 m0, s6, 0x18000
	s_nop 0
	global_load_lds_dwordx4 v[128:129], off
	s_add_i32 m0, s7, 0x18000
	s_nop 0
	global_load_lds_dwordx4 v[130:131], off
	s_add_i32 m0, s38, 0x18000
	s_nop 0
	global_load_lds_dwordx4 v[146:147], off
	s_add_i32 m0, s40, 0x18000
	s_nop 0
	global_load_lds_dwordx4 v[148:149], off
	s_add_u32 s42, s4, 0x10000
	s_addc_u32 s43, s5, 0
	v_lshl_add_u64 v[128:129], s[42:43], 0, v[198:199]
	v_lshl_add_u64 v[130:131], s[42:43], 0, v[200:201]
	v_lshl_add_u64 v[146:147], s[42:43], 0, v[202:203]
	v_lshl_add_u64 v[148:149], s[42:43], 0, v[204:205]
	s_mov_b32 m0, s6
	s_nop 0
	global_load_lds_dwordx4 v[128:129], off
	s_mov_b32 m0, s7
	s_nop 0
	global_load_lds_dwordx4 v[130:131], off
	s_mov_b32 m0, s38
	s_nop 0
	global_load_lds_dwordx4 v[146:147], off
	s_mov_b32 m0, s40
	s_nop 0
	global_load_lds_dwordx4 v[148:149], off
	v_lshlrev_b32_e32 v135, 16, v236
	v_and_b32_e32 v137, 0xffff0000, v236
	v_mul_f32_e32 v135, v179, v135
	v_mul_f32_e32 v137, v179, v137
	v_cvt_pk_bf16_f32 v128, v135, v137
	v_lshlrev_b32_e32 v135, 16, v237
	v_and_b32_e32 v137, 0xffff0000, v237
	v_mul_f32_e32 v135, v179, v135
	v_mul_f32_e32 v137, v179, v137
	v_cvt_pk_bf16_f32 v129, v135, v137
	v_lshlrev_b32_e32 v135, 16, v238
	v_and_b32_e32 v137, 0xffff0000, v238
	v_mul_f32_e32 v135, v179, v135
	v_mul_f32_e32 v137, v179, v137
	v_cvt_pk_bf16_f32 v130, v135, v137
	v_lshlrev_b32_e32 v135, 16, v239
	v_and_b32_e32 v137, 0xffff0000, v239
	v_mul_f32_e32 v135, v179, v135
	v_mul_f32_e32 v137, v179, v137
	v_cvt_pk_bf16_f32 v131, v135, v137
	v_lshlrev_b32_e32 v135, 16, v240
	v_and_b32_e32 v137, 0xffff0000, v240
	v_mul_f32_e32 v135, v179, v135
	v_mul_f32_e32 v137, v179, v137
	v_cvt_pk_bf16_f32 v146, v135, v137
	v_lshlrev_b32_e32 v135, 16, v241
	v_and_b32_e32 v137, 0xffff0000, v241
	v_mul_f32_e32 v135, v179, v135
	v_mul_f32_e32 v137, v179, v137
	v_cvt_pk_bf16_f32 v147, v135, v137
	v_lshlrev_b32_e32 v135, 16, v242
	v_and_b32_e32 v137, 0xffff0000, v242
	v_mul_f32_e32 v135, v179, v135
	v_mul_f32_e32 v137, v179, v137
	v_cvt_pk_bf16_f32 v148, v135, v137
	v_lshlrev_b32_e32 v135, 16, v243
	v_and_b32_e32 v137, 0xffff0000, v243
	v_mul_f32_e32 v135, v179, v135
	v_mul_f32_e32 v137, v179, v137
	v_cvt_pk_bf16_f32 v149, v135, v137
	v_add_u32_e32 v133, 0x10000, v175
	ds_read_b64_tr_b16 v[150:151], v133 offset:0
	v_add_u32_e32 v135, 0x10000, v181
	ds_read_b64_tr_b16 v[152:153], v135 offset:0
	ds_read_b64_tr_b16 v[182:183], v133 offset:0x200
	ds_read_b64_tr_b16 v[184:185], v135 offset:0x200
	ds_read_b64_tr_b16 v[186:187], v133 offset:0x400
	ds_read_b64_tr_b16 v[188:189], v135 offset:0x400
	ds_read_b64_tr_b16 v[190:191], v133 offset:0x600
	ds_read_b64_tr_b16 v[192:193], v135 offset:0x600
	s_waitcnt lgkmcnt(0)
	s_nop 0
	v_mfma_f32_32x32x16_bf16 v[16:31], v[128:131], v[150:153], v[16:31]
	ds_read_b64_tr_b16 v[150:151], v133 offset:0x1000
	ds_read_b64_tr_b16 v[152:153], v135 offset:0x1000
	v_mfma_f32_32x32x16_bf16 v[0:15], v[128:131], v[182:185], v[0:15]
	ds_read_b64_tr_b16 v[182:183], v133 offset:0x1200
	ds_read_b64_tr_b16 v[184:185], v135 offset:0x1200
	v_mfma_f32_32x32x16_bf16 v[32:47], v[128:131], v[186:189], v[32:47]
	ds_read_b64_tr_b16 v[186:187], v133 offset:0x1400
	ds_read_b64_tr_b16 v[188:189], v135 offset:0x1400
	ds_read_b64_tr_b16 v[194:195], v133 offset:0x1600
	ds_read_b64_tr_b16 v[196:197], v135 offset:0x1600
	s_waitcnt lgkmcnt(0)
	v_mfma_f32_32x32x16_bf16 v[48:63], v[128:131], v[190:193], v[48:63]
	v_mfma_f32_32x32x16_bf16 v[16:31], v[146:149], v[150:153], v[16:31]
	v_add_u32_e32 v133, 0x2000, v133
	ds_read_b64_tr_b16 v[150:151], v133 offset:0
	v_add_u32_e32 v135, 0x2000, v135
	ds_read_b64_tr_b16 v[152:153], v135 offset:0
	v_mfma_f32_32x32x16_bf16 v[0:15], v[146:149], v[182:185], v[0:15]
	ds_read_b64_tr_b16 v[182:183], v133 offset:0x200
	ds_read_b64_tr_b16 v[184:185], v135 offset:0x200
	v_mfma_f32_32x32x16_bf16 v[32:47], v[146:149], v[186:189], v[32:47]
	ds_read_b64_tr_b16 v[186:187], v133 offset:0x400
	ds_read_b64_tr_b16 v[188:189], v135 offset:0x400
	ds_read_b64_tr_b16 v[190:191], v133 offset:0x600
	ds_read_b64_tr_b16 v[192:193], v135 offset:0x600
	s_waitcnt lgkmcnt(0)
	v_mfma_f32_32x32x16_bf16 v[48:63], v[146:149], v[194:197], v[48:63]
	v_mfma_f32_32x32x16_bf16 v[96:111], v[128:131], v[150:153], v[96:111]
	ds_read_b64_tr_b16 v[150:151], v133 offset:0x1000
	ds_read_b64_tr_b16 v[152:153], v135 offset:0x1000
	v_mfma_f32_32x32x16_bf16 v[112:127], v[128:131], v[182:185], v[112:127]
	ds_read_b64_tr_b16 v[182:183], v133 offset:0x1200
	ds_read_b64_tr_b16 v[184:185], v135 offset:0x1200
	v_mfma_f32_32x32x16_bf16 v[80:95], v[128:131], v[186:189], v[80:95]
	ds_read_b64_tr_b16 v[186:187], v133 offset:0x1400
	ds_read_b64_tr_b16 v[188:189], v135 offset:0x1400
	ds_read_b64_tr_b16 v[194:195], v133 offset:0x1600
	ds_read_b64_tr_b16 v[196:197], v135 offset:0x1600
	s_waitcnt lgkmcnt(0)
	v_mfma_f32_32x32x16_bf16 v[64:79], v[128:131], v[190:193], v[64:79]
	v_mfma_f32_32x32x16_bf16 v[96:111], v[146:149], v[150:153], v[96:111]
	v_mfma_f32_32x32x16_bf16 v[112:127], v[146:149], v[182:185], v[112:127]
	v_mfma_f32_32x32x16_bf16 v[80:95], v[146:149], v[186:189], v[80:95]
	v_mfma_f32_32x32x16_bf16 v[64:79], v[146:149], v[194:197], v[64:79]
	s_waitcnt vmcnt(4) lgkmcnt(0)
	s_barrier
; #define VM_WAIT() asm volatile("s_waitcnt vmcnt(0)" ::: "memory")
; template <int DK, int DV, bool MLSTM>
; __device__ __forceinline__ void out_unit2(LAS unsigned char* lds, LAS unsigned char* ldstab, const OutArgs a, const int wv) {
;     ...
;     for (int pc = 4; pc < 4 + 2 * NCP; ++pc) {
;         VM_WAIT(); __syncthreads();
;         if (pc + 1 < 4 + 2 * NCP) OUT_DMA(pc + 1);
;         const int cq = pc - 4, dirb = cq >= NCP, cp = dirb ? cq - NCP : cq;
;         const float qs = dirb ? qsb : qsf;
;         const unsigned qa = QP + (cp >> 2) * 32768u + 512u * (cp & 3) + 8192u * rb;
;         const bf16x8 af0 = scale_frag(lds_r128(qa + rb0), qs), af1 = scale_frag(lds_r128(qa + rb1), qs);
;         OUT_MMA(pc & 1);
;     }
	s_add_u32 s42, s4, 0x18000
	s_addc_u32 s43, s5, 0
	v_lshl_add_u64 v[128:129], s[42:43], 0, v[198:199]
	v_lshl_add_u64 v[130:131], s[42:43], 0, v[200:201]
	v_lshl_add_u64 v[146:147], s[42:43], 0, v[202:203]
	v_lshl_add_u64 v[148:149], s[42:43], 0, v[204:205]
	s_add_i32 m0, s6, 0x10000
	s_nop 0
	global_load_lds_dwordx4 v[128:129], off
	s_add_i32 m0, s7, 0x10000
	s_nop 0
	global_load_lds_dwordx4 v[130:131], off
	s_add_i32 m0, s38, 0x10000
	s_nop 0
	global_load_lds_dwordx4 v[146:147], off
	s_add_i32 m0, s40, 0x10000
	s_nop 0
	global_load_lds_dwordx4 v[148:149], off
	v_lshlrev_b32_e32 v135, 16, v244
	v_and_b32_e32 v137, 0xffff0000, v244
	v_mul_f32_e32 v135, v179, v135
	v_mul_f32_e32 v137, v179, v137
	v_cvt_pk_bf16_f32 v128, v135, v137
	v_lshlrev_b32_e32 v135, 16, v245
	v_and_b32_e32 v137, 0xffff0000, v245
	v_mul_f32_e32 v135, v179, v135
	v_mul_f32_e32 v137, v179, v137
	v_cvt_pk_bf16_f32 v129, v135, v137
	v_lshlrev_b32_e32 v135, 16, v246
	v_and_b32_e32 v137, 0xffff0000, v246
	v_mul_f32_e32 v135, v179, v135
	v_mul_f32_e32 v137, v179, v137
	v_cvt_pk_bf16_f32 v130, v135, v137
	v_lshlrev_b32_e32 v135, 16, v247
	v_and_b32_e32 v137, 0xffff0000, v247
	v_mul_f32_e32 v135, v179, v135
	v_mul_f32_e32 v137, v179, v137
	v_cvt_pk_bf16_f32 v131, v135, v137
	v_lshlrev_b32_e32 v135, 16, v248
	v_and_b32_e32 v137, 0xffff0000, v248
	v_mul_f32_e32 v135, v179, v135
	v_mul_f32_e32 v137, v179, v137
	v_cvt_pk_bf16_f32 v146, v135, v137
	v_lshlrev_b32_e32 v135, 16, v249
	v_and_b32_e32 v137, 0xffff0000, v249
	v_mul_f32_e32 v135, v179, v135
	v_mul_f32_e32 v137, v179, v137
	v_cvt_pk_bf16_f32 v147, v135, v137
	v_lshlrev_b32_e32 v135, 16, v250
	v_and_b32_e32 v137, 0xffff0000, v250
	v_mul_f32_e32 v135, v179, v135
	v_mul_f32_e32 v137, v179, v137
	v_cvt_pk_bf16_f32 v148, v135, v137
	v_lshlrev_b32_e32 v135, 16, v251
	v_and_b32_e32 v137, 0xffff0000, v251
	v_mul_f32_e32 v135, v179, v135
	v_mul_f32_e32 v137, v179, v137
	v_cvt_pk_bf16_f32 v149, v135, v137
	v_add_u32_e32 v133, 0x18000, v175
	ds_read_b64_tr_b16 v[150:151], v133 offset:0
	v_add_u32_e32 v135, 0x18000, v181
	ds_read_b64_tr_b16 v[152:153], v135 offset:0
	ds_read_b64_tr_b16 v[182:183], v133 offset:0x200
	ds_read_b64_tr_b16 v[184:185], v135 offset:0x200
	ds_read_b64_tr_b16 v[186:187], v133 offset:0x400
	ds_read_b64_tr_b16 v[188:189], v135 offset:0x400
	ds_read_b64_tr_b16 v[190:191], v133 offset:0x600
	ds_read_b64_tr_b16 v[192:193], v135 offset:0x600
	s_waitcnt lgkmcnt(0)
	s_nop 0
	v_mfma_f32_32x32x16_bf16 v[16:31], v[128:131], v[150:153], v[16:31]
	ds_read_b64_tr_b16 v[150:151], v133 offset:0x1000
	ds_read_b64_tr_b16 v[152:153], v135 offset:0x1000
	v_mfma_f32_32x32x16_bf16 v[0:15], v[128:131], v[182:185], v[0:15]
	ds_read_b64_tr_b16 v[182:183], v133 offset:0x1200
	ds_read_b64_tr_b16 v[184:185], v135 offset:0x1200
	v_mfma_f32_32x32x16_bf16 v[32:47], v[128:131], v[186:189], v[32:47]
	ds_read_b64_tr_b16 v[186:187], v133 offset:0x1400
	ds_read_b64_tr_b16 v[188:189], v135 offset:0x1400
	ds_read_b64_tr_b16 v[194:195], v133 offset:0x1600
	ds_read_b64_tr_b16 v[196:197], v135 offset:0x1600
	s_waitcnt lgkmcnt(0)
	v_mfma_f32_32x32x16_bf16 v[48:63], v[128:131], v[190:193], v[48:63]
	v_mfma_f32_32x32x16_bf16 v[16:31], v[146:149], v[150:153], v[16:31]
	v_add_u32_e32 v133, 0x2000, v133
	ds_read_b64_tr_b16 v[150:151], v133 offset:0
	v_add_u32_e32 v135, 0x2000, v135
	ds_read_b64_tr_b16 v[152:153], v135 offset:0
	v_mfma_f32_32x32x16_bf16 v[0:15], v[146:149], v[182:185], v[0:15]
	ds_read_b64_tr_b16 v[182:183], v133 offset:0x200
	ds_read_b64_tr_b16 v[184:185], v135 offset:0x200
	v_mfma_f32_32x32x16_bf16 v[32:47], v[146:149], v[186:189], v[32:47]
	ds_read_b64_tr_b16 v[186:187], v133 offset:0x400
	ds_read_b64_tr_b16 v[188:189], v135 offset:0x400
	ds_read_b64_tr_b16 v[190:191], v133 offset:0x600
	ds_read_b64_tr_b16 v[192:193], v135 offset:0x600
	s_waitcnt lgkmcnt(0)
	v_mfma_f32_32x32x16_bf16 v[48:63], v[146:149], v[194:197], v[48:63]
	v_mfma_f32_32x32x16_bf16 v[96:111], v[128:131], v[150:153], v[96:111]
	ds_read_b64_tr_b16 v[150:151], v133 offset:0x1000
	ds_read_b64_tr_b16 v[152:153], v135 offset:0x1000
	v_mfma_f32_32x32x16_bf16 v[112:127], v[128:131], v[182:185], v[112:127]
	ds_read_b64_tr_b16 v[182:183], v133 offset:0x1200
	ds_read_b64_tr_b16 v[184:185], v135 offset:0x1200
	v_mfma_f32_32x32x16_bf16 v[80:95], v[128:131], v[186:189], v[80:95]
	ds_read_b64_tr_b16 v[186:187], v133 offset:0x1400
	ds_read_b64_tr_b16 v[188:189], v135 offset:0x1400
	ds_read_b64_tr_b16 v[194:195], v133 offset:0x1600
	ds_read_b64_tr_b16 v[196:197], v135 offset:0x1600
	s_waitcnt lgkmcnt(0)
	v_mfma_f32_32x32x16_bf16 v[64:79], v[128:131], v[190:193], v[64:79]
	v_mfma_f32_32x32x16_bf16 v[96:111], v[146:149], v[150:153], v[96:111]
	v_mfma_f32_32x32x16_bf16 v[112:127], v[146:149], v[182:185], v[112:127]
	v_mfma_f32_32x32x16_bf16 v[80:95], v[146:149], v[186:189], v[80:95]
	v_mfma_f32_32x32x16_bf16 v[64:79], v[146:149], v[194:197], v[64:79]
	s_waitcnt vmcnt(4) lgkmcnt(0)
	s_barrier
; #define VM_WAIT() asm volatile("s_waitcnt vmcnt(0)" ::: "memory")
; template <int DK, int DV, bool MLSTM>
; __device__ __forceinline__ void out_unit2(LAS unsigned char* lds, LAS unsigned char* ldstab, const OutArgs a, const int wv) {
;     ...
;     for (int pc = 4; pc < 4 + 2 * NCP; ++pc) {
;         VM_WAIT(); __syncthreads();
;         if (pc + 1 < 4 + 2 * NCP) OUT_DMA(pc + 1);
;         const int cq = pc - 4, dirb = cq >= NCP, cp = dirb ? cq - NCP : cq;
;         const float qs = dirb ? qsb : qsf;
;         const unsigned qa = QP + (cp >> 2) * 32768u + 512u * (cp & 3) + 8192u * rb;
;         const bf16x8 af0 = scale_frag(lds_r128(qa + rb0), qs), af1 = scale_frag(lds_r128(qa + rb1), qs);
;         OUT_MMA(pc & 1);
;     }
	s_add_u32 s42, s4, 0x20000
	s_addc_u32 s43, s5, 0
	v_lshl_add_u64 v[128:129], s[42:43], 0, v[198:199]
	v_lshl_add_u64 v[130:131], s[42:43], 0, v[200:201]
	v_lshl_add_u64 v[146:147], s[42:43], 0, v[202:203]
	v_lshl_add_u64 v[148:149], s[42:43], 0, v[204:205]
	s_add_i32 m0, s6, 0x18000
	s_nop 0
	global_load_lds_dwordx4 v[128:129], off
	s_add_i32 m0, s7, 0x18000
	s_nop 0
	global_load_lds_dwordx4 v[130:131], off
	s_add_i32 m0, s38, 0x18000
	s_nop 0
	global_load_lds_dwordx4 v[146:147], off
	s_add_i32 m0, s40, 0x18000
	s_nop 0
	global_load_lds_dwordx4 v[148:149], off
	v_lshlrev_b32_e32 v135, 16, v252
	v_and_b32_e32 v137, 0xffff0000, v252
	v_mul_f32_e32 v135, v179, v135
	v_mul_f32_e32 v137, v179, v137
	v_cvt_pk_bf16_f32 v128, v135, v137
	v_lshlrev_b32_e32 v135, 16, v253
	v_and_b32_e32 v137, 0xffff0000, v253
	v_mul_f32_e32 v135, v179, v135
	v_mul_f32_e32 v137, v179, v137
	v_cvt_pk_bf16_f32 v129, v135, v137
	v_lshlrev_b32_e32 v135, 16, v254
	v_and_b32_e32 v137, 0xffff0000, v254
	v_mul_f32_e32 v135, v179, v135
	v_mul_f32_e32 v137, v179, v137
	v_cvt_pk_bf16_f32 v130, v135, v137
	v_lshlrev_b32_e32 v135, 16, v255
	v_and_b32_e32 v137, 0xffff0000, v255
	v_mul_f32_e32 v135, v179, v135
	v_mul_f32_e32 v137, v179, v137
	v_cvt_pk_bf16_f32 v131, v135, v137
	v_lshlrev_b32_e32 v135, 16, v218
	v_and_b32_e32 v137, 0xffff0000, v218
	v_mul_f32_e32 v135, v179, v135
	v_mul_f32_e32 v137, v179, v137
	v_cvt_pk_bf16_f32 v146, v135, v137
	v_lshlrev_b32_e32 v135, 16, v219
	v_and_b32_e32 v137, 0xffff0000, v219
	v_mul_f32_e32 v135, v179, v135
	v_mul_f32_e32 v137, v179, v137
	v_cvt_pk_bf16_f32 v147, v135, v137
	v_lshlrev_b32_e32 v135, 16, v220
	v_and_b32_e32 v137, 0xffff0000, v220
	v_mul_f32_e32 v135, v179, v135
	v_mul_f32_e32 v137, v179, v137
	v_cvt_pk_bf16_f32 v148, v135, v137
	v_lshlrev_b32_e32 v135, 16, v221
	v_and_b32_e32 v137, 0xffff0000, v221
	v_mul_f32_e32 v135, v179, v135
	v_mul_f32_e32 v137, v179, v137
	v_cvt_pk_bf16_f32 v149, v135, v137
	v_mov_b32_e32 v133, v175
	ds_read_b64_tr_b16 v[150:151], v133 offset:0
	v_mov_b32_e32 v135, v181
	ds_read_b64_tr_b16 v[152:153], v135 offset:0
	ds_read_b64_tr_b16 v[182:183], v133 offset:0x200
	ds_read_b64_tr_b16 v[184:185], v135 offset:0x200
	ds_read_b64_tr_b16 v[186:187], v133 offset:0x400
	ds_read_b64_tr_b16 v[188:189], v135 offset:0x400
	ds_read_b64_tr_b16 v[190:191], v133 offset:0x600
	ds_read_b64_tr_b16 v[192:193], v135 offset:0x600
	s_waitcnt lgkmcnt(0)
	s_nop 0
	v_mfma_f32_32x32x16_bf16 v[16:31], v[128:131], v[150:153], v[16:31]
	ds_read_b64_tr_b16 v[150:151], v133 offset:0x1000
	ds_read_b64_tr_b16 v[152:153], v135 offset:0x1000
	v_mfma_f32_32x32x16_bf16 v[0:15], v[128:131], v[182:185], v[0:15]
	ds_read_b64_tr_b16 v[182:183], v133 offset:0x1200
	ds_read_b64_tr_b16 v[184:185], v135 offset:0x1200
	v_mfma_f32_32x32x16_bf16 v[32:47], v[128:131], v[186:189], v[32:47]
	ds_read_b64_tr_b16 v[186:187], v133 offset:0x1400
	ds_read_b64_tr_b16 v[188:189], v135 offset:0x1400
	ds_read_b64_tr_b16 v[194:195], v133 offset:0x1600
	ds_read_b64_tr_b16 v[196:197], v135 offset:0x1600
	s_waitcnt lgkmcnt(0)
	v_mfma_f32_32x32x16_bf16 v[48:63], v[128:131], v[190:193], v[48:63]
	v_mfma_f32_32x32x16_bf16 v[16:31], v[146:149], v[150:153], v[16:31]
	v_add_u32_e32 v133, 0x2000, v133
	ds_read_b64_tr_b16 v[150:151], v133 offset:0
	v_add_u32_e32 v135, 0x2000, v135
	ds_read_b64_tr_b16 v[152:153], v135 offset:0
	v_mfma_f32_32x32x16_bf16 v[0:15], v[146:149], v[182:185], v[0:15]
	ds_read_b64_tr_b16 v[182:183], v133 offset:0x200
	ds_read_b64_tr_b16 v[184:185], v135 offset:0x200
	v_mfma_f32_32x32x16_bf16 v[32:47], v[146:149], v[186:189], v[32:47]
	ds_read_b64_tr_b16 v[186:187], v133 offset:0x400
	ds_read_b64_tr_b16 v[188:189], v135 offset:0x400
	ds_read_b64_tr_b16 v[190:191], v133 offset:0x600
	ds_read_b64_tr_b16 v[192:193], v135 offset:0x600
	s_waitcnt lgkmcnt(0)
	v_mfma_f32_32x32x16_bf16 v[48:63], v[146:149], v[194:197], v[48:63]
	v_mfma_f32_32x32x16_bf16 v[96:111], v[128:131], v[150:153], v[96:111]
	ds_read_b64_tr_b16 v[150:151], v133 offset:0x1000
	ds_read_b64_tr_b16 v[152:153], v135 offset:0x1000
	v_mfma_f32_32x32x16_bf16 v[112:127], v[128:131], v[182:185], v[112:127]
	ds_read_b64_tr_b16 v[182:183], v133 offset:0x1200
	ds_read_b64_tr_b16 v[184:185], v135 offset:0x1200
	v_mfma_f32_32x32x16_bf16 v[80:95], v[128:131], v[186:189], v[80:95]
	ds_read_b64_tr_b16 v[186:187], v133 offset:0x1400
	ds_read_b64_tr_b16 v[188:189], v135 offset:0x1400
	ds_read_b64_tr_b16 v[194:195], v133 offset:0x1600
	ds_read_b64_tr_b16 v[196:197], v135 offset:0x1600
	s_waitcnt lgkmcnt(0)
	v_mfma_f32_32x32x16_bf16 v[64:79], v[128:131], v[190:193], v[64:79]
	v_mfma_f32_32x32x16_bf16 v[96:111], v[146:149], v[150:153], v[96:111]
	v_mfma_f32_32x32x16_bf16 v[112:127], v[146:149], v[182:185], v[112:127]
	v_mfma_f32_32x32x16_bf16 v[80:95], v[146:149], v[186:189], v[80:95]
	v_mfma_f32_32x32x16_bf16 v[64:79], v[146:149], v[194:197], v[64:79]
	s_waitcnt vmcnt(4) lgkmcnt(0)
	s_barrier
; #define VM_WAIT() asm volatile("s_waitcnt vmcnt(0)" ::: "memory")
; template <int DK, int DV, bool MLSTM>
; __device__ __forceinline__ void out_unit2(LAS unsigned char* lds, LAS unsigned char* ldstab, const OutArgs a, const int wv) {
;     ...
;     for (int pc = 4; pc < 4 + 2 * NCP; ++pc) {
;         VM_WAIT(); __syncthreads();
;         if (pc + 1 < 4 + 2 * NCP) OUT_DMA(pc + 1);
;         const int cq = pc - 4, dirb = cq >= NCP, cp = dirb ? cq - NCP : cq;
;         const float qs = dirb ? qsb : qsf;
;         const unsigned qa = QP + (cp >> 2) * 32768u + 512u * (cp & 3) + 8192u * rb;
;         const bf16x8 af0 = scale_frag(lds_r128(qa + rb0), qs), af1 = scale_frag(lds_r128(qa + rb1), qs);
;         OUT_MMA(pc & 1);
;     }
	s_add_u32 s42, s4, 0x28000
	s_addc_u32 s43, s5, 0
	v_lshl_add_u64 v[128:129], s[42:43], 0, v[198:199]
	v_lshl_add_u64 v[130:131], s[42:43], 0, v[200:201]
	v_lshl_add_u64 v[146:147], s[42:43], 0, v[202:203]
	v_lshl_add_u64 v[148:149], s[42:43], 0, v[204:205]
	s_mov_b32 m0, s6
	s_nop 0
	global_load_lds_dwordx4 v[128:129], off
	s_mov_b32 m0, s7
	s_nop 0
	global_load_lds_dwordx4 v[130:131], off
	s_mov_b32 m0, s38
	s_nop 0
	global_load_lds_dwordx4 v[146:147], off
	s_mov_b32 m0, s40
	s_nop 0
	global_load_lds_dwordx4 v[148:149], off
	v_lshlrev_b32_e32 v135, 16, v222
	v_and_b32_e32 v137, 0xffff0000, v222
	v_mul_f32_e32 v135, v179, v135
	v_mul_f32_e32 v137, v179, v137
	v_cvt_pk_bf16_f32 v128, v135, v137
	v_lshlrev_b32_e32 v135, 16, v223
	v_and_b32_e32 v137, 0xffff0000, v223
	v_mul_f32_e32 v135, v179, v135
	v_mul_f32_e32 v137, v179, v137
	v_cvt_pk_bf16_f32 v129, v135, v137
	v_lshlrev_b32_e32 v135, 16, v224
	v_and_b32_e32 v137, 0xffff0000, v224
	v_mul_f32_e32 v135, v179, v135
	v_mul_f32_e32 v137, v179, v137
	v_cvt_pk_bf16_f32 v130, v135, v137
	v_lshlrev_b32_e32 v135, 16, v225
	v_and_b32_e32 v137, 0xffff0000, v225
	v_mul_f32_e32 v135, v179, v135
	v_mul_f32_e32 v137, v179, v137
	v_cvt_pk_bf16_f32 v131, v135, v137
	v_lshlrev_b32_e32 v135, 16, v206
	v_and_b32_e32 v137, 0xffff0000, v206
	v_mul_f32_e32 v135, v179, v135
	v_mul_f32_e32 v137, v179, v137
	v_cvt_pk_bf16_f32 v146, v135, v137
	v_lshlrev_b32_e32 v135, 16, v207
	v_and_b32_e32 v137, 0xffff0000, v207
	v_mul_f32_e32 v135, v179, v135
	v_mul_f32_e32 v137, v179, v137
	v_cvt_pk_bf16_f32 v147, v135, v137
	v_lshlrev_b32_e32 v135, 16, v208
	v_and_b32_e32 v137, 0xffff0000, v208
	v_mul_f32_e32 v135, v179, v135
	v_mul_f32_e32 v137, v179, v137
	v_cvt_pk_bf16_f32 v148, v135, v137
	v_lshlrev_b32_e32 v135, 16, v209
	v_and_b32_e32 v137, 0xffff0000, v209
	v_mul_f32_e32 v135, v179, v135
	v_mul_f32_e32 v137, v179, v137
	v_cvt_pk_bf16_f32 v149, v135, v137
	v_add_u32_e32 v133, 0x10000, v175
	ds_read_b64_tr_b16 v[150:151], v133 offset:0
	v_add_u32_e32 v135, 0x10000, v181
	ds_read_b64_tr_b16 v[152:153], v135 offset:0
	ds_read_b64_tr_b16 v[182:183], v133 offset:0x200
	ds_read_b64_tr_b16 v[184:185], v135 offset:0x200
	ds_read_b64_tr_b16 v[186:187], v133 offset:0x400
	ds_read_b64_tr_b16 v[188:189], v135 offset:0x400
	ds_read_b64_tr_b16 v[190:191], v133 offset:0x600
	ds_read_b64_tr_b16 v[192:193], v135 offset:0x600
	s_waitcnt lgkmcnt(0)
	s_nop 0
	v_mfma_f32_32x32x16_bf16 v[16:31], v[128:131], v[150:153], v[16:31]
	ds_read_b64_tr_b16 v[150:151], v133 offset:0x1000
	ds_read_b64_tr_b16 v[152:153], v135 offset:0x1000
	v_mfma_f32_32x32x16_bf16 v[0:15], v[128:131], v[182:185], v[0:15]
	ds_read_b64_tr_b16 v[182:183], v133 offset:0x1200
	ds_read_b64_tr_b16 v[184:185], v135 offset:0x1200
	v_mfma_f32_32x32x16_bf16 v[32:47], v[128:131], v[186:189], v[32:47]
	ds_read_b64_tr_b16 v[186:187], v133 offset:0x1400
	ds_read_b64_tr_b16 v[188:189], v135 offset:0x1400
	ds_read_b64_tr_b16 v[194:195], v133 offset:0x1600
	ds_read_b64_tr_b16 v[196:197], v135 offset:0x1600
	s_waitcnt lgkmcnt(0)
	v_mfma_f32_32x32x16_bf16 v[48:63], v[128:131], v[190:193], v[48:63]
	v_mfma_f32_32x32x16_bf16 v[16:31], v[146:149], v[150:153], v[16:31]
	v_add_u32_e32 v133, 0x2000, v133
	ds_read_b64_tr_b16 v[150:151], v133 offset:0
	v_add_u32_e32 v135, 0x2000, v135
	ds_read_b64_tr_b16 v[152:153], v135 offset:0
	v_mfma_f32_32x32x16_bf16 v[0:15], v[146:149], v[182:185], v[0:15]
	ds_read_b64_tr_b16 v[182:183], v133 offset:0x200
	ds_read_b64_tr_b16 v[184:185], v135 offset:0x200
	v_mfma_f32_32x32x16_bf16 v[32:47], v[146:149], v[186:189], v[32:47]
	ds_read_b64_tr_b16 v[186:187], v133 offset:0x400
	ds_read_b64_tr_b16 v[188:189], v135 offset:0x400
	ds_read_b64_tr_b16 v[190:191], v133 offset:0x600
	ds_read_b64_tr_b16 v[192:193], v135 offset:0x600
	s_waitcnt lgkmcnt(0)
	v_mfma_f32_32x32x16_bf16 v[48:63], v[146:149], v[194:197], v[48:63]
	v_mfma_f32_32x32x16_bf16 v[96:111], v[128:131], v[150:153], v[96:111]
	ds_read_b64_tr_b16 v[150:151], v133 offset:0x1000
	ds_read_b64_tr_b16 v[152:153], v135 offset:0x1000
	v_mfma_f32_32x32x16_bf16 v[112:127], v[128:131], v[182:185], v[112:127]
	ds_read_b64_tr_b16 v[182:183], v133 offset:0x1200
	ds_read_b64_tr_b16 v[184:185], v135 offset:0x1200
	v_mfma_f32_32x32x16_bf16 v[80:95], v[128:131], v[186:189], v[80:95]
	ds_read_b64_tr_b16 v[186:187], v133 offset:0x1400
	ds_read_b64_tr_b16 v[188:189], v135 offset:0x1400
	ds_read_b64_tr_b16 v[194:195], v133 offset:0x1600
	ds_read_b64_tr_b16 v[196:197], v135 offset:0x1600
	s_waitcnt lgkmcnt(0)
	v_mfma_f32_32x32x16_bf16 v[64:79], v[128:131], v[190:193], v[64:79]
	v_mfma_f32_32x32x16_bf16 v[96:111], v[146:149], v[150:153], v[96:111]
	v_mfma_f32_32x32x16_bf16 v[112:127], v[146:149], v[182:185], v[112:127]
	v_mfma_f32_32x32x16_bf16 v[80:95], v[146:149], v[186:189], v[80:95]
	v_mfma_f32_32x32x16_bf16 v[64:79], v[146:149], v[194:197], v[64:79]
	s_waitcnt vmcnt(4) lgkmcnt(0)
	s_barrier
; #define VM_WAIT() asm volatile("s_waitcnt vmcnt(0)" ::: "memory")
; __device__ __forceinline__ unsigned cvt_pk_bf16(float lo, float hi) { unsigned r; asm volatile("v_cvt_pk_bf16_f32 %0, %1, %2" : "=v"(r) : "v"(lo), "v"(hi)); return r; }
; __device__ __forceinline__ bf16x8 scale_frag(bf16x8 f, float s) {
;     u32x4 w = __builtin_bit_cast(u32x4, f); u32x4 o;
;     o.x = cvt_pk_bf16(bf_lo(w.x) * s, bf_hi(w.x) * s); o.y = cvt_pk_bf16(bf_lo(w.y) * s, bf_hi(w.y) * s);
;     o.z = cvt_pk_bf16(bf_lo(w.z) * s, bf_hi(w.z) * s); o.w = cvt_pk_bf16(bf_lo(w.w) * s, bf_hi(w.w) * s);
;     return __builtin_bit_cast(bf16x8, o);
; template <int DK, int DV, bool MLSTM>
; __device__ __forceinline__ void out_unit2(LAS unsigned char* lds, LAS unsigned char* ldstab, const OutArgs a, const int wv) {
;     ...
; #pragma unroll
;     for (int pc = 0; pc < 4; ++pc) {
;         VM_WAIT(); __syncthreads();
;         OUT_DMA(pc + 1);
;         const bf16x8 af0 = pa[2 * pc], af1 = pa[2 * pc + 1];
;         OUT_MMA(pc & 1);
;     }
; #pragma unroll 1
;     for (int pc = 4; pc < 4 + 2 * NCP; ++pc) {
;         VM_WAIT(); __syncthreads();
;         if (pc + 1 < 4 + 2 * NCP) OUT_DMA(pc + 1);
;         const int cq = pc - 4, dirb = cq >= NCP, cp = dirb ? cq - NCP : cq;
;         const float qs = dirb ? qsb : qsf;
;         const unsigned qa = QP + (cp >> 2) * 32768u + 512u * (cp & 3) + 8192u * rb;
;         const bf16x8 af0 = scale_frag(lds_r128(qa + rb0), qs), af1 = scale_frag(lds_r128(qa + rb1), qs);
;         OUT_MMA(pc & 1);
;     }
	s_add_u32 s42, s4, 0x30000
	s_addc_u32 s43, s5, 0
	v_lshl_add_u64 v[128:129], s[42:43], 0, v[198:199]
	v_lshl_add_u64 v[130:131], s[42:43], 0, v[200:201]
	v_lshl_add_u64 v[146:147], s[42:43], 0, v[202:203]
	v_lshl_add_u64 v[148:149], s[42:43], 0, v[204:205]
	s_add_i32 m0, s6, 0x10000
	s_nop 0
	global_load_lds_dwordx4 v[128:129], off
	s_add_i32 m0, s7, 0x10000
	s_nop 0
	global_load_lds_dwordx4 v[130:131], off
	s_add_i32 m0, s38, 0x10000
	s_nop 0
	global_load_lds_dwordx4 v[146:147], off
	s_add_i32 m0, s40, 0x10000
	s_nop 0
	global_load_lds_dwordx4 v[148:149], off
	v_add_u32_e32 v133, s13, v173
	v_add_u32_e32 v135, s13, v177
	ds_read_b128 v[128:131], v133 offset:32768
	ds_read_b128 v[146:149], v135 offset:32768
	s_waitcnt lgkmcnt(0)
	v_lshlrev_b32_e32 v135, 16, v128
	v_and_b32_e32 v137, 0xffff0000, v128
	v_mul_f32_e32 v135, v179, v135
	v_mul_f32_e32 v137, v179, v137
	v_cvt_pk_bf16_f32 v128, v135, v137
	v_lshlrev_b32_e32 v135, 16, v129
	v_and_b32_e32 v137, 0xffff0000, v129
	v_mul_f32_e32 v135, v179, v135
	v_mul_f32_e32 v137, v179, v137
	v_cvt_pk_bf16_f32 v129, v135, v137
	v_lshlrev_b32_e32 v135, 16, v130
	v_and_b32_e32 v137, 0xffff0000, v130
	v_mul_f32_e32 v135, v179, v135
	v_mul_f32_e32 v137, v179, v137
	v_cvt_pk_bf16_f32 v130, v135, v137
	v_lshlrev_b32_e32 v135, 16, v131
	v_and_b32_e32 v137, 0xffff0000, v131
	v_mul_f32_e32 v135, v179, v135
	v_mul_f32_e32 v137, v179, v137
	v_cvt_pk_bf16_f32 v131, v135, v137
	v_lshlrev_b32_e32 v135, 16, v146
	v_and_b32_e32 v137, 0xffff0000, v146
	v_mul_f32_e32 v135, v179, v135
	v_mul_f32_e32 v137, v179, v137
	v_cvt_pk_bf16_f32 v146, v135, v137
	v_lshlrev_b32_e32 v135, 16, v147
	v_and_b32_e32 v137, 0xffff0000, v147
	v_mul_f32_e32 v135, v179, v135
	v_mul_f32_e32 v137, v179, v137
	v_cvt_pk_bf16_f32 v147, v135, v137
	v_lshlrev_b32_e32 v135, 16, v148
	v_and_b32_e32 v137, 0xffff0000, v148
	v_mul_f32_e32 v135, v179, v135
	v_mul_f32_e32 v137, v179, v137
	v_cvt_pk_bf16_f32 v148, v135, v137
	v_lshlrev_b32_e32 v135, 16, v149
	v_and_b32_e32 v137, 0xffff0000, v149
	v_mul_f32_e32 v135, v179, v135
	v_mul_f32_e32 v137, v179, v137
	v_cvt_pk_bf16_f32 v149, v135, v137
	v_add_u32_e32 v133, 0x18000, v175
	ds_read_b64_tr_b16 v[150:151], v133 offset:0
	v_add_u32_e32 v135, 0x18000, v181
	ds_read_b64_tr_b16 v[152:153], v135 offset:0
	ds_read_b64_tr_b16 v[182:183], v133 offset:0x200
	ds_read_b64_tr_b16 v[184:185], v135 offset:0x200
	ds_read_b64_tr_b16 v[186:187], v133 offset:0x400
	ds_read_b64_tr_b16 v[188:189], v135 offset:0x400
	ds_read_b64_tr_b16 v[190:191], v133 offset:0x600
	ds_read_b64_tr_b16 v[192:193], v135 offset:0x600
	s_waitcnt lgkmcnt(0)
	s_nop 0
	v_mfma_f32_32x32x16_bf16 v[16:31], v[128:131], v[150:153], v[16:31]
	ds_read_b64_tr_b16 v[150:151], v133 offset:0x1000
	ds_read_b64_tr_b16 v[152:153], v135 offset:0x1000
	v_mfma_f32_32x32x16_bf16 v[0:15], v[128:131], v[182:185], v[0:15]
	ds_read_b64_tr_b16 v[182:183], v133 offset:0x1200
	ds_read_b64_tr_b16 v[184:185], v135 offset:0x1200
	v_mfma_f32_32x32x16_bf16 v[32:47], v[128:131], v[186:189], v[32:47]
	ds_read_b64_tr_b16 v[186:187], v133 offset:0x1400
	ds_read_b64_tr_b16 v[188:189], v135 offset:0x1400
	ds_read_b64_tr_b16 v[194:195], v133 offset:0x1600
	ds_read_b64_tr_b16 v[196:197], v135 offset:0x1600
	s_waitcnt lgkmcnt(0)
	v_mfma_f32_32x32x16_bf16 v[48:63], v[128:131], v[190:193], v[48:63]
	v_mfma_f32_32x32x16_bf16 v[16:31], v[146:149], v[150:153], v[16:31]
	v_add_u32_e32 v133, 0x2000, v133
	ds_read_b64_tr_b16 v[150:151], v133 offset:0
	v_add_u32_e32 v135, 0x2000, v135
	ds_read_b64_tr_b16 v[152:153], v135 offset:0
	v_mfma_f32_32x32x16_bf16 v[0:15], v[146:149], v[182:185], v[0:15]
	ds_read_b64_tr_b16 v[182:183], v133 offset:0x200
	ds_read_b64_tr_b16 v[184:185], v135 offset:0x200
	v_mfma_f32_32x32x16_bf16 v[32:47], v[146:149], v[186:189], v[32:47]
	ds_read_b64_tr_b16 v[186:187], v133 offset:0x400
	ds_read_b64_tr_b16 v[188:189], v135 offset:0x400
	ds_read_b64_tr_b16 v[190:191], v133 offset:0x600
	ds_read_b64_tr_b16 v[192:193], v135 offset:0x600
	s_waitcnt lgkmcnt(0)
	v_mfma_f32_32x32x16_bf16 v[48:63], v[146:149], v[194:197], v[48:63]
	v_mfma_f32_32x32x16_bf16 v[96:111], v[128:131], v[150:153], v[96:111]
	ds_read_b64_tr_b16 v[150:151], v133 offset:0x1000
	ds_read_b64_tr_b16 v[152:153], v135 offset:0x1000
	v_mfma_f32_32x32x16_bf16 v[112:127], v[128:131], v[182:185], v[112:127]
	ds_read_b64_tr_b16 v[182:183], v133 offset:0x1200
	ds_read_b64_tr_b16 v[184:185], v135 offset:0x1200
	v_mfma_f32_32x32x16_bf16 v[80:95], v[128:131], v[186:189], v[80:95]
	ds_read_b64_tr_b16 v[186:187], v133 offset:0x1400
	ds_read_b64_tr_b16 v[188:189], v135 offset:0x1400
	ds_read_b64_tr_b16 v[194:195], v133 offset:0x1600
	ds_read_b64_tr_b16 v[196:197], v135 offset:0x1600
	s_waitcnt lgkmcnt(0)
	v_mfma_f32_32x32x16_bf16 v[64:79], v[128:131], v[190:193], v[64:79]
	v_mfma_f32_32x32x16_bf16 v[96:111], v[146:149], v[150:153], v[96:111]
	v_mfma_f32_32x32x16_bf16 v[112:127], v[146:149], v[182:185], v[112:127]
	v_mfma_f32_32x32x16_bf16 v[80:95], v[146:149], v[186:189], v[80:95]
	v_mfma_f32_32x32x16_bf16 v[64:79], v[146:149], v[194:197], v[64:79]
	s_waitcnt vmcnt(4) lgkmcnt(0)
	s_barrier
; #define VM_WAIT() asm volatile("s_waitcnt vmcnt(0)" ::: "memory")
; __device__ __forceinline__ unsigned cvt_pk_bf16(float lo, float hi) { unsigned r; asm volatile("v_cvt_pk_bf16_f32 %0, %1, %2" : "=v"(r) : "v"(lo), "v"(hi)); return r; }
; __device__ __forceinline__ bf16x8 scale_frag(bf16x8 f, float s) {
;     u32x4 w = __builtin_bit_cast(u32x4, f); u32x4 o;
;     o.x = cvt_pk_bf16(bf_lo(w.x) * s, bf_hi(w.x) * s); o.y = cvt_pk_bf16(bf_lo(w.y) * s, bf_hi(w.y) * s);
;     o.z = cvt_pk_bf16(bf_lo(w.z) * s, bf_hi(w.z) * s); o.w = cvt_pk_bf16(bf_lo(w.w) * s, bf_hi(w.w) * s);
;     return __builtin_bit_cast(bf16x8, o);
; template <int DK, int DV, bool MLSTM>
; __device__ __forceinline__ void out_unit2(LAS unsigned char* lds, LAS unsigned char* ldstab, const OutArgs a, const int wv) {
;     ...
; #pragma unroll
;     for (int pc = 0; pc < 4; ++pc) {
;         VM_WAIT(); __syncthreads();
;         OUT_DMA(pc + 1);
;         const bf16x8 af0 = pa[2 * pc], af1 = pa[2 * pc + 1];
;         OUT_MMA(pc & 1);
;     }
; #pragma unroll 1
;     for (int pc = 4; pc < 4 + 2 * NCP; ++pc) {
;         VM_WAIT(); __syncthreads();
;         if (pc + 1 < 4 + 2 * NCP) OUT_DMA(pc + 1);
;         const int cq = pc - 4, dirb = cq >= NCP, cp = dirb ? cq - NCP : cq;
;         const float qs = dirb ? qsb : qsf;
;         const unsigned qa = QP + (cp >> 2) * 32768u + 512u * (cp & 3) + 8192u * rb;
;         const bf16x8 af0 = scale_frag(lds_r128(qa + rb0), qs), af1 = scale_frag(lds_r128(qa + rb1), qs);
;         OUT_MMA(pc & 1);
;     }
	s_add_u32 s42, s4, 0x38000
	s_addc_u32 s43, s5, 0
	v_lshl_add_u64 v[128:129], s[42:43], 0, v[198:199]
	v_lshl_add_u64 v[130:131], s[42:43], 0, v[200:201]
	v_lshl_add_u64 v[146:147], s[42:43], 0, v[202:203]
	v_lshl_add_u64 v[148:149], s[42:43], 0, v[204:205]
	s_add_i32 m0, s6, 0x18000
	s_nop 0
	global_load_lds_dwordx4 v[128:129], off
	s_add_i32 m0, s7, 0x18000
	s_nop 0
	global_load_lds_dwordx4 v[130:131], off
	s_add_i32 m0, s38, 0x18000
	s_nop 0
	global_load_lds_dwordx4 v[146:147], off
	s_add_i32 m0, s40, 0x18000
	s_nop 0
	global_load_lds_dwordx4 v[148:149], off
	v_add_u32_e32 v133, s13, v173
	v_add_u32_e32 v135, s13, v177
	ds_read_b128 v[128:131], v133 offset:33280
	ds_read_b128 v[146:149], v135 offset:33280
	s_waitcnt lgkmcnt(0)
	v_lshlrev_b32_e32 v135, 16, v128
	v_and_b32_e32 v137, 0xffff0000, v128
	v_mul_f32_e32 v135, v179, v135
	v_mul_f32_e32 v137, v179, v137
	v_cvt_pk_bf16_f32 v128, v135, v137
	v_lshlrev_b32_e32 v135, 16, v129
	v_and_b32_e32 v137, 0xffff0000, v129
	v_mul_f32_e32 v135, v179, v135
	v_mul_f32_e32 v137, v179, v137
	v_cvt_pk_bf16_f32 v129, v135, v137
	v_lshlrev_b32_e32 v135, 16, v130
	v_and_b32_e32 v137, 0xffff0000, v130
	v_mul_f32_e32 v135, v179, v135
	v_mul_f32_e32 v137, v179, v137
	v_cvt_pk_bf16_f32 v130, v135, v137
	v_lshlrev_b32_e32 v135, 16, v131
	v_and_b32_e32 v137, 0xffff0000, v131
	v_mul_f32_e32 v135, v179, v135
	v_mul_f32_e32 v137, v179, v137
	v_cvt_pk_bf16_f32 v131, v135, v137
	v_lshlrev_b32_e32 v135, 16, v146
	v_and_b32_e32 v137, 0xffff0000, v146
	v_mul_f32_e32 v135, v179, v135
	v_mul_f32_e32 v137, v179, v137
	v_cvt_pk_bf16_f32 v146, v135, v137
	v_lshlrev_b32_e32 v135, 16, v147
	v_and_b32_e32 v137, 0xffff0000, v147
	v_mul_f32_e32 v135, v179, v135
	v_mul_f32_e32 v137, v179, v137
	v_cvt_pk_bf16_f32 v147, v135, v137
	v_lshlrev_b32_e32 v135, 16, v148
	v_and_b32_e32 v137, 0xffff0000, v148
	v_mul_f32_e32 v135, v179, v135
	v_mul_f32_e32 v137, v179, v137
	v_cvt_pk_bf16_f32 v148, v135, v137
	v_lshlrev_b32_e32 v135, 16, v149
	v_and_b32_e32 v137, 0xffff0000, v149
	v_mul_f32_e32 v135, v179, v135
	v_mul_f32_e32 v137, v179, v137
	v_cvt_pk_bf16_f32 v149, v135, v137
	v_mov_b32_e32 v133, v175
	ds_read_b64_tr_b16 v[150:151], v133 offset:0
	v_mov_b32_e32 v135, v181
	ds_read_b64_tr_b16 v[152:153], v135 offset:0
	ds_read_b64_tr_b16 v[182:183], v133 offset:0x200
	ds_read_b64_tr_b16 v[184:185], v135 offset:0x200
	ds_read_b64_tr_b16 v[186:187], v133 offset:0x400
	ds_read_b64_tr_b16 v[188:189], v135 offset:0x400
	ds_read_b64_tr_b16 v[190:191], v133 offset:0x600
	ds_read_b64_tr_b16 v[192:193], v135 offset:0x600
	s_waitcnt lgkmcnt(0)
	s_nop 0
	v_mfma_f32_32x32x16_bf16 v[16:31], v[128:131], v[150:153], v[16:31]
	ds_read_b64_tr_b16 v[150:151], v133 offset:0x1000
	ds_read_b64_tr_b16 v[152:153], v135 offset:0x1000
	v_mfma_f32_32x32x16_bf16 v[0:15], v[128:131], v[182:185], v[0:15]
	ds_read_b64_tr_b16 v[182:183], v133 offset:0x1200
	ds_read_b64_tr_b16 v[184:185], v135 offset:0x1200
	v_mfma_f32_32x32x16_bf16 v[32:47], v[128:131], v[186:189], v[32:47]
	ds_read_b64_tr_b16 v[186:187], v133 offset:0x1400
	ds_read_b64_tr_b16 v[188:189], v135 offset:0x1400
	ds_read_b64_tr_b16 v[194:195], v133 offset:0x1600
	ds_read_b64_tr_b16 v[196:197], v135 offset:0x1600
	s_waitcnt lgkmcnt(0)
	v_mfma_f32_32x32x16_bf16 v[48:63], v[128:131], v[190:193], v[48:63]
	v_mfma_f32_32x32x16_bf16 v[16:31], v[146:149], v[150:153], v[16:31]
	v_add_u32_e32 v133, 0x2000, v133
	ds_read_b64_tr_b16 v[150:151], v133 offset:0
	v_add_u32_e32 v135, 0x2000, v135
	ds_read_b64_tr_b16 v[152:153], v135 offset:0
	v_mfma_f32_32x32x16_bf16 v[0:15], v[146:149], v[182:185], v[0:15]
	ds_read_b64_tr_b16 v[182:183], v133 offset:0x200
	ds_read_b64_tr_b16 v[184:185], v135 offset:0x200
	v_mfma_f32_32x32x16_bf16 v[32:47], v[146:149], v[186:189], v[32:47]
	ds_read_b64_tr_b16 v[186:187], v133 offset:0x400
	ds_read_b64_tr_b16 v[188:189], v135 offset:0x400
	ds_read_b64_tr_b16 v[190:191], v133 offset:0x600
	ds_read_b64_tr_b16 v[192:193], v135 offset:0x600
	s_waitcnt lgkmcnt(0)
	v_mfma_f32_32x32x16_bf16 v[48:63], v[146:149], v[194:197], v[48:63]
	v_mfma_f32_32x32x16_bf16 v[96:111], v[128:131], v[150:153], v[96:111]
	ds_read_b64_tr_b16 v[150:151], v133 offset:0x1000
	ds_read_b64_tr_b16 v[152:153], v135 offset:0x1000
	v_mfma_f32_32x32x16_bf16 v[112:127], v[128:131], v[182:185], v[112:127]
	ds_read_b64_tr_b16 v[182:183], v133 offset:0x1200
	ds_read_b64_tr_b16 v[184:185], v135 offset:0x1200
	v_mfma_f32_32x32x16_bf16 v[80:95], v[128:131], v[186:189], v[80:95]
	ds_read_b64_tr_b16 v[186:187], v133 offset:0x1400
	ds_read_b64_tr_b16 v[188:189], v135 offset:0x1400
	ds_read_b64_tr_b16 v[194:195], v133 offset:0x1600
	ds_read_b64_tr_b16 v[196:197], v135 offset:0x1600
	s_waitcnt lgkmcnt(0)
	v_mfma_f32_32x32x16_bf16 v[64:79], v[128:131], v[190:193], v[64:79]
	v_mfma_f32_32x32x16_bf16 v[96:111], v[146:149], v[150:153], v[96:111]
	v_mfma_f32_32x32x16_bf16 v[112:127], v[146:149], v[182:185], v[112:127]
	v_mfma_f32_32x32x16_bf16 v[80:95], v[146:149], v[186:189], v[80:95]
	v_mfma_f32_32x32x16_bf16 v[64:79], v[146:149], v[194:197], v[64:79]
	s_waitcnt vmcnt(4) lgkmcnt(0)
	s_barrier
; #define VM_WAIT() asm volatile("s_waitcnt vmcnt(0)" ::: "memory")
; __device__ __forceinline__ unsigned cvt_pk_bf16(float lo, float hi) { unsigned r; asm volatile("v_cvt_pk_bf16_f32 %0, %1, %2" : "=v"(r) : "v"(lo), "v"(hi)); return r; }
; __device__ __forceinline__ bf16x8 scale_frag(bf16x8 f, float s) {
;     u32x4 w = __builtin_bit_cast(u32x4, f); u32x4 o;
;     o.x = cvt_pk_bf16(bf_lo(w.x) * s, bf_hi(w.x) * s); o.y = cvt_pk_bf16(bf_lo(w.y) * s, bf_hi(w.y) * s);
;     o.z = cvt_pk_bf16(bf_lo(w.z) * s, bf_hi(w.z) * s); o.w = cvt_pk_bf16(bf_lo(w.w) * s, bf_hi(w.w) * s);
;     return __builtin_bit_cast(bf16x8, o);
; template <int DK, int DV, bool MLSTM>
; __device__ __forceinline__ void out_unit2(LAS unsigned char* lds, LAS unsigned char* ldstab, const OutArgs a, const int wv) {
;     ...
; #pragma unroll
;     for (int pc = 0; pc < 4; ++pc) {
;         VM_WAIT(); __syncthreads();
;         OUT_DMA(pc + 1);
;         const bf16x8 af0 = pa[2 * pc], af1 = pa[2 * pc + 1];
;         OUT_MMA(pc & 1);
;     }
; #pragma unroll 1
;     for (int pc = 4; pc < 4 + 2 * NCP; ++pc) {
;         VM_WAIT(); __syncthreads();
;         if (pc + 1 < 4 + 2 * NCP) OUT_DMA(pc + 1);
;         const int cq = pc - 4, dirb = cq >= NCP, cp = dirb ? cq - NCP : cq;
;         const float qs = dirb ? qsb : qsf;
;         const unsigned qa = QP + (cp >> 2) * 32768u + 512u * (cp & 3) + 8192u * rb;
;         const bf16x8 af0 = scale_frag(lds_r128(qa + rb0), qs), af1 = scale_frag(lds_r128(qa + rb1), qs);
;         OUT_MMA(pc & 1);
;     }
	s_add_u32 s42, s11, 0x0
	s_addc_u32 s43, s12, 0
	v_lshl_add_u64 v[128:129], s[42:43], 0, v[198:199]
	v_lshl_add_u64 v[130:131], s[42:43], 0, v[200:201]
	v_lshl_add_u64 v[146:147], s[42:43], 0, v[202:203]
	v_lshl_add_u64 v[148:149], s[42:43], 0, v[204:205]
	s_mov_b32 m0, s6
	s_nop 0
	global_load_lds_dwordx4 v[128:129], off
	s_mov_b32 m0, s7
	s_nop 0
	global_load_lds_dwordx4 v[130:131], off
	s_mov_b32 m0, s38
	s_nop 0
	global_load_lds_dwordx4 v[146:147], off
	s_mov_b32 m0, s40
	s_nop 0
	global_load_lds_dwordx4 v[148:149], off
	v_add_u32_e32 v133, s13, v173
	v_add_u32_e32 v135, s13, v177
	ds_read_b128 v[128:131], v133 offset:33792
	ds_read_b128 v[146:149], v135 offset:33792
	s_waitcnt lgkmcnt(0)
	v_lshlrev_b32_e32 v135, 16, v128
	v_and_b32_e32 v137, 0xffff0000, v128
	v_mul_f32_e32 v135, v179, v135
	v_mul_f32_e32 v137, v179, v137
	v_cvt_pk_bf16_f32 v128, v135, v137
	v_lshlrev_b32_e32 v135, 16, v129
	v_and_b32_e32 v137, 0xffff0000, v129
	v_mul_f32_e32 v135, v179, v135
	v_mul_f32_e32 v137, v179, v137
	v_cvt_pk_bf16_f32 v129, v135, v137
	v_lshlrev_b32_e32 v135, 16, v130
	v_and_b32_e32 v137, 0xffff0000, v130
	v_mul_f32_e32 v135, v179, v135
	v_mul_f32_e32 v137, v179, v137
	v_cvt_pk_bf16_f32 v130, v135, v137
	v_lshlrev_b32_e32 v135, 16, v131
	v_and_b32_e32 v137, 0xffff0000, v131
	v_mul_f32_e32 v135, v179, v135
	v_mul_f32_e32 v137, v179, v137
	v_cvt_pk_bf16_f32 v131, v135, v137
	v_lshlrev_b32_e32 v135, 16, v146
	v_and_b32_e32 v137, 0xffff0000, v146
	v_mul_f32_e32 v135, v179, v135
	v_mul_f32_e32 v137, v179, v137
	v_cvt_pk_bf16_f32 v146, v135, v137
	v_lshlrev_b32_e32 v135, 16, v147
	v_and_b32_e32 v137, 0xffff0000, v147
	v_mul_f32_e32 v135, v179, v135
	v_mul_f32_e32 v137, v179, v137
	v_cvt_pk_bf16_f32 v147, v135, v137
	v_lshlrev_b32_e32 v135, 16, v148
	v_and_b32_e32 v137, 0xffff0000, v148
	v_mul_f32_e32 v135, v179, v135
	v_mul_f32_e32 v137, v179, v137
	v_cvt_pk_bf16_f32 v148, v135, v137
	v_lshlrev_b32_e32 v135, 16, v149
	v_and_b32_e32 v137, 0xffff0000, v149
	v_mul_f32_e32 v135, v179, v135
	v_mul_f32_e32 v137, v179, v137
	v_cvt_pk_bf16_f32 v149, v135, v137
	v_add_u32_e32 v133, 0x10000, v175
	ds_read_b64_tr_b16 v[150:151], v133 offset:0
	v_add_u32_e32 v135, 0x10000, v181
	ds_read_b64_tr_b16 v[152:153], v135 offset:0
	ds_read_b64_tr_b16 v[182:183], v133 offset:0x200
	ds_read_b64_tr_b16 v[184:185], v135 offset:0x200
	ds_read_b64_tr_b16 v[186:187], v133 offset:0x400
	ds_read_b64_tr_b16 v[188:189], v135 offset:0x400
	ds_read_b64_tr_b16 v[190:191], v133 offset:0x600
	ds_read_b64_tr_b16 v[192:193], v135 offset:0x600
	s_waitcnt lgkmcnt(0)
	s_nop 0
	v_mfma_f32_32x32x16_bf16 v[16:31], v[128:131], v[150:153], v[16:31]
	ds_read_b64_tr_b16 v[150:151], v133 offset:0x1000
	ds_read_b64_tr_b16 v[152:153], v135 offset:0x1000
	v_mfma_f32_32x32x16_bf16 v[0:15], v[128:131], v[182:185], v[0:15]
	ds_read_b64_tr_b16 v[182:183], v133 offset:0x1200
	ds_read_b64_tr_b16 v[184:185], v135 offset:0x1200
	v_mfma_f32_32x32x16_bf16 v[32:47], v[128:131], v[186:189], v[32:47]
	ds_read_b64_tr_b16 v[186:187], v133 offset:0x1400
	ds_read_b64_tr_b16 v[188:189], v135 offset:0x1400
	ds_read_b64_tr_b16 v[194:195], v133 offset:0x1600
	ds_read_b64_tr_b16 v[196:197], v135 offset:0x1600
	s_waitcnt lgkmcnt(0)
	v_mfma_f32_32x32x16_bf16 v[48:63], v[128:131], v[190:193], v[48:63]
	v_mfma_f32_32x32x16_bf16 v[16:31], v[146:149], v[150:153], v[16:31]
	v_add_u32_e32 v133, 0x2000, v133
	ds_read_b64_tr_b16 v[150:151], v133 offset:0
	v_add_u32_e32 v135, 0x2000, v135
	ds_read_b64_tr_b16 v[152:153], v135 offset:0
	v_mfma_f32_32x32x16_bf16 v[0:15], v[146:149], v[182:185], v[0:15]
	ds_read_b64_tr_b16 v[182:183], v133 offset:0x200
	ds_read_b64_tr_b16 v[184:185], v135 offset:0x200
	v_mfma_f32_32x32x16_bf16 v[32:47], v[146:149], v[186:189], v[32:47]
	ds_read_b64_tr_b16 v[186:187], v133 offset:0x400
	ds_read_b64_tr_b16 v[188:189], v135 offset:0x400
	ds_read_b64_tr_b16 v[190:191], v133 offset:0x600
	ds_read_b64_tr_b16 v[192:193], v135 offset:0x600
	s_waitcnt lgkmcnt(0)
	v_mfma_f32_32x32x16_bf16 v[48:63], v[146:149], v[194:197], v[48:63]
	v_mfma_f32_32x32x16_bf16 v[96:111], v[128:131], v[150:153], v[96:111]
	ds_read_b64_tr_b16 v[150:151], v133 offset:0x1000
	ds_read_b64_tr_b16 v[152:153], v135 offset:0x1000
	v_mfma_f32_32x32x16_bf16 v[112:127], v[128:131], v[182:185], v[112:127]
	ds_read_b64_tr_b16 v[182:183], v133 offset:0x1200
	ds_read_b64_tr_b16 v[184:185], v135 offset:0x1200
	v_mfma_f32_32x32x16_bf16 v[80:95], v[128:131], v[186:189], v[80:95]
	ds_read_b64_tr_b16 v[186:187], v133 offset:0x1400
	ds_read_b64_tr_b16 v[188:189], v135 offset:0x1400
	ds_read_b64_tr_b16 v[194:195], v133 offset:0x1600
	ds_read_b64_tr_b16 v[196:197], v135 offset:0x1600
	s_waitcnt lgkmcnt(0)
	v_mfma_f32_32x32x16_bf16 v[64:79], v[128:131], v[190:193], v[64:79]
	v_mfma_f32_32x32x16_bf16 v[96:111], v[146:149], v[150:153], v[96:111]
	v_mfma_f32_32x32x16_bf16 v[112:127], v[146:149], v[182:185], v[112:127]
	v_mfma_f32_32x32x16_bf16 v[80:95], v[146:149], v[186:189], v[80:95]
	v_mfma_f32_32x32x16_bf16 v[64:79], v[146:149], v[194:197], v[64:79]
	s_waitcnt vmcnt(4) lgkmcnt(0)
	s_barrier
; #define VM_WAIT() asm volatile("s_waitcnt vmcnt(0)" ::: "memory")
; __device__ __forceinline__ unsigned cvt_pk_bf16(float lo, float hi) { unsigned r; asm volatile("v_cvt_pk_bf16_f32 %0, %1, %2" : "=v"(r) : "v"(lo), "v"(hi)); return r; }
; __device__ __forceinline__ bf16x8 scale_frag(bf16x8 f, float s) {
;     u32x4 w = __builtin_bit_cast(u32x4, f); u32x4 o;
;     o.x = cvt_pk_bf16(bf_lo(w.x) * s, bf_hi(w.x) * s); o.y = cvt_pk_bf16(bf_lo(w.y) * s, bf_hi(w.y) * s);
;     o.z = cvt_pk_bf16(bf_lo(w.z) * s, bf_hi(w.z) * s); o.w = cvt_pk_bf16(bf_lo(w.w) * s, bf_hi(w.w) * s);
;     return __builtin_bit_cast(bf16x8, o);
; template <int DK, int DV, bool MLSTM>
; __device__ __forceinline__ void out_unit2(LAS unsigned char* lds, LAS unsigned char* ldstab, const OutArgs a, const int wv) {
;     ...
; #pragma unroll
;     for (int pc = 0; pc < 4; ++pc) {
;         VM_WAIT(); __syncthreads();
;         OUT_DMA(pc + 1);
;         const bf16x8 af0 = pa[2 * pc], af1 = pa[2 * pc + 1];
;         OUT_MMA(pc & 1);
;     }
; #pragma unroll 1
;     for (int pc = 4; pc < 4 + 2 * NCP; ++pc) {
;         VM_WAIT(); __syncthreads();
;         if (pc + 1 < 4 + 2 * NCP) OUT_DMA(pc + 1);
;         const int cq = pc - 4, dirb = cq >= NCP, cp = dirb ? cq - NCP : cq;
;         const float qs = dirb ? qsb : qsf;
;         const unsigned qa = QP + (cp >> 2) * 32768u + 512u * (cp & 3) + 8192u * rb;
;         const bf16x8 af0 = scale_frag(lds_r128(qa + rb0), qs), af1 = scale_frag(lds_r128(qa + rb1), qs);
;         OUT_MMA(pc & 1);
;     }
	s_add_u32 s42, s11, 0x8000
	s_addc_u32 s43, s12, 0
	v_lshl_add_u64 v[128:129], s[42:43], 0, v[198:199]
	v_lshl_add_u64 v[130:131], s[42:43], 0, v[200:201]
	v_lshl_add_u64 v[146:147], s[42:43], 0, v[202:203]
	v_lshl_add_u64 v[148:149], s[42:43], 0, v[204:205]
	s_add_i32 m0, s6, 0x10000
	s_nop 0
	global_load_lds_dwordx4 v[128:129], off
	s_add_i32 m0, s7, 0x10000
	s_nop 0
	global_load_lds_dwordx4 v[130:131], off
	s_add_i32 m0, s38, 0x10000
	s_nop 0
	global_load_lds_dwordx4 v[146:147], off
	s_add_i32 m0, s40, 0x10000
	s_nop 0
	global_load_lds_dwordx4 v[148:149], off
	v_add_u32_e32 v133, s13, v173
	v_add_u32_e32 v135, s13, v177
	ds_read_b128 v[128:131], v133 offset:34304
	ds_read_b128 v[146:149], v135 offset:34304
	s_waitcnt lgkmcnt(0)
	v_lshlrev_b32_e32 v135, 16, v128
	v_and_b32_e32 v137, 0xffff0000, v128
	v_mul_f32_e32 v135, v179, v135
	v_mul_f32_e32 v137, v179, v137
	v_cvt_pk_bf16_f32 v128, v135, v137
	v_lshlrev_b32_e32 v135, 16, v129
	v_and_b32_e32 v137, 0xffff0000, v129
	v_mul_f32_e32 v135, v179, v135
	v_mul_f32_e32 v137, v179, v137
	v_cvt_pk_bf16_f32 v129, v135, v137
	v_lshlrev_b32_e32 v135, 16, v130
	v_and_b32_e32 v137, 0xffff0000, v130
	v_mul_f32_e32 v135, v179, v135
	v_mul_f32_e32 v137, v179, v137
	v_cvt_pk_bf16_f32 v130, v135, v137
	v_lshlrev_b32_e32 v135, 16, v131
	v_and_b32_e32 v137, 0xffff0000, v131
	v_mul_f32_e32 v135, v179, v135
	v_mul_f32_e32 v137, v179, v137
	v_cvt_pk_bf16_f32 v131, v135, v137
	v_lshlrev_b32_e32 v135, 16, v146
	v_and_b32_e32 v137, 0xffff0000, v146
	v_mul_f32_e32 v135, v179, v135
	v_mul_f32_e32 v137, v179, v137
	v_cvt_pk_bf16_f32 v146, v135, v137
	v_lshlrev_b32_e32 v135, 16, v147
	v_and_b32_e32 v137, 0xffff0000, v147
	v_mul_f32_e32 v135, v179, v135
	v_mul_f32_e32 v137, v179, v137
	v_cvt_pk_bf16_f32 v147, v135, v137
	v_lshlrev_b32_e32 v135, 16, v148
	v_and_b32_e32 v137, 0xffff0000, v148
	v_mul_f32_e32 v135, v179, v135
	v_mul_f32_e32 v137, v179, v137
	v_cvt_pk_bf16_f32 v148, v135, v137
	v_lshlrev_b32_e32 v135, 16, v149
	v_and_b32_e32 v137, 0xffff0000, v149
	v_mul_f32_e32 v135, v179, v135
	v_mul_f32_e32 v137, v179, v137
	v_cvt_pk_bf16_f32 v149, v135, v137
	v_add_u32_e32 v133, 0x18000, v175
	ds_read_b64_tr_b16 v[150:151], v133 offset:0
	v_add_u32_e32 v135, 0x18000, v181
	ds_read_b64_tr_b16 v[152:153], v135 offset:0
	ds_read_b64_tr_b16 v[182:183], v133 offset:0x200
	ds_read_b64_tr_b16 v[184:185], v135 offset:0x200
	ds_read_b64_tr_b16 v[186:187], v133 offset:0x400
	ds_read_b64_tr_b16 v[188:189], v135 offset:0x400
	ds_read_b64_tr_b16 v[190:191], v133 offset:0x600
	ds_read_b64_tr_b16 v[192:193], v135 offset:0x600
	s_waitcnt lgkmcnt(0)
	s_nop 0
	v_mfma_f32_32x32x16_bf16 v[16:31], v[128:131], v[150:153], v[16:31]
	ds_read_b64_tr_b16 v[150:151], v133 offset:0x1000
	ds_read_b64_tr_b16 v[152:153], v135 offset:0x1000
	v_mfma_f32_32x32x16_bf16 v[0:15], v[128:131], v[182:185], v[0:15]
	ds_read_b64_tr_b16 v[182:183], v133 offset:0x1200
	ds_read_b64_tr_b16 v[184:185], v135 offset:0x1200
	v_mfma_f32_32x32x16_bf16 v[32:47], v[128:131], v[186:189], v[32:47]
	ds_read_b64_tr_b16 v[186:187], v133 offset:0x1400
	ds_read_b64_tr_b16 v[188:189], v135 offset:0x1400
	ds_read_b64_tr_b16 v[194:195], v133 offset:0x1600
	ds_read_b64_tr_b16 v[196:197], v135 offset:0x1600
	s_waitcnt lgkmcnt(0)
	v_mfma_f32_32x32x16_bf16 v[48:63], v[128:131], v[190:193], v[48:63]
	v_mfma_f32_32x32x16_bf16 v[16:31], v[146:149], v[150:153], v[16:31]
	v_add_u32_e32 v133, 0x2000, v133
	ds_read_b64_tr_b16 v[150:151], v133 offset:0
	v_add_u32_e32 v135, 0x2000, v135
	ds_read_b64_tr_b16 v[152:153], v135 offset:0
	v_mfma_f32_32x32x16_bf16 v[0:15], v[146:149], v[182:185], v[0:15]
	ds_read_b64_tr_b16 v[182:183], v133 offset:0x200
	ds_read_b64_tr_b16 v[184:185], v135 offset:0x200
	v_mfma_f32_32x32x16_bf16 v[32:47], v[146:149], v[186:189], v[32:47]
	ds_read_b64_tr_b16 v[186:187], v133 offset:0x400
	ds_read_b64_tr_b16 v[188:189], v135 offset:0x400
	ds_read_b64_tr_b16 v[190:191], v133 offset:0x600
	ds_read_b64_tr_b16 v[192:193], v135 offset:0x600
	s_waitcnt lgkmcnt(0)
	v_mfma_f32_32x32x16_bf16 v[48:63], v[146:149], v[194:197], v[48:63]
	v_mfma_f32_32x32x16_bf16 v[96:111], v[128:131], v[150:153], v[96:111]
	ds_read_b64_tr_b16 v[150:151], v133 offset:0x1000
	ds_read_b64_tr_b16 v[152:153], v135 offset:0x1000
	v_mfma_f32_32x32x16_bf16 v[112:127], v[128:131], v[182:185], v[112:127]
	ds_read_b64_tr_b16 v[182:183], v133 offset:0x1200
	ds_read_b64_tr_b16 v[184:185], v135 offset:0x1200
	v_mfma_f32_32x32x16_bf16 v[80:95], v[128:131], v[186:189], v[80:95]
	ds_read_b64_tr_b16 v[186:187], v133 offset:0x1400
	ds_read_b64_tr_b16 v[188:189], v135 offset:0x1400
	ds_read_b64_tr_b16 v[194:195], v133 offset:0x1600
	ds_read_b64_tr_b16 v[196:197], v135 offset:0x1600
	s_waitcnt lgkmcnt(0)
	v_mfma_f32_32x32x16_bf16 v[64:79], v[128:131], v[190:193], v[64:79]
	v_mfma_f32_32x32x16_bf16 v[96:111], v[146:149], v[150:153], v[96:111]
	v_mfma_f32_32x32x16_bf16 v[112:127], v[146:149], v[182:185], v[112:127]
	v_mfma_f32_32x32x16_bf16 v[80:95], v[146:149], v[186:189], v[80:95]
	v_mfma_f32_32x32x16_bf16 v[64:79], v[146:149], v[194:197], v[64:79]
	s_waitcnt vmcnt(4) lgkmcnt(0)
	s_barrier
; #define VM_WAIT() asm volatile("s_waitcnt vmcnt(0)" ::: "memory")
; __device__ __forceinline__ unsigned cvt_pk_bf16(float lo, float hi) { unsigned r; asm volatile("v_cvt_pk_bf16_f32 %0, %1, %2" : "=v"(r) : "v"(lo), "v"(hi)); return r; }
; __device__ __forceinline__ bf16x8 scale_frag(bf16x8 f, float s) {
;     u32x4 w = __builtin_bit_cast(u32x4, f); u32x4 o;
;     o.x = cvt_pk_bf16(bf_lo(w.x) * s, bf_hi(w.x) * s); o.y = cvt_pk_bf16(bf_lo(w.y) * s, bf_hi(w.y) * s);
;     o.z = cvt_pk_bf16(bf_lo(w.z) * s, bf_hi(w.z) * s); o.w = cvt_pk_bf16(bf_lo(w.w) * s, bf_hi(w.w) * s);
;     return __builtin_bit_cast(bf16x8, o);
; template <int DK, int DV, bool MLSTM>
; __device__ __forceinline__ void out_unit2(LAS unsigned char* lds, LAS unsigned char* ldstab, const OutArgs a, const int wv) {
;     ...
; #pragma unroll
;     for (int pc = 0; pc < 4; ++pc) {
;         VM_WAIT(); __syncthreads();
;         OUT_DMA(pc + 1);
;         const bf16x8 af0 = pa[2 * pc], af1 = pa[2 * pc + 1];
;         OUT_MMA(pc & 1);
;     }
; #pragma unroll 1
;     for (int pc = 4; pc < 4 + 2 * NCP; ++pc) {
;         VM_WAIT(); __syncthreads();
;         if (pc + 1 < 4 + 2 * NCP) OUT_DMA(pc + 1);
;         const int cq = pc - 4, dirb = cq >= NCP, cp = dirb ? cq - NCP : cq;
;         const float qs = dirb ? qsb : qsf;
;         const unsigned qa = QP + (cp >> 2) * 32768u + 512u * (cp & 3) + 8192u * rb;
;         const bf16x8 af0 = scale_frag(lds_r128(qa + rb0), qs), af1 = scale_frag(lds_r128(qa + rb1), qs);
;         OUT_MMA(pc & 1);
;     }
	s_add_u32 s42, s11, 0x10000
	s_addc_u32 s43, s12, 0
	v_lshl_add_u64 v[128:129], s[42:43], 0, v[198:199]
	v_lshl_add_u64 v[130:131], s[42:43], 0, v[200:201]
	v_lshl_add_u64 v[146:147], s[42:43], 0, v[202:203]
	v_lshl_add_u64 v[148:149], s[42:43], 0, v[204:205]
	s_add_i32 m0, s6, 0x18000
	s_nop 0
	global_load_lds_dwordx4 v[128:129], off
	s_add_i32 m0, s7, 0x18000
	s_nop 0
	global_load_lds_dwordx4 v[130:131], off
	s_add_i32 m0, s38, 0x18000
	s_nop 0
	global_load_lds_dwordx4 v[146:147], off
	s_add_i32 m0, s40, 0x18000
	s_nop 0
	global_load_lds_dwordx4 v[148:149], off
	v_lshlrev_b32_e32 v135, 16, v236
	v_and_b32_e32 v137, 0xffff0000, v236
	v_mul_f32_e32 v135, v144, v135
	v_mul_f32_e32 v137, v144, v137
	v_cvt_pk_bf16_f32 v128, v135, v137
	v_lshlrev_b32_e32 v135, 16, v237
	v_and_b32_e32 v137, 0xffff0000, v237
	v_mul_f32_e32 v135, v144, v135
	v_mul_f32_e32 v137, v144, v137
	v_cvt_pk_bf16_f32 v129, v135, v137
	v_lshlrev_b32_e32 v135, 16, v238
	v_and_b32_e32 v137, 0xffff0000, v238
	v_mul_f32_e32 v135, v144, v135
	v_mul_f32_e32 v137, v144, v137
	v_cvt_pk_bf16_f32 v130, v135, v137
	v_lshlrev_b32_e32 v135, 16, v239
	v_and_b32_e32 v137, 0xffff0000, v239
	v_mul_f32_e32 v135, v144, v135
	v_mul_f32_e32 v137, v144, v137
	v_cvt_pk_bf16_f32 v131, v135, v137
	v_lshlrev_b32_e32 v135, 16, v240
	v_and_b32_e32 v137, 0xffff0000, v240
	v_mul_f32_e32 v135, v144, v135
	v_mul_f32_e32 v137, v144, v137
	v_cvt_pk_bf16_f32 v146, v135, v137
	v_lshlrev_b32_e32 v135, 16, v241
	v_and_b32_e32 v137, 0xffff0000, v241
	v_mul_f32_e32 v135, v144, v135
	v_mul_f32_e32 v137, v144, v137
	v_cvt_pk_bf16_f32 v147, v135, v137
	v_lshlrev_b32_e32 v135, 16, v242
	v_and_b32_e32 v137, 0xffff0000, v242
	v_mul_f32_e32 v135, v144, v135
	v_mul_f32_e32 v137, v144, v137
	v_cvt_pk_bf16_f32 v148, v135, v137
	v_lshlrev_b32_e32 v135, 16, v243
	v_and_b32_e32 v137, 0xffff0000, v243
	v_mul_f32_e32 v135, v144, v135
	v_mul_f32_e32 v137, v144, v137
	v_cvt_pk_bf16_f32 v149, v135, v137
	v_mov_b32_e32 v133, v175
	ds_read_b64_tr_b16 v[150:151], v133 offset:0
	v_mov_b32_e32 v135, v181
	ds_read_b64_tr_b16 v[152:153], v135 offset:0
	ds_read_b64_tr_b16 v[182:183], v133 offset:0x200
	ds_read_b64_tr_b16 v[184:185], v135 offset:0x200
	ds_read_b64_tr_b16 v[186:187], v133 offset:0x400
	ds_read_b64_tr_b16 v[188:189], v135 offset:0x400
	ds_read_b64_tr_b16 v[190:191], v133 offset:0x600
	ds_read_b64_tr_b16 v[192:193], v135 offset:0x600
	s_waitcnt lgkmcnt(0)
	s_nop 0
	v_mfma_f32_32x32x16_bf16 v[16:31], v[128:131], v[150:153], v[16:31]
	ds_read_b64_tr_b16 v[150:151], v133 offset:0x1000
	ds_read_b64_tr_b16 v[152:153], v135 offset:0x1000
	v_mfma_f32_32x32x16_bf16 v[0:15], v[128:131], v[182:185], v[0:15]
	ds_read_b64_tr_b16 v[182:183], v133 offset:0x1200
	ds_read_b64_tr_b16 v[184:185], v135 offset:0x1200
	v_mfma_f32_32x32x16_bf16 v[32:47], v[128:131], v[186:189], v[32:47]
	ds_read_b64_tr_b16 v[186:187], v133 offset:0x1400
	ds_read_b64_tr_b16 v[188:189], v135 offset:0x1400
	ds_read_b64_tr_b16 v[194:195], v133 offset:0x1600
	ds_read_b64_tr_b16 v[196:197], v135 offset:0x1600
	s_waitcnt lgkmcnt(0)
	v_mfma_f32_32x32x16_bf16 v[48:63], v[128:131], v[190:193], v[48:63]
	v_mfma_f32_32x32x16_bf16 v[16:31], v[146:149], v[150:153], v[16:31]
	v_add_u32_e32 v133, 0x2000, v133
	ds_read_b64_tr_b16 v[150:151], v133 offset:0
	v_add_u32_e32 v135, 0x2000, v135
	ds_read_b64_tr_b16 v[152:153], v135 offset:0
	v_mfma_f32_32x32x16_bf16 v[0:15], v[146:149], v[182:185], v[0:15]
	ds_read_b64_tr_b16 v[182:183], v133 offset:0x200
	ds_read_b64_tr_b16 v[184:185], v135 offset:0x200
	v_mfma_f32_32x32x16_bf16 v[32:47], v[146:149], v[186:189], v[32:47]
	ds_read_b64_tr_b16 v[186:187], v133 offset:0x400
	ds_read_b64_tr_b16 v[188:189], v135 offset:0x400
	ds_read_b64_tr_b16 v[190:191], v133 offset:0x600
	ds_read_b64_tr_b16 v[192:193], v135 offset:0x600
	s_waitcnt lgkmcnt(0)
	v_mfma_f32_32x32x16_bf16 v[48:63], v[146:149], v[194:197], v[48:63]
	v_mfma_f32_32x32x16_bf16 v[96:111], v[128:131], v[150:153], v[96:111]
	ds_read_b64_tr_b16 v[150:151], v133 offset:0x1000
	ds_read_b64_tr_b16 v[152:153], v135 offset:0x1000
	v_mfma_f32_32x32x16_bf16 v[112:127], v[128:131], v[182:185], v[112:127]
	ds_read_b64_tr_b16 v[182:183], v133 offset:0x1200
	ds_read_b64_tr_b16 v[184:185], v135 offset:0x1200
	v_mfma_f32_32x32x16_bf16 v[80:95], v[128:131], v[186:189], v[80:95]
	ds_read_b64_tr_b16 v[186:187], v133 offset:0x1400
	ds_read_b64_tr_b16 v[188:189], v135 offset:0x1400
	ds_read_b64_tr_b16 v[194:195], v133 offset:0x1600
	ds_read_b64_tr_b16 v[196:197], v135 offset:0x1600
	s_waitcnt lgkmcnt(0)
	v_mfma_f32_32x32x16_bf16 v[64:79], v[128:131], v[190:193], v[64:79]
	v_mfma_f32_32x32x16_bf16 v[96:111], v[146:149], v[150:153], v[96:111]
	v_mfma_f32_32x32x16_bf16 v[112:127], v[146:149], v[182:185], v[112:127]
	v_mfma_f32_32x32x16_bf16 v[80:95], v[146:149], v[186:189], v[80:95]
	v_mfma_f32_32x32x16_bf16 v[64:79], v[146:149], v[194:197], v[64:79]
	s_waitcnt vmcnt(4) lgkmcnt(0)
	s_barrier
; #define VM_WAIT() asm volatile("s_waitcnt vmcnt(0)" ::: "memory")
; __device__ __forceinline__ unsigned cvt_pk_bf16(float lo, float hi) { unsigned r; asm volatile("v_cvt_pk_bf16_f32 %0, %1, %2" : "=v"(r) : "v"(lo), "v"(hi)); return r; }
; __device__ __forceinline__ bf16x8 scale_frag(bf16x8 f, float s) {
;     u32x4 w = __builtin_bit_cast(u32x4, f); u32x4 o;
;     o.x = cvt_pk_bf16(bf_lo(w.x) * s, bf_hi(w.x) * s); o.y = cvt_pk_bf16(bf_lo(w.y) * s, bf_hi(w.y) * s);
;     o.z = cvt_pk_bf16(bf_lo(w.z) * s, bf_hi(w.z) * s); o.w = cvt_pk_bf16(bf_lo(w.w) * s, bf_hi(w.w) * s);
;     return __builtin_bit_cast(bf16x8, o);
; template <int DK, int DV, bool MLSTM>
; __device__ __forceinline__ void out_unit2(LAS unsigned char* lds, LAS unsigned char* ldstab, const OutArgs a, const int wv) {
;     ...
; #pragma unroll
;     for (int pc = 0; pc < 4; ++pc) {
;         VM_WAIT(); __syncthreads();
;         OUT_DMA(pc + 1);
;         const bf16x8 af0 = pa[2 * pc], af1 = pa[2 * pc + 1];
;         OUT_MMA(pc & 1);
;     }
; #pragma unroll 1
;     for (int pc = 4; pc < 4 + 2 * NCP; ++pc) {
;         VM_WAIT(); __syncthreads();
;         if (pc + 1 < 4 + 2 * NCP) OUT_DMA(pc + 1);
;         const int cq = pc - 4, dirb = cq >= NCP, cp = dirb ? cq - NCP : cq;
;         const float qs = dirb ? qsb : qsf;
;         const unsigned qa = QP + (cp >> 2) * 32768u + 512u * (cp & 3) + 8192u * rb;
;         const bf16x8 af0 = scale_frag(lds_r128(qa + rb0), qs), af1 = scale_frag(lds_r128(qa + rb1), qs);
;         OUT_MMA(pc & 1);
;     }
	s_add_u32 s42, s11, 0x18000
	s_addc_u32 s43, s12, 0
	v_lshl_add_u64 v[128:129], s[42:43], 0, v[198:199]
	v_lshl_add_u64 v[130:131], s[42:43], 0, v[200:201]
	v_lshl_add_u64 v[146:147], s[42:43], 0, v[202:203]
	v_lshl_add_u64 v[148:149], s[42:43], 0, v[204:205]
	s_mov_b32 m0, s6
	s_nop 0
	global_load_lds_dwordx4 v[128:129], off
	s_mov_b32 m0, s7
	s_nop 0
	global_load_lds_dwordx4 v[130:131], off
	s_mov_b32 m0, s38
	s_nop 0
	global_load_lds_dwordx4 v[146:147], off
	s_mov_b32 m0, s40
	s_nop 0
	global_load_lds_dwordx4 v[148:149], off
	v_lshlrev_b32_e32 v135, 16, v244
	v_and_b32_e32 v137, 0xffff0000, v244
	v_mul_f32_e32 v135, v144, v135
	v_mul_f32_e32 v137, v144, v137
	v_cvt_pk_bf16_f32 v128, v135, v137
	v_lshlrev_b32_e32 v135, 16, v245
	v_and_b32_e32 v137, 0xffff0000, v245
	v_mul_f32_e32 v135, v144, v135
	v_mul_f32_e32 v137, v144, v137
	v_cvt_pk_bf16_f32 v129, v135, v137
	v_lshlrev_b32_e32 v135, 16, v246
	v_and_b32_e32 v137, 0xffff0000, v246
	v_mul_f32_e32 v135, v144, v135
	v_mul_f32_e32 v137, v144, v137
	v_cvt_pk_bf16_f32 v130, v135, v137
	v_lshlrev_b32_e32 v135, 16, v247
	v_and_b32_e32 v137, 0xffff0000, v247
	v_mul_f32_e32 v135, v144, v135
	v_mul_f32_e32 v137, v144, v137
	v_cvt_pk_bf16_f32 v131, v135, v137
	v_lshlrev_b32_e32 v135, 16, v248
	v_and_b32_e32 v137, 0xffff0000, v248
	v_mul_f32_e32 v135, v144, v135
	v_mul_f32_e32 v137, v144, v137
	v_cvt_pk_bf16_f32 v146, v135, v137
	v_lshlrev_b32_e32 v135, 16, v249
	v_and_b32_e32 v137, 0xffff0000, v249
	v_mul_f32_e32 v135, v144, v135
	v_mul_f32_e32 v137, v144, v137
	v_cvt_pk_bf16_f32 v147, v135, v137
	v_lshlrev_b32_e32 v135, 16, v250
	v_and_b32_e32 v137, 0xffff0000, v250
	v_mul_f32_e32 v135, v144, v135
	v_mul_f32_e32 v137, v144, v137
	v_cvt_pk_bf16_f32 v148, v135, v137
	v_lshlrev_b32_e32 v135, 16, v251
	v_and_b32_e32 v137, 0xffff0000, v251
	v_mul_f32_e32 v135, v144, v135
	v_mul_f32_e32 v137, v144, v137
	v_cvt_pk_bf16_f32 v149, v135, v137
	v_add_u32_e32 v133, 0x10000, v175
	ds_read_b64_tr_b16 v[150:151], v133 offset:0
	v_add_u32_e32 v135, 0x10000, v181
	ds_read_b64_tr_b16 v[152:153], v135 offset:0
	ds_read_b64_tr_b16 v[182:183], v133 offset:0x200
	ds_read_b64_tr_b16 v[184:185], v135 offset:0x200
	ds_read_b64_tr_b16 v[186:187], v133 offset:0x400
	ds_read_b64_tr_b16 v[188:189], v135 offset:0x400
	ds_read_b64_tr_b16 v[190:191], v133 offset:0x600
	ds_read_b64_tr_b16 v[192:193], v135 offset:0x600
	s_waitcnt lgkmcnt(0)
	s_nop 0
	v_mfma_f32_32x32x16_bf16 v[16:31], v[128:131], v[150:153], v[16:31]
	ds_read_b64_tr_b16 v[150:151], v133 offset:0x1000
	ds_read_b64_tr_b16 v[152:153], v135 offset:0x1000
	v_mfma_f32_32x32x16_bf16 v[0:15], v[128:131], v[182:185], v[0:15]
	ds_read_b64_tr_b16 v[182:183], v133 offset:0x1200
	ds_read_b64_tr_b16 v[184:185], v135 offset:0x1200
	v_mfma_f32_32x32x16_bf16 v[32:47], v[128:131], v[186:189], v[32:47]
	ds_read_b64_tr_b16 v[186:187], v133 offset:0x1400
	ds_read_b64_tr_b16 v[188:189], v135 offset:0x1400
	ds_read_b64_tr_b16 v[194:195], v133 offset:0x1600
	ds_read_b64_tr_b16 v[196:197], v135 offset:0x1600
	s_waitcnt lgkmcnt(0)
	v_mfma_f32_32x32x16_bf16 v[48:63], v[128:131], v[190:193], v[48:63]
	v_mfma_f32_32x32x16_bf16 v[16:31], v[146:149], v[150:153], v[16:31]
	v_add_u32_e32 v133, 0x2000, v133
	ds_read_b64_tr_b16 v[150:151], v133 offset:0
	v_add_u32_e32 v135, 0x2000, v135
	ds_read_b64_tr_b16 v[152:153], v135 offset:0
	v_mfma_f32_32x32x16_bf16 v[0:15], v[146:149], v[182:185], v[0:15]
	ds_read_b64_tr_b16 v[182:183], v133 offset:0x200
	ds_read_b64_tr_b16 v[184:185], v135 offset:0x200
	v_mfma_f32_32x32x16_bf16 v[32:47], v[146:149], v[186:189], v[32:47]
	ds_read_b64_tr_b16 v[186:187], v133 offset:0x400
	ds_read_b64_tr_b16 v[188:189], v135 offset:0x400
	ds_read_b64_tr_b16 v[190:191], v133 offset:0x600
	ds_read_b64_tr_b16 v[192:193], v135 offset:0x600
	s_waitcnt lgkmcnt(0)
	v_mfma_f32_32x32x16_bf16 v[48:63], v[146:149], v[194:197], v[48:63]
	v_mfma_f32_32x32x16_bf16 v[96:111], v[128:131], v[150:153], v[96:111]
	ds_read_b64_tr_b16 v[150:151], v133 offset:0x1000
	ds_read_b64_tr_b16 v[152:153], v135 offset:0x1000
	v_mfma_f32_32x32x16_bf16 v[112:127], v[128:131], v[182:185], v[112:127]
	ds_read_b64_tr_b16 v[182:183], v133 offset:0x1200
	ds_read_b64_tr_b16 v[184:185], v135 offset:0x1200
	v_mfma_f32_32x32x16_bf16 v[80:95], v[128:131], v[186:189], v[80:95]
	ds_read_b64_tr_b16 v[186:187], v133 offset:0x1400
	ds_read_b64_tr_b16 v[188:189], v135 offset:0x1400
	ds_read_b64_tr_b16 v[194:195], v133 offset:0x1600
	ds_read_b64_tr_b16 v[196:197], v135 offset:0x1600
	s_waitcnt lgkmcnt(0)
	v_mfma_f32_32x32x16_bf16 v[64:79], v[128:131], v[190:193], v[64:79]
	v_mfma_f32_32x32x16_bf16 v[96:111], v[146:149], v[150:153], v[96:111]
	v_mfma_f32_32x32x16_bf16 v[112:127], v[146:149], v[182:185], v[112:127]
	v_mfma_f32_32x32x16_bf16 v[80:95], v[146:149], v[186:189], v[80:95]
	v_mfma_f32_32x32x16_bf16 v[64:79], v[146:149], v[194:197], v[64:79]
	s_waitcnt vmcnt(4) lgkmcnt(0)
	s_barrier
; #define VM_WAIT() asm volatile("s_waitcnt vmcnt(0)" ::: "memory")
; __device__ __forceinline__ unsigned cvt_pk_bf16(float lo, float hi) { unsigned r; asm volatile("v_cvt_pk_bf16_f32 %0, %1, %2" : "=v"(r) : "v"(lo), "v"(hi)); return r; }
; __device__ __forceinline__ bf16x8 scale_frag(bf16x8 f, float s) {
;     u32x4 w = __builtin_bit_cast(u32x4, f); u32x4 o;
;     o.x = cvt_pk_bf16(bf_lo(w.x) * s, bf_hi(w.x) * s); o.y = cvt_pk_bf16(bf_lo(w.y) * s, bf_hi(w.y) * s);
;     o.z = cvt_pk_bf16(bf_lo(w.z) * s, bf_hi(w.z) * s); o.w = cvt_pk_bf16(bf_lo(w.w) * s, bf_hi(w.w) * s);
;     return __builtin_bit_cast(bf16x8, o);
; template <int DK, int DV, bool MLSTM>
; __device__ __forceinline__ void out_unit2(LAS unsigned char* lds, LAS unsigned char* ldstab, const OutArgs a, const int wv) {
;     ...
; #pragma unroll
;     for (int pc = 0; pc < 4; ++pc) {
;         VM_WAIT(); __syncthreads();
;         OUT_DMA(pc + 1);
;         const bf16x8 af0 = pa[2 * pc], af1 = pa[2 * pc + 1];
;         OUT_MMA(pc & 1);
;     }
; #pragma unroll 1
;     for (int pc = 4; pc < 4 + 2 * NCP; ++pc) {
;         VM_WAIT(); __syncthreads();
;         if (pc + 1 < 4 + 2 * NCP) OUT_DMA(pc + 1);
;         const int cq = pc - 4, dirb = cq >= NCP, cp = dirb ? cq - NCP : cq;
;         const float qs = dirb ? qsb : qsf;
;         const unsigned qa = QP + (cp >> 2) * 32768u + 512u * (cp & 3) + 8192u * rb;
;         const bf16x8 af0 = scale_frag(lds_r128(qa + rb0), qs), af1 = scale_frag(lds_r128(qa + rb1), qs);
;         OUT_MMA(pc & 1);
;     }
	s_add_u32 s42, s11, 0x20000
	s_addc_u32 s43, s12, 0
	v_lshl_add_u64 v[128:129], s[42:43], 0, v[198:199]
	v_lshl_add_u64 v[130:131], s[42:43], 0, v[200:201]
	v_lshl_add_u64 v[146:147], s[42:43], 0, v[202:203]
	v_lshl_add_u64 v[148:149], s[42:43], 0, v[204:205]
	s_add_i32 m0, s6, 0x10000
	s_nop 0
	global_load_lds_dwordx4 v[128:129], off
	s_add_i32 m0, s7, 0x10000
	s_nop 0
	global_load_lds_dwordx4 v[130:131], off
	s_add_i32 m0, s38, 0x10000
	s_nop 0
	global_load_lds_dwordx4 v[146:147], off
	s_add_i32 m0, s40, 0x10000
	s_nop 0
	global_load_lds_dwordx4 v[148:149], off
	v_lshlrev_b32_e32 v135, 16, v252
	v_and_b32_e32 v137, 0xffff0000, v252
	v_mul_f32_e32 v135, v144, v135
	v_mul_f32_e32 v137, v144, v137
	v_cvt_pk_bf16_f32 v128, v135, v137
	v_lshlrev_b32_e32 v135, 16, v253
	v_and_b32_e32 v137, 0xffff0000, v253
	v_mul_f32_e32 v135, v144, v135
	v_mul_f32_e32 v137, v144, v137
	v_cvt_pk_bf16_f32 v129, v135, v137
	v_lshlrev_b32_e32 v135, 16, v254
	v_and_b32_e32 v137, 0xffff0000, v254
	v_mul_f32_e32 v135, v144, v135
	v_mul_f32_e32 v137, v144, v137
	v_cvt_pk_bf16_f32 v130, v135, v137
	v_lshlrev_b32_e32 v135, 16, v255
	v_and_b32_e32 v137, 0xffff0000, v255
	v_mul_f32_e32 v135, v144, v135
	v_mul_f32_e32 v137, v144, v137
	v_cvt_pk_bf16_f32 v131, v135, v137
	v_lshlrev_b32_e32 v135, 16, v218
	v_and_b32_e32 v137, 0xffff0000, v218
	v_mul_f32_e32 v135, v144, v135
	v_mul_f32_e32 v137, v144, v137
	v_cvt_pk_bf16_f32 v146, v135, v137
	v_lshlrev_b32_e32 v135, 16, v219
	v_and_b32_e32 v137, 0xffff0000, v219
	v_mul_f32_e32 v135, v144, v135
	v_mul_f32_e32 v137, v144, v137
	v_cvt_pk_bf16_f32 v147, v135, v137
	v_lshlrev_b32_e32 v135, 16, v220
	v_and_b32_e32 v137, 0xffff0000, v220
	v_mul_f32_e32 v135, v144, v135
	v_mul_f32_e32 v137, v144, v137
	v_cvt_pk_bf16_f32 v148, v135, v137
	v_lshlrev_b32_e32 v135, 16, v221
	v_and_b32_e32 v137, 0xffff0000, v221
	v_mul_f32_e32 v135, v144, v135
	v_mul_f32_e32 v137, v144, v137
	v_cvt_pk_bf16_f32 v149, v135, v137
	v_add_u32_e32 v133, 0x18000, v175
	ds_read_b64_tr_b16 v[150:151], v133 offset:0
	v_add_u32_e32 v135, 0x18000, v181
	ds_read_b64_tr_b16 v[152:153], v135 offset:0
	ds_read_b64_tr_b16 v[182:183], v133 offset:0x200
	ds_read_b64_tr_b16 v[184:185], v135 offset:0x200
	ds_read_b64_tr_b16 v[186:187], v133 offset:0x400
	ds_read_b64_tr_b16 v[188:189], v135 offset:0x400
	ds_read_b64_tr_b16 v[190:191], v133 offset:0x600
	ds_read_b64_tr_b16 v[192:193], v135 offset:0x600
	s_waitcnt lgkmcnt(0)
	s_nop 0
	v_mfma_f32_32x32x16_bf16 v[16:31], v[128:131], v[150:153], v[16:31]
	ds_read_b64_tr_b16 v[150:151], v133 offset:0x1000
	ds_read_b64_tr_b16 v[152:153], v135 offset:0x1000
	v_mfma_f32_32x32x16_bf16 v[0:15], v[128:131], v[182:185], v[0:15]
	ds_read_b64_tr_b16 v[182:183], v133 offset:0x1200
	ds_read_b64_tr_b16 v[184:185], v135 offset:0x1200
	v_mfma_f32_32x32x16_bf16 v[32:47], v[128:131], v[186:189], v[32:47]
	ds_read_b64_tr_b16 v[186:187], v133 offset:0x1400
	ds_read_b64_tr_b16 v[188:189], v135 offset:0x1400
	ds_read_b64_tr_b16 v[194:195], v133 offset:0x1600
	ds_read_b64_tr_b16 v[196:197], v135 offset:0x1600
	s_waitcnt lgkmcnt(0)
	v_mfma_f32_32x32x16_bf16 v[48:63], v[128:131], v[190:193], v[48:63]
	v_mfma_f32_32x32x16_bf16 v[16:31], v[146:149], v[150:153], v[16:31]
	v_add_u32_e32 v133, 0x2000, v133
	ds_read_b64_tr_b16 v[150:151], v133 offset:0
	v_add_u32_e32 v135, 0x2000, v135
	ds_read_b64_tr_b16 v[152:153], v135 offset:0
	v_mfma_f32_32x32x16_bf16 v[0:15], v[146:149], v[182:185], v[0:15]
	ds_read_b64_tr_b16 v[182:183], v133 offset:0x200
	ds_read_b64_tr_b16 v[184:185], v135 offset:0x200
	v_mfma_f32_32x32x16_bf16 v[32:47], v[146:149], v[186:189], v[32:47]
	ds_read_b64_tr_b16 v[186:187], v133 offset:0x400
	ds_read_b64_tr_b16 v[188:189], v135 offset:0x400
	ds_read_b64_tr_b16 v[190:191], v133 offset:0x600
	ds_read_b64_tr_b16 v[192:193], v135 offset:0x600
	s_waitcnt lgkmcnt(0)
	v_mfma_f32_32x32x16_bf16 v[48:63], v[146:149], v[194:197], v[48:63]
	v_mfma_f32_32x32x16_bf16 v[96:111], v[128:131], v[150:153], v[96:111]
	ds_read_b64_tr_b16 v[150:151], v133 offset:0x1000
	ds_read_b64_tr_b16 v[152:153], v135 offset:0x1000
	v_mfma_f32_32x32x16_bf16 v[112:127], v[128:131], v[182:185], v[112:127]
	ds_read_b64_tr_b16 v[182:183], v133 offset:0x1200
	ds_read_b64_tr_b16 v[184:185], v135 offset:0x1200
	v_mfma_f32_32x32x16_bf16 v[80:95], v[128:131], v[186:189], v[80:95]
	ds_read_b64_tr_b16 v[186:187], v133 offset:0x1400
	ds_read_b64_tr_b16 v[188:189], v135 offset:0x1400
	ds_read_b64_tr_b16 v[194:195], v133 offset:0x1600
	ds_read_b64_tr_b16 v[196:197], v135 offset:0x1600
	s_waitcnt lgkmcnt(0)
	v_mfma_f32_32x32x16_bf16 v[64:79], v[128:131], v[190:193], v[64:79]
	v_mfma_f32_32x32x16_bf16 v[96:111], v[146:149], v[150:153], v[96:111]
	v_mfma_f32_32x32x16_bf16 v[112:127], v[146:149], v[182:185], v[112:127]
	v_mfma_f32_32x32x16_bf16 v[80:95], v[146:149], v[186:189], v[80:95]
	v_mfma_f32_32x32x16_bf16 v[64:79], v[146:149], v[194:197], v[64:79]
	s_waitcnt vmcnt(4) lgkmcnt(0)
	s_barrier
; #define VM_WAIT() asm volatile("s_waitcnt vmcnt(0)" ::: "memory")
; __device__ __forceinline__ unsigned cvt_pk_bf16(float lo, float hi) { unsigned r; asm volatile("v_cvt_pk_bf16_f32 %0, %1, %2" : "=v"(r) : "v"(lo), "v"(hi)); return r; }
; __device__ __forceinline__ bf16x8 scale_frag(bf16x8 f, float s) {
;     u32x4 w = __builtin_bit_cast(u32x4, f); u32x4 o;
;     o.x = cvt_pk_bf16(bf_lo(w.x) * s, bf_hi(w.x) * s); o.y = cvt_pk_bf16(bf_lo(w.y) * s, bf_hi(w.y) * s);
;     o.z = cvt_pk_bf16(bf_lo(w.z) * s, bf_hi(w.z) * s); o.w = cvt_pk_bf16(bf_lo(w.w) * s, bf_hi(w.w) * s);
;     return __builtin_bit_cast(bf16x8, o);
; template <int DK, int DV, bool MLSTM>
; __device__ __forceinline__ void out_unit2(LAS unsigned char* lds, LAS unsigned char* ldstab, const OutArgs a, const int wv) {
;     ...
; #pragma unroll
;     for (int pc = 0; pc < 4; ++pc) {
;         VM_WAIT(); __syncthreads();
;         OUT_DMA(pc + 1);
;         const bf16x8 af0 = pa[2 * pc], af1 = pa[2 * pc + 1];
;         OUT_MMA(pc & 1);
;     }
; #pragma unroll 1
;     for (int pc = 4; pc < 4 + 2 * NCP; ++pc) {
;         VM_WAIT(); __syncthreads();
;         if (pc + 1 < 4 + 2 * NCP) OUT_DMA(pc + 1);
;         const int cq = pc - 4, dirb = cq >= NCP, cp = dirb ? cq - NCP : cq;
;         const float qs = dirb ? qsb : qsf;
;         const unsigned qa = QP + (cp >> 2) * 32768u + 512u * (cp & 3) + 8192u * rb;
;         const bf16x8 af0 = scale_frag(lds_r128(qa + rb0), qs), af1 = scale_frag(lds_r128(qa + rb1), qs);
;         OUT_MMA(pc & 1);
;     }
	s_add_u32 s42, s11, 0x28000
	s_addc_u32 s43, s12, 0
	v_lshl_add_u64 v[128:129], s[42:43], 0, v[198:199]
	v_lshl_add_u64 v[130:131], s[42:43], 0, v[200:201]
	v_lshl_add_u64 v[146:147], s[42:43], 0, v[202:203]
	v_lshl_add_u64 v[148:149], s[42:43], 0, v[204:205]
	s_add_i32 m0, s6, 0x18000
	s_nop 0
	global_load_lds_dwordx4 v[128:129], off
	s_add_i32 m0, s7, 0x18000
	s_nop 0
	global_load_lds_dwordx4 v[130:131], off
	s_add_i32 m0, s38, 0x18000
	s_nop 0
	global_load_lds_dwordx4 v[146:147], off
	s_add_i32 m0, s40, 0x18000
	s_nop 0
	global_load_lds_dwordx4 v[148:149], off
	v_lshlrev_b32_e32 v135, 16, v222
	v_and_b32_e32 v137, 0xffff0000, v222
	v_mul_f32_e32 v135, v144, v135
	v_mul_f32_e32 v137, v144, v137
	v_cvt_pk_bf16_f32 v128, v135, v137
	v_lshlrev_b32_e32 v135, 16, v223
	v_and_b32_e32 v137, 0xffff0000, v223
	v_mul_f32_e32 v135, v144, v135
	v_mul_f32_e32 v137, v144, v137
	v_cvt_pk_bf16_f32 v129, v135, v137
	v_lshlrev_b32_e32 v135, 16, v224
	v_and_b32_e32 v137, 0xffff0000, v224
	v_mul_f32_e32 v135, v144, v135
	v_mul_f32_e32 v137, v144, v137
	v_cvt_pk_bf16_f32 v130, v135, v137
	v_lshlrev_b32_e32 v135, 16, v225
	v_and_b32_e32 v137, 0xffff0000, v225
	v_mul_f32_e32 v135, v144, v135
	v_mul_f32_e32 v137, v144, v137
	v_cvt_pk_bf16_f32 v131, v135, v137
	v_lshlrev_b32_e32 v135, 16, v206
	v_and_b32_e32 v137, 0xffff0000, v206
	v_mul_f32_e32 v135, v144, v135
	v_mul_f32_e32 v137, v144, v137
	v_cvt_pk_bf16_f32 v146, v135, v137
	v_lshlrev_b32_e32 v135, 16, v207
	v_and_b32_e32 v137, 0xffff0000, v207
	v_mul_f32_e32 v135, v144, v135
	v_mul_f32_e32 v137, v144, v137
	v_cvt_pk_bf16_f32 v147, v135, v137
	v_lshlrev_b32_e32 v135, 16, v208
	v_and_b32_e32 v137, 0xffff0000, v208
	v_mul_f32_e32 v135, v144, v135
	v_mul_f32_e32 v137, v144, v137
	v_cvt_pk_bf16_f32 v148, v135, v137
	v_lshlrev_b32_e32 v135, 16, v209
	v_and_b32_e32 v137, 0xffff0000, v209
	v_mul_f32_e32 v135, v144, v135
	v_mul_f32_e32 v137, v144, v137
	v_cvt_pk_bf16_f32 v149, v135, v137
	v_mov_b32_e32 v133, v175
	ds_read_b64_tr_b16 v[150:151], v133 offset:0
	v_mov_b32_e32 v135, v181
	ds_read_b64_tr_b16 v[152:153], v135 offset:0
	ds_read_b64_tr_b16 v[182:183], v133 offset:0x200
	ds_read_b64_tr_b16 v[184:185], v135 offset:0x200
	ds_read_b64_tr_b16 v[186:187], v133 offset:0x400
	ds_read_b64_tr_b16 v[188:189], v135 offset:0x400
	ds_read_b64_tr_b16 v[190:191], v133 offset:0x600
	ds_read_b64_tr_b16 v[192:193], v135 offset:0x600
	s_waitcnt lgkmcnt(0)
	s_nop 0
	v_mfma_f32_32x32x16_bf16 v[16:31], v[128:131], v[150:153], v[16:31]
	ds_read_b64_tr_b16 v[150:151], v133 offset:0x1000
	ds_read_b64_tr_b16 v[152:153], v135 offset:0x1000
	v_mfma_f32_32x32x16_bf16 v[0:15], v[128:131], v[182:185], v[0:15]
	ds_read_b64_tr_b16 v[182:183], v133 offset:0x1200
	ds_read_b64_tr_b16 v[184:185], v135 offset:0x1200
	v_mfma_f32_32x32x16_bf16 v[32:47], v[128:131], v[186:189], v[32:47]
	ds_read_b64_tr_b16 v[186:187], v133 offset:0x1400
	ds_read_b64_tr_b16 v[188:189], v135 offset:0x1400
	ds_read_b64_tr_b16 v[194:195], v133 offset:0x1600
	ds_read_b64_tr_b16 v[196:197], v135 offset:0x1600
	s_waitcnt lgkmcnt(0)
	v_mfma_f32_32x32x16_bf16 v[48:63], v[128:131], v[190:193], v[48:63]
	v_mfma_f32_32x32x16_bf16 v[16:31], v[146:149], v[150:153], v[16:31]
	v_add_u32_e32 v133, 0x2000, v133
	ds_read_b64_tr_b16 v[150:151], v133 offset:0
	v_add_u32_e32 v135, 0x2000, v135
	ds_read_b64_tr_b16 v[152:153], v135 offset:0
	v_mfma_f32_32x32x16_bf16 v[0:15], v[146:149], v[182:185], v[0:15]
	ds_read_b64_tr_b16 v[182:183], v133 offset:0x200
	ds_read_b64_tr_b16 v[184:185], v135 offset:0x200
	v_mfma_f32_32x32x16_bf16 v[32:47], v[146:149], v[186:189], v[32:47]
	ds_read_b64_tr_b16 v[186:187], v133 offset:0x400
	ds_read_b64_tr_b16 v[188:189], v135 offset:0x400
	ds_read_b64_tr_b16 v[190:191], v133 offset:0x600
	ds_read_b64_tr_b16 v[192:193], v135 offset:0x600
	s_waitcnt lgkmcnt(0)
	v_mfma_f32_32x32x16_bf16 v[48:63], v[146:149], v[194:197], v[48:63]
	v_mfma_f32_32x32x16_bf16 v[96:111], v[128:131], v[150:153], v[96:111]
	ds_read_b64_tr_b16 v[150:151], v133 offset:0x1000
	ds_read_b64_tr_b16 v[152:153], v135 offset:0x1000
	v_mfma_f32_32x32x16_bf16 v[112:127], v[128:131], v[182:185], v[112:127]
	ds_read_b64_tr_b16 v[182:183], v133 offset:0x1200
	ds_read_b64_tr_b16 v[184:185], v135 offset:0x1200
	v_mfma_f32_32x32x16_bf16 v[80:95], v[128:131], v[186:189], v[80:95]
	ds_read_b64_tr_b16 v[186:187], v133 offset:0x1400
	ds_read_b64_tr_b16 v[188:189], v135 offset:0x1400
	ds_read_b64_tr_b16 v[194:195], v133 offset:0x1600
	ds_read_b64_tr_b16 v[196:197], v135 offset:0x1600
	s_waitcnt lgkmcnt(0)
	v_mfma_f32_32x32x16_bf16 v[64:79], v[128:131], v[190:193], v[64:79]
	v_mfma_f32_32x32x16_bf16 v[96:111], v[146:149], v[150:153], v[96:111]
	v_mfma_f32_32x32x16_bf16 v[112:127], v[146:149], v[182:185], v[112:127]
	v_mfma_f32_32x32x16_bf16 v[80:95], v[146:149], v[186:189], v[80:95]
	v_mfma_f32_32x32x16_bf16 v[64:79], v[146:149], v[194:197], v[64:79]
	s_waitcnt vmcnt(4) lgkmcnt(0)
	s_barrier
; #define VM_WAIT() asm volatile("s_waitcnt vmcnt(0)" ::: "memory")
; __device__ __forceinline__ unsigned cvt_pk_bf16(float lo, float hi) { unsigned r; asm volatile("v_cvt_pk_bf16_f32 %0, %1, %2" : "=v"(r) : "v"(lo), "v"(hi)); return r; }
; __device__ __forceinline__ bf16x8 scale_frag(bf16x8 f, float s) {
;     u32x4 w = __builtin_bit_cast(u32x4, f); u32x4 o;
;     o.x = cvt_pk_bf16(bf_lo(w.x) * s, bf_hi(w.x) * s); o.y = cvt_pk_bf16(bf_lo(w.y) * s, bf_hi(w.y) * s);
;     o.z = cvt_pk_bf16(bf_lo(w.z) * s, bf_hi(w.z) * s); o.w = cvt_pk_bf16(bf_lo(w.w) * s, bf_hi(w.w) * s);
;     return __builtin_bit_cast(bf16x8, o);
; template <int DK, int DV, bool MLSTM>
; __device__ __forceinline__ void out_unit2(LAS unsigned char* lds, LAS unsigned char* ldstab, const OutArgs a, const int wv) {
;     ...
; #pragma unroll
;     for (int pc = 0; pc < 4; ++pc) {
;         VM_WAIT(); __syncthreads();
;         OUT_DMA(pc + 1);
;         const bf16x8 af0 = pa[2 * pc], af1 = pa[2 * pc + 1];
;         OUT_MMA(pc & 1);
;     }
; #pragma unroll 1
;     for (int pc = 4; pc < 4 + 2 * NCP; ++pc) {
;         VM_WAIT(); __syncthreads();
;         if (pc + 1 < 4 + 2 * NCP) OUT_DMA(pc + 1);
;         const int cq = pc - 4, dirb = cq >= NCP, cp = dirb ? cq - NCP : cq;
;         const float qs = dirb ? qsb : qsf;
;         const unsigned qa = QP + (cp >> 2) * 32768u + 512u * (cp & 3) + 8192u * rb;
;         const bf16x8 af0 = scale_frag(lds_r128(qa + rb0), qs), af1 = scale_frag(lds_r128(qa + rb1), qs);
;         OUT_MMA(pc & 1);
;     }
	s_add_u32 s42, s11, 0x30000
	s_addc_u32 s43, s12, 0
	v_lshl_add_u64 v[128:129], s[42:43], 0, v[198:199]
	v_lshl_add_u64 v[130:131], s[42:43], 0, v[200:201]
	v_lshl_add_u64 v[146:147], s[42:43], 0, v[202:203]
	v_lshl_add_u64 v[148:149], s[42:43], 0, v[204:205]
	s_mov_b32 m0, s6
	s_nop 0
	global_load_lds_dwordx4 v[128:129], off
	s_mov_b32 m0, s7
	s_nop 0
	global_load_lds_dwordx4 v[130:131], off
	s_mov_b32 m0, s38
	s_nop 0
	global_load_lds_dwordx4 v[146:147], off
	s_mov_b32 m0, s40
	s_nop 0
	global_load_lds_dwordx4 v[148:149], off
	v_add_u32_e32 v133, s13, v173
	v_add_u32_e32 v135, s13, v177
	ds_read_b128 v[128:131], v133 offset:32768
	ds_read_b128 v[146:149], v135 offset:32768
	s_waitcnt lgkmcnt(0)
	v_lshlrev_b32_e32 v135, 16, v128
	v_and_b32_e32 v137, 0xffff0000, v128
	v_mul_f32_e32 v135, v144, v135
	v_mul_f32_e32 v137, v144, v137
	v_cvt_pk_bf16_f32 v128, v135, v137
	v_lshlrev_b32_e32 v135, 16, v129
	v_and_b32_e32 v137, 0xffff0000, v129
	v_mul_f32_e32 v135, v144, v135
	v_mul_f32_e32 v137, v144, v137
	v_cvt_pk_bf16_f32 v129, v135, v137
	v_lshlrev_b32_e32 v135, 16, v130
	v_and_b32_e32 v137, 0xffff0000, v130
	v_mul_f32_e32 v135, v144, v135
	v_mul_f32_e32 v137, v144, v137
	v_cvt_pk_bf16_f32 v130, v135, v137
	v_lshlrev_b32_e32 v135, 16, v131
	v_and_b32_e32 v137, 0xffff0000, v131
	v_mul_f32_e32 v135, v144, v135
	v_mul_f32_e32 v137, v144, v137
	v_cvt_pk_bf16_f32 v131, v135, v137
	v_lshlrev_b32_e32 v135, 16, v146
	v_and_b32_e32 v137, 0xffff0000, v146
	v_mul_f32_e32 v135, v144, v135
	v_mul_f32_e32 v137, v144, v137
	v_cvt_pk_bf16_f32 v146, v135, v137
	v_lshlrev_b32_e32 v135, 16, v147
	v_and_b32_e32 v137, 0xffff0000, v147
	v_mul_f32_e32 v135, v144, v135
	v_mul_f32_e32 v137, v144, v137
	v_cvt_pk_bf16_f32 v147, v135, v137
	v_lshlrev_b32_e32 v135, 16, v148
	v_and_b32_e32 v137, 0xffff0000, v148
	v_mul_f32_e32 v135, v144, v135
	v_mul_f32_e32 v137, v144, v137
	v_cvt_pk_bf16_f32 v148, v135, v137
	v_lshlrev_b32_e32 v135, 16, v149
	v_and_b32_e32 v137, 0xffff0000, v149
	v_mul_f32_e32 v135, v144, v135
	v_mul_f32_e32 v137, v144, v137
	v_cvt_pk_bf16_f32 v149, v135, v137
	v_add_u32_e32 v133, 0x10000, v175
	ds_read_b64_tr_b16 v[150:151], v133 offset:0
	v_add_u32_e32 v135, 0x10000, v181
	ds_read_b64_tr_b16 v[152:153], v135 offset:0
	ds_read_b64_tr_b16 v[182:183], v133 offset:0x200
	ds_read_b64_tr_b16 v[184:185], v135 offset:0x200
	ds_read_b64_tr_b16 v[186:187], v133 offset:0x400
	ds_read_b64_tr_b16 v[188:189], v135 offset:0x400
	ds_read_b64_tr_b16 v[190:191], v133 offset:0x600
	ds_read_b64_tr_b16 v[192:193], v135 offset:0x600
	s_waitcnt lgkmcnt(0)
	s_nop 0
	v_mfma_f32_32x32x16_bf16 v[16:31], v[128:131], v[150:153], v[16:31]
	ds_read_b64_tr_b16 v[150:151], v133 offset:0x1000
	ds_read_b64_tr_b16 v[152:153], v135 offset:0x1000
	v_mfma_f32_32x32x16_bf16 v[0:15], v[128:131], v[182:185], v[0:15]
	ds_read_b64_tr_b16 v[182:183], v133 offset:0x1200
	ds_read_b64_tr_b16 v[184:185], v135 offset:0x1200
	v_mfma_f32_32x32x16_bf16 v[32:47], v[128:131], v[186:189], v[32:47]
	ds_read_b64_tr_b16 v[186:187], v133 offset:0x1400
	ds_read_b64_tr_b16 v[188:189], v135 offset:0x1400
	ds_read_b64_tr_b16 v[194:195], v133 offset:0x1600
	ds_read_b64_tr_b16 v[196:197], v135 offset:0x1600
	s_waitcnt lgkmcnt(0)
	v_mfma_f32_32x32x16_bf16 v[48:63], v[128:131], v[190:193], v[48:63]
	v_mfma_f32_32x32x16_bf16 v[16:31], v[146:149], v[150:153], v[16:31]
	v_add_u32_e32 v133, 0x2000, v133
	ds_read_b64_tr_b16 v[150:151], v133 offset:0
	v_add_u32_e32 v135, 0x2000, v135
	ds_read_b64_tr_b16 v[152:153], v135 offset:0
	v_mfma_f32_32x32x16_bf16 v[0:15], v[146:149], v[182:185], v[0:15]
	ds_read_b64_tr_b16 v[182:183], v133 offset:0x200
	ds_read_b64_tr_b16 v[184:185], v135 offset:0x200
	v_mfma_f32_32x32x16_bf16 v[32:47], v[146:149], v[186:189], v[32:47]
	ds_read_b64_tr_b16 v[186:187], v133 offset:0x400
	ds_read_b64_tr_b16 v[188:189], v135 offset:0x400
	ds_read_b64_tr_b16 v[190:191], v133 offset:0x600
	ds_read_b64_tr_b16 v[192:193], v135 offset:0x600
	s_waitcnt lgkmcnt(0)
	v_mfma_f32_32x32x16_bf16 v[48:63], v[146:149], v[194:197], v[48:63]
	v_mfma_f32_32x32x16_bf16 v[96:111], v[128:131], v[150:153], v[96:111]
	ds_read_b64_tr_b16 v[150:151], v133 offset:0x1000
	ds_read_b64_tr_b16 v[152:153], v135 offset:0x1000
	v_mfma_f32_32x32x16_bf16 v[112:127], v[128:131], v[182:185], v[112:127]
	ds_read_b64_tr_b16 v[182:183], v133 offset:0x1200
	ds_read_b64_tr_b16 v[184:185], v135 offset:0x1200
	v_mfma_f32_32x32x16_bf16 v[80:95], v[128:131], v[186:189], v[80:95]
	ds_read_b64_tr_b16 v[186:187], v133 offset:0x1400
	ds_read_b64_tr_b16 v[188:189], v135 offset:0x1400
	ds_read_b64_tr_b16 v[194:195], v133 offset:0x1600
	ds_read_b64_tr_b16 v[196:197], v135 offset:0x1600
	s_waitcnt lgkmcnt(0)
	v_mfma_f32_32x32x16_bf16 v[64:79], v[128:131], v[190:193], v[64:79]
	v_mfma_f32_32x32x16_bf16 v[96:111], v[146:149], v[150:153], v[96:111]
	v_mfma_f32_32x32x16_bf16 v[112:127], v[146:149], v[182:185], v[112:127]
	v_mfma_f32_32x32x16_bf16 v[80:95], v[146:149], v[186:189], v[80:95]
	v_mfma_f32_32x32x16_bf16 v[64:79], v[146:149], v[194:197], v[64:79]
	s_waitcnt vmcnt(4) lgkmcnt(0)
	s_barrier
; #define VM_WAIT() asm volatile("s_waitcnt vmcnt(0)" ::: "memory")
; __device__ __forceinline__ unsigned cvt_pk_bf16(float lo, float hi) { unsigned r; asm volatile("v_cvt_pk_bf16_f32 %0, %1, %2" : "=v"(r) : "v"(lo), "v"(hi)); return r; }
; __device__ __forceinline__ bf16x8 scale_frag(bf16x8 f, float s) {
;     u32x4 w = __builtin_bit_cast(u32x4, f); u32x4 o;
;     o.x = cvt_pk_bf16(bf_lo(w.x) * s, bf_hi(w.x) * s); o.y = cvt_pk_bf16(bf_lo(w.y) * s, bf_hi(w.y) * s);
;     o.z = cvt_pk_bf16(bf_lo(w.z) * s, bf_hi(w.z) * s); o.w = cvt_pk_bf16(bf_lo(w.w) * s, bf_hi(w.w) * s);
;     return __builtin_bit_cast(bf16x8, o);
; template <int DK, int DV, bool MLSTM>
; __device__ __forceinline__ void out_unit2(LAS unsigned char* lds, LAS unsigned char* ldstab, const OutArgs a, const int wv) {
;     ...
; #pragma unroll
;     for (int pc = 0; pc < 4; ++pc) {
;         VM_WAIT(); __syncthreads();
;         OUT_DMA(pc + 1);
;         const bf16x8 af0 = pa[2 * pc], af1 = pa[2 * pc + 1];
;         OUT_MMA(pc & 1);
;     }
; #pragma unroll 1
;     for (int pc = 4; pc < 4 + 2 * NCP; ++pc) {
;         VM_WAIT(); __syncthreads();
;         if (pc + 1 < 4 + 2 * NCP) OUT_DMA(pc + 1);
;         const int cq = pc - 4, dirb = cq >= NCP, cp = dirb ? cq - NCP : cq;
;         const float qs = dirb ? qsb : qsf;
;         const unsigned qa = QP + (cp >> 2) * 32768u + 512u * (cp & 3) + 8192u * rb;
;         const bf16x8 af0 = scale_frag(lds_r128(qa + rb0), qs), af1 = scale_frag(lds_r128(qa + rb1), qs);
;         OUT_MMA(pc & 1);
;     }
	s_add_u32 s42, s11, 0x38000
	s_addc_u32 s43, s12, 0
	v_lshl_add_u64 v[128:129], s[42:43], 0, v[198:199]
	v_lshl_add_u64 v[130:131], s[42:43], 0, v[200:201]
	v_lshl_add_u64 v[146:147], s[42:43], 0, v[202:203]
	v_lshl_add_u64 v[148:149], s[42:43], 0, v[204:205]
	s_add_i32 m0, s6, 0x10000
	s_nop 0
	global_load_lds_dwordx4 v[128:129], off
	s_add_i32 m0, s7, 0x10000
	s_nop 0
	global_load_lds_dwordx4 v[130:131], off
	s_add_i32 m0, s38, 0x10000
	s_nop 0
	global_load_lds_dwordx4 v[146:147], off
	s_add_i32 m0, s40, 0x10000
	s_nop 0
	global_load_lds_dwordx4 v[148:149], off
	v_add_u32_e32 v133, s13, v173
	v_add_u32_e32 v135, s13, v177
	ds_read_b128 v[128:131], v133 offset:33280
	ds_read_b128 v[146:149], v135 offset:33280
	s_waitcnt lgkmcnt(0)
	v_lshlrev_b32_e32 v135, 16, v128
	v_and_b32_e32 v137, 0xffff0000, v128
	v_mul_f32_e32 v135, v144, v135
	v_mul_f32_e32 v137, v144, v137
	v_cvt_pk_bf16_f32 v128, v135, v137
	v_lshlrev_b32_e32 v135, 16, v129
	v_and_b32_e32 v137, 0xffff0000, v129
	v_mul_f32_e32 v135, v144, v135
	v_mul_f32_e32 v137, v144, v137
	v_cvt_pk_bf16_f32 v129, v135, v137
	v_lshlrev_b32_e32 v135, 16, v130
	v_and_b32_e32 v137, 0xffff0000, v130
	v_mul_f32_e32 v135, v144, v135
	v_mul_f32_e32 v137, v144, v137
	v_cvt_pk_bf16_f32 v130, v135, v137
	v_lshlrev_b32_e32 v135, 16, v131
	v_and_b32_e32 v137, 0xffff0000, v131
	v_mul_f32_e32 v135, v144, v135
	v_mul_f32_e32 v137, v144, v137
	v_cvt_pk_bf16_f32 v131, v135, v137
	v_lshlrev_b32_e32 v135, 16, v146
	v_and_b32_e32 v137, 0xffff0000, v146
	v_mul_f32_e32 v135, v144, v135
	v_mul_f32_e32 v137, v144, v137
	v_cvt_pk_bf16_f32 v146, v135, v137
	v_lshlrev_b32_e32 v135, 16, v147
	v_and_b32_e32 v137, 0xffff0000, v147
	v_mul_f32_e32 v135, v144, v135
	v_mul_f32_e32 v137, v144, v137
	v_cvt_pk_bf16_f32 v147, v135, v137
	v_lshlrev_b32_e32 v135, 16, v148
	v_and_b32_e32 v137, 0xffff0000, v148
	v_mul_f32_e32 v135, v144, v135
	v_mul_f32_e32 v137, v144, v137
	v_cvt_pk_bf16_f32 v148, v135, v137
	v_lshlrev_b32_e32 v135, 16, v149
	v_and_b32_e32 v137, 0xffff0000, v149
	v_mul_f32_e32 v135, v144, v135
	v_mul_f32_e32 v137, v144, v137
	v_cvt_pk_bf16_f32 v149, v135, v137
	v_add_u32_e32 v133, 0x18000, v175
	ds_read_b64_tr_b16 v[150:151], v133 offset:0
	v_add_u32_e32 v135, 0x18000, v181
	ds_read_b64_tr_b16 v[152:153], v135 offset:0
	ds_read_b64_tr_b16 v[182:183], v133 offset:0x200
	ds_read_b64_tr_b16 v[184:185], v135 offset:0x200
	ds_read_b64_tr_b16 v[186:187], v133 offset:0x400
	ds_read_b64_tr_b16 v[188:189], v135 offset:0x400
	ds_read_b64_tr_b16 v[190:191], v133 offset:0x600
	ds_read_b64_tr_b16 v[192:193], v135 offset:0x600
	s_waitcnt lgkmcnt(0)
	s_nop 0
	v_mfma_f32_32x32x16_bf16 v[16:31], v[128:131], v[150:153], v[16:31]
	ds_read_b64_tr_b16 v[150:151], v133 offset:0x1000
	ds_read_b64_tr_b16 v[152:153], v135 offset:0x1000
	v_mfma_f32_32x32x16_bf16 v[0:15], v[128:131], v[182:185], v[0:15]
	ds_read_b64_tr_b16 v[182:183], v133 offset:0x1200
	ds_read_b64_tr_b16 v[184:185], v135 offset:0x1200
	v_mfma_f32_32x32x16_bf16 v[32:47], v[128:131], v[186:189], v[32:47]
	ds_read_b64_tr_b16 v[186:187], v133 offset:0x1400
	ds_read_b64_tr_b16 v[188:189], v135 offset:0x1400
	ds_read_b64_tr_b16 v[194:195], v133 offset:0x1600
	ds_read_b64_tr_b16 v[196:197], v135 offset:0x1600
	s_waitcnt lgkmcnt(0)
	v_mfma_f32_32x32x16_bf16 v[48:63], v[128:131], v[190:193], v[48:63]
	v_mfma_f32_32x32x16_bf16 v[16:31], v[146:149], v[150:153], v[16:31]
	v_add_u32_e32 v133, 0x2000, v133
	ds_read_b64_tr_b16 v[150:151], v133 offset:0
	v_add_u32_e32 v135, 0x2000, v135
	ds_read_b64_tr_b16 v[152:153], v135 offset:0
	v_mfma_f32_32x32x16_bf16 v[0:15], v[146:149], v[182:185], v[0:15]
	ds_read_b64_tr_b16 v[182:183], v133 offset:0x200
	ds_read_b64_tr_b16 v[184:185], v135 offset:0x200
	v_mfma_f32_32x32x16_bf16 v[32:47], v[146:149], v[186:189], v[32:47]
	ds_read_b64_tr_b16 v[186:187], v133 offset:0x400
	ds_read_b64_tr_b16 v[188:189], v135 offset:0x400
	ds_read_b64_tr_b16 v[190:191], v133 offset:0x600
	ds_read_b64_tr_b16 v[192:193], v135 offset:0x600
	s_waitcnt lgkmcnt(0)
	v_mfma_f32_32x32x16_bf16 v[48:63], v[146:149], v[194:197], v[48:63]
	v_mfma_f32_32x32x16_bf16 v[96:111], v[128:131], v[150:153], v[96:111]
	ds_read_b64_tr_b16 v[150:151], v133 offset:0x1000
	ds_read_b64_tr_b16 v[152:153], v135 offset:0x1000
	v_mfma_f32_32x32x16_bf16 v[112:127], v[128:131], v[182:185], v[112:127]
	ds_read_b64_tr_b16 v[182:183], v133 offset:0x1200
	ds_read_b64_tr_b16 v[184:185], v135 offset:0x1200
	v_mfma_f32_32x32x16_bf16 v[80:95], v[128:131], v[186:189], v[80:95]
	ds_read_b64_tr_b16 v[186:187], v133 offset:0x1400
	ds_read_b64_tr_b16 v[188:189], v135 offset:0x1400
	ds_read_b64_tr_b16 v[194:195], v133 offset:0x1600
	ds_read_b64_tr_b16 v[196:197], v135 offset:0x1600
	s_waitcnt lgkmcnt(0)
	v_mfma_f32_32x32x16_bf16 v[64:79], v[128:131], v[190:193], v[64:79]
	v_mfma_f32_32x32x16_bf16 v[96:111], v[146:149], v[150:153], v[96:111]
	v_mfma_f32_32x32x16_bf16 v[112:127], v[146:149], v[182:185], v[112:127]
	v_mfma_f32_32x32x16_bf16 v[80:95], v[146:149], v[186:189], v[80:95]
	v_mfma_f32_32x32x16_bf16 v[64:79], v[146:149], v[194:197], v[64:79]
	s_waitcnt vmcnt(4) lgkmcnt(0)
	s_barrier
; #define VM_WAIT() asm volatile("s_waitcnt vmcnt(0)" ::: "memory")
; __device__ __forceinline__ unsigned cvt_pk_bf16(float lo, float hi) { unsigned r; asm volatile("v_cvt_pk_bf16_f32 %0, %1, %2" : "=v"(r) : "v"(lo), "v"(hi)); return r; }
; __device__ __forceinline__ bf16x8 scale_frag(bf16x8 f, float s) {
;     u32x4 w = __builtin_bit_cast(u32x4, f); u32x4 o;
;     o.x = cvt_pk_bf16(bf_lo(w.x) * s, bf_hi(w.x) * s); o.y = cvt_pk_bf16(bf_lo(w.y) * s, bf_hi(w.y) * s);
;     o.z = cvt_pk_bf16(bf_lo(w.z) * s, bf_hi(w.z) * s); o.w = cvt_pk_bf16(bf_lo(w.w) * s, bf_hi(w.w) * s);
;     return __builtin_bit_cast(bf16x8, o);
; template <int DK, int DV, bool MLSTM>
; __device__ __forceinline__ void out_unit2(LAS unsigned char* lds, LAS unsigned char* ldstab, const OutArgs a, const int wv) {
;     ...
; #pragma unroll
;     for (int pc = 0; pc < 4; ++pc) {
;         VM_WAIT(); __syncthreads();
;         OUT_DMA(pc + 1);
;         const bf16x8 af0 = pa[2 * pc], af1 = pa[2 * pc + 1];
;         OUT_MMA(pc & 1);
;     }
; #pragma unroll 1
;     for (int pc = 4; pc < 4 + 2 * NCP; ++pc) {
;         VM_WAIT(); __syncthreads();
;         if (pc + 1 < 4 + 2 * NCP) OUT_DMA(pc + 1);
;         const int cq = pc - 4, dirb = cq >= NCP, cp = dirb ? cq - NCP : cq;
;         const float qs = dirb ? qsb : qsf;
;         const unsigned qa = QP + (cp >> 2) * 32768u + 512u * (cp & 3) + 8192u * rb;
;         const bf16x8 af0 = scale_frag(lds_r128(qa + rb0), qs), af1 = scale_frag(lds_r128(qa + rb1), qs);
;         OUT_MMA(pc & 1);
;     }
	v_add_u32_e32 v133, s13, v173
	v_add_u32_e32 v135, s13, v177
	ds_read_b128 v[128:131], v133 offset:33792
	ds_read_b128 v[146:149], v135 offset:33792
	s_waitcnt lgkmcnt(0)
	v_lshlrev_b32_e32 v135, 16, v128
	v_and_b32_e32 v137, 0xffff0000, v128
	v_mul_f32_e32 v135, v144, v135
	v_mul_f32_e32 v137, v144, v137
	v_cvt_pk_bf16_f32 v128, v135, v137
	v_lshlrev_b32_e32 v135, 16, v129
	v_and_b32_e32 v137, 0xffff0000, v129
	v_mul_f32_e32 v135, v144, v135
	v_mul_f32_e32 v137, v144, v137
	v_cvt_pk_bf16_f32 v129, v135, v137
	v_lshlrev_b32_e32 v135, 16, v130
	v_and_b32_e32 v137, 0xffff0000, v130
	v_mul_f32_e32 v135, v144, v135
	v_mul_f32_e32 v137, v144, v137
	v_cvt_pk_bf16_f32 v130, v135, v137
	v_lshlrev_b32_e32 v135, 16, v131
	v_and_b32_e32 v137, 0xffff0000, v131
	v_mul_f32_e32 v135, v144, v135
	v_mul_f32_e32 v137, v144, v137
	v_cvt_pk_bf16_f32 v131, v135, v137
	v_lshlrev_b32_e32 v135, 16, v146
	v_and_b32_e32 v137, 0xffff0000, v146
	v_mul_f32_e32 v135, v144, v135
	v_mul_f32_e32 v137, v144, v137
	v_cvt_pk_bf16_f32 v146, v135, v137
	v_lshlrev_b32_e32 v135, 16, v147
	v_and_b32_e32 v137, 0xffff0000, v147
	v_mul_f32_e32 v135, v144, v135
	v_mul_f32_e32 v137, v144, v137
	v_cvt_pk_bf16_f32 v147, v135, v137
	v_lshlrev_b32_e32 v135, 16, v148
	v_and_b32_e32 v137, 0xffff0000, v148
	v_mul_f32_e32 v135, v144, v135
	v_mul_f32_e32 v137, v144, v137
	v_cvt_pk_bf16_f32 v148, v135, v137
	v_lshlrev_b32_e32 v135, 16, v149
	v_and_b32_e32 v137, 0xffff0000, v149
	v_mul_f32_e32 v135, v144, v135
	v_mul_f32_e32 v137, v144, v137
	v_cvt_pk_bf16_f32 v149, v135, v137
	v_mov_b32_e32 v133, v175
	ds_read_b64_tr_b16 v[150:151], v133 offset:0
	v_mov_b32_e32 v135, v181
	ds_read_b64_tr_b16 v[152:153], v135 offset:0
	ds_read_b64_tr_b16 v[182:183], v133 offset:0x200
	ds_read_b64_tr_b16 v[184:185], v135 offset:0x200
	ds_read_b64_tr_b16 v[186:187], v133 offset:0x400
	ds_read_b64_tr_b16 v[188:189], v135 offset:0x400
	ds_read_b64_tr_b16 v[190:191], v133 offset:0x600
	ds_read_b64_tr_b16 v[192:193], v135 offset:0x600
	s_waitcnt lgkmcnt(0)
	s_nop 0
	v_mfma_f32_32x32x16_bf16 v[16:31], v[128:131], v[150:153], v[16:31]
	ds_read_b64_tr_b16 v[150:151], v133 offset:0x1000
	ds_read_b64_tr_b16 v[152:153], v135 offset:0x1000
	v_mfma_f32_32x32x16_bf16 v[0:15], v[128:131], v[182:185], v[0:15]
	ds_read_b64_tr_b16 v[182:183], v133 offset:0x1200
	ds_read_b64_tr_b16 v[184:185], v135 offset:0x1200
	v_mfma_f32_32x32x16_bf16 v[32:47], v[128:131], v[186:189], v[32:47]
	ds_read_b64_tr_b16 v[186:187], v133 offset:0x1400
	ds_read_b64_tr_b16 v[188:189], v135 offset:0x1400
	ds_read_b64_tr_b16 v[194:195], v133 offset:0x1600
	ds_read_b64_tr_b16 v[196:197], v135 offset:0x1600
	s_waitcnt lgkmcnt(0)
	v_mfma_f32_32x32x16_bf16 v[48:63], v[128:131], v[190:193], v[48:63]
	v_mfma_f32_32x32x16_bf16 v[16:31], v[146:149], v[150:153], v[16:31]
	v_add_u32_e32 v133, 0x2000, v133
	ds_read_b64_tr_b16 v[150:151], v133 offset:0
	v_add_u32_e32 v135, 0x2000, v135
	ds_read_b64_tr_b16 v[152:153], v135 offset:0
	v_mfma_f32_32x32x16_bf16 v[0:15], v[146:149], v[182:185], v[0:15]
	ds_read_b64_tr_b16 v[182:183], v133 offset:0x200
	ds_read_b64_tr_b16 v[184:185], v135 offset:0x200
	v_mfma_f32_32x32x16_bf16 v[32:47], v[146:149], v[186:189], v[32:47]
	ds_read_b64_tr_b16 v[186:187], v133 offset:0x400
	ds_read_b64_tr_b16 v[188:189], v135 offset:0x400
	ds_read_b64_tr_b16 v[190:191], v133 offset:0x600
	ds_read_b64_tr_b16 v[192:193], v135 offset:0x600
	s_waitcnt lgkmcnt(0)
	v_mfma_f32_32x32x16_bf16 v[48:63], v[146:149], v[194:197], v[48:63]
	v_mfma_f32_32x32x16_bf16 v[96:111], v[128:131], v[150:153], v[96:111]
	ds_read_b64_tr_b16 v[150:151], v133 offset:0x1000
	ds_read_b64_tr_b16 v[152:153], v135 offset:0x1000
	v_mfma_f32_32x32x16_bf16 v[112:127], v[128:131], v[182:185], v[112:127]
	ds_read_b64_tr_b16 v[182:183], v133 offset:0x1200
	ds_read_b64_tr_b16 v[184:185], v135 offset:0x1200
	v_mfma_f32_32x32x16_bf16 v[80:95], v[128:131], v[186:189], v[80:95]
	ds_read_b64_tr_b16 v[186:187], v133 offset:0x1400
	ds_read_b64_tr_b16 v[188:189], v135 offset:0x1400
	ds_read_b64_tr_b16 v[194:195], v133 offset:0x1600
	ds_read_b64_tr_b16 v[196:197], v135 offset:0x1600
	s_waitcnt lgkmcnt(0)
	v_mfma_f32_32x32x16_bf16 v[64:79], v[128:131], v[190:193], v[64:79]
	v_mfma_f32_32x32x16_bf16 v[96:111], v[146:149], v[150:153], v[96:111]
	v_mfma_f32_32x32x16_bf16 v[112:127], v[146:149], v[182:185], v[112:127]
	v_mfma_f32_32x32x16_bf16 v[80:95], v[146:149], v[186:189], v[80:95]
	v_mfma_f32_32x32x16_bf16 v[64:79], v[146:149], v[194:197], v[64:79]
	s_waitcnt vmcnt(0) lgkmcnt(0)
	s_barrier
; #define VM_WAIT() asm volatile("s_waitcnt vmcnt(0)" ::: "memory")
; __device__ __forceinline__ unsigned cvt_pk_bf16(float lo, float hi) { unsigned r; asm volatile("v_cvt_pk_bf16_f32 %0, %1, %2" : "=v"(r) : "v"(lo), "v"(hi)); return r; }
; __device__ __forceinline__ bf16x8 scale_frag(bf16x8 f, float s) {
;     u32x4 w = __builtin_bit_cast(u32x4, f); u32x4 o;
;     o.x = cvt_pk_bf16(bf_lo(w.x) * s, bf_hi(w.x) * s); o.y = cvt_pk_bf16(bf_lo(w.y) * s, bf_hi(w.y) * s);
;     o.z = cvt_pk_bf16(bf_lo(w.z) * s, bf_hi(w.z) * s); o.w = cvt_pk_bf16(bf_lo(w.w) * s, bf_hi(w.w) * s);
;     return __builtin_bit_cast(bf16x8, o);
; template <int DK, int DV, bool MLSTM>
; __device__ __forceinline__ void out_unit2(LAS unsigned char* lds, LAS unsigned char* ldstab, const OutArgs a, const int wv) {
;     ...
; #pragma unroll
;     for (int pc = 0; pc < 4; ++pc) {
;         VM_WAIT(); __syncthreads();
;         OUT_DMA(pc + 1);
;         const bf16x8 af0 = pa[2 * pc], af1 = pa[2 * pc + 1];
;         OUT_MMA(pc & 1);
;     }
; #pragma unroll 1
;     for (int pc = 4; pc < 4 + 2 * NCP; ++pc) {
;         VM_WAIT(); __syncthreads();
;         if (pc + 1 < 4 + 2 * NCP) OUT_DMA(pc + 1);
;         const int cq = pc - 4, dirb = cq >= NCP, cp = dirb ? cq - NCP : cq;
;         const float qs = dirb ? qsb : qsf;
;         const unsigned qa = QP + (cp >> 2) * 32768u + 512u * (cp & 3) + 8192u * rb;
;         const bf16x8 af0 = scale_frag(lds_r128(qa + rb0), qs), af1 = scale_frag(lds_r128(qa + rb1), qs);
;         OUT_MMA(pc & 1);
;     }
	v_add_u32_e32 v133, s13, v173
	v_add_u32_e32 v135, s13, v177
	ds_read_b128 v[128:131], v133 offset:34304
	ds_read_b128 v[146:149], v135 offset:34304
	s_waitcnt lgkmcnt(0)
	v_lshlrev_b32_e32 v135, 16, v128
	v_and_b32_e32 v137, 0xffff0000, v128
	v_mul_f32_e32 v135, v144, v135
	v_mul_f32_e32 v137, v144, v137
	v_cvt_pk_bf16_f32 v128, v135, v137
	v_lshlrev_b32_e32 v135, 16, v129
	v_and_b32_e32 v137, 0xffff0000, v129
	v_mul_f32_e32 v135, v144, v135
	v_mul_f32_e32 v137, v144, v137
	v_cvt_pk_bf16_f32 v129, v135, v137
	v_lshlrev_b32_e32 v135, 16, v130
	v_and_b32_e32 v137, 0xffff0000, v130
	v_mul_f32_e32 v135, v144, v135
	v_mul_f32_e32 v137, v144, v137
	v_cvt_pk_bf16_f32 v130, v135, v137
	v_lshlrev_b32_e32 v135, 16, v131
	v_and_b32_e32 v137, 0xffff0000, v131
	v_mul_f32_e32 v135, v144, v135
	v_mul_f32_e32 v137, v144, v137
	v_cvt_pk_bf16_f32 v131, v135, v137
	v_lshlrev_b32_e32 v135, 16, v146
	v_and_b32_e32 v137, 0xffff0000, v146
	v_mul_f32_e32 v135, v144, v135
	v_mul_f32_e32 v137, v144, v137
	v_cvt_pk_bf16_f32 v146, v135, v137
	v_lshlrev_b32_e32 v135, 16, v147
	v_and_b32_e32 v137, 0xffff0000, v147
	v_mul_f32_e32 v135, v144, v135
	v_mul_f32_e32 v137, v144, v137
	v_cvt_pk_bf16_f32 v147, v135, v137
	v_lshlrev_b32_e32 v135, 16, v148
	v_and_b32_e32 v137, 0xffff0000, v148
	v_mul_f32_e32 v135, v144, v135
	v_mul_f32_e32 v137, v144, v137
	v_cvt_pk_bf16_f32 v148, v135, v137
	v_lshlrev_b32_e32 v135, 16, v149
	v_and_b32_e32 v137, 0xffff0000, v149
	v_mul_f32_e32 v135, v144, v135
	v_mul_f32_e32 v137, v144, v137
	v_cvt_pk_bf16_f32 v149, v135, v137
	v_add_u32_e32 v133, 0x10000, v175
	ds_read_b64_tr_b16 v[150:151], v133 offset:0
	v_add_u32_e32 v135, 0x10000, v181
	ds_read_b64_tr_b16 v[152:153], v135 offset:0
	ds_read_b64_tr_b16 v[182:183], v133 offset:0x200
	ds_read_b64_tr_b16 v[184:185], v135 offset:0x200
	ds_read_b64_tr_b16 v[186:187], v133 offset:0x400
	ds_read_b64_tr_b16 v[188:189], v135 offset:0x400
	ds_read_b64_tr_b16 v[190:191], v133 offset:0x600
	ds_read_b64_tr_b16 v[192:193], v135 offset:0x600
	s_waitcnt lgkmcnt(0)
	s_nop 0
	v_mfma_f32_32x32x16_bf16 v[16:31], v[128:131], v[150:153], v[16:31]
	ds_read_b64_tr_b16 v[150:151], v133 offset:0x1000
	ds_read_b64_tr_b16 v[152:153], v135 offset:0x1000
	v_mfma_f32_32x32x16_bf16 v[0:15], v[128:131], v[182:185], v[0:15]
	ds_read_b64_tr_b16 v[182:183], v133 offset:0x1200
	ds_read_b64_tr_b16 v[184:185], v135 offset:0x1200
	v_mfma_f32_32x32x16_bf16 v[32:47], v[128:131], v[186:189], v[32:47]
	ds_read_b64_tr_b16 v[186:187], v133 offset:0x1400
	ds_read_b64_tr_b16 v[188:189], v135 offset:0x1400
	ds_read_b64_tr_b16 v[194:195], v133 offset:0x1600
	ds_read_b64_tr_b16 v[196:197], v135 offset:0x1600
	s_waitcnt lgkmcnt(0)
	v_mfma_f32_32x32x16_bf16 v[48:63], v[128:131], v[190:193], v[48:63]
	v_mfma_f32_32x32x16_bf16 v[16:31], v[146:149], v[150:153], v[16:31]
	v_add_u32_e32 v133, 0x2000, v133
	ds_read_b64_tr_b16 v[150:151], v133 offset:0
	v_add_u32_e32 v135, 0x2000, v135
	ds_read_b64_tr_b16 v[152:153], v135 offset:0
	v_mfma_f32_32x32x16_bf16 v[0:15], v[146:149], v[182:185], v[0:15]
	ds_read_b64_tr_b16 v[182:183], v133 offset:0x200
	ds_read_b64_tr_b16 v[184:185], v135 offset:0x200
	v_mfma_f32_32x32x16_bf16 v[32:47], v[146:149], v[186:189], v[32:47]
	ds_read_b64_tr_b16 v[186:187], v133 offset:0x400
	ds_read_b64_tr_b16 v[188:189], v135 offset:0x400
	ds_read_b64_tr_b16 v[190:191], v133 offset:0x600
	ds_read_b64_tr_b16 v[192:193], v135 offset:0x600
	s_waitcnt lgkmcnt(0)
	v_mfma_f32_32x32x16_bf16 v[48:63], v[146:149], v[194:197], v[48:63]
	v_mfma_f32_32x32x16_bf16 v[96:111], v[128:131], v[150:153], v[96:111]
	ds_read_b64_tr_b16 v[150:151], v133 offset:0x1000
	ds_read_b64_tr_b16 v[152:153], v135 offset:0x1000
	v_mfma_f32_32x32x16_bf16 v[112:127], v[128:131], v[182:185], v[112:127]
	ds_read_b64_tr_b16 v[182:183], v133 offset:0x1200
	ds_read_b64_tr_b16 v[184:185], v135 offset:0x1200
	v_mfma_f32_32x32x16_bf16 v[80:95], v[128:131], v[186:189], v[80:95]
	ds_read_b64_tr_b16 v[186:187], v133 offset:0x1400
	ds_read_b64_tr_b16 v[188:189], v135 offset:0x1400
	ds_read_b64_tr_b16 v[194:195], v133 offset:0x1600
	ds_read_b64_tr_b16 v[196:197], v135 offset:0x1600
	s_waitcnt lgkmcnt(0)
	v_mfma_f32_32x32x16_bf16 v[64:79], v[128:131], v[190:193], v[64:79]
	v_mfma_f32_32x32x16_bf16 v[96:111], v[146:149], v[150:153], v[96:111]
	v_mfma_f32_32x32x16_bf16 v[112:127], v[146:149], v[182:185], v[112:127]
	v_mfma_f32_32x32x16_bf16 v[80:95], v[146:149], v[186:189], v[80:95]
	v_mfma_f32_32x32x16_bf16 v[64:79], v[146:149], v[194:197], v[64:79]

; #define VM_WAIT() asm volatile("s_waitcnt vmcnt(0)" ::: "memory")
; #define FENCE() do { asm volatile("" ::: "memory"); __builtin_amdgcn_sched_barrier(0); } while (0)
; template <int DK, int DV, bool MLSTM>
; __device__ __forceinline__ void out_unit2(LAS unsigned char* lds, LAS unsigned char* ldstab, const OutArgs a, const int wv) {
;     ...
;     VM_WAIT(); __syncthreads();
;     f32x16 p[4];
; #pragma unroll
;     for (int kb = 0; kb < 4; ++kb) p[kb] = (f32x16){};
;     float qnf = 0.f, qnb = 0.f;
; #pragma unroll
;     for (int ks = 0; ks < NKS; ++ks) {
;         const unsigned po = (ks >> 3) * 32768u + ((ks & 1) ? rb1 : rb0) + 512u * ((ks & 7) >> 1);
;         const bf16x8 qf = lds_r128(QP + po + 8192u * rb);
;         bf16x8 kf[4];
; #pragma unroll
;         for (int kb = 0; kb < 4; ++kb) kf[kb] = lds_r128(KP + po + 8192u * kb);
; #pragma unroll
;         for (int kb = 0; kb < 4; ++kb) p[kb] = __builtin_amdgcn_mfma_f32_32x32x16_bf16(kf[kb], qf, p[kb], 0, 0, 0);
;         FENCE();
;     }
.LBB0_4304:
	s_or_b64 exec, exec, s[4:5]
	s_lshl_b32 s4, s6, 10
	s_add_u32 s37, s7, s4
	s_addc_u32 s16, s12, 0
	s_add_u32 s6, s37, 0x1000
	s_addc_u32 s7, s16, 0
	s_lshl_b32 s12, s11, 1
	s_ashr_i32 s13, s12, 31
	s_lshl_b64 s[4:5], s[12:13], 23
	s_add_u32 s4, s49, s4
	s_addc_u32 s5, s50, s5
	s_lshl_b32 s13, s10, 18
	s_add_u32 s4, s4, s13
	s_addc_u32 s5, s5, 0
	s_or_b32 s10, s12, 1
	v_lshlrev_b32_e32 v1, 6, v171
	s_ashr_i32 s11, s10, 31
	v_lshlrev_b32_e32 v0, 8, v171
	v_and_b32_e32 v1, 0x1c0, v1
	s_lshl_b64 s[10:11], s[10:11], 23
	v_and_or_b32 v71, v0, s64, v1
	v_bitop3_b32 v0, v5, v72, 3 bitop3:0x6c
	s_add_u32 s10, s49, s10
	v_lshlrev_b32_e32 v74, 4, v0
	s_addc_u32 s12, s50, s11
	v_or_b32_e32 v173, v74, v71
	s_add_u32 s11, s10, s13
	v_add_u32_e32 v0, s68, v173
	s_addc_u32 s12, s12, 0
	s_and_b32 s10, s36, 3
	s_lshl_b32 s13, s9, 6
	s_waitcnt vmcnt(0)
	s_waitcnt vmcnt(0) lgkmcnt(0)
	s_barrier
	ds_read_b128 v[0:3], v0
	s_and_b32 s39, s13, 0xffffc000
	v_lshlrev_b32_e32 v8, 11, v72
	s_lshl_b32 s13, s10, 13
	v_lshlrev_b32_e32 v9, 4, v171
	s_add_i32 s13, s13, 0
	v_and_or_b32 v12, v9, s66, v8
	v_add_u32_e32 v8, s70, v173
	v_add_u32_e32 v4, s13, v173
	ds_read_b128 v[8:11], v8
	ds_read_b128 v[4:7], v4
	s_waitcnt lgkmcnt(0)
	v_mfma_f32_32x32x16_bf16 v[48:63], v[0:3], v[4:7], 0
	v_lshrrev_b32_e32 v0, 3, v232
	v_bfe_u32 v1, v232, 1, 1
	v_and_or_b32 v0, v0, 2, v1
	v_lshlrev_b32_e32 v0, 4, v0
	v_bitop3_b32 v13, v0, v232, 32 bitop3:0x78
	v_add_u32_e32 v0, s71, v173
	ds_read_b128 v[0:3], v0
	v_mfma_f32_32x32x16_bf16 v[32:47], v[8:11], v[4:7], 0
	v_lshlrev_b32_e32 v8, 3, v171
	v_and_b32_e32 v8, 8, v8
	v_or3_b32 v68, v13, v12, v8
	v_add_u32_e32 v8, s72, v173
	ds_read_b128 v[8:11], v8
	v_and_b32_e32 v233, 31, v232
	s_lshl_b32 s10, s10, 5
	v_or_b32_e32 v66, s10, v233
	s_waitcnt lgkmcnt(1)
	v_mfma_f32_32x32x16_bf16 v[16:31], v[0:3], v[4:7], 0
	v_add_u32_e32 v0, 1, v66
	v_cvt_f32_ubyte0_e32 v67, v0
	v_sub_u32_e32 v0, 0x80, v66
	v_cvt_f32_ubyte0_e32 v70, v0
	s_mov_b32 s15, 4
	v_or_b32_e32 v175, s39, v68
	s_waitcnt lgkmcnt(0)
	v_mfma_f32_32x32x16_bf16 v[0:15], v[8:11], v[4:7], 0
	s_movk_i32 s14, 0x80
	v_mul_f32_e32 v69, v64, v67
	v_bitop3_b32 v177, v74, 32, v71 bitop3:0x36
	v_add_u32_e32 v71, s68, v177
	ds_read_b128 v[74:77], v71
	v_add_u32_e32 v71, s13, v177
	ds_read_b128 v[78:81], v71
	v_add_u32_e32 v71, s70, v177
	s_waitcnt lgkmcnt(0)
	v_mfma_f32_32x32x16_bf16 v[48:63], v[74:77], v[78:81], v[48:63]
	ds_read_b128 v[74:77], v71
	v_add_u32_e32 v71, s71, v177
	s_waitcnt lgkmcnt(0)
	v_mfma_f32_32x32x16_bf16 v[32:47], v[74:77], v[78:81], v[32:47]
	ds_read_b128 v[74:77], v71
	v_add_u32_e32 v71, s72, v177
	s_waitcnt lgkmcnt(0)
	v_mfma_f32_32x32x16_bf16 v[16:31], v[74:77], v[78:81], v[16:31]
	ds_read_b128 v[74:77], v71
	s_waitcnt lgkmcnt(0)
	v_mfma_f32_32x32x16_bf16 v[0:15], v[74:77], v[78:81], v[0:15]
	v_or_b32_e32 v71, 0x200, v173
	v_add_u32_e32 v74, s68, v71
	ds_read_b128 v[74:77], v74
	v_add_u32_e32 v78, s13, v71
	ds_read_b128 v[78:81], v78
	v_add_u32_e32 v82, s70, v71
	s_waitcnt lgkmcnt(0)
	v_mfma_f32_32x32x16_bf16 v[48:63], v[74:77], v[78:81], v[48:63]
	ds_read_b128 v[74:77], v82
	v_add_u32_e32 v82, s71, v71
	v_add_u32_e32 v71, s72, v71
	s_waitcnt lgkmcnt(0)
	v_mfma_f32_32x32x16_bf16 v[32:47], v[74:77], v[78:81], v[32:47]
	ds_read_b128 v[74:77], v82
	s_waitcnt lgkmcnt(0)
	v_mfma_f32_32x32x16_bf16 v[16:31], v[74:77], v[78:81], v[16:31]
	ds_read_b128 v[74:77], v71
	s_waitcnt lgkmcnt(0)
	v_mfma_f32_32x32x16_bf16 v[0:15], v[74:77], v[78:81], v[0:15]
	v_bitop3_b32 v71, v173, s73, 32 bitop3:0xde
	v_add_u32_e32 v74, s68, v71
	ds_read_b128 v[74:77], v74
	v_add_u32_e32 v78, s13, v71
	ds_read_b128 v[78:81], v78
	v_add_u32_e32 v82, s70, v71
	s_waitcnt lgkmcnt(0)
	v_mfma_f32_32x32x16_bf16 v[48:63], v[74:77], v[78:81], v[48:63]
	ds_read_b128 v[74:77], v82
	v_add_u32_e32 v82, s71, v71
	v_add_u32_e32 v71, s72, v71
	s_waitcnt lgkmcnt(0)
	v_mfma_f32_32x32x16_bf16 v[32:47], v[74:77], v[78:81], v[32:47]
	ds_read_b128 v[74:77], v82
	s_waitcnt lgkmcnt(0)
	v_mfma_f32_32x32x16_bf16 v[16:31], v[74:77], v[78:81], v[16:31]
	ds_read_b128 v[74:77], v71
	s_waitcnt lgkmcnt(0)
	v_mfma_f32_32x32x16_bf16 v[0:15], v[74:77], v[78:81], v[0:15]
	v_or_b32_e32 v71, 0x400, v173
	v_add_u32_e32 v74, s68, v71
	ds_read_b128 v[74:77], v74
	v_add_u32_e32 v78, s13, v71
	ds_read_b128 v[78:81], v78
	v_add_u32_e32 v82, s70, v71
	s_waitcnt lgkmcnt(0)
	v_mfma_f32_32x32x16_bf16 v[48:63], v[74:77], v[78:81], v[48:63]
	ds_read_b128 v[74:77], v82
	v_add_u32_e32 v82, s71, v71
	v_add_u32_e32 v71, s72, v71
	s_waitcnt lgkmcnt(0)
	v_mfma_f32_32x32x16_bf16 v[32:47], v[74:77], v[78:81], v[32:47]
	ds_read_b128 v[74:77], v82
	s_waitcnt lgkmcnt(0)
	v_mfma_f32_32x32x16_bf16 v[16:31], v[74:77], v[78:81], v[16:31]
	ds_read_b128 v[74:77], v71
	s_waitcnt lgkmcnt(0)
	v_mfma_f32_32x32x16_bf16 v[0:15], v[74:77], v[78:81], v[0:15]
	v_bitop3_b32 v71, v173, s74, 32 bitop3:0xde
	v_add_u32_e32 v74, s68, v71
	ds_read_b128 v[74:77], v74
	v_add_u32_e32 v78, s13, v71
	ds_read_b128 v[78:81], v78
	v_add_u32_e32 v82, s70, v71
	s_waitcnt lgkmcnt(0)
	v_mfma_f32_32x32x16_bf16 v[48:63], v[74:77], v[78:81], v[48:63]
	ds_read_b128 v[74:77], v82
	v_add_u32_e32 v82, s71, v71
	v_add_u32_e32 v71, s72, v71
	s_waitcnt lgkmcnt(0)
	v_mfma_f32_32x32x16_bf16 v[32:47], v[74:77], v[78:81], v[32:47]
	ds_read_b128 v[74:77], v82
	s_waitcnt lgkmcnt(0)
	v_mfma_f32_32x32x16_bf16 v[16:31], v[74:77], v[78:81], v[16:31]
	ds_read_b128 v[74:77], v71
	s_waitcnt lgkmcnt(0)
	v_mfma_f32_32x32x16_bf16 v[0:15], v[74:77], v[78:81], v[0:15]
	v_or_b32_e32 v71, 0x600, v173
	v_add_u32_e32 v74, s68, v71
	ds_read_b128 v[74:77], v74
	v_add_u32_e32 v78, s13, v71
	ds_read_b128 v[78:81], v78
	v_add_u32_e32 v82, s70, v71
	s_waitcnt lgkmcnt(0)
; #define FENCE() do { asm volatile("" ::: "memory"); __builtin_amdgcn_sched_barrier(0); } while (0)
; template <int DK, int DV, bool MLSTM>
; __device__ __forceinline__ void out_unit2(LAS unsigned char* lds, LAS unsigned char* ldstab, const OutArgs a, const int wv) {
;     ...
; #pragma unroll
;     for (int ks = 0; ks < NKS; ++ks) {
;         const unsigned po = (ks >> 3) * 32768u + ((ks & 1) ? rb1 : rb0) + 512u * ((ks & 7) >> 1);
;         const bf16x8 qf = lds_r128(QP + po + 8192u * rb);
;         bf16x8 kf[4];
; #pragma unroll
;         for (int kb = 0; kb < 4; ++kb) kf[kb] = lds_r128(KP + po + 8192u * kb);
; #pragma unroll
;         for (int kb = 0; kb < 4; ++kb) p[kb] = __builtin_amdgcn_mfma_f32_32x32x16_bf16(kf[kb], qf, p[kb], 0, 0, 0);
;         FENCE();
;     }
	v_mfma_f32_32x32x16_bf16 v[48:63], v[74:77], v[78:81], v[48:63]
	ds_read_b128 v[74:77], v82
	v_add_u32_e32 v82, s71, v71
	v_add_u32_e32 v71, s72, v71
	s_waitcnt lgkmcnt(0)
	v_mfma_f32_32x32x16_bf16 v[32:47], v[74:77], v[78:81], v[32:47]
	ds_read_b128 v[74:77], v82
	s_waitcnt lgkmcnt(0)
	v_mfma_f32_32x32x16_bf16 v[16:31], v[74:77], v[78:81], v[16:31]
	ds_read_b128 v[74:77], v71
	s_waitcnt lgkmcnt(0)
	v_mfma_f32_32x32x16_bf16 v[0:15], v[74:77], v[78:81], v[0:15]
	v_bitop3_b32 v71, v173, s75, 32 bitop3:0xde
	v_add_u32_e32 v74, s68, v71
	ds_read_b128 v[74:77], v74
	v_add_u32_e32 v78, s13, v71
	ds_read_b128 v[78:81], v78
	v_add_u32_e32 v82, s70, v71
	s_waitcnt lgkmcnt(0)
	v_mfma_f32_32x32x16_bf16 v[48:63], v[74:77], v[78:81], v[48:63]
	ds_read_b128 v[74:77], v82
	v_add_u32_e32 v82, s71, v71
	v_add_u32_e32 v71, s72, v71
	s_waitcnt lgkmcnt(0)
	v_mfma_f32_32x32x16_bf16 v[32:47], v[74:77], v[78:81], v[32:47]
	ds_read_b128 v[74:77], v82
	s_waitcnt lgkmcnt(0)
	v_mfma_f32_32x32x16_bf16 v[16:31], v[74:77], v[78:81], v[16:31]
	ds_read_b128 v[74:77], v71
	s_waitcnt lgkmcnt(0)
	v_mfma_f32_32x32x16_bf16 v[0:15], v[74:77], v[78:81], v[0:15]
	v_or_b32_e32 v71, 0x8000, v173
	v_add_u32_e32 v74, s68, v71
	ds_read_b128 v[74:77], v74
	v_add_u32_e32 v78, s13, v71
	ds_read_b128 v[78:81], v78
	v_add_u32_e32 v82, s70, v71
	s_waitcnt lgkmcnt(0)
	v_mfma_f32_32x32x16_bf16 v[48:63], v[74:77], v[78:81], v[48:63]
	ds_read_b128 v[74:77], v82
	v_add_u32_e32 v82, s71, v71
	v_add_u32_e32 v71, s72, v71
	s_waitcnt lgkmcnt(0)
	v_mfma_f32_32x32x16_bf16 v[32:47], v[74:77], v[78:81], v[32:47]
	ds_read_b128 v[74:77], v82
	s_waitcnt lgkmcnt(0)
	v_mfma_f32_32x32x16_bf16 v[16:31], v[74:77], v[78:81], v[16:31]
	ds_read_b128 v[74:77], v71
	s_waitcnt lgkmcnt(0)
	v_mfma_f32_32x32x16_bf16 v[0:15], v[74:77], v[78:81], v[0:15]
	v_bitop3_b32 v71, v173, s76, 32 bitop3:0xde
	v_add_u32_e32 v74, s68, v71
	ds_read_b128 v[74:77], v74
	v_add_u32_e32 v78, s13, v71
	ds_read_b128 v[78:81], v78
	v_add_u32_e32 v82, s70, v71
	s_waitcnt lgkmcnt(0)
	v_mfma_f32_32x32x16_bf16 v[48:63], v[74:77], v[78:81], v[48:63]
	ds_read_b128 v[74:77], v82
	v_add_u32_e32 v82, s71, v71
	v_add_u32_e32 v71, s72, v71
	s_waitcnt lgkmcnt(0)
	v_mfma_f32_32x32x16_bf16 v[32:47], v[74:77], v[78:81], v[32:47]
	ds_read_b128 v[74:77], v82
	s_waitcnt lgkmcnt(0)
	v_mfma_f32_32x32x16_bf16 v[16:31], v[74:77], v[78:81], v[16:31]
	ds_read_b128 v[74:77], v71
	s_waitcnt lgkmcnt(0)
	v_mfma_f32_32x32x16_bf16 v[0:15], v[74:77], v[78:81], v[0:15]
	v_or_b32_e32 v71, 0x8200, v173
	v_add_u32_e32 v74, s68, v71
	ds_read_b128 v[74:77], v74
	v_add_u32_e32 v78, s13, v71
	ds_read_b128 v[78:81], v78
	v_add_u32_e32 v82, s70, v71
	s_waitcnt lgkmcnt(0)
	v_mfma_f32_32x32x16_bf16 v[48:63], v[74:77], v[78:81], v[48:63]
	ds_read_b128 v[74:77], v82
	v_add_u32_e32 v82, s71, v71
	v_add_u32_e32 v71, s72, v71
	s_waitcnt lgkmcnt(0)
	v_mfma_f32_32x32x16_bf16 v[32:47], v[74:77], v[78:81], v[32:47]
	ds_read_b128 v[74:77], v82
	s_waitcnt lgkmcnt(0)
	v_mfma_f32_32x32x16_bf16 v[16:31], v[74:77], v[78:81], v[16:31]
	ds_read_b128 v[74:77], v71
	s_waitcnt lgkmcnt(0)
	v_mfma_f32_32x32x16_bf16 v[0:15], v[74:77], v[78:81], v[0:15]
	v_bitop3_b32 v71, v173, s77, 32 bitop3:0xde
	v_add_u32_e32 v74, s68, v71
	ds_read_b128 v[74:77], v74
	v_add_u32_e32 v78, s13, v71
	ds_read_b128 v[78:81], v78
	v_add_u32_e32 v82, s70, v71
	s_waitcnt lgkmcnt(0)
	v_mfma_f32_32x32x16_bf16 v[48:63], v[74:77], v[78:81], v[48:63]
	ds_read_b128 v[74:77], v82
	v_add_u32_e32 v82, s71, v71
	v_add_u32_e32 v71, s72, v71
	s_waitcnt lgkmcnt(0)
	v_mfma_f32_32x32x16_bf16 v[32:47], v[74:77], v[78:81], v[32:47]
	ds_read_b128 v[74:77], v82
	s_waitcnt lgkmcnt(0)
	v_mfma_f32_32x32x16_bf16 v[16:31], v[74:77], v[78:81], v[16:31]
	ds_read_b128 v[74:77], v71
	s_waitcnt lgkmcnt(0)
	v_mfma_f32_32x32x16_bf16 v[0:15], v[74:77], v[78:81], v[0:15]
	v_or_b32_e32 v71, 0x8400, v173
	v_add_u32_e32 v74, s68, v71
	ds_read_b128 v[74:77], v74
	v_add_u32_e32 v78, s13, v71
	ds_read_b128 v[78:81], v78
	v_add_u32_e32 v82, s70, v71
	s_waitcnt lgkmcnt(0)
	v_mfma_f32_32x32x16_bf16 v[48:63], v[74:77], v[78:81], v[48:63]
	ds_read_b128 v[74:77], v82
	v_add_u32_e32 v82, s71, v71
	v_add_u32_e32 v71, s72, v71
	s_waitcnt lgkmcnt(0)
	v_mfma_f32_32x32x16_bf16 v[32:47], v[74:77], v[78:81], v[32:47]
	ds_read_b128 v[74:77], v82
	s_waitcnt lgkmcnt(0)
	v_mfma_f32_32x32x16_bf16 v[16:31], v[74:77], v[78:81], v[16:31]
	ds_read_b128 v[74:77], v71
	s_waitcnt lgkmcnt(0)
	v_mfma_f32_32x32x16_bf16 v[0:15], v[74:77], v[78:81], v[0:15]
	v_bitop3_b32 v71, v173, s78, 32 bitop3:0xde
	v_add_u32_e32 v74, s68, v71
	ds_read_b128 v[74:77], v74
	v_add_u32_e32 v78, s13, v71
	ds_read_b128 v[78:81], v78
	v_add_u32_e32 v82, s70, v71
	s_waitcnt lgkmcnt(0)
	v_mfma_f32_32x32x16_bf16 v[48:63], v[74:77], v[78:81], v[48:63]
	ds_read_b128 v[74:77], v82
	v_add_u32_e32 v82, s71, v71
	v_add_u32_e32 v71, s72, v71
	s_waitcnt lgkmcnt(0)
	v_mfma_f32_32x32x16_bf16 v[32:47], v[74:77], v[78:81], v[32:47]
	ds_read_b128 v[74:77], v82
	s_waitcnt lgkmcnt(0)
	v_mfma_f32_32x32x16_bf16 v[16:31], v[74:77], v[78:81], v[16:31]
	ds_read_b128 v[74:77], v71
	s_waitcnt lgkmcnt(0)
	v_mfma_f32_32x32x16_bf16 v[0:15], v[74:77], v[78:81], v[0:15]
	v_or_b32_e32 v71, 0x8600, v173
	v_add_u32_e32 v74, s68, v71
	ds_read_b128 v[74:77], v74
	v_add_u32_e32 v78, s13, v71
	ds_read_b128 v[78:81], v78
	v_add_u32_e32 v82, s70, v71
	s_waitcnt lgkmcnt(0)
	v_mfma_f32_32x32x16_bf16 v[48:63], v[74:77], v[78:81], v[48:63]
	ds_read_b128 v[74:77], v82
	v_add_u32_e32 v82, s71, v71
	v_add_u32_e32 v71, s72, v71
	s_waitcnt lgkmcnt(0)
	v_mfma_f32_32x32x16_bf16 v[32:47], v[74:77], v[78:81], v[32:47]
	ds_read_b128 v[74:77], v82
	s_waitcnt lgkmcnt(0)
; #define LAS __attribute__((address_space(3)))
; template <int R, int NP>
; __device__ __forceinline__ void dma_tile(int wid, int lane, unsigned lds_base, const bf16_t* src, int ld) {
;     constexpr int NQ = R * NP / 4, PER = NQ / 8;
;     static_assert(NQ % 8 == 0 && R % 8 == 0, "dma_tile geometry");
;     const int r7 = (lane >> 2) & 7, x = lane & 3, hi = lane >> 5;
; #pragma unroll
;     for (int j = 0; j < PER; ++j) {
;         const int q = wid * PER + j;
;         const int sub = 2 * q + hi, panel = sub / (R / 2), psub = sub % (R / 2), rg = psub >> 2, cblk = psub & 3;
;         const int row = 8 * rg + r7, chlo = x ^ ((row >> 2) & 3);
;         const bf16_t* g = src + (size_t)row * ld + 128 * panel + 32 * cblk + 8 * chlo;
;         __builtin_amdgcn_global_load_lds((const unsigned*)g, (LAS unsigned*)(uintptr_t)(lds_base + q * 1024u), 16, 0, 0);
;     }
; template <int DK, int DV, bool MLSTM>
; __device__ __forceinline__ void out_unit2(LAS unsigned char* lds, LAS unsigned char* ldstab, const OutArgs a, const int wv) {
;     ...
;     __syncthreads();
;     dma_tile<32, NPV>(wid, lane, SB, a.V, a.ldv);
	v_mfma_f32_32x32x16_bf16 v[16:31], v[74:77], v[78:81], v[16:31]
	ds_read_b128 v[74:77], v71
	s_waitcnt lgkmcnt(0)
	v_mfma_f32_32x32x16_bf16 v[0:15], v[74:77], v[78:81], v[0:15]
	v_bitop3_b32 v71, v173, s79, 32 bitop3:0xde
	v_add_u32_e32 v74, s68, v71
	ds_read_b128 v[74:77], v74
	v_add_u32_e32 v78, s13, v71
	ds_read_b128 v[78:81], v78
	v_add_u32_e32 v82, s70, v71
	s_waitcnt lgkmcnt(0)
	v_mfma_f32_32x32x16_bf16 v[48:63], v[74:77], v[78:81], v[48:63]
	ds_read_b128 v[74:77], v82
	v_add_u32_e32 v82, s71, v71
	v_add_u32_e32 v71, s72, v71
	s_waitcnt lgkmcnt(0)
	v_mfma_f32_32x32x16_bf16 v[32:47], v[74:77], v[78:81], v[32:47]
	ds_read_b128 v[74:77], v82
	s_waitcnt lgkmcnt(0)
	v_mfma_f32_32x32x16_bf16 v[16:31], v[74:77], v[78:81], v[16:31]
	ds_read_b128 v[74:77], v71
	s_waitcnt lgkmcnt(0)
	v_mfma_f32_32x32x16_bf16 v[0:15], v[74:77], v[78:81], v[0:15]
	v_or_b32_e32 v74, s38, v72
	v_ashrrev_i32_e32 v75, 31, v74
	v_lshrrev_b32_e32 v75, 28, v75
	v_add_u32_e32 v78, v74, v75
	v_and_b32_e32 v75, -16, v78
	v_sub_u32_e32 v79, v74, v75
	v_lshlrev_b32_e32 v78, 3, v78
	v_lshlrev_b32_e32 v74, 1, v79
	v_and_b32_e32 v158, 0xffffff80, v78
	v_and_or_b32 v182, v74, -16, v73
	v_mov_b64_e32 v[74:75], s[6:7]
	v_ashrrev_i32_e32 v159, 31, v158
	v_lshlrev_b32_e32 v78, 5, v79
	v_mad_i64_i32 v[76:77], s[6:7], v182, s57, v[74:75]
	v_lshlrev_b64 v[184:185], 1, v[158:159]
	v_and_b32_e32 v162, 32, v78
	v_lshl_add_u64 v[76:77], v[76:77], 0, v[184:185]
	v_lshlrev_b32_e32 v160, 1, v162
	s_lshl_b32 s6, s36, 12
	s_lshl_b32 s44, s36, 2
	v_lshl_add_u64 v[76:77], v[76:77], 0, v[160:161]
	s_add_i32 s40, s6, s68
	v_lshl_add_u64 v[76:77], v[76:77], 0, v[156:157]
	s_mov_b32 m0, s40
	s_or_b32 s7, s44, 1
	s_barrier
	s_mov_b32 s98, 0x60000
	s_mov_b32 s99, 0
	global_load_lds_dwordx4 v[76:77], off
	v_lshl_add_u64 v[86:87], v[76:77], 0, s[98:99]
	s_add_i32 m0, m0, 0x8000
	s_nop 0
	global_load_lds_dwordx4 v[86:87], off
	v_lshl_or_b32 v76, s7, 1, v72
	v_ashrrev_i32_e32 v77, 31, v76
	v_lshrrev_b32_e32 v77, 28, v77
	v_add_u32_e32 v78, v76, v77
	v_and_b32_e32 v77, -16, v78
	v_sub_u32_e32 v79, v76, v77
	v_lshlrev_b32_e32 v76, 1, v79
	v_and_or_b32 v186, v76, -8, v73
	v_lshlrev_b32_e32 v78, 3, v78
	v_lshrrev_b32_e32 v76, 2, v186
	v_and_b32_e32 v164, 0xffffff80, v78
	v_xor_b32_e32 v80, v76, v232
	v_ashrrev_i32_e32 v165, 31, v164
	v_lshlrev_b32_e32 v78, 5, v79
	v_mad_i64_i32 v[76:77], s[42:43], v186, s57, v[74:75]
	v_lshlrev_b64 v[188:189], 1, v[164:165]
	v_and_b32_e32 v170, 0x60, v78
	v_lshlrev_b32_e32 v78, 3, v80
	v_lshl_add_u64 v[76:77], v[76:77], 0, v[188:189]
	v_lshlrev_b32_e32 v190, 1, v170
	v_mov_b32_e32 v191, v161
	v_and_b32_e32 v172, 24, v78
	s_lshl_b32 s7, s7, 10
	v_lshl_add_u64 v[76:77], v[76:77], 0, v[190:191]
	v_lshlrev_b32_e32 v192, 1, v172
	v_mov_b32_e32 v193, v161
	s_add_i32 s41, s7, s68
	v_lshl_add_u64 v[76:77], v[76:77], 0, v[192:193]
	s_mov_b32 m0, s41
	s_or_b32 s36, s44, 2
	global_load_lds_dwordx4 v[76:77], off
	v_lshl_add_u64 v[88:89], v[76:77], 0, s[98:99]
	s_add_i32 m0, m0, 0x8000
	s_nop 0
	global_load_lds_dwordx4 v[88:89], off
	v_lshl_or_b32 v76, s36, 1, v72
	v_ashrrev_i32_e32 v77, 31, v76
	v_lshrrev_b32_e32 v77, 28, v77
	v_add_u32_e32 v78, v76, v77
	v_and_b32_e32 v77, -16, v78
	v_sub_u32_e32 v79, v76, v77
	v_lshlrev_b32_e32 v76, 1, v79
	v_and_or_b32 v194, v76, -8, v73
	v_lshlrev_b32_e32 v78, 3, v78
	v_lshrrev_b32_e32 v76, 2, v194
	v_and_b32_e32 v166, 0xffffff80, v78
	v_xor_b32_e32 v80, v76, v232
	v_ashrrev_i32_e32 v167, 31, v166
	v_lshlrev_b32_e32 v78, 5, v79
	v_mad_i64_i32 v[76:77], s[42:43], v194, s57, v[74:75]
	v_lshlrev_b64 v[196:197], 1, v[166:167]
	v_and_b32_e32 v174, 0x60, v78
	v_lshlrev_b32_e32 v78, 3, v80
	v_lshl_add_u64 v[76:77], v[76:77], 0, v[196:197]
	v_lshlrev_b32_e32 v198, 1, v174
	v_mov_b32_e32 v199, v161
	v_and_b32_e32 v176, 24, v78
	s_lshl_b32 s36, s36, 10
	v_lshl_add_u64 v[76:77], v[76:77], 0, v[198:199]
	v_lshlrev_b32_e32 v200, 1, v176
	v_mov_b32_e32 v201, v161
	s_add_i32 s42, s36, s68
	v_lshl_add_u64 v[76:77], v[76:77], 0, v[200:201]
	s_mov_b32 m0, s42
	s_or_b32 s38, s44, 3
	global_load_lds_dwordx4 v[76:77], off
	v_lshl_add_u64 v[90:91], v[76:77], 0, s[98:99]
	s_add_i32 m0, m0, 0x8000
	s_nop 0
	global_load_lds_dwordx4 v[90:91], off
	v_lshl_or_b32 v76, s38, 1, v72
	v_ashrrev_i32_e32 v77, 31, v76
	v_lshrrev_b32_e32 v77, 28, v77
	v_add_u32_e32 v77, v76, v77
	v_and_b32_e32 v78, -16, v77
	v_sub_u32_e32 v76, v76, v78
	v_lshlrev_b32_e32 v78, 1, v76
	v_and_or_b32 v202, v78, -8, v73
	v_lshlrev_b32_e32 v77, 3, v77
	v_lshrrev_b32_e32 v73, 2, v202
	v_and_b32_e32 v168, 0xffffff80, v77
	v_xor_b32_e32 v73, v73, v232
	v_ashrrev_i32_e32 v169, 31, v168
	v_lshlrev_b32_e32 v76, 5, v76
	v_mad_i64_i32 v[74:75], s[44:45], v202, s57, v[74:75]
	v_lshlrev_b64 v[204:205], 1, v[168:169]
	v_and_b32_e32 v178, 0x60, v76
	v_lshlrev_b32_e32 v73, 3, v73
	v_lshl_add_u64 v[74:75], v[74:75], 0, v[204:205]
	v_lshlrev_b32_e32 v206, 1, v178
	v_mov_b32_e32 v207, v161
	v_and_b32_e32 v180, 24, v73
	s_lshl_b32 s38, s38, 10
	v_lshl_add_u64 v[74:75], v[74:75], 0, v[206:207]
	v_lshlrev_b32_e32 v208, 1, v180
	v_mov_b32_e32 v209, v161
	s_add_i32 s43, s38, s68
	v_lshl_add_u64 v[74:75], v[74:75], 0, v[208:209]
	s_mov_b32 m0, s43
	s_add_i32 s44, 0, 0x21500
	v_lshlrev_b32_e32 v73, 4, v72
	global_load_lds_dwordx4 v[74:75], off
	v_lshl_add_u64 v[92:93], v[74:75], 0, s[98:99]
	s_add_i32 m0, m0, 0x8000
	s_nop 0
	global_load_lds_dwordx4 v[92:93], off
	v_add_u32_e32 v74, s44, v73
	s_add_i32 s45, 0, 0x21700
	v_add_u32_e32 v73, s45, v73
	ds_read_b128 v[74:77], v74
	ds_read_b128 v[78:81], v73
	v_lshlrev_b32_e32 v234, 2, v72
	v_cmp_le_i32_e32 vcc, v234, v66
	v_or_b32_e32 v84, 8, v234
	s_waitcnt lgkmcnt(0)
; #define FENCE() do { asm volatile("" ::: "memory"); __builtin_amdgcn_sched_barrier(0); } while (0)
; __device__ __forceinline__ int crow(int r, int hi) { return (r & 3) + 8 * (r >> 2) + 4 * hi; }
; __device__ __forceinline__ int crow(int r, int hi) { return (r & 3) + 8 * (r >> 2) + 4 * hi; }
; template <int DK, int DV, bool MLSTM>
; __device__ __forceinline__ void out_unit2(LAS unsigned char* lds, LAS unsigned char* ldstab, const OutArgs a, const int wv) {
;     ...
;     int l2 = l; asm volatile("" : "+v"(l2));
; #pragma unroll
;     for (int kb = 0; kb < 4; ++kb) {
; #pragma unroll
;         for (int r = 0; r < 16; ++r) { const int s = 32 * kb + crow(r, hi);
;             const float xf = a_fl - akf[s], xb = a_bl - akb[s];
;             const float wf = __expf((s <= l2) ? xf : -1.0e30f), wb = __expf((s >= l2) ? xb : -1.0e30f);
;             p[kb][r] *= (wf * rf + wb * rbk); }
;         FENCE(); }
	v_fma_f32 v72, v64, v67, -v74
	v_fma_f32 v73, v65, v70, -v78
	v_mul_f32_e32 v72, 0x3fb8aa3b, v72
	v_fma_f32 v75, v64, v67, -v75
	v_cndmask_b32_e32 v72, v230, v72, vcc
	v_mul_f32_e32 v73, 0x3fb8aa3b, v73
	v_cmp_lt_i32_e32 vcc, v234, v66
	v_or_b32_e32 v74, 1, v234
	v_fma_f32 v78, v65, v70, -v79
	v_mul_f32_e32 v75, 0x3fb8aa3b, v75
	v_cndmask_b32_e32 v73, v73, v230, vcc
	v_cndmask_b32_e32 v75, v230, v75, vcc
	v_mul_f32_e32 v78, 0x3fb8aa3b, v78
	v_cmp_ge_i32_e32 vcc, v74, v66
	v_exp_f32_e32 v72, v72
	v_exp_f32_e32 v73, v73
	v_cndmask_b32_e32 v74, v230, v78, vcc
	v_exp_f32_e32 v75, v75
	v_exp_f32_e32 v74, v74
	v_add_f32_e32 v72, v72, v73
	v_mul_f32_e32 v48, v48, v72
	v_fma_f32 v73, v64, v67, -v76
	v_add_f32_e32 v72, v75, v74
	v_mul_f32_e32 v49, v49, v72
	v_or_b32_e32 v72, 2, v234
	v_mul_f32_e32 v73, 0x3fb8aa3b, v73
	v_cmp_le_i32_e32 vcc, v72, v66
	v_fma_f32 v74, v65, v70, -v80
	v_mul_f32_e32 v71, v65, v70
	v_cndmask_b32_e32 v73, v230, v73, vcc
	v_exp_f32_e32 v80, v73
	v_mul_f32_e32 v73, 0x3fb8aa3b, v74
	v_cmp_ge_i32_e32 vcc, v72, v66
	v_fma_f32 v74, v65, v70, -v81
	v_ashrrev_i32_e32 v183, 31, v182
	v_cndmask_b32_e32 v72, v230, v73, vcc
	v_exp_f32_e32 v82, v72
	v_or_b32_e32 v72, 3, v234
	v_fma_f32 v73, v64, v67, -v77
	v_mul_f32_e32 v73, 0x3fb8aa3b, v73
	v_cmp_le_i32_e32 vcc, v72, v66
	v_add_f32_e32 v80, v80, v82
	v_mul_f32_e32 v50, v50, v80
	v_cndmask_b32_e32 v73, v230, v73, vcc
	v_exp_f32_e32 v81, v73
	v_mul_f32_e32 v73, 0x3fb8aa3b, v74
	v_cmp_ge_i32_e32 vcc, v72, v66
	v_ashrrev_i32_e32 v187, 31, v186
	v_ashrrev_i32_e32 v195, 31, v194
	v_cndmask_b32_e32 v72, v230, v73, vcc
	v_exp_f32_e32 v83, v72
	v_lshlrev_b32_e32 v72, 2, v84
	v_add_u32_e32 v73, s44, v72
	v_add_u32_e32 v76, s45, v72
	ds_read_b128 v[72:75], v73
	ds_read_b128 v[76:79], v76
	v_cmp_le_i32_e32 vcc, v84, v66
	v_add_f32_e32 v80, v81, v83
	v_or_b32_e32 v81, 9, v234
	s_waitcnt lgkmcnt(0)
	v_fma_f32 v72, v64, v67, -v72
	v_fma_f32 v76, v65, v70, -v76
	v_mul_f32_e32 v72, 0x3fb8aa3b, v72
	v_cndmask_b32_e32 v72, v230, v72, vcc
	v_mul_f32_e32 v76, 0x3fb8aa3b, v76
	v_cmp_ge_i32_e32 vcc, v84, v66
	v_fma_f32 v73, v64, v67, -v73
	v_fma_f32 v77, v65, v70, -v77
	v_cndmask_b32_e32 v76, v230, v76, vcc
	v_mul_f32_e32 v73, 0x3fb8aa3b, v73
	v_cmp_le_i32_e32 vcc, v81, v66
	v_mul_f32_e32 v77, 0x3fb8aa3b, v77
	v_exp_f32_e32 v72, v72
	v_cndmask_b32_e32 v73, v230, v73, vcc
	v_cmp_ge_i32_e32 vcc, v81, v66
	v_exp_f32_e32 v76, v76
	v_exp_f32_e32 v73, v73
	v_cndmask_b32_e32 v77, v230, v77, vcc
	v_exp_f32_e32 v77, v77
	v_add_f32_e32 v72, v72, v76
	v_mul_f32_e32 v52, v52, v72
	v_mul_f32_e32 v51, v51, v80
	v_add_f32_e32 v72, v73, v77
	v_mul_f32_e32 v53, v53, v72
	v_or_b32_e32 v72, 10, v234
	v_fma_f32 v73, v64, v67, -v74
	v_mul_f32_e32 v73, 0x3fb8aa3b, v73
	v_cmp_le_i32_e32 vcc, v72, v66
	v_fma_f32 v74, v65, v70, -v78
	v_or_b32_e32 v84, 16, v234
	v_cndmask_b32_e32 v73, v230, v73, vcc
	v_exp_f32_e32 v80, v73
	v_mul_f32_e32 v73, 0x3fb8aa3b, v74
	v_cmp_ge_i32_e32 vcc, v72, v66
	v_fma_f32 v74, v65, v70, -v79
	v_ashrrev_i32_e32 v203, 31, v202
	v_cndmask_b32_e32 v72, v230, v73, vcc
	v_exp_f32_e32 v81, v72
	v_or_b32_e32 v72, 11, v234
	v_fma_f32 v73, v64, v67, -v75
	v_mul_f32_e32 v73, 0x3fb8aa3b, v73
	v_cmp_le_i32_e32 vcc, v72, v66
	v_add_f32_e32 v80, v80, v81
	v_mul_f32_e32 v54, v54, v80
	v_cndmask_b32_e32 v73, v230, v73, vcc
	v_exp_f32_e32 v82, v73
	v_mul_f32_e32 v73, 0x3fb8aa3b, v74
	v_cmp_ge_i32_e32 vcc, v72, v66
	s_nop 1
	v_cndmask_b32_e32 v72, v230, v73, vcc
	v_exp_f32_e32 v83, v72
	v_lshlrev_b32_e32 v72, 2, v84
	v_add_u32_e32 v73, s44, v72
	v_add_u32_e32 v76, s45, v72
	ds_read_b128 v[72:75], v73
	ds_read_b128 v[76:79], v76
	v_cmp_le_i32_e32 vcc, v84, v66
	v_add_f32_e32 v80, v82, v83
	s_waitcnt lgkmcnt(0)
	v_fma_f32 v72, v64, v67, -v72
	v_mul_f32_e32 v72, 0x3fb8aa3b, v72
	v_fma_f32 v76, v65, v70, -v76
	v_cndmask_b32_e32 v72, v230, v72, vcc
	v_exp_f32_e32 v81, v72
	v_mul_f32_e32 v72, 0x3fb8aa3b, v76
	v_cmp_ge_i32_e32 vcc, v84, v66
	v_fma_f32 v73, v64, v67, -v73
	v_fma_f32 v77, v65, v70, -v77
	v_cndmask_b32_e32 v72, v230, v72, vcc
	v_exp_f32_e32 v76, v72
	v_or_b32_e32 v72, 17, v234
	v_mul_f32_e32 v73, 0x3fb8aa3b, v73
	v_cmp_le_i32_e32 vcc, v72, v66
	v_mul_f32_e32 v77, 0x3fb8aa3b, v77
	v_fma_f32 v75, v64, v67, -v75
	v_cndmask_b32_e32 v73, v230, v73, vcc
	v_cmp_ge_i32_e32 vcc, v72, v66
	v_exp_f32_e32 v73, v73
	v_mul_f32_e32 v75, 0x3fb8aa3b, v75
	v_cndmask_b32_e32 v72, v230, v77, vcc
	v_exp_f32_e32 v77, v72
	v_mul_f32_e32 v72, v55, v80
	v_add_f32_e32 v55, v81, v76
	v_mul_f32_e32 v55, v56, v55
	v_add_f32_e32 v56, v73, v77
	v_mul_f32_e32 v56, v57, v56
	v_or_b32_e32 v57, 18, v234
	v_fma_f32 v73, v64, v67, -v74
	v_fma_f32 v74, v65, v70, -v78
	v_mul_f32_e32 v73, 0x3fb8aa3b, v73
	v_cmp_le_i32_e32 vcc, v57, v66
	v_mul_f32_e32 v74, 0x3fb8aa3b, v74
	v_fma_f32 v76, v65, v70, -v79
	v_cndmask_b32_e32 v73, v230, v73, vcc
	v_cmp_ge_i32_e32 vcc, v57, v66
	v_or_b32_e32 v84, 24, v234
	v_exp_f32_e32 v73, v73
	v_cndmask_b32_e32 v57, v230, v74, vcc
	v_or_b32_e32 v74, 19, v234
	v_cmp_le_i32_e32 vcc, v74, v66
	v_exp_f32_e32 v57, v57
	s_nop 0
	v_cndmask_b32_e32 v75, v230, v75, vcc
	v_exp_f32_e32 v82, v75
	v_mul_f32_e32 v75, 0x3fb8aa3b, v76
	v_cmp_ge_i32_e32 vcc, v74, v66
	v_add_f32_e32 v57, v73, v57
	v_mul_f32_e32 v57, v58, v57
	v_cndmask_b32_e32 v74, v230, v75, vcc
	v_exp_f32_e32 v83, v74
	v_lshlrev_b32_e32 v74, 2, v84
	v_add_u32_e32 v75, s44, v74
	v_add_u32_e32 v78, s45, v74
	ds_read_b128 v[74:77], v75
	ds_read_b128 v[78:81], v78
	v_cmp_le_i32_e32 vcc, v84, v66
	v_add_f32_e32 v58, v82, v83
	v_mul_f32_e32 v58, v59, v58
	s_waitcnt lgkmcnt(0)
; #define FENCE() do { asm volatile("" ::: "memory"); __builtin_amdgcn_sched_barrier(0); } while (0)
; __device__ __forceinline__ int crow(int r, int hi) { return (r & 3) + 8 * (r >> 2) + 4 * hi; }
; __device__ __forceinline__ int crow(int r, int hi) { return (r & 3) + 8 * (r >> 2) + 4 * hi; }
; template <int DK, int DV, bool MLSTM>
; __device__ __forceinline__ void out_unit2(LAS unsigned char* lds, LAS unsigned char* ldstab, const OutArgs a, const int wv) {
;     ...
;     int l2 = l; asm volatile("" : "+v"(l2));
; #pragma unroll
;     for (int kb = 0; kb < 4; ++kb) {
; #pragma unroll
;         for (int r = 0; r < 16; ++r) { const int s = 32 * kb + crow(r, hi);
;             const float xf = a_fl - akf[s], xb = a_bl - akb[s];
;             const float wf = __expf((s <= l2) ? xf : -1.0e30f), wb = __expf((s >= l2) ? xb : -1.0e30f);
;             p[kb][r] *= (wf * rf + wb * rbk); }
;         FENCE(); }
	v_fma_f32 v73, v64, v67, -v74
	v_fma_f32 v74, v65, v70, -v78
	v_mul_f32_e32 v73, 0x3fb8aa3b, v73
	v_cndmask_b32_e32 v73, v230, v73, vcc
	v_mul_f32_e32 v74, 0x3fb8aa3b, v74
	v_cmp_ge_i32_e32 vcc, v84, v66
	v_or_b32_e32 v78, 25, v234
	v_fma_f32 v75, v64, v67, -v75
	v_cndmask_b32_e32 v74, v230, v74, vcc
	v_fma_f32 v79, v65, v70, -v79
	v_mul_f32_e32 v75, 0x3fb8aa3b, v75
	v_cmp_le_i32_e32 vcc, v78, v66
	v_mul_f32_e32 v79, 0x3fb8aa3b, v79
	v_exp_f32_e32 v73, v73
	v_cndmask_b32_e32 v75, v230, v75, vcc
	v_cmp_ge_i32_e32 vcc, v78, v66
	v_exp_f32_e32 v74, v74
	v_exp_f32_e32 v75, v75
	v_cndmask_b32_e32 v78, v230, v79, vcc
	v_exp_f32_e32 v78, v78
	v_add_f32_e32 v59, v73, v74
	v_or_b32_e32 v73, 26, v234
	v_fma_f32 v74, v64, v67, -v76
	v_mul_f32_e32 v59, v60, v59
	v_add_f32_e32 v60, v75, v78
	v_fma_f32 v75, v65, v70, -v80
	v_mul_f32_e32 v74, 0x3fb8aa3b, v74
	v_cmp_le_i32_e32 vcc, v73, v66
	v_mul_f32_e32 v75, 0x3fb8aa3b, v75
	v_fma_f32 v76, v64, v67, -v77
	v_cndmask_b32_e32 v74, v230, v74, vcc
	v_cmp_ge_i32_e32 vcc, v73, v66
	v_fma_f32 v77, v65, v70, -v81
	v_mul_f32_e32 v76, 0x3fb8aa3b, v76
	v_cndmask_b32_e32 v73, v230, v75, vcc
	v_or_b32_e32 v75, 27, v234
	v_cmp_le_i32_e32 vcc, v75, v66
	v_mul_f32_e32 v77, 0x3fb8aa3b, v77
	v_exp_f32_e32 v74, v74
	v_cndmask_b32_e32 v76, v230, v76, vcc
	v_cmp_ge_i32_e32 vcc, v75, v66
	v_exp_f32_e32 v73, v73
	v_exp_f32_e32 v76, v76
	v_cndmask_b32_e32 v75, v230, v77, vcc
	v_exp_f32_e32 v75, v75
	v_mul_f32_e32 v60, v61, v60
	v_add_f32_e32 v61, v74, v73
	v_mul_f32_e32 v61, v62, v61
	v_add_f32_e32 v62, v76, v75
	v_mul_f32_e32 v62, v63, v62
	v_or_b32_e32 v63, 32, v234
	v_lshlrev_b32_e32 v73, 2, v63
	v_add_u32_e32 v74, s44, v73
	v_add_u32_e32 v73, s45, v73
	ds_read_b128 v[74:77], v74
	ds_read_b128 v[78:81], v73
	v_cmp_le_i32_e32 vcc, v63, v66
	v_or_b32_e32 v84, 40, v234
	s_waitcnt lgkmcnt(0)
	v_fma_f32 v73, v64, v67, -v74
	v_fma_f32 v74, v65, v70, -v78
	v_mul_f32_e32 v73, 0x3fb8aa3b, v73
	v_cndmask_b32_e32 v73, v230, v73, vcc
	v_mul_f32_e32 v74, 0x3fb8aa3b, v74
	v_cmp_ge_i32_e32 vcc, v63, v66
	v_fma_f32 v75, v64, v67, -v75
	v_fma_f32 v78, v65, v70, -v79
	v_cndmask_b32_e32 v63, v230, v74, vcc
	v_or_b32_e32 v74, 33, v234
	v_mul_f32_e32 v75, 0x3fb8aa3b, v75
	v_cmp_le_i32_e32 vcc, v74, v66
	v_mul_f32_e32 v78, 0x3fb8aa3b, v78
	v_exp_f32_e32 v73, v73
	v_cndmask_b32_e32 v75, v230, v75, vcc
	v_cmp_ge_i32_e32 vcc, v74, v66
	v_exp_f32_e32 v63, v63
	v_exp_f32_e32 v75, v75
	v_cndmask_b32_e32 v74, v230, v78, vcc
	v_exp_f32_e32 v74, v74
	v_add_f32_e32 v63, v73, v63
	v_mul_f32_e32 v32, v32, v63
	v_fma_f32 v73, v64, v67, -v76
	v_add_f32_e32 v63, v75, v74
	v_mul_f32_e32 v33, v33, v63
	v_or_b32_e32 v63, 34, v234
	v_fma_f32 v74, v65, v70, -v80
	v_mul_f32_e32 v73, 0x3fb8aa3b, v73
	v_cmp_le_i32_e32 vcc, v63, v66
	v_mul_f32_e32 v74, 0x3fb8aa3b, v74
	v_fma_f32 v75, v64, v67, -v77
	v_cndmask_b32_e32 v73, v230, v73, vcc
	v_cmp_ge_i32_e32 vcc, v63, v66
	v_mul_f32_e32 v75, 0x3fb8aa3b, v75
	v_fma_f32 v76, v65, v70, -v81
	v_cndmask_b32_e32 v63, v230, v74, vcc
	v_or_b32_e32 v74, 35, v234
	v_cmp_le_i32_e32 vcc, v74, v66
	v_exp_f32_e32 v73, v73
	v_exp_f32_e32 v63, v63
	v_cndmask_b32_e32 v75, v230, v75, vcc
	v_exp_f32_e32 v82, v75
	v_mul_f32_e32 v75, 0x3fb8aa3b, v76
	v_cmp_ge_i32_e32 vcc, v74, v66
	v_add_f32_e32 v63, v73, v63
	v_mul_f32_e32 v34, v34, v63
	v_cndmask_b32_e32 v74, v230, v75, vcc
	v_exp_f32_e32 v83, v74
	v_lshlrev_b32_e32 v74, 2, v84
	v_add_u32_e32 v75, s44, v74
	v_add_u32_e32 v78, s45, v74
	ds_read_b128 v[74:77], v75
	ds_read_b128 v[78:81], v78
	v_cmp_le_i32_e32 vcc, v84, v66
	v_add_f32_e32 v63, v82, v83
	v_mul_f32_e32 v35, v35, v63
	s_waitcnt lgkmcnt(0)
	v_fma_f32 v73, v64, v67, -v74
	v_fma_f32 v74, v65, v70, -v78
	v_mul_f32_e32 v73, 0x3fb8aa3b, v73
	v_cndmask_b32_e32 v73, v230, v73, vcc
	v_mul_f32_e32 v74, 0x3fb8aa3b, v74
	v_cmp_ge_i32_e32 vcc, v84, v66
	v_or_b32_e32 v78, 41, v234
	v_fma_f32 v75, v64, v67, -v75
	v_cndmask_b32_e32 v74, v230, v74, vcc
	v_fma_f32 v79, v65, v70, -v79
	v_mul_f32_e32 v75, 0x3fb8aa3b, v75
	v_cmp_le_i32_e32 vcc, v78, v66
	v_mul_f32_e32 v79, 0x3fb8aa3b, v79
	v_exp_f32_e32 v73, v73
	v_cndmask_b32_e32 v75, v230, v75, vcc
	v_cmp_ge_i32_e32 vcc, v78, v66
	v_exp_f32_e32 v74, v74
	v_exp_f32_e32 v75, v75
	v_cndmask_b32_e32 v78, v230, v79, vcc
	v_exp_f32_e32 v78, v78
	v_add_f32_e32 v63, v73, v74
	v_mul_f32_e32 v36, v36, v63
	v_fma_f32 v73, v64, v67, -v76
	v_add_f32_e32 v63, v75, v78
	v_mul_f32_e32 v37, v37, v63
	v_or_b32_e32 v63, 42, v234
	v_fma_f32 v74, v65, v70, -v80
	v_mul_f32_e32 v73, 0x3fb8aa3b, v73
	v_cmp_le_i32_e32 vcc, v63, v66
	v_mul_f32_e32 v74, 0x3fb8aa3b, v74
	v_fma_f32 v75, v64, v67, -v77
	v_cndmask_b32_e32 v73, v230, v73, vcc
	v_cmp_ge_i32_e32 vcc, v63, v66
	v_mul_f32_e32 v75, 0x3fb8aa3b, v75
	v_fma_f32 v76, v65, v70, -v81
	v_cndmask_b32_e32 v63, v230, v74, vcc
	v_or_b32_e32 v74, 43, v234
	v_cmp_le_i32_e32 vcc, v74, v66
	v_or_b32_e32 v84, 48, v234
	v_exp_f32_e32 v73, v73
	v_cndmask_b32_e32 v75, v230, v75, vcc
	v_exp_f32_e32 v82, v75
	v_mul_f32_e32 v75, 0x3fb8aa3b, v76
	v_cmp_ge_i32_e32 vcc, v74, v66
	v_exp_f32_e32 v63, v63
	s_nop 0
	v_cndmask_b32_e32 v74, v230, v75, vcc
	v_exp_f32_e32 v83, v74
	v_lshlrev_b32_e32 v74, 2, v84
	v_add_u32_e32 v75, s44, v74
	v_add_u32_e32 v78, s45, v74
	ds_read_b128 v[74:77], v75
	ds_read_b128 v[78:81], v78
	v_add_f32_e32 v63, v73, v63
	v_cmp_le_i32_e32 vcc, v84, v66
	v_mul_f32_e32 v38, v38, v63
	s_waitcnt lgkmcnt(0)
; #define FENCE() do { asm volatile("" ::: "memory"); __builtin_amdgcn_sched_barrier(0); } while (0)
; __device__ __forceinline__ int crow(int r, int hi) { return (r & 3) + 8 * (r >> 2) + 4 * hi; }
; __device__ __forceinline__ int crow(int r, int hi) { return (r & 3) + 8 * (r >> 2) + 4 * hi; }
; template <int DK, int DV, bool MLSTM>
; __device__ __forceinline__ void out_unit2(LAS unsigned char* lds, LAS unsigned char* ldstab, const OutArgs a, const int wv) {
;     ...
;     int l2 = l; asm volatile("" : "+v"(l2));
; #pragma unroll
;     for (int kb = 0; kb < 4; ++kb) {
; #pragma unroll
;         for (int r = 0; r < 16; ++r) { const int s = 32 * kb + crow(r, hi);
;             const float xf = a_fl - akf[s], xb = a_bl - akb[s];
;             const float wf = __expf((s <= l2) ? xf : -1.0e30f), wb = __expf((s >= l2) ? xb : -1.0e30f);
;             p[kb][r] *= (wf * rf + wb * rbk); }
;         FENCE(); }
	v_fma_f32 v73, v64, v67, -v74
	v_fma_f32 v74, v65, v70, -v78
	v_mul_f32_e32 v73, 0x3fb8aa3b, v73
	v_cndmask_b32_e32 v73, v230, v73, vcc
	v_mul_f32_e32 v74, 0x3fb8aa3b, v74
	v_cmp_ge_i32_e32 vcc, v84, v66
	v_or_b32_e32 v78, 49, v234
	v_fma_f32 v75, v64, v67, -v75
	v_cndmask_b32_e32 v74, v230, v74, vcc
	v_fma_f32 v79, v65, v70, -v79
	v_mul_f32_e32 v75, 0x3fb8aa3b, v75
	v_cmp_le_i32_e32 vcc, v78, v66
	v_mul_f32_e32 v79, 0x3fb8aa3b, v79
	v_exp_f32_e32 v73, v73
	v_cndmask_b32_e32 v75, v230, v75, vcc
	v_cmp_ge_i32_e32 vcc, v78, v66
	v_exp_f32_e32 v74, v74
	v_exp_f32_e32 v75, v75
	v_cndmask_b32_e32 v78, v230, v79, vcc
	v_exp_f32_e32 v78, v78
	v_add_f32_e32 v63, v82, v83
	v_mul_f32_e32 v63, v39, v63
	v_add_f32_e32 v39, v73, v74
	v_mul_f32_e32 v39, v40, v39
	v_add_f32_e32 v40, v75, v78
	v_mul_f32_e32 v40, v41, v40
	v_or_b32_e32 v41, 50, v234
	v_fma_f32 v73, v64, v67, -v76
	v_fma_f32 v74, v65, v70, -v80
	v_mul_f32_e32 v73, 0x3fb8aa3b, v73
	v_cmp_le_i32_e32 vcc, v41, v66
	v_mul_f32_e32 v74, 0x3fb8aa3b, v74
	v_fma_f32 v75, v64, v67, -v77
	v_cndmask_b32_e32 v73, v230, v73, vcc
	v_cmp_ge_i32_e32 vcc, v41, v66
	v_mul_f32_e32 v75, 0x3fb8aa3b, v75
	v_fma_f32 v76, v65, v70, -v81
	v_cndmask_b32_e32 v41, v230, v74, vcc
	v_or_b32_e32 v74, 51, v234
	v_cmp_le_i32_e32 vcc, v74, v66
	v_or_b32_e32 v84, 56, v234
	v_exp_f32_e32 v73, v73
	v_cndmask_b32_e32 v75, v230, v75, vcc
	v_exp_f32_e32 v82, v75
	v_mul_f32_e32 v75, 0x3fb8aa3b, v76
	v_cmp_ge_i32_e32 vcc, v74, v66
	v_exp_f32_e32 v41, v41
	s_nop 0
	v_cndmask_b32_e32 v74, v230, v75, vcc
	v_exp_f32_e32 v83, v74
	v_lshlrev_b32_e32 v74, 2, v84
	v_add_u32_e32 v75, s44, v74
	v_add_u32_e32 v78, s45, v74
	ds_read_b128 v[74:77], v75
	ds_read_b128 v[78:81], v78
	v_add_f32_e32 v41, v73, v41
	v_cmp_le_i32_e32 vcc, v84, v66
	v_mul_f32_e32 v41, v42, v41
	s_waitcnt lgkmcnt(0)
	v_fma_f32 v73, v64, v67, -v74
	v_fma_f32 v74, v65, v70, -v78
	v_mul_f32_e32 v73, 0x3fb8aa3b, v73
	v_cndmask_b32_e32 v73, v230, v73, vcc
	v_mul_f32_e32 v74, 0x3fb8aa3b, v74
	v_cmp_ge_i32_e32 vcc, v84, v66
	v_or_b32_e32 v78, 57, v234
	v_fma_f32 v75, v64, v67, -v75
	v_cndmask_b32_e32 v74, v230, v74, vcc
	v_fma_f32 v79, v65, v70, -v79
	v_mul_f32_e32 v75, 0x3fb8aa3b, v75
	v_cmp_le_i32_e32 vcc, v78, v66
	v_mul_f32_e32 v79, 0x3fb8aa3b, v79
	v_exp_f32_e32 v73, v73
	v_cndmask_b32_e32 v75, v230, v75, vcc
	v_cmp_ge_i32_e32 vcc, v78, v66
	v_exp_f32_e32 v74, v74
	v_exp_f32_e32 v75, v75
	v_cndmask_b32_e32 v78, v230, v79, vcc
	v_exp_f32_e32 v78, v78
	v_add_f32_e32 v42, v82, v83
	v_mul_f32_e32 v42, v43, v42
	v_add_f32_e32 v43, v73, v74
	v_or_b32_e32 v73, 58, v234
	v_fma_f32 v74, v64, v67, -v76
	v_mul_f32_e32 v43, v44, v43
	v_add_f32_e32 v44, v75, v78
	v_fma_f32 v75, v65, v70, -v80
	v_mul_f32_e32 v74, 0x3fb8aa3b, v74
	v_cmp_le_i32_e32 vcc, v73, v66
	v_mul_f32_e32 v75, 0x3fb8aa3b, v75
	v_fma_f32 v76, v64, v67, -v77
	v_cndmask_b32_e32 v74, v230, v74, vcc
	v_cmp_ge_i32_e32 vcc, v73, v66
	v_fma_f32 v77, v65, v70, -v81
	v_mul_f32_e32 v76, 0x3fb8aa3b, v76
	v_cndmask_b32_e32 v73, v230, v75, vcc
	v_or_b32_e32 v75, 59, v234
	v_cmp_le_i32_e32 vcc, v75, v66
	v_mul_f32_e32 v77, 0x3fb8aa3b, v77
	v_exp_f32_e32 v74, v74
	v_cndmask_b32_e32 v76, v230, v76, vcc
	v_cmp_ge_i32_e32 vcc, v75, v66
	v_exp_f32_e32 v73, v73
	v_exp_f32_e32 v76, v76
	v_cndmask_b32_e32 v75, v230, v77, vcc
	v_exp_f32_e32 v75, v75
	v_mul_f32_e32 v44, v45, v44
	v_add_f32_e32 v45, v74, v73
	v_mul_f32_e32 v45, v46, v45
	v_add_f32_e32 v46, v76, v75
	v_mul_f32_e32 v46, v47, v46
	v_or_b32_e32 v47, 64, v234
	v_lshlrev_b32_e32 v73, 2, v47
	v_add_u32_e32 v74, s44, v73
	v_add_u32_e32 v73, s45, v73
	ds_read_b128 v[74:77], v74
	ds_read_b128 v[78:81], v73
	v_cmp_le_i32_e32 vcc, v47, v66
	v_or_b32_e32 v84, 0x48, v234
	s_waitcnt lgkmcnt(0)
	v_fma_f32 v73, v64, v67, -v74
	v_fma_f32 v74, v65, v70, -v78
	v_mul_f32_e32 v73, 0x3fb8aa3b, v73
	v_cndmask_b32_e32 v73, v230, v73, vcc
	v_mul_f32_e32 v74, 0x3fb8aa3b, v74
	v_cmp_ge_i32_e32 vcc, v47, v66
	v_fma_f32 v75, v64, v67, -v75
	v_fma_f32 v78, v65, v70, -v79
	v_cndmask_b32_e32 v47, v230, v74, vcc
	v_or_b32_e32 v74, 0x41, v234
	v_mul_f32_e32 v75, 0x3fb8aa3b, v75
	v_cmp_le_i32_e32 vcc, v74, v66
	v_mul_f32_e32 v78, 0x3fb8aa3b, v78
	v_exp_f32_e32 v73, v73
	v_cndmask_b32_e32 v75, v230, v75, vcc
	v_cmp_ge_i32_e32 vcc, v74, v66
	v_exp_f32_e32 v47, v47
	v_exp_f32_e32 v75, v75
	v_cndmask_b32_e32 v74, v230, v78, vcc
	v_exp_f32_e32 v74, v74
	v_add_f32_e32 v47, v73, v47
	v_mul_f32_e32 v16, v16, v47
	v_fma_f32 v73, v64, v67, -v76
	v_add_f32_e32 v47, v75, v74
	v_mul_f32_e32 v17, v17, v47
	v_or_b32_e32 v47, 0x42, v234
	v_fma_f32 v74, v65, v70, -v80
	v_mul_f32_e32 v73, 0x3fb8aa3b, v73
	v_cmp_le_i32_e32 vcc, v47, v66
	v_mul_f32_e32 v74, 0x3fb8aa3b, v74
	v_fma_f32 v75, v64, v67, -v77
	v_cndmask_b32_e32 v73, v230, v73, vcc
	v_cmp_ge_i32_e32 vcc, v47, v66
	v_mul_f32_e32 v75, 0x3fb8aa3b, v75
	v_fma_f32 v76, v65, v70, -v81
	v_cndmask_b32_e32 v47, v230, v74, vcc
	v_or_b32_e32 v74, 0x43, v234
	v_cmp_le_i32_e32 vcc, v74, v66
	v_exp_f32_e32 v73, v73
	v_exp_f32_e32 v47, v47
	v_cndmask_b32_e32 v75, v230, v75, vcc
	v_exp_f32_e32 v82, v75
	v_mul_f32_e32 v75, 0x3fb8aa3b, v76
	v_cmp_ge_i32_e32 vcc, v74, v66
	v_add_f32_e32 v47, v73, v47
	v_mul_f32_e32 v47, v18, v47
	v_cndmask_b32_e32 v74, v230, v75, vcc
	v_exp_f32_e32 v83, v74
	v_lshlrev_b32_e32 v74, 2, v84
	v_add_u32_e32 v75, s44, v74
	v_add_u32_e32 v78, s45, v74
	ds_read_b128 v[74:77], v75
	ds_read_b128 v[78:81], v78
	v_cmp_le_i32_e32 vcc, v84, v66
	v_add_f32_e32 v18, v82, v83
	s_waitcnt lgkmcnt(0)
; #define FENCE() do { asm volatile("" ::: "memory"); __builtin_amdgcn_sched_barrier(0); } while (0)
; __device__ __forceinline__ int crow(int r, int hi) { return (r & 3) + 8 * (r >> 2) + 4 * hi; }
; __device__ __forceinline__ int crow(int r, int hi) { return (r & 3) + 8 * (r >> 2) + 4 * hi; }
; template <int DK, int DV, bool MLSTM>
; __device__ __forceinline__ void out_unit2(LAS unsigned char* lds, LAS unsigned char* ldstab, const OutArgs a, const int wv) {
;     ...
;     int l2 = l; asm volatile("" : "+v"(l2));
; #pragma unroll
;     for (int kb = 0; kb < 4; ++kb) {
; #pragma unroll
;         for (int r = 0; r < 16; ++r) { const int s = 32 * kb + crow(r, hi);
;             const float xf = a_fl - akf[s], xb = a_bl - akb[s];
;             const float wf = __expf((s <= l2) ? xf : -1.0e30f), wb = __expf((s >= l2) ? xb : -1.0e30f);
;             p[kb][r] *= (wf * rf + wb * rbk); }
;         FENCE(); }
	v_fma_f32 v73, v64, v67, -v74
	v_fma_f32 v74, v65, v70, -v78
	v_mul_f32_e32 v73, 0x3fb8aa3b, v73
	v_cndmask_b32_e32 v73, v230, v73, vcc
	v_mul_f32_e32 v74, 0x3fb8aa3b, v74
	v_cmp_ge_i32_e32 vcc, v84, v66
	v_or_b32_e32 v78, 0x49, v234
	v_fma_f32 v75, v64, v67, -v75
	v_cndmask_b32_e32 v74, v230, v74, vcc
	v_fma_f32 v79, v65, v70, -v79
	v_mul_f32_e32 v75, 0x3fb8aa3b, v75
	v_cmp_le_i32_e32 vcc, v78, v66
	v_mul_f32_e32 v79, 0x3fb8aa3b, v79
	v_exp_f32_e32 v73, v73
	v_cndmask_b32_e32 v75, v230, v75, vcc
	v_cmp_ge_i32_e32 vcc, v78, v66
	v_exp_f32_e32 v74, v74
	v_exp_f32_e32 v75, v75
	v_cndmask_b32_e32 v78, v230, v79, vcc
	v_exp_f32_e32 v78, v78
	v_mul_f32_e32 v79, v19, v18
	v_add_f32_e32 v18, v73, v74
	v_mul_f32_e32 v73, v20, v18
	v_add_f32_e32 v18, v75, v78
	v_mul_f32_e32 v78, v21, v18
	v_or_b32_e32 v18, 0x4a, v234
	v_fma_f32 v19, v64, v67, -v76
	v_mul_f32_e32 v19, 0x3fb8aa3b, v19
	v_cmp_le_i32_e32 vcc, v18, v66
	v_fma_f32 v20, v65, v70, -v80
	v_or_b32_e32 v84, 0x50, v234
	v_cndmask_b32_e32 v19, v230, v19, vcc
	v_exp_f32_e32 v80, v19
	v_mul_f32_e32 v19, 0x3fb8aa3b, v20
	v_cmp_ge_i32_e32 vcc, v18, v66
	v_fma_f32 v20, v65, v70, -v81
	s_nop 0
	v_cndmask_b32_e32 v18, v230, v19, vcc
	v_exp_f32_e32 v82, v18
	v_or_b32_e32 v18, 0x4b, v234
	v_fma_f32 v19, v64, v67, -v77
	v_mul_f32_e32 v19, 0x3fb8aa3b, v19
	v_cmp_le_i32_e32 vcc, v18, v66
	v_add_f32_e32 v80, v80, v82
	v_mul_f32_e32 v80, v22, v80
	v_cndmask_b32_e32 v19, v230, v19, vcc
	v_exp_f32_e32 v81, v19
	v_mul_f32_e32 v19, 0x3fb8aa3b, v20
	v_cmp_ge_i32_e32 vcc, v18, v66
	s_nop 1
	v_cndmask_b32_e32 v18, v230, v19, vcc
	v_exp_f32_e32 v83, v18
	v_lshlrev_b32_e32 v18, 2, v84
	v_add_u32_e32 v19, s44, v18
	v_add_u32_e32 v74, s45, v18
	ds_read_b128 v[18:21], v19
	ds_read_b128 v[74:77], v74
	v_cmp_le_i32_e32 vcc, v84, v66
	v_add_f32_e32 v22, v81, v83
	v_or_b32_e32 v81, 0x51, v234
	s_waitcnt lgkmcnt(0)
	v_fma_f32 v18, v64, v67, -v18
	v_fma_f32 v74, v65, v70, -v74
	v_mul_f32_e32 v18, 0x3fb8aa3b, v18
	v_cndmask_b32_e32 v18, v230, v18, vcc
	v_mul_f32_e32 v74, 0x3fb8aa3b, v74
	v_cmp_ge_i32_e32 vcc, v84, v66
	v_fma_f32 v19, v64, v67, -v19
	v_fma_f32 v75, v65, v70, -v75
	v_cndmask_b32_e32 v74, v230, v74, vcc
	v_mul_f32_e32 v19, 0x3fb8aa3b, v19
	v_cmp_le_i32_e32 vcc, v81, v66
	v_mul_f32_e32 v75, 0x3fb8aa3b, v75
	v_exp_f32_e32 v18, v18
	v_cndmask_b32_e32 v19, v230, v19, vcc
	v_cmp_ge_i32_e32 vcc, v81, v66
	v_exp_f32_e32 v74, v74
	v_exp_f32_e32 v19, v19
	v_cndmask_b32_e32 v75, v230, v75, vcc
	v_exp_f32_e32 v75, v75
	v_add_f32_e32 v18, v18, v74
	v_mul_f32_e32 v74, v24, v18
	v_or_b32_e32 v84, 0x58, v234
	v_add_f32_e32 v18, v19, v75
	v_mul_f32_e32 v75, v25, v18
	v_or_b32_e32 v18, 0x52, v234
	v_fma_f32 v19, v64, v67, -v20
	v_mul_f32_e32 v19, 0x3fb8aa3b, v19
	v_cmp_le_i32_e32 vcc, v18, v66
	v_fma_f32 v20, v65, v70, -v76
	v_mul_f32_e32 v81, v23, v22
	v_cndmask_b32_e32 v19, v230, v19, vcc
	v_exp_f32_e32 v76, v19
	v_mul_f32_e32 v19, 0x3fb8aa3b, v20
	v_cmp_ge_i32_e32 vcc, v18, v66
	v_fma_f32 v20, v65, v70, -v77
	s_nop 0
	v_cndmask_b32_e32 v18, v230, v19, vcc
	v_exp_f32_e32 v82, v18
	v_or_b32_e32 v18, 0x53, v234
	v_fma_f32 v19, v64, v67, -v21
	v_mul_f32_e32 v19, 0x3fb8aa3b, v19
	v_cmp_le_i32_e32 vcc, v18, v66
	v_add_f32_e32 v76, v76, v82
	v_mul_f32_e32 v26, v26, v76
	v_cndmask_b32_e32 v19, v230, v19, vcc
	v_exp_f32_e32 v77, v19
	v_mul_f32_e32 v19, 0x3fb8aa3b, v20
	v_cmp_ge_i32_e32 vcc, v18, v66
	s_nop 1
	v_cndmask_b32_e32 v18, v230, v19, vcc
	v_exp_f32_e32 v83, v18
	v_lshlrev_b32_e32 v18, 2, v84
	v_add_u32_e32 v19, s44, v18
	v_add_u32_e32 v22, s45, v18
	ds_read_b128 v[18:21], v19
	ds_read_b128 v[22:25], v22
	v_cmp_le_i32_e32 vcc, v84, v66
	v_add_f32_e32 v76, v77, v83
	v_or_b32_e32 v77, 0x59, v234
	s_waitcnt lgkmcnt(0)
	v_fma_f32 v18, v64, v67, -v18
	v_fma_f32 v22, v65, v70, -v22
	v_mul_f32_e32 v18, 0x3fb8aa3b, v18
	v_cndmask_b32_e32 v18, v230, v18, vcc
	v_mul_f32_e32 v22, 0x3fb8aa3b, v22
	v_cmp_ge_i32_e32 vcc, v84, v66
	v_fma_f32 v19, v64, v67, -v19
	v_fma_f32 v23, v65, v70, -v23
	v_cndmask_b32_e32 v22, v230, v22, vcc
	v_mul_f32_e32 v19, 0x3fb8aa3b, v19
	v_cmp_le_i32_e32 vcc, v77, v66
	v_mul_f32_e32 v23, 0x3fb8aa3b, v23
	v_exp_f32_e32 v18, v18
	v_cndmask_b32_e32 v19, v230, v19, vcc
	v_cmp_ge_i32_e32 vcc, v77, v66
	v_exp_f32_e32 v22, v22
	v_exp_f32_e32 v19, v19
	v_cndmask_b32_e32 v23, v230, v23, vcc
	v_exp_f32_e32 v23, v23
	v_add_f32_e32 v18, v18, v22
	v_mul_f32_e32 v28, v28, v18
	v_fma_f32 v20, v64, v67, -v20
	v_add_f32_e32 v18, v19, v23
	v_or_b32_e32 v19, 0x5a, v234
	v_fma_f32 v22, v65, v70, -v24
	v_mul_f32_e32 v20, 0x3fb8aa3b, v20
	v_cmp_le_i32_e32 vcc, v19, v66
	v_mul_f32_e32 v22, 0x3fb8aa3b, v22
	v_fma_f32 v21, v64, v67, -v21
	v_cndmask_b32_e32 v20, v230, v20, vcc
	v_cmp_ge_i32_e32 vcc, v19, v66
	v_fma_f32 v23, v65, v70, -v25
	v_mul_f32_e32 v21, 0x3fb8aa3b, v21
	v_cndmask_b32_e32 v19, v230, v22, vcc
	v_or_b32_e32 v22, 0x5b, v234
	v_cmp_le_i32_e32 vcc, v22, v66
	v_mul_f32_e32 v23, 0x3fb8aa3b, v23
	v_exp_f32_e32 v20, v20
	v_cndmask_b32_e32 v21, v230, v21, vcc
	v_cmp_ge_i32_e32 vcc, v22, v66
	v_exp_f32_e32 v19, v19
	v_exp_f32_e32 v21, v21
	v_cndmask_b32_e32 v22, v230, v23, vcc
	v_exp_f32_e32 v22, v22
	v_mul_f32_e32 v29, v29, v18
	v_add_f32_e32 v18, v20, v19
	v_mul_f32_e32 v30, v30, v18
	v_add_f32_e32 v18, v21, v22
	v_mul_f32_e32 v27, v27, v76
	v_mul_f32_e32 v31, v31, v18
	v_or_b32_e32 v76, 0x60, v234
	v_lshlrev_b32_e32 v18, 2, v76
	v_add_u32_e32 v19, s44, v18
	v_add_u32_e32 v22, s45, v18
	ds_read_b128 v[18:21], v19
	ds_read_b128 v[22:25], v22
	v_cmp_le_i32_e32 vcc, v76, v66
	v_or_b32_e32 v84, 0x68, v234
	s_waitcnt lgkmcnt(0)
; #define FENCE() do { asm volatile("" ::: "memory"); __builtin_amdgcn_sched_barrier(0); } while (0)
; __device__ __forceinline__ int crow(int r, int hi) { return (r & 3) + 8 * (r >> 2) + 4 * hi; }
; __device__ __forceinline__ int crow(int r, int hi) { return (r & 3) + 8 * (r >> 2) + 4 * hi; }
; template <int DK, int DV, bool MLSTM>
; __device__ __forceinline__ void out_unit2(LAS unsigned char* lds, LAS unsigned char* ldstab, const OutArgs a, const int wv) {
;     ...
;     int l2 = l; asm volatile("" : "+v"(l2));
; #pragma unroll
;     for (int kb = 0; kb < 4; ++kb) {
; #pragma unroll
;         for (int r = 0; r < 16; ++r) { const int s = 32 * kb + crow(r, hi);
;             const float xf = a_fl - akf[s], xb = a_bl - akb[s];
;             const float wf = __expf((s <= l2) ? xf : -1.0e30f), wb = __expf((s >= l2) ? xb : -1.0e30f);
;             p[kb][r] *= (wf * rf + wb * rbk); }
;         FENCE(); }
	v_fma_f32 v18, v64, v67, -v18
	v_fma_f32 v22, v65, v70, -v22
	v_mul_f32_e32 v18, 0x3fb8aa3b, v18
	v_cndmask_b32_e32 v18, v230, v18, vcc
	v_mul_f32_e32 v22, 0x3fb8aa3b, v22
	v_cmp_ge_i32_e32 vcc, v76, v66
	v_or_b32_e32 v76, 0x61, v234
	v_fma_f32 v19, v64, v67, -v19
	v_cndmask_b32_e32 v22, v230, v22, vcc
	v_fma_f32 v23, v65, v70, -v23
	v_mul_f32_e32 v19, 0x3fb8aa3b, v19
	v_cmp_le_i32_e32 vcc, v76, v66
	v_mul_f32_e32 v23, 0x3fb8aa3b, v23
	v_exp_f32_e32 v18, v18
	v_cndmask_b32_e32 v19, v230, v19, vcc
	v_cmp_ge_i32_e32 vcc, v76, v66
	v_exp_f32_e32 v22, v22
	v_exp_f32_e32 v19, v19
	v_cndmask_b32_e32 v23, v230, v23, vcc
	v_exp_f32_e32 v23, v23
	v_add_f32_e32 v18, v18, v22
	v_mul_f32_e32 v76, v0, v18
	v_fma_f32 v18, v65, v70, -v24
	v_add_f32_e32 v0, v19, v23
	v_mul_f32_e32 v77, v1, v0
	v_or_b32_e32 v0, 0x62, v234
	v_fma_f32 v1, v64, v67, -v20
	v_mul_f32_e32 v1, 0x3fb8aa3b, v1
	v_cmp_le_i32_e32 vcc, v0, v66
	v_mul_f32_e32 v18, 0x3fb8aa3b, v18
	v_fma_f32 v19, v64, v67, -v21
	v_cndmask_b32_e32 v1, v230, v1, vcc
	v_cmp_ge_i32_e32 vcc, v0, v66
	v_mul_f32_e32 v19, 0x3fb8aa3b, v19
	v_fma_f32 v20, v65, v70, -v25
	v_cndmask_b32_e32 v0, v230, v18, vcc
	v_or_b32_e32 v18, 0x63, v234
	v_cmp_le_i32_e32 vcc, v18, v66
	v_exp_f32_e32 v1, v1
	v_exp_f32_e32 v0, v0
	v_cndmask_b32_e32 v19, v230, v19, vcc
	v_exp_f32_e32 v82, v19
	v_mul_f32_e32 v19, 0x3fb8aa3b, v20
	v_cmp_ge_i32_e32 vcc, v18, v66
	v_add_f32_e32 v0, v1, v0
	v_mul_f32_e32 v85, v2, v0
	v_cndmask_b32_e32 v18, v230, v19, vcc
	v_exp_f32_e32 v83, v18
	v_lshlrev_b32_e32 v18, 2, v84
	v_add_u32_e32 v19, s44, v18
	v_add_u32_e32 v22, s45, v18
	ds_read_b128 v[18:21], v19
	ds_read_b128 v[22:25], v22
	v_cmp_le_i32_e32 vcc, v84, v66
	v_add_f32_e32 v0, v82, v83
	v_or_b32_e32 v83, 0x70, v234
	s_waitcnt lgkmcnt(0)
	v_fma_f32 v1, v64, v67, -v18
	v_fma_f32 v2, v65, v70, -v22
	v_mul_f32_e32 v1, 0x3fb8aa3b, v1
	v_cndmask_b32_e32 v1, v230, v1, vcc
	v_mul_f32_e32 v2, 0x3fb8aa3b, v2
	v_cmp_ge_i32_e32 vcc, v84, v66
	v_or_b32_e32 v18, 0x69, v234
	v_fma_f32 v19, v64, v67, -v19
	v_cndmask_b32_e32 v2, v230, v2, vcc
	v_fma_f32 v22, v65, v70, -v23
	v_mul_f32_e32 v19, 0x3fb8aa3b, v19
	v_cmp_le_i32_e32 vcc, v18, v66
	v_mul_f32_e32 v22, 0x3fb8aa3b, v22
	v_exp_f32_e32 v1, v1
	v_cndmask_b32_e32 v19, v230, v19, vcc
	v_cmp_ge_i32_e32 vcc, v18, v66
	v_exp_f32_e32 v2, v2
	v_exp_f32_e32 v19, v19
	v_cndmask_b32_e32 v18, v230, v22, vcc
	v_exp_f32_e32 v18, v18
	v_mul_f32_e32 v22, v3, v0
	v_add_f32_e32 v0, v1, v2
	v_mul_f32_e32 v23, v4, v0
	v_add_f32_e32 v0, v19, v18
	v_mul_f32_e32 v82, v5, v0
	v_or_b32_e32 v0, 0x6a, v234
	v_fma_f32 v1, v64, v67, -v20
	v_mul_f32_e32 v1, 0x3fb8aa3b, v1
	v_cmp_le_i32_e32 vcc, v0, v66
	v_fma_f32 v2, v65, v70, -v24
	s_nop 0
	v_cndmask_b32_e32 v1, v230, v1, vcc
	v_exp_f32_e32 v4, v1
	v_mul_f32_e32 v1, 0x3fb8aa3b, v2
	v_cmp_ge_i32_e32 vcc, v0, v66
	v_fma_f32 v2, v65, v70, -v25
	s_nop 0
	v_cndmask_b32_e32 v0, v230, v1, vcc
	v_exp_f32_e32 v5, v0
	v_or_b32_e32 v0, 0x6b, v234
	v_fma_f32 v1, v64, v67, -v21
	v_mul_f32_e32 v1, 0x3fb8aa3b, v1
	v_cmp_le_i32_e32 vcc, v0, v66
	v_add_f32_e32 v4, v4, v5
	v_mul_f32_e32 v84, v6, v4
	v_cndmask_b32_e32 v1, v230, v1, vcc
	v_exp_f32_e32 v24, v1
	v_mul_f32_e32 v1, 0x3fb8aa3b, v2
	v_cmp_ge_i32_e32 vcc, v0, v66
	v_or_b32_e32 v6, 0x71, v234
	s_nop 0
	v_cndmask_b32_e32 v0, v230, v1, vcc
	v_exp_f32_e32 v25, v0
	v_lshlrev_b32_e32 v0, 2, v83
	v_add_u32_e32 v1, s44, v0
	v_add_u32_e32 v18, s45, v0
	ds_read_b128 v[0:3], v1
	ds_read_b128 v[18:21], v18
	v_cmp_le_i32_e32 vcc, v83, v66
	v_add_f32_e32 v4, v24, v25
	v_or_b32_e32 v25, 0x78, v234
	s_waitcnt lgkmcnt(0)
	v_fma_f32 v0, v64, v67, -v0
	v_fma_f32 v5, v65, v70, -v18
	v_mul_f32_e32 v0, 0x3fb8aa3b, v0
	v_cndmask_b32_e32 v0, v230, v0, vcc
	v_mul_f32_e32 v5, 0x3fb8aa3b, v5
	v_cmp_ge_i32_e32 vcc, v83, v66
	v_fma_f32 v1, v64, v67, -v1
	v_fma_f32 v18, v65, v70, -v19
	v_cndmask_b32_e32 v5, v230, v5, vcc
	v_mul_f32_e32 v1, 0x3fb8aa3b, v1
	v_cmp_le_i32_e32 vcc, v6, v66
	v_mul_f32_e32 v18, 0x3fb8aa3b, v18
	v_exp_f32_e32 v0, v0
	v_cndmask_b32_e32 v1, v230, v1, vcc
	v_cmp_ge_i32_e32 vcc, v6, v66
	v_exp_f32_e32 v5, v5
	v_exp_f32_e32 v1, v1
	v_cndmask_b32_e32 v6, v230, v18, vcc
	v_exp_f32_e32 v6, v6
	v_add_f32_e32 v0, v0, v5
	v_mul_f32_e32 v8, v8, v0
	v_mul_f32_e32 v18, v7, v4
	v_add_f32_e32 v0, v1, v6
	v_mul_f32_e32 v9, v9, v0
	v_or_b32_e32 v0, 0x72, v234
	v_fma_f32 v1, v64, v67, -v2
	v_mul_f32_e32 v1, 0x3fb8aa3b, v1
	v_cmp_le_i32_e32 vcc, v0, v66
	v_fma_f32 v2, v65, v70, -v20
	s_nop 0
	v_cndmask_b32_e32 v1, v230, v1, vcc
	v_exp_f32_e32 v19, v1
	v_mul_f32_e32 v1, 0x3fb8aa3b, v2
	v_cmp_ge_i32_e32 vcc, v0, v66
	v_fma_f32 v2, v65, v70, -v21
	s_nop 0
	v_cndmask_b32_e32 v0, v230, v1, vcc
	v_exp_f32_e32 v20, v0
	v_or_b32_e32 v0, 0x73, v234
	v_fma_f32 v1, v64, v67, -v3
	v_mul_f32_e32 v1, 0x3fb8aa3b, v1
	v_cmp_le_i32_e32 vcc, v0, v66
	v_add_f32_e32 v19, v19, v20
	v_or_b32_e32 v20, 0x79, v234
	v_cndmask_b32_e32 v1, v230, v1, vcc
	v_exp_f32_e32 v21, v1
	v_mul_f32_e32 v1, 0x3fb8aa3b, v2
	v_cmp_ge_i32_e32 vcc, v0, v66
	v_mul_f32_e32 v10, v10, v19
	s_nop 0
	v_cndmask_b32_e32 v0, v230, v1, vcc
	v_exp_f32_e32 v24, v0
	v_lshlrev_b32_e32 v0, 2, v25
	v_add_u32_e32 v1, s44, v0
	v_add_u32_e32 v4, s45, v0
	ds_read_b128 v[0:3], v1
	ds_read_b128 v[4:7], v4
	v_cmp_le_i32_e32 vcc, v25, v66
	v_add_f32_e32 v19, v21, v24
	s_waitcnt lgkmcnt(0)
; #define VM_WAIT() asm volatile("s_waitcnt vmcnt(0)" ::: "memory")
; #define FENCE() do { asm volatile("" ::: "memory"); __builtin_amdgcn_sched_barrier(0); } while (0)
; __device__ __forceinline__ int crow(int r, int hi) { return (r & 3) + 8 * (r >> 2) + 4 * hi; }
; __device__ __forceinline__ int crow(int r, int hi) { return (r & 3) + 8 * (r >> 2) + 4 * hi; }
; template <int DK, int DV, bool MLSTM>
; __device__ __forceinline__ void out_unit2(LAS unsigned char* lds, LAS unsigned char* ldstab, const OutArgs a, const int wv) {
;     ...
; #pragma unroll
;     for (int kb = 0; kb < 4; ++kb) {
; #pragma unroll
;         for (int r = 0; r < 16; ++r) { const int s = 32 * kb + crow(r, hi);
;             const float xf = a_fl - akf[s], xb = a_bl - akb[s];
;             const float wf = __expf((s <= l2) ? xf : -1.0e30f), wb = __expf((s >= l2) ? xb : -1.0e30f);
;             p[kb][r] *= (wf * rf + wb * rbk); }
;         FENCE(); }
;     const float qsf = __expf(a_fl) * rf, qsb = __expf(a_bl) * rbk;
;     bf16x8 pa[8];
;     ...
; #pragma unroll
;     for (int kb = 0; kb < 4; ++kb) { LA_PK4(p[kb], 0, pa[2 * kb]); LA_PK4(p[kb], 8, pa[2 * kb + 1]); }
;     ...
;     f32x16 o[NB];
; #pragma unroll
;     for (int nb = 0; nb < NB; ++nb) o[nb] = (f32x16){};
;     ...
; #pragma unroll
;     for (int pc = 0; pc < 4; ++pc) {
;         VM_WAIT(); __syncthreads();
;         OUT_DMA(pc + 1);
;         const bf16x8 af0 = pa[2 * pc], af1 = pa[2 * pc + 1];
;         OUT_MMA(pc & 1);
	v_fma_f32 v0, v64, v67, -v0
	v_fma_f32 v4, v65, v70, -v4
	v_mul_f32_e32 v0, 0x3fb8aa3b, v0
	v_cndmask_b32_e32 v0, v230, v0, vcc
	v_mul_f32_e32 v4, 0x3fb8aa3b, v4
	v_cmp_ge_i32_e32 vcc, v25, v66
	v_fma_f32 v1, v64, v67, -v1
	v_fma_f32 v5, v65, v70, -v5
	v_cndmask_b32_e32 v4, v230, v4, vcc
	v_mul_f32_e32 v1, 0x3fb8aa3b, v1
	v_cmp_le_i32_e32 vcc, v20, v66
	v_mul_f32_e32 v5, 0x3fb8aa3b, v5
	v_exp_f32_e32 v0, v0
	v_cndmask_b32_e32 v1, v230, v1, vcc
	v_cmp_ge_i32_e32 vcc, v20, v66
	v_exp_f32_e32 v4, v4
	v_exp_f32_e32 v1, v1
	v_cndmask_b32_e32 v5, v230, v5, vcc
	v_exp_f32_e32 v5, v5
	v_add_f32_e32 v0, v0, v4
	v_or_b32_e32 v4, 0x7a, v234
	v_fma_f32 v2, v64, v67, -v2
	v_add_f32_e32 v1, v1, v5
	v_fma_f32 v5, v65, v70, -v6
	v_mul_f32_e32 v2, 0x3fb8aa3b, v2
	v_cmp_le_i32_e32 vcc, v4, v66
	v_mul_f32_e32 v5, 0x3fb8aa3b, v5
	v_fma_f32 v3, v64, v67, -v3
	v_cndmask_b32_e32 v2, v230, v2, vcc
	v_cmp_ge_i32_e32 vcc, v4, v66
	v_fma_f32 v6, v65, v70, -v7
	v_mul_f32_e32 v3, 0x3fb8aa3b, v3
	v_cndmask_b32_e32 v4, v230, v5, vcc
	v_or_b32_e32 v5, 0x7b, v234
	v_cmp_le_i32_e32 vcc, v5, v66
	v_mul_f32_e32 v6, 0x3fb8aa3b, v6
	v_exp_f32_e32 v2, v2
	v_cndmask_b32_e32 v3, v230, v3, vcc
	v_cmp_ge_i32_e32 vcc, v5, v66
	v_exp_f32_e32 v4, v4
	v_exp_f32_e32 v3, v3
	v_cndmask_b32_e32 v5, v230, v6, vcc
	v_exp_f32_e32 v5, v5
	v_add_f32_e32 v2, v2, v4
	v_mul_f32_e32 v11, v11, v19
	v_mul_f32_e32 v0, v12, v0
	v_add_f32_e32 v3, v3, v5
	v_mul_f32_e32 v1, v13, v1
	v_mul_f32_e32 v2, v14, v2
	v_mul_f32_e32 v3, v15, v3
	s_add_u32 s44, s37, 0x61000
	s_addc_u32 s45, s16, 0
	v_cvt_pk_bf16_f32 v64, v48, v49
	v_cvt_pk_bf16_f32 v65, v50, v51
	v_cvt_pk_bf16_f32 v66, v52, v53
	v_cvt_pk_bf16_f32 v67, v54, v72
	v_cvt_pk_bf16_f32 v152, v55, v56
	v_cvt_pk_bf16_f32 v153, v57, v58
	v_cvt_pk_bf16_f32 v154, v59, v60
	v_cvt_pk_bf16_f32 v155, v61, v62
	v_cvt_pk_bf16_f32 v148, v32, v33
	v_cvt_pk_bf16_f32 v149, v34, v35
	v_cvt_pk_bf16_f32 v150, v36, v37
	v_cvt_pk_bf16_f32 v151, v38, v63
	v_cvt_pk_bf16_f32 v144, v39, v40
	v_cvt_pk_bf16_f32 v145, v41, v42
	v_cvt_pk_bf16_f32 v146, v43, v44
	v_cvt_pk_bf16_f32 v147, v45, v46
	v_cvt_pk_bf16_f32 v140, v16, v17
	v_cvt_pk_bf16_f32 v141, v47, v79
	v_cvt_pk_bf16_f32 v142, v73, v78
	v_cvt_pk_bf16_f32 v143, v80, v81
	v_cvt_pk_bf16_f32 v136, v74, v75
	v_cvt_pk_bf16_f32 v137, v26, v27
	v_cvt_pk_bf16_f32 v138, v28, v29
	v_cvt_pk_bf16_f32 v139, v30, v31
	v_cvt_pk_bf16_f32 v132, v76, v77
	v_cvt_pk_bf16_f32 v133, v85, v22
	v_cvt_pk_bf16_f32 v134, v23, v82
	v_cvt_pk_bf16_f32 v135, v84, v18
	v_cvt_pk_bf16_f32 v128, v8, v9
	v_cvt_pk_bf16_f32 v129, v10, v11
	v_cvt_pk_bf16_f32 v130, v0, v1
	v_mov_b64_e32 v[0:1], s[44:45]
	v_cvt_pk_bf16_f32 v131, v2, v3
	v_mad_i64_i32 v[2:3], s[44:45], v182, s57, v[0:1]
	v_lshl_add_u64 v[2:3], v[2:3], 0, v[184:185]
	v_lshl_add_u64 v[2:3], v[2:3], 0, v[160:161]
	s_add_i32 s94, s6, s80
	v_lshl_add_u64 v[2:3], v[2:3], 0, v[156:157]
	s_mov_b32 m0, s94
	s_waitcnt vmcnt(0)
	s_waitcnt vmcnt(0)
	s_barrier
	v_mad_i64_i32 v[2:3], s[44:45], v186, s57, v[0:1]
	v_lshl_add_u64 v[2:3], v[2:3], 0, v[188:189]
	v_lshl_add_u64 v[2:3], v[2:3], 0, v[190:191]
	s_add_i32 s44, s7, s80
	v_lshl_add_u64 v[2:3], v[2:3], 0, v[192:193]
	s_mov_b32 m0, s44
	s_add_i32 s45, s36, s80
	v_mad_i64_i32 v[2:3], s[96:97], v194, s57, v[0:1]
	v_lshl_add_u64 v[2:3], v[2:3], 0, v[196:197]
	v_mad_i64_i32 v[0:1], s[96:97], v202, s57, v[0:1]
	v_lshl_add_u64 v[2:3], v[2:3], 0, v[198:199]
	v_lshl_add_u64 v[0:1], v[0:1], 0, v[204:205]
	v_lshl_add_u64 v[2:3], v[2:3], 0, v[200:201]
	s_mov_b32 m0, s45
	v_lshl_add_u64 v[0:1], v[0:1], 0, v[206:207]
	s_add_i32 s93, s38, s80
	v_lshl_add_u64 v[0:1], v[0:1], 0, v[208:209]
	s_mov_b32 m0, s93
	v_lshl_add_u64 v[2:3], s[4:5], 0, v[188:189]
	v_mul_f32_e32 v0, 0x3fb8aa3b, v69
	v_exp_f32_e32 v179, v0
	v_lshl_add_u64 v[0:1], s[4:5], 0, v[184:185]
	v_lshl_add_u64 v[0:1], v[0:1], 0, v[160:161]
	v_lshl_add_u64 v[0:1], v[0:1], 0, v[156:157]
	v_lshl_add_u64 v[2:3], v[2:3], 0, v[190:191]
	v_lshl_add_u64 v[4:5], s[4:5], 0, v[196:197]
	v_lshlrev_b64 v[210:211], 10, v[182:183]
	v_lshl_add_u64 v[2:3], v[2:3], 0, v[192:193]
	v_lshl_add_u64 v[4:5], v[4:5], 0, v[198:199]
	v_lshl_add_u64 v[6:7], s[4:5], 0, v[204:205]
	v_lshl_add_u64 v[222:223], v[0:1], 0, v[210:211]
	v_lshlrev_b64 v[212:213], 10, v[186:187]
	v_lshlrev_b64 v[214:215], 10, v[194:195]
	v_bitop3_b32 v183, v68, 16, s39 bitop3:0x36
	v_add_u32_e32 v195, s68, v175
	ds_read_b64_tr_b16 v[0:1], v195 offset:0
	v_lshl_add_u64 v[4:5], v[4:5], 0, v[200:201]
	v_lshl_add_u64 v[6:7], v[6:7], 0, v[206:207]
	v_lshl_add_u64 v[224:225], v[2:3], 0, v[212:213]
	v_lshlrev_b64 v[216:217], 10, v[202:203]
	v_add_u32_e32 v203, s81, v183
	ds_read_b64_tr_b16 v[2:3], v203 offset:0
	v_lshl_add_u64 v[6:7], v[6:7], 0, v[208:209]
	v_lshl_add_u64 v[218:219], v[4:5], 0, v[214:215]
	ds_read_b64_tr_b16 v[4:5], v195 offset:0x200
	v_lshl_add_u64 v[220:221], v[6:7], 0, v[216:217]
	ds_read_b64_tr_b16 v[6:7], v203 offset:0x200
	ds_read_b64_tr_b16 v[32:33], v195 offset:0x400
	ds_read_b64_tr_b16 v[34:35], v203 offset:0x400
	ds_read_b64_tr_b16 v[48:49], v195 offset:0x600
	ds_read_b64_tr_b16 v[50:51], v203 offset:0x600
	s_waitcnt lgkmcnt(0)
; #define VM_WAIT() asm volatile("s_waitcnt vmcnt(0)" ::: "memory")
; template <int DK, int DV, bool MLSTM>
; __device__ __forceinline__ void out_unit2(LAS unsigned char* lds, LAS unsigned char* ldstab, const OutArgs a, const int wv) {
;     ...
; #pragma unroll
;     for (int kb = 0; kb < 4; ++kb) { LA_PK4(p[kb], 0, pa[2 * kb]); LA_PK4(p[kb], 8, pa[2 * kb + 1]); }
;     ...
;     f32x16 o[NB];
; #pragma unroll
;     for (int nb = 0; nb < NB; ++nb) o[nb] = (f32x16){};
;     ...
; #pragma unroll
;     for (int pc = 0; pc < 4; ++pc) {
;         VM_WAIT(); __syncthreads();
;         OUT_DMA(pc + 1);
;         const bf16x8 af0 = pa[2 * pc], af1 = pa[2 * pc + 1];
;         OUT_MMA(pc & 1);
	v_permlane32_swap_b32_e32 v64, v66
	v_permlane32_swap_b32_e32 v65, v67
	v_permlane32_swap_b32_e32 v144, v146
	v_permlane32_swap_b32_e32 v140, v142
	v_permlane32_swap_b32_e32 v136, v138
	v_permlane32_swap_b32_e32 v132, v134
	v_add_u32_e32 v181, 0x100, v183
	v_mul_f32_e32 v235, 0x3fb8aa3b, v71
	v_permlane32_swap_b32_e32 v152, v154
	v_permlane32_swap_b32_e32 v153, v155
	v_permlane32_swap_b32_e32 v148, v150
	v_permlane32_swap_b32_e32 v149, v151
	v_permlane32_swap_b32_e32 v145, v147
	v_permlane32_swap_b32_e32 v141, v143
	v_permlane32_swap_b32_e32 v137, v139
	v_permlane32_swap_b32_e32 v133, v135
	v_permlane32_swap_b32_e32 v128, v130
	v_permlane32_swap_b32_e32 v129, v131
	ds_read_b64_tr_b16 v[68:69], v195 offset:0x1000
	ds_read_b64_tr_b16 v[70:71], v203 offset:0x1000
	ds_read_b64_tr_b16 v[72:73], v195 offset:0x1200
	v_mfma_f32_32x32x16_bf16 v[16:31], v[64:67], v[0:3], 0
	ds_read_b64_tr_b16 v[74:75], v203 offset:0x1200
	ds_read_b64_tr_b16 v[76:77], v195 offset:0x1400
	ds_read_b64_tr_b16 v[78:79], v203 offset:0x1400
	ds_read_b64_tr_b16 v[80:81], v195 offset:0x1600
	ds_read_b64_tr_b16 v[82:83], v203 offset:0x1600
	s_waitcnt lgkmcnt(0)
	v_mfma_f32_32x32x16_bf16 v[0:15], v[64:67], v[4:7], 0
	v_mfma_f32_32x32x16_bf16 v[32:47], v[64:67], v[32:35], 0
	v_mfma_f32_32x32x16_bf16 v[48:63], v[64:67], v[48:51], 0
	v_mfma_f32_32x32x16_bf16 v[16:31], v[152:155], v[68:71], v[16:31]
	v_add_u32_e32 v252, s70, v175
	ds_read_b64_tr_b16 v[68:69], v252 offset:0
	v_add_u32_e32 v253, s82, v183
	ds_read_b64_tr_b16 v[70:71], v253 offset:0
	v_mfma_f32_32x32x16_bf16 v[0:15], v[152:155], v[72:75], v[0:15]
	ds_read_b64_tr_b16 v[72:73], v252 offset:0x200
	ds_read_b64_tr_b16 v[74:75], v253 offset:0x200
	v_mfma_f32_32x32x16_bf16 v[32:47], v[152:155], v[76:79], v[32:47]
	ds_read_b64_tr_b16 v[76:77], v252 offset:0x400
	ds_read_b64_tr_b16 v[78:79], v253 offset:0x400
	ds_read_b64_tr_b16 v[236:237], v252 offset:0x600
	ds_read_b64_tr_b16 v[238:239], v253 offset:0x600
	s_waitcnt lgkmcnt(0)
	v_mfma_f32_32x32x16_bf16 v[48:63], v[152:155], v[80:83], v[48:63]
	v_mfma_f32_32x32x16_bf16 v[96:111], v[64:67], v[68:71], 0
	v_mfma_f32_32x32x16_bf16 v[112:127], v[64:67], v[72:75], 0
	v_mfma_f32_32x32x16_bf16 v[80:95], v[64:67], v[76:79], 0
	v_mfma_f32_32x32x16_bf16 v[64:79], v[64:67], v[236:239], 0
	ds_read_b64_tr_b16 v[236:237], v252 offset:0x1000
	ds_read_b64_tr_b16 v[238:239], v253 offset:0x1000
	ds_read_b64_tr_b16 v[240:241], v252 offset:0x1200
	ds_read_b64_tr_b16 v[242:243], v253 offset:0x1200
	ds_read_b64_tr_b16 v[244:245], v252 offset:0x1400
	ds_read_b64_tr_b16 v[246:247], v253 offset:0x1400
	ds_read_b64_tr_b16 v[248:249], v252 offset:0x1600
	ds_read_b64_tr_b16 v[250:251], v253 offset:0x1600
	s_waitcnt lgkmcnt(0)
	s_add_u32 s96, s37, 0xc1000
	s_addc_u32 s97, s16, 0
	v_mfma_f32_32x32x16_bf16 v[96:111], v[152:155], v[236:239], v[96:111]
	v_mov_b64_e32 v[236:237], s[96:97]
	v_mad_i64_i32 v[238:239], s[96:97], v182, s57, v[236:237]
	v_lshl_add_u64 v[238:239], v[238:239], 0, v[184:185]
	v_lshl_add_u64 v[238:239], v[238:239], 0, v[160:161]
	s_mov_b32 m0, s40
	v_lshl_add_u64 v[238:239], v[238:239], 0, v[156:157]
	s_waitcnt vmcnt(0)
	s_waitcnt vmcnt(0) lgkmcnt(0)
	s_barrier
	global_load_lds_dwordx4 v[238:239], off
	v_mad_i64_i32 v[238:239], s[96:97], v186, s57, v[236:237]
	v_lshl_add_u64 v[238:239], v[238:239], 0, v[188:189]
	v_lshl_add_u64 v[238:239], v[238:239], 0, v[190:191]
	v_lshl_add_u64 v[238:239], v[238:239], 0, v[192:193]
	s_mov_b32 m0, s41
	v_mfma_f32_32x32x16_bf16 v[112:127], v[152:155], v[240:243], v[112:127]
	global_load_lds_dwordx4 v[238:239], off
	v_mad_i64_i32 v[238:239], s[96:97], v194, s57, v[236:237]
	v_lshl_add_u64 v[238:239], v[238:239], 0, v[196:197]
	v_mad_i64_i32 v[236:237], s[96:97], v202, s57, v[236:237]
	v_lshl_add_u64 v[238:239], v[238:239], 0, v[198:199]
	v_lshl_add_u64 v[236:237], v[236:237], 0, v[204:205]
	v_lshl_add_u64 v[238:239], v[238:239], 0, v[200:201]
	s_mov_b32 m0, s42
	v_lshl_add_u64 v[236:237], v[236:237], 0, v[206:207]
	global_load_lds_dwordx4 v[238:239], off
	v_lshl_add_u64 v[236:237], v[236:237], 0, v[208:209]
	s_mov_b32 m0, s43
	v_mfma_f32_32x32x16_bf16 v[80:95], v[152:155], v[244:247], v[80:95]
	global_load_lds_dwordx4 v[236:237], off
	v_add_u32_e32 v254, s80, v175
	v_add_u32_e32 v255, s83, v183
	v_mfma_f32_32x32x16_bf16 v[64:79], v[152:155], v[248:251], v[64:79]
	ds_read_b64_tr_b16 v[152:153], v254 offset:0
	ds_read_b64_tr_b16 v[154:155], v255 offset:0
	ds_read_b64_tr_b16 v[236:237], v254 offset:0x200
	ds_read_b64_tr_b16 v[238:239], v255 offset:0x200
	ds_read_b64_tr_b16 v[240:241], v254 offset:0x400
	ds_read_b64_tr_b16 v[242:243], v255 offset:0x400
	ds_read_b64_tr_b16 v[244:245], v254 offset:0x600
	ds_read_b64_tr_b16 v[246:247], v255 offset:0x600
	s_waitcnt lgkmcnt(0)
	s_nop 0
	v_mfma_f32_32x32x16_bf16 v[16:31], v[148:151], v[152:155], v[16:31]
	ds_read_b64_tr_b16 v[152:153], v254 offset:0x1000
	ds_read_b64_tr_b16 v[154:155], v255 offset:0x1000
	v_mfma_f32_32x32x16_bf16 v[0:15], v[148:151], v[236:239], v[0:15]
	ds_read_b64_tr_b16 v[236:237], v254 offset:0x1200
	ds_read_b64_tr_b16 v[238:239], v255 offset:0x1200
	v_mfma_f32_32x32x16_bf16 v[32:47], v[148:151], v[240:243], v[32:47]
	ds_read_b64_tr_b16 v[240:241], v254 offset:0x1400
	ds_read_b64_tr_b16 v[242:243], v255 offset:0x1400
	ds_read_b64_tr_b16 v[248:249], v254 offset:0x1600
	ds_read_b64_tr_b16 v[250:251], v255 offset:0x1600
	s_waitcnt lgkmcnt(0)
; #define VM_WAIT() asm volatile("s_waitcnt vmcnt(0)" ::: "memory")
; template <int DK, int DV, bool MLSTM>
; __device__ __forceinline__ void out_unit2(LAS unsigned char* lds, LAS unsigned char* ldstab, const OutArgs a, const int wv) {
;     ...
; #pragma unroll
;     for (int pc = 0; pc < 4; ++pc) {
;         VM_WAIT(); __syncthreads();
;         OUT_DMA(pc + 1);
;         const bf16x8 af0 = pa[2 * pc], af1 = pa[2 * pc + 1];
;         OUT_MMA(pc & 1);
	v_mfma_f32_32x32x16_bf16 v[48:63], v[148:151], v[244:247], v[48:63]
	v_mfma_f32_32x32x16_bf16 v[16:31], v[144:147], v[152:155], v[16:31]
	v_add_u32_e32 v226, s84, v175
	ds_read_b64_tr_b16 v[152:153], v226 offset:0
	v_add_u32_e32 v227, s85, v183
	ds_read_b64_tr_b16 v[154:155], v227 offset:0
	v_mfma_f32_32x32x16_bf16 v[0:15], v[144:147], v[236:239], v[0:15]
	ds_read_b64_tr_b16 v[236:237], v226 offset:0x200
	ds_read_b64_tr_b16 v[238:239], v227 offset:0x200
	v_mfma_f32_32x32x16_bf16 v[32:47], v[144:147], v[240:243], v[32:47]
	ds_read_b64_tr_b16 v[240:241], v226 offset:0x400
	ds_read_b64_tr_b16 v[242:243], v227 offset:0x400
	ds_read_b64_tr_b16 v[244:245], v226 offset:0x600
	ds_read_b64_tr_b16 v[246:247], v227 offset:0x600
	s_waitcnt lgkmcnt(0)
	v_mfma_f32_32x32x16_bf16 v[48:63], v[144:147], v[248:251], v[48:63]
	v_mfma_f32_32x32x16_bf16 v[96:111], v[148:151], v[152:155], v[96:111]
	ds_read_b64_tr_b16 v[152:153], v226 offset:0x1000
	ds_read_b64_tr_b16 v[154:155], v227 offset:0x1000
	v_mfma_f32_32x32x16_bf16 v[112:127], v[148:151], v[236:239], v[112:127]
	ds_read_b64_tr_b16 v[236:237], v226 offset:0x1200
	ds_read_b64_tr_b16 v[238:239], v227 offset:0x1200
	v_mfma_f32_32x32x16_bf16 v[80:95], v[148:151], v[240:243], v[80:95]
	ds_read_b64_tr_b16 v[240:241], v226 offset:0x1400
	ds_read_b64_tr_b16 v[242:243], v227 offset:0x1400
	ds_read_b64_tr_b16 v[248:249], v226 offset:0x1600
	ds_read_b64_tr_b16 v[250:251], v227 offset:0x1600
	s_waitcnt lgkmcnt(0)
	v_mfma_f32_32x32x16_bf16 v[64:79], v[148:151], v[244:247], v[64:79]
	s_mov_b32 m0, s94
	s_add_u32 s94, s37, 0x121000
	s_addc_u32 s95, s16, 0
	v_mov_b64_e32 v[148:149], s[94:95]
	v_mad_i64_i32 v[150:151], s[94:95], v182, s57, v[148:149]
	v_lshl_add_u64 v[150:151], v[150:151], 0, v[184:185]
	v_lshl_add_u64 v[150:151], v[150:151], 0, v[160:161]
	v_lshl_add_u64 v[150:151], v[150:151], 0, v[156:157]
	s_waitcnt vmcnt(0)
	s_waitcnt vmcnt(0) lgkmcnt(0)
	s_barrier
	global_load_lds_dwordx4 v[150:151], off
	v_mad_i64_i32 v[150:151], s[94:95], v186, s57, v[148:149]
	v_lshl_add_u64 v[150:151], v[150:151], 0, v[188:189]
	v_lshl_add_u64 v[150:151], v[150:151], 0, v[190:191]
	v_lshl_add_u64 v[150:151], v[150:151], 0, v[192:193]
	s_mov_b32 m0, s44
	v_mfma_f32_32x32x16_bf16 v[96:111], v[144:147], v[152:155], v[96:111]
	global_load_lds_dwordx4 v[150:151], off
	v_mad_i64_i32 v[150:151], s[94:95], v194, s57, v[148:149]
	v_lshl_add_u64 v[150:151], v[150:151], 0, v[196:197]
	s_mov_b32 m0, s45
	v_mad_i64_i32 v[148:149], s[44:45], v202, s57, v[148:149]
	v_lshl_add_u64 v[150:151], v[150:151], 0, v[198:199]
	v_lshl_add_u64 v[148:149], v[148:149], 0, v[204:205]
	v_lshl_add_u64 v[150:151], v[150:151], 0, v[200:201]
	v_lshl_add_u64 v[148:149], v[148:149], 0, v[206:207]
	global_load_lds_dwordx4 v[150:151], off
	v_lshl_add_u64 v[148:149], v[148:149], 0, v[208:209]
	s_mov_b32 m0, s93
	v_mfma_f32_32x32x16_bf16 v[112:127], v[144:147], v[236:239], v[112:127]
	global_load_lds_dwordx4 v[148:149], off
	v_mfma_f32_32x32x16_bf16 v[80:95], v[144:147], v[240:243], v[80:95]
	v_mfma_f32_32x32x16_bf16 v[64:79], v[144:147], v[248:251], v[64:79]
	ds_read_b64_tr_b16 v[144:145], v195 offset:0
	ds_read_b64_tr_b16 v[146:147], v203 offset:0
	ds_read_b64_tr_b16 v[148:149], v195 offset:0x200
	ds_read_b64_tr_b16 v[150:151], v203 offset:0x200
	ds_read_b64_tr_b16 v[152:153], v195 offset:0x400
	ds_read_b64_tr_b16 v[154:155], v203 offset:0x400
	ds_read_b64_tr_b16 v[182:183], v195 offset:0x600
	ds_read_b64_tr_b16 v[184:185], v203 offset:0x600
	s_waitcnt lgkmcnt(0)
	s_nop 0
	v_mfma_f32_32x32x16_bf16 v[16:31], v[140:143], v[144:147], v[16:31]
	ds_read_b64_tr_b16 v[144:145], v195 offset:0x1000
	ds_read_b64_tr_b16 v[146:147], v203 offset:0x1000
	v_mfma_f32_32x32x16_bf16 v[0:15], v[140:143], v[148:151], v[0:15]
	ds_read_b64_tr_b16 v[148:149], v195 offset:0x1200
	ds_read_b64_tr_b16 v[150:151], v203 offset:0x1200
	v_mfma_f32_32x32x16_bf16 v[32:47], v[140:143], v[152:155], v[32:47]
	ds_read_b64_tr_b16 v[152:153], v195 offset:0x1400
	ds_read_b64_tr_b16 v[154:155], v203 offset:0x1400
	ds_read_b64_tr_b16 v[186:187], v195 offset:0x1600
	ds_read_b64_tr_b16 v[188:189], v203 offset:0x1600
	s_waitcnt lgkmcnt(0)
	v_mfma_f32_32x32x16_bf16 v[48:63], v[140:143], v[182:185], v[48:63]
	v_mfma_f32_32x32x16_bf16 v[16:31], v[136:139], v[144:147], v[16:31]
	ds_read_b64_tr_b16 v[144:145], v252 offset:0
	ds_read_b64_tr_b16 v[146:147], v253 offset:0
	v_mfma_f32_32x32x16_bf16 v[0:15], v[136:139], v[148:151], v[0:15]
	ds_read_b64_tr_b16 v[148:149], v252 offset:0x200
	ds_read_b64_tr_b16 v[150:151], v253 offset:0x200
	v_mfma_f32_32x32x16_bf16 v[32:47], v[136:139], v[152:155], v[32:47]
	ds_read_b64_tr_b16 v[152:153], v252 offset:0x400
	ds_read_b64_tr_b16 v[154:155], v253 offset:0x400
	ds_read_b64_tr_b16 v[182:183], v252 offset:0x600
	ds_read_b64_tr_b16 v[184:185], v253 offset:0x600
	s_waitcnt lgkmcnt(0)
	v_mfma_f32_32x32x16_bf16 v[48:63], v[136:139], v[186:189], v[48:63]
	v_mfma_f32_32x32x16_bf16 v[96:111], v[140:143], v[144:147], v[96:111]
	ds_read_b64_tr_b16 v[144:145], v252 offset:0x1000
	ds_read_b64_tr_b16 v[146:147], v253 offset:0x1000
	v_mfma_f32_32x32x16_bf16 v[112:127], v[140:143], v[148:151], v[112:127]
	ds_read_b64_tr_b16 v[148:149], v252 offset:0x1200
	ds_read_b64_tr_b16 v[150:151], v253 offset:0x1200
	v_mfma_f32_32x32x16_bf16 v[80:95], v[140:143], v[152:155], v[80:95]
	ds_read_b64_tr_b16 v[152:153], v252 offset:0x1400
	ds_read_b64_tr_b16 v[154:155], v253 offset:0x1400
	ds_read_b64_tr_b16 v[186:187], v252 offset:0x1600
	ds_read_b64_tr_b16 v[188:189], v253 offset:0x1600
	s_waitcnt lgkmcnt(0)
	v_mfma_f32_32x32x16_bf16 v[64:79], v[140:143], v[182:185], v[64:79]
	s_mov_b32 m0, s40
	s_waitcnt vmcnt(0)
	s_waitcnt vmcnt(0) lgkmcnt(0)
	s_barrier
; #define VM_WAIT() asm volatile("s_waitcnt vmcnt(0)" ::: "memory")
; template <int DK, int DV, bool MLSTM>
; __device__ __forceinline__ void out_unit2(LAS unsigned char* lds, LAS unsigned char* ldstab, const OutArgs a, const int wv) {
;     ...
; #pragma unroll
;     for (int pc = 0; pc < 4; ++pc) {
;         VM_WAIT(); __syncthreads();
;         OUT_DMA(pc + 1);
;         const bf16x8 af0 = pa[2 * pc], af1 = pa[2 * pc + 1];
;         OUT_MMA(pc & 1);
;     }
; #pragma unroll 1
;     for (int pc = 4; pc < 4 + 2 * NCP; ++pc) {
;         VM_WAIT(); __syncthreads();
;         if (pc + 1 < 4 + 2 * NCP) OUT_DMA(pc + 1);
;         const int cq = pc - 4, dirb = cq >= NCP, cp = dirb ? cq - NCP : cq;
;         const float qs = dirb ? qsb : qsf;
;         const unsigned qa = QP + (cp >> 2) * 32768u + 512u * (cp & 3) + 8192u * rb;
;         const bf16x8 af0 = scale_frag(lds_r128(qa + rb0), qs), af1 = scale_frag(lds_r128(qa + rb1), qs);
	global_load_lds_dwordx4 v[222:223], off
	s_mov_b32 m0, s41
	v_mfma_f32_32x32x16_bf16 v[96:111], v[136:139], v[144:147], v[96:111]
	global_load_lds_dwordx4 v[224:225], off
	s_mov_b32 m0, s42
	s_nop 0
	global_load_lds_dwordx4 v[218:219], off
	s_mov_b32 m0, s43
	v_mfma_f32_32x32x16_bf16 v[112:127], v[136:139], v[148:151], v[112:127]
	global_load_lds_dwordx4 v[220:221], off
	ds_read_b64_tr_b16 v[140:141], v254 offset:0
	ds_read_b64_tr_b16 v[142:143], v255 offset:0
	ds_read_b64_tr_b16 v[144:145], v254 offset:0x200
	ds_read_b64_tr_b16 v[146:147], v255 offset:0x200
	ds_read_b64_tr_b16 v[148:149], v254 offset:0x400
	v_mfma_f32_32x32x16_bf16 v[80:95], v[136:139], v[152:155], v[80:95]
	ds_read_b64_tr_b16 v[150:151], v255 offset:0x400
	ds_read_b64_tr_b16 v[152:153], v254 offset:0x600
	ds_read_b64_tr_b16 v[154:155], v255 offset:0x600
	s_waitcnt lgkmcnt(0)
	v_mfma_f32_32x32x16_bf16 v[64:79], v[136:139], v[186:189], v[64:79]
	ds_read_b64_tr_b16 v[136:137], v254 offset:0x1000
	ds_read_b64_tr_b16 v[138:139], v255 offset:0x1000
	v_mfma_f32_32x32x16_bf16 v[16:31], v[132:135], v[140:143], v[16:31]
	ds_read_b64_tr_b16 v[140:141], v254 offset:0x1200
	ds_read_b64_tr_b16 v[142:143], v255 offset:0x1200
	v_mfma_f32_32x32x16_bf16 v[0:15], v[132:135], v[144:147], v[0:15]
	ds_read_b64_tr_b16 v[144:145], v254 offset:0x1400
	ds_read_b64_tr_b16 v[146:147], v255 offset:0x1400
	v_mfma_f32_32x32x16_bf16 v[32:47], v[132:135], v[148:151], v[32:47]
	ds_read_b64_tr_b16 v[148:149], v254 offset:0x1600
	ds_read_b64_tr_b16 v[150:151], v255 offset:0x1600
	s_waitcnt lgkmcnt(0)
	v_mfma_f32_32x32x16_bf16 v[48:63], v[132:135], v[152:155], v[48:63]
	v_mfma_f32_32x32x16_bf16 v[16:31], v[128:131], v[136:139], v[16:31]
	ds_read_b64_tr_b16 v[136:137], v226 offset:0
	ds_read_b64_tr_b16 v[138:139], v227 offset:0
	v_mfma_f32_32x32x16_bf16 v[0:15], v[128:131], v[140:143], v[0:15]
	ds_read_b64_tr_b16 v[140:141], v226 offset:0x200
	ds_read_b64_tr_b16 v[142:143], v227 offset:0x200
	v_mfma_f32_32x32x16_bf16 v[32:47], v[128:131], v[144:147], v[32:47]
	ds_read_b64_tr_b16 v[144:145], v226 offset:0x400
	ds_read_b64_tr_b16 v[146:147], v227 offset:0x400
	ds_read_b64_tr_b16 v[152:153], v226 offset:0x600
	ds_read_b64_tr_b16 v[154:155], v227 offset:0x600
	s_waitcnt lgkmcnt(0)
	v_mfma_f32_32x32x16_bf16 v[48:63], v[128:131], v[148:151], v[48:63]
	v_mfma_f32_32x32x16_bf16 v[96:111], v[132:135], v[136:139], v[96:111]
	ds_read_b64_tr_b16 v[136:137], v226 offset:0x1000
	ds_read_b64_tr_b16 v[138:139], v227 offset:0x1000
	v_mfma_f32_32x32x16_bf16 v[112:127], v[132:135], v[140:143], v[112:127]
	ds_read_b64_tr_b16 v[140:141], v226 offset:0x1200
	ds_read_b64_tr_b16 v[142:143], v227 offset:0x1200
	v_mfma_f32_32x32x16_bf16 v[80:95], v[132:135], v[144:147], v[80:95]
	ds_read_b64_tr_b16 v[146:147], v226 offset:0x1400
	ds_read_b64_tr_b16 v[148:149], v227 offset:0x1400
	ds_read_b64_tr_b16 v[182:183], v226 offset:0x1600
	ds_read_b64_tr_b16 v[184:185], v227 offset:0x1600
	s_waitcnt lgkmcnt(0)
	v_mfma_f32_32x32x16_bf16 v[64:79], v[132:135], v[152:155], v[64:79]
	v_mfma_f32_32x32x16_bf16 v[96:111], v[128:131], v[136:139], v[96:111]
	v_add_u32_e32 v226, s13, v173
	v_add_u32_e32 v227, s13, v177
	ds_read_b128 v[236:239], v226 offset:0
	ds_read_b128 v[240:243], v227 offset:0
	ds_read_b128 v[244:247], v226 offset:512
	ds_read_b128 v[248:251], v227 offset:512
	ds_read_b128 v[252:255], v226 offset:1024
	ds_read_b128 v[218:221], v227 offset:1024
	ds_read_b128 v[222:225], v226 offset:1536
	ds_read_b128 v[206:209], v227 offset:1536
	v_exp_f32_e32 v144, v235
	s_mov_b32 s37, 0x28000
	s_movk_i32 s39, 0x800
	v_lshlrev_b32_e32 v160, 1, v162
	v_lshlrev_b32_e32 v132, 1, v170
	v_lshlrev_b32_e32 v134, 1, v172
	v_lshlrev_b32_e32 v136, 1, v174
	v_mfma_f32_32x32x16_bf16 v[112:127], v[128:131], v[140:143], v[112:127]
	v_lshlrev_b32_e32 v138, 1, v176
	v_lshlrev_b32_e32 v140, 1, v178
	v_lshlrev_b32_e32 v142, 1, v180
	v_mfma_f32_32x32x16_bf16 v[80:95], v[128:131], v[146:149], v[80:95]
	v_mfma_f32_32x32x16_bf16 v[64:79], v[128:131], v[182:185], v[64:79]
	v_lshl_add_u64 v[198:199], v[158:159], 1, v[210:211]
	v_lshl_add_u64 v[198:199], v[198:199], 0, v[160:161]
	v_mov_b32_e32 v157, v161
	v_lshl_add_u64 v[198:199], v[198:199], 0, v[156:157]
	v_mov_b32_e32 v133, v161
	v_mov_b32_e32 v135, v161
	v_lshl_add_u64 v[200:201], v[164:165], 1, v[212:213]
	v_lshl_add_u64 v[200:201], v[200:201], 0, v[132:133]
	v_lshl_add_u64 v[200:201], v[200:201], 0, v[134:135]
	v_mov_b32_e32 v137, v161
	v_mov_b32_e32 v139, v161
	v_lshl_add_u64 v[202:203], v[166:167], 1, v[214:215]
	v_lshl_add_u64 v[202:203], v[202:203], 0, v[136:137]
	v_lshl_add_u64 v[202:203], v[202:203], 0, v[138:139]
	v_mov_b32_e32 v141, v161
	v_mov_b32_e32 v143, v161
	v_lshl_add_u64 v[204:205], v[168:169], 1, v[216:217]
	v_lshl_add_u64 v[204:205], v[204:205], 0, v[140:141]
	v_lshl_add_u64 v[204:205], v[204:205], 0, v[142:143]
	s_waitcnt vmcnt(0) lgkmcnt(0)
	s_barrier
; #define VM_WAIT() asm volatile("s_waitcnt vmcnt(0)" ::: "memory")
; template <int DK, int DV, bool MLSTM>
; __device__ __forceinline__ void out_unit2(LAS unsigned char* lds, LAS unsigned char* ldstab, const OutArgs a, const int wv) {
;     ...
; #pragma unroll
;     for (int pc = 0; pc < 4; ++pc) {
;         VM_WAIT(); __syncthreads();
;         OUT_DMA(pc + 1);
;         const bf16x8 af0 = pa[2 * pc], af1 = pa[2 * pc + 1];
;         OUT_MMA(pc & 1);
;     }
; #pragma unroll 1
;     for (int pc = 4; pc < 4 + 2 * NCP; ++pc) {
;         VM_WAIT(); __syncthreads();
;         if (pc + 1 < 4 + 2 * NCP) OUT_DMA(pc + 1);
;         const int cq = pc - 4, dirb = cq >= NCP, cp = dirb ? cq - NCP : cq;
;         const float qs = dirb ? qsb : qsf;
;         const unsigned qa = QP + (cp >> 2) * 32768u + 512u * (cp & 3) + 8192u * rb;
;         const bf16x8 af0 = scale_frag(lds_r128(qa + rb0), qs), af1 = scale_frag(lds_r128(qa + rb1), qs);
;         OUT_MMA(pc & 1);
;     }
	s_add_u32 s40, s4, 0x8000
	s_addc_u32 s41, s5, 0
	v_lshl_add_u64 v[128:129], s[40:41], 0, v[198:199]
	v_lshl_add_u64 v[130:131], s[40:41], 0, v[200:201]
	v_lshl_add_u64 v[146:147], s[40:41], 0, v[202:203]
	v_lshl_add_u64 v[148:149], s[40:41], 0, v[204:205]
	s_add_i32 m0, s6, 0x18000
	s_nop 0
	global_load_lds_dwordx4 v[128:129], off
	s_add_i32 m0, s7, 0x18000
	s_nop 0
	global_load_lds_dwordx4 v[130:131], off
	s_add_i32 m0, s36, 0x18000
	s_nop 0
	global_load_lds_dwordx4 v[146:147], off
	s_add_i32 m0, s38, 0x18000
	s_nop 0
	global_load_lds_dwordx4 v[148:149], off
	s_add_u32 s40, s4, 0x10000
	s_addc_u32 s41, s5, 0
	v_lshl_add_u64 v[128:129], s[40:41], 0, v[198:199]
	v_lshl_add_u64 v[130:131], s[40:41], 0, v[200:201]
	v_lshl_add_u64 v[146:147], s[40:41], 0, v[202:203]
	v_lshl_add_u64 v[148:149], s[40:41], 0, v[204:205]
	s_mov_b32 m0, s6
	s_nop 0
	global_load_lds_dwordx4 v[128:129], off
	s_mov_b32 m0, s7
	s_nop 0
	global_load_lds_dwordx4 v[130:131], off
	s_mov_b32 m0, s36
	s_nop 0
	global_load_lds_dwordx4 v[146:147], off
	s_mov_b32 m0, s38
	s_nop 0
	global_load_lds_dwordx4 v[148:149], off
	v_lshlrev_b32_e32 v135, 16, v236
	v_and_b32_e32 v137, 0xffff0000, v236
	v_mul_f32_e32 v135, v179, v135
	v_mul_f32_e32 v137, v179, v137
	v_cvt_pk_bf16_f32 v128, v135, v137
	v_lshlrev_b32_e32 v135, 16, v237
	v_and_b32_e32 v137, 0xffff0000, v237
	v_mul_f32_e32 v135, v179, v135
	v_mul_f32_e32 v137, v179, v137
	v_cvt_pk_bf16_f32 v129, v135, v137
	v_lshlrev_b32_e32 v135, 16, v238
	v_and_b32_e32 v137, 0xffff0000, v238
	v_mul_f32_e32 v135, v179, v135
	v_mul_f32_e32 v137, v179, v137
	v_cvt_pk_bf16_f32 v130, v135, v137
	v_lshlrev_b32_e32 v135, 16, v239
	v_and_b32_e32 v137, 0xffff0000, v239
	v_mul_f32_e32 v135, v179, v135
	v_mul_f32_e32 v137, v179, v137
	v_cvt_pk_bf16_f32 v131, v135, v137
	v_lshlrev_b32_e32 v135, 16, v240
	v_and_b32_e32 v137, 0xffff0000, v240
	v_mul_f32_e32 v135, v179, v135
	v_mul_f32_e32 v137, v179, v137
	v_cvt_pk_bf16_f32 v146, v135, v137
	v_lshlrev_b32_e32 v135, 16, v241
	v_and_b32_e32 v137, 0xffff0000, v241
	v_mul_f32_e32 v135, v179, v135
	v_mul_f32_e32 v137, v179, v137
	v_cvt_pk_bf16_f32 v147, v135, v137
	v_lshlrev_b32_e32 v135, 16, v242
	v_and_b32_e32 v137, 0xffff0000, v242
	v_mul_f32_e32 v135, v179, v135
	v_mul_f32_e32 v137, v179, v137
	v_cvt_pk_bf16_f32 v148, v135, v137
	v_lshlrev_b32_e32 v135, 16, v243
	v_and_b32_e32 v137, 0xffff0000, v243
	v_mul_f32_e32 v135, v179, v135
	v_mul_f32_e32 v137, v179, v137
	v_cvt_pk_bf16_f32 v149, v135, v137
	v_add_u32_e32 v133, 0x10000, v175
	ds_read_b64_tr_b16 v[150:151], v133 offset:0
	v_add_u32_e32 v135, 0x10000, v181
	ds_read_b64_tr_b16 v[152:153], v135 offset:0
	ds_read_b64_tr_b16 v[182:183], v133 offset:0x200
	ds_read_b64_tr_b16 v[184:185], v135 offset:0x200
	ds_read_b64_tr_b16 v[186:187], v133 offset:0x400
	ds_read_b64_tr_b16 v[188:189], v135 offset:0x400
	ds_read_b64_tr_b16 v[190:191], v133 offset:0x600
	ds_read_b64_tr_b16 v[192:193], v135 offset:0x600
	s_waitcnt lgkmcnt(0)
	s_nop 0
	v_mfma_f32_32x32x16_bf16 v[16:31], v[128:131], v[150:153], v[16:31]
	ds_read_b64_tr_b16 v[150:151], v133 offset:0x1000
	ds_read_b64_tr_b16 v[152:153], v135 offset:0x1000
	v_mfma_f32_32x32x16_bf16 v[0:15], v[128:131], v[182:185], v[0:15]
	ds_read_b64_tr_b16 v[182:183], v133 offset:0x1200
	ds_read_b64_tr_b16 v[184:185], v135 offset:0x1200
	v_mfma_f32_32x32x16_bf16 v[32:47], v[128:131], v[186:189], v[32:47]
	ds_read_b64_tr_b16 v[186:187], v133 offset:0x1400
	ds_read_b64_tr_b16 v[188:189], v135 offset:0x1400
	ds_read_b64_tr_b16 v[194:195], v133 offset:0x1600
	ds_read_b64_tr_b16 v[196:197], v135 offset:0x1600
	s_waitcnt lgkmcnt(0)
	v_mfma_f32_32x32x16_bf16 v[48:63], v[128:131], v[190:193], v[48:63]
	v_mfma_f32_32x32x16_bf16 v[16:31], v[146:149], v[150:153], v[16:31]
	v_add_u32_e32 v133, 0x2000, v133
	ds_read_b64_tr_b16 v[150:151], v133 offset:0
	v_add_u32_e32 v135, 0x2000, v135
	ds_read_b64_tr_b16 v[152:153], v135 offset:0
	v_mfma_f32_32x32x16_bf16 v[0:15], v[146:149], v[182:185], v[0:15]
	ds_read_b64_tr_b16 v[182:183], v133 offset:0x200
	ds_read_b64_tr_b16 v[184:185], v135 offset:0x200
	v_mfma_f32_32x32x16_bf16 v[32:47], v[146:149], v[186:189], v[32:47]
	ds_read_b64_tr_b16 v[186:187], v133 offset:0x400
	ds_read_b64_tr_b16 v[188:189], v135 offset:0x400
	ds_read_b64_tr_b16 v[190:191], v133 offset:0x600
	ds_read_b64_tr_b16 v[192:193], v135 offset:0x600
	s_waitcnt lgkmcnt(0)
	v_mfma_f32_32x32x16_bf16 v[48:63], v[146:149], v[194:197], v[48:63]
	v_mfma_f32_32x32x16_bf16 v[96:111], v[128:131], v[150:153], v[96:111]
	ds_read_b64_tr_b16 v[150:151], v133 offset:0x1000
	ds_read_b64_tr_b16 v[152:153], v135 offset:0x1000
	v_mfma_f32_32x32x16_bf16 v[112:127], v[128:131], v[182:185], v[112:127]
	ds_read_b64_tr_b16 v[182:183], v133 offset:0x1200
	ds_read_b64_tr_b16 v[184:185], v135 offset:0x1200
	v_mfma_f32_32x32x16_bf16 v[80:95], v[128:131], v[186:189], v[80:95]
	ds_read_b64_tr_b16 v[186:187], v133 offset:0x1400
	ds_read_b64_tr_b16 v[188:189], v135 offset:0x1400
	ds_read_b64_tr_b16 v[194:195], v133 offset:0x1600
	ds_read_b64_tr_b16 v[196:197], v135 offset:0x1600
	s_waitcnt lgkmcnt(0)
	v_mfma_f32_32x32x16_bf16 v[64:79], v[128:131], v[190:193], v[64:79]
	v_mfma_f32_32x32x16_bf16 v[96:111], v[146:149], v[150:153], v[96:111]
	v_mfma_f32_32x32x16_bf16 v[112:127], v[146:149], v[182:185], v[112:127]
	v_mfma_f32_32x32x16_bf16 v[80:95], v[146:149], v[186:189], v[80:95]
	v_mfma_f32_32x32x16_bf16 v[64:79], v[146:149], v[194:197], v[64:79]
	s_waitcnt vmcnt(4) lgkmcnt(0)
	s_barrier
; #define VM_WAIT() asm volatile("s_waitcnt vmcnt(0)" ::: "memory")
; template <int DK, int DV, bool MLSTM>
; __device__ __forceinline__ void out_unit2(LAS unsigned char* lds, LAS unsigned char* ldstab, const OutArgs a, const int wv) {
;     ...
; #pragma unroll
;     for (int pc = 0; pc < 4; ++pc) {
;         VM_WAIT(); __syncthreads();
;         OUT_DMA(pc + 1);
;         const bf16x8 af0 = pa[2 * pc], af1 = pa[2 * pc + 1];
;         OUT_MMA(pc & 1);
;     }
; #pragma unroll 1
;     for (int pc = 4; pc < 4 + 2 * NCP; ++pc) {
;         VM_WAIT(); __syncthreads();
;         if (pc + 1 < 4 + 2 * NCP) OUT_DMA(pc + 1);
;         const int cq = pc - 4, dirb = cq >= NCP, cp = dirb ? cq - NCP : cq;
;         const float qs = dirb ? qsb : qsf;
;         const unsigned qa = QP + (cp >> 2) * 32768u + 512u * (cp & 3) + 8192u * rb;
;         const bf16x8 af0 = scale_frag(lds_r128(qa + rb0), qs), af1 = scale_frag(lds_r128(qa + rb1), qs);
;         OUT_MMA(pc & 1);
;     }
	s_add_u32 s40, s4, 0x18000
	s_addc_u32 s41, s5, 0
	v_lshl_add_u64 v[128:129], s[40:41], 0, v[198:199]
	v_lshl_add_u64 v[130:131], s[40:41], 0, v[200:201]
	v_lshl_add_u64 v[146:147], s[40:41], 0, v[202:203]
	v_lshl_add_u64 v[148:149], s[40:41], 0, v[204:205]
	s_add_i32 m0, s6, 0x10000
	s_nop 0
	global_load_lds_dwordx4 v[128:129], off
	s_add_i32 m0, s7, 0x10000
	s_nop 0
	global_load_lds_dwordx4 v[130:131], off
	s_add_i32 m0, s36, 0x10000
	s_nop 0
	global_load_lds_dwordx4 v[146:147], off
	s_add_i32 m0, s38, 0x10000
	s_nop 0
	global_load_lds_dwordx4 v[148:149], off
	v_lshlrev_b32_e32 v135, 16, v244
	v_and_b32_e32 v137, 0xffff0000, v244
	v_mul_f32_e32 v135, v179, v135
	v_mul_f32_e32 v137, v179, v137
	v_cvt_pk_bf16_f32 v128, v135, v137
	v_lshlrev_b32_e32 v135, 16, v245
	v_and_b32_e32 v137, 0xffff0000, v245
	v_mul_f32_e32 v135, v179, v135
	v_mul_f32_e32 v137, v179, v137
	v_cvt_pk_bf16_f32 v129, v135, v137
	v_lshlrev_b32_e32 v135, 16, v246
	v_and_b32_e32 v137, 0xffff0000, v246
	v_mul_f32_e32 v135, v179, v135
	v_mul_f32_e32 v137, v179, v137
	v_cvt_pk_bf16_f32 v130, v135, v137
	v_lshlrev_b32_e32 v135, 16, v247
	v_and_b32_e32 v137, 0xffff0000, v247
	v_mul_f32_e32 v135, v179, v135
	v_mul_f32_e32 v137, v179, v137
	v_cvt_pk_bf16_f32 v131, v135, v137
	v_lshlrev_b32_e32 v135, 16, v248
	v_and_b32_e32 v137, 0xffff0000, v248
	v_mul_f32_e32 v135, v179, v135
	v_mul_f32_e32 v137, v179, v137
	v_cvt_pk_bf16_f32 v146, v135, v137
	v_lshlrev_b32_e32 v135, 16, v249
	v_and_b32_e32 v137, 0xffff0000, v249
	v_mul_f32_e32 v135, v179, v135
	v_mul_f32_e32 v137, v179, v137
	v_cvt_pk_bf16_f32 v147, v135, v137
	v_lshlrev_b32_e32 v135, 16, v250
	v_and_b32_e32 v137, 0xffff0000, v250
	v_mul_f32_e32 v135, v179, v135
	v_mul_f32_e32 v137, v179, v137
	v_cvt_pk_bf16_f32 v148, v135, v137
	v_lshlrev_b32_e32 v135, 16, v251
	v_and_b32_e32 v137, 0xffff0000, v251
	v_mul_f32_e32 v135, v179, v135
	v_mul_f32_e32 v137, v179, v137
	v_cvt_pk_bf16_f32 v149, v135, v137
	v_add_u32_e32 v133, 0x18000, v175
	ds_read_b64_tr_b16 v[150:151], v133 offset:0
	v_add_u32_e32 v135, 0x18000, v181
	ds_read_b64_tr_b16 v[152:153], v135 offset:0
	ds_read_b64_tr_b16 v[182:183], v133 offset:0x200
	ds_read_b64_tr_b16 v[184:185], v135 offset:0x200
	ds_read_b64_tr_b16 v[186:187], v133 offset:0x400
	ds_read_b64_tr_b16 v[188:189], v135 offset:0x400
	ds_read_b64_tr_b16 v[190:191], v133 offset:0x600
	ds_read_b64_tr_b16 v[192:193], v135 offset:0x600
	s_waitcnt lgkmcnt(0)
	s_nop 0
	v_mfma_f32_32x32x16_bf16 v[16:31], v[128:131], v[150:153], v[16:31]
	ds_read_b64_tr_b16 v[150:151], v133 offset:0x1000
	ds_read_b64_tr_b16 v[152:153], v135 offset:0x1000
	v_mfma_f32_32x32x16_bf16 v[0:15], v[128:131], v[182:185], v[0:15]
	ds_read_b64_tr_b16 v[182:183], v133 offset:0x1200
	ds_read_b64_tr_b16 v[184:185], v135 offset:0x1200
	v_mfma_f32_32x32x16_bf16 v[32:47], v[128:131], v[186:189], v[32:47]
	ds_read_b64_tr_b16 v[186:187], v133 offset:0x1400
	ds_read_b64_tr_b16 v[188:189], v135 offset:0x1400
	ds_read_b64_tr_b16 v[194:195], v133 offset:0x1600
	ds_read_b64_tr_b16 v[196:197], v135 offset:0x1600
	s_waitcnt lgkmcnt(0)
	v_mfma_f32_32x32x16_bf16 v[48:63], v[128:131], v[190:193], v[48:63]
	v_mfma_f32_32x32x16_bf16 v[16:31], v[146:149], v[150:153], v[16:31]
	v_add_u32_e32 v133, 0x2000, v133
	ds_read_b64_tr_b16 v[150:151], v133 offset:0
	v_add_u32_e32 v135, 0x2000, v135
	ds_read_b64_tr_b16 v[152:153], v135 offset:0
	v_mfma_f32_32x32x16_bf16 v[0:15], v[146:149], v[182:185], v[0:15]
	ds_read_b64_tr_b16 v[182:183], v133 offset:0x200
	ds_read_b64_tr_b16 v[184:185], v135 offset:0x200
	v_mfma_f32_32x32x16_bf16 v[32:47], v[146:149], v[186:189], v[32:47]
	ds_read_b64_tr_b16 v[186:187], v133 offset:0x400
	ds_read_b64_tr_b16 v[188:189], v135 offset:0x400
	ds_read_b64_tr_b16 v[190:191], v133 offset:0x600
	ds_read_b64_tr_b16 v[192:193], v135 offset:0x600
	s_waitcnt lgkmcnt(0)
	v_mfma_f32_32x32x16_bf16 v[48:63], v[146:149], v[194:197], v[48:63]
	v_mfma_f32_32x32x16_bf16 v[96:111], v[128:131], v[150:153], v[96:111]
	ds_read_b64_tr_b16 v[150:151], v133 offset:0x1000
	ds_read_b64_tr_b16 v[152:153], v135 offset:0x1000
	v_mfma_f32_32x32x16_bf16 v[112:127], v[128:131], v[182:185], v[112:127]
	ds_read_b64_tr_b16 v[182:183], v133 offset:0x1200
	ds_read_b64_tr_b16 v[184:185], v135 offset:0x1200
	v_mfma_f32_32x32x16_bf16 v[80:95], v[128:131], v[186:189], v[80:95]
	ds_read_b64_tr_b16 v[186:187], v133 offset:0x1400
	ds_read_b64_tr_b16 v[188:189], v135 offset:0x1400
	ds_read_b64_tr_b16 v[194:195], v133 offset:0x1600
	ds_read_b64_tr_b16 v[196:197], v135 offset:0x1600
	s_waitcnt lgkmcnt(0)
	v_mfma_f32_32x32x16_bf16 v[64:79], v[128:131], v[190:193], v[64:79]
	v_mfma_f32_32x32x16_bf16 v[96:111], v[146:149], v[150:153], v[96:111]
	v_mfma_f32_32x32x16_bf16 v[112:127], v[146:149], v[182:185], v[112:127]
	v_mfma_f32_32x32x16_bf16 v[80:95], v[146:149], v[186:189], v[80:95]
	v_mfma_f32_32x32x16_bf16 v[64:79], v[146:149], v[194:197], v[64:79]
	s_waitcnt vmcnt(4) lgkmcnt(0)
	s_barrier
; #define VM_WAIT() asm volatile("s_waitcnt vmcnt(0)" ::: "memory")
; template <int DK, int DV, bool MLSTM>
; __device__ __forceinline__ void out_unit2(LAS unsigned char* lds, LAS unsigned char* ldstab, const OutArgs a, const int wv) {
;     ...
; #pragma unroll
;     for (int pc = 0; pc < 4; ++pc) {
;         VM_WAIT(); __syncthreads();
;         OUT_DMA(pc + 1);
;         const bf16x8 af0 = pa[2 * pc], af1 = pa[2 * pc + 1];
;         OUT_MMA(pc & 1);
;     }
; #pragma unroll 1
;     for (int pc = 4; pc < 4 + 2 * NCP; ++pc) {
;         VM_WAIT(); __syncthreads();
;         if (pc + 1 < 4 + 2 * NCP) OUT_DMA(pc + 1);
;         const int cq = pc - 4, dirb = cq >= NCP, cp = dirb ? cq - NCP : cq;
;         const float qs = dirb ? qsb : qsf;
;         const unsigned qa = QP + (cp >> 2) * 32768u + 512u * (cp & 3) + 8192u * rb;
;         const bf16x8 af0 = scale_frag(lds_r128(qa + rb0), qs), af1 = scale_frag(lds_r128(qa + rb1), qs);
;         OUT_MMA(pc & 1);
;     }
	s_add_u32 s40, s4, 0x20000
	s_addc_u32 s41, s5, 0
	v_lshl_add_u64 v[128:129], s[40:41], 0, v[198:199]
	v_lshl_add_u64 v[130:131], s[40:41], 0, v[200:201]
	v_lshl_add_u64 v[146:147], s[40:41], 0, v[202:203]
	v_lshl_add_u64 v[148:149], s[40:41], 0, v[204:205]
	s_add_i32 m0, s6, 0x18000
	s_nop 0
	global_load_lds_dwordx4 v[128:129], off
	s_add_i32 m0, s7, 0x18000
	s_nop 0
	global_load_lds_dwordx4 v[130:131], off
	s_add_i32 m0, s36, 0x18000
	s_nop 0
	global_load_lds_dwordx4 v[146:147], off
	s_add_i32 m0, s38, 0x18000
	s_nop 0
	global_load_lds_dwordx4 v[148:149], off
	v_lshlrev_b32_e32 v135, 16, v252
	v_and_b32_e32 v137, 0xffff0000, v252
	v_mul_f32_e32 v135, v179, v135
	v_mul_f32_e32 v137, v179, v137
	v_cvt_pk_bf16_f32 v128, v135, v137
	v_lshlrev_b32_e32 v135, 16, v253
	v_and_b32_e32 v137, 0xffff0000, v253
	v_mul_f32_e32 v135, v179, v135
	v_mul_f32_e32 v137, v179, v137
	v_cvt_pk_bf16_f32 v129, v135, v137
	v_lshlrev_b32_e32 v135, 16, v254
	v_and_b32_e32 v137, 0xffff0000, v254
	v_mul_f32_e32 v135, v179, v135
	v_mul_f32_e32 v137, v179, v137
	v_cvt_pk_bf16_f32 v130, v135, v137
	v_lshlrev_b32_e32 v135, 16, v255
	v_and_b32_e32 v137, 0xffff0000, v255
	v_mul_f32_e32 v135, v179, v135
	v_mul_f32_e32 v137, v179, v137
	v_cvt_pk_bf16_f32 v131, v135, v137
	v_lshlrev_b32_e32 v135, 16, v218
	v_and_b32_e32 v137, 0xffff0000, v218
	v_mul_f32_e32 v135, v179, v135
	v_mul_f32_e32 v137, v179, v137
	v_cvt_pk_bf16_f32 v146, v135, v137
	v_lshlrev_b32_e32 v135, 16, v219
	v_and_b32_e32 v137, 0xffff0000, v219
	v_mul_f32_e32 v135, v179, v135
	v_mul_f32_e32 v137, v179, v137
	v_cvt_pk_bf16_f32 v147, v135, v137
	v_lshlrev_b32_e32 v135, 16, v220
	v_and_b32_e32 v137, 0xffff0000, v220
	v_mul_f32_e32 v135, v179, v135
	v_mul_f32_e32 v137, v179, v137
	v_cvt_pk_bf16_f32 v148, v135, v137
	v_lshlrev_b32_e32 v135, 16, v221
	v_and_b32_e32 v137, 0xffff0000, v221
	v_mul_f32_e32 v135, v179, v135
	v_mul_f32_e32 v137, v179, v137
	v_cvt_pk_bf16_f32 v149, v135, v137
	v_mov_b32_e32 v133, v175
	ds_read_b64_tr_b16 v[150:151], v133 offset:0
	v_mov_b32_e32 v135, v181
	ds_read_b64_tr_b16 v[152:153], v135 offset:0
	ds_read_b64_tr_b16 v[182:183], v133 offset:0x200
	ds_read_b64_tr_b16 v[184:185], v135 offset:0x200
	ds_read_b64_tr_b16 v[186:187], v133 offset:0x400
	ds_read_b64_tr_b16 v[188:189], v135 offset:0x400
	ds_read_b64_tr_b16 v[190:191], v133 offset:0x600
	ds_read_b64_tr_b16 v[192:193], v135 offset:0x600
	s_waitcnt lgkmcnt(0)
	s_nop 0
	v_mfma_f32_32x32x16_bf16 v[16:31], v[128:131], v[150:153], v[16:31]
	ds_read_b64_tr_b16 v[150:151], v133 offset:0x1000
	ds_read_b64_tr_b16 v[152:153], v135 offset:0x1000
	v_mfma_f32_32x32x16_bf16 v[0:15], v[128:131], v[182:185], v[0:15]
	ds_read_b64_tr_b16 v[182:183], v133 offset:0x1200
	ds_read_b64_tr_b16 v[184:185], v135 offset:0x1200
	v_mfma_f32_32x32x16_bf16 v[32:47], v[128:131], v[186:189], v[32:47]
	ds_read_b64_tr_b16 v[186:187], v133 offset:0x1400
	ds_read_b64_tr_b16 v[188:189], v135 offset:0x1400
	ds_read_b64_tr_b16 v[194:195], v133 offset:0x1600
	ds_read_b64_tr_b16 v[196:197], v135 offset:0x1600
	s_waitcnt lgkmcnt(0)
	v_mfma_f32_32x32x16_bf16 v[48:63], v[128:131], v[190:193], v[48:63]
	v_mfma_f32_32x32x16_bf16 v[16:31], v[146:149], v[150:153], v[16:31]
	v_add_u32_e32 v133, 0x2000, v133
	ds_read_b64_tr_b16 v[150:151], v133 offset:0
	v_add_u32_e32 v135, 0x2000, v135
	ds_read_b64_tr_b16 v[152:153], v135 offset:0
	v_mfma_f32_32x32x16_bf16 v[0:15], v[146:149], v[182:185], v[0:15]
	ds_read_b64_tr_b16 v[182:183], v133 offset:0x200
	ds_read_b64_tr_b16 v[184:185], v135 offset:0x200
	v_mfma_f32_32x32x16_bf16 v[32:47], v[146:149], v[186:189], v[32:47]
	ds_read_b64_tr_b16 v[186:187], v133 offset:0x400
	ds_read_b64_tr_b16 v[188:189], v135 offset:0x400
	ds_read_b64_tr_b16 v[190:191], v133 offset:0x600
	ds_read_b64_tr_b16 v[192:193], v135 offset:0x600
	s_waitcnt lgkmcnt(0)
	v_mfma_f32_32x32x16_bf16 v[48:63], v[146:149], v[194:197], v[48:63]
	v_mfma_f32_32x32x16_bf16 v[96:111], v[128:131], v[150:153], v[96:111]
	ds_read_b64_tr_b16 v[150:151], v133 offset:0x1000
	ds_read_b64_tr_b16 v[152:153], v135 offset:0x1000
	v_mfma_f32_32x32x16_bf16 v[112:127], v[128:131], v[182:185], v[112:127]
	ds_read_b64_tr_b16 v[182:183], v133 offset:0x1200
	ds_read_b64_tr_b16 v[184:185], v135 offset:0x1200
	v_mfma_f32_32x32x16_bf16 v[80:95], v[128:131], v[186:189], v[80:95]
	ds_read_b64_tr_b16 v[186:187], v133 offset:0x1400
	ds_read_b64_tr_b16 v[188:189], v135 offset:0x1400
	ds_read_b64_tr_b16 v[194:195], v133 offset:0x1600
	ds_read_b64_tr_b16 v[196:197], v135 offset:0x1600
	s_waitcnt lgkmcnt(0)
	v_mfma_f32_32x32x16_bf16 v[64:79], v[128:131], v[190:193], v[64:79]
	v_mfma_f32_32x32x16_bf16 v[96:111], v[146:149], v[150:153], v[96:111]
	v_mfma_f32_32x32x16_bf16 v[112:127], v[146:149], v[182:185], v[112:127]
	v_mfma_f32_32x32x16_bf16 v[80:95], v[146:149], v[186:189], v[80:95]
	v_mfma_f32_32x32x16_bf16 v[64:79], v[146:149], v[194:197], v[64:79]
	s_waitcnt vmcnt(4) lgkmcnt(0)
	s_barrier
; #define VM_WAIT() asm volatile("s_waitcnt vmcnt(0)" ::: "memory")
; template <int DK, int DV, bool MLSTM>
; __device__ __forceinline__ void out_unit2(LAS unsigned char* lds, LAS unsigned char* ldstab, const OutArgs a, const int wv) {
;     ...
; #pragma unroll
;     for (int pc = 0; pc < 4; ++pc) {
;         VM_WAIT(); __syncthreads();
;         OUT_DMA(pc + 1);
;         const bf16x8 af0 = pa[2 * pc], af1 = pa[2 * pc + 1];
;         OUT_MMA(pc & 1);
;     }
; #pragma unroll 1
;     for (int pc = 4; pc < 4 + 2 * NCP; ++pc) {
;         VM_WAIT(); __syncthreads();
;         if (pc + 1 < 4 + 2 * NCP) OUT_DMA(pc + 1);
;         const int cq = pc - 4, dirb = cq >= NCP, cp = dirb ? cq - NCP : cq;
;         const float qs = dirb ? qsb : qsf;
;         const unsigned qa = QP + (cp >> 2) * 32768u + 512u * (cp & 3) + 8192u * rb;
;         const bf16x8 af0 = scale_frag(lds_r128(qa + rb0), qs), af1 = scale_frag(lds_r128(qa + rb1), qs);
;         OUT_MMA(pc & 1);
;     }
	s_add_u32 s40, s4, 0x28000
	s_addc_u32 s41, s5, 0
	v_lshl_add_u64 v[128:129], s[40:41], 0, v[198:199]
	v_lshl_add_u64 v[130:131], s[40:41], 0, v[200:201]
	v_lshl_add_u64 v[146:147], s[40:41], 0, v[202:203]
	v_lshl_add_u64 v[148:149], s[40:41], 0, v[204:205]
	s_mov_b32 m0, s6
	s_nop 0
	global_load_lds_dwordx4 v[128:129], off
	s_mov_b32 m0, s7
	s_nop 0
	global_load_lds_dwordx4 v[130:131], off
	s_mov_b32 m0, s36
	s_nop 0
	global_load_lds_dwordx4 v[146:147], off
	s_mov_b32 m0, s38
	s_nop 0
	global_load_lds_dwordx4 v[148:149], off
	v_lshlrev_b32_e32 v135, 16, v222
	v_and_b32_e32 v137, 0xffff0000, v222
	v_mul_f32_e32 v135, v179, v135
	v_mul_f32_e32 v137, v179, v137
	v_cvt_pk_bf16_f32 v128, v135, v137
	v_lshlrev_b32_e32 v135, 16, v223
	v_and_b32_e32 v137, 0xffff0000, v223
	v_mul_f32_e32 v135, v179, v135
	v_mul_f32_e32 v137, v179, v137
	v_cvt_pk_bf16_f32 v129, v135, v137
	v_lshlrev_b32_e32 v135, 16, v224
	v_and_b32_e32 v137, 0xffff0000, v224
	v_mul_f32_e32 v135, v179, v135
	v_mul_f32_e32 v137, v179, v137
	v_cvt_pk_bf16_f32 v130, v135, v137
	v_lshlrev_b32_e32 v135, 16, v225
	v_and_b32_e32 v137, 0xffff0000, v225
	v_mul_f32_e32 v135, v179, v135
	v_mul_f32_e32 v137, v179, v137
	v_cvt_pk_bf16_f32 v131, v135, v137
	v_lshlrev_b32_e32 v135, 16, v206
	v_and_b32_e32 v137, 0xffff0000, v206
	v_mul_f32_e32 v135, v179, v135
	v_mul_f32_e32 v137, v179, v137
	v_cvt_pk_bf16_f32 v146, v135, v137
	v_lshlrev_b32_e32 v135, 16, v207
	v_and_b32_e32 v137, 0xffff0000, v207
	v_mul_f32_e32 v135, v179, v135
	v_mul_f32_e32 v137, v179, v137
	v_cvt_pk_bf16_f32 v147, v135, v137
	v_lshlrev_b32_e32 v135, 16, v208
	v_and_b32_e32 v137, 0xffff0000, v208
	v_mul_f32_e32 v135, v179, v135
	v_mul_f32_e32 v137, v179, v137
	v_cvt_pk_bf16_f32 v148, v135, v137
	v_lshlrev_b32_e32 v135, 16, v209
	v_and_b32_e32 v137, 0xffff0000, v209
	v_mul_f32_e32 v135, v179, v135
	v_mul_f32_e32 v137, v179, v137
	v_cvt_pk_bf16_f32 v149, v135, v137
	v_add_u32_e32 v133, 0x10000, v175
	ds_read_b64_tr_b16 v[150:151], v133 offset:0
	v_add_u32_e32 v135, 0x10000, v181
	ds_read_b64_tr_b16 v[152:153], v135 offset:0
	ds_read_b64_tr_b16 v[182:183], v133 offset:0x200
	ds_read_b64_tr_b16 v[184:185], v135 offset:0x200
	ds_read_b64_tr_b16 v[186:187], v133 offset:0x400
	ds_read_b64_tr_b16 v[188:189], v135 offset:0x400
	ds_read_b64_tr_b16 v[190:191], v133 offset:0x600
	ds_read_b64_tr_b16 v[192:193], v135 offset:0x600
	s_waitcnt lgkmcnt(0)
	s_nop 0
	v_mfma_f32_32x32x16_bf16 v[16:31], v[128:131], v[150:153], v[16:31]
	ds_read_b64_tr_b16 v[150:151], v133 offset:0x1000
	ds_read_b64_tr_b16 v[152:153], v135 offset:0x1000
	v_mfma_f32_32x32x16_bf16 v[0:15], v[128:131], v[182:185], v[0:15]
	ds_read_b64_tr_b16 v[182:183], v133 offset:0x1200
	ds_read_b64_tr_b16 v[184:185], v135 offset:0x1200
	v_mfma_f32_32x32x16_bf16 v[32:47], v[128:131], v[186:189], v[32:47]
	ds_read_b64_tr_b16 v[186:187], v133 offset:0x1400
	ds_read_b64_tr_b16 v[188:189], v135 offset:0x1400
	ds_read_b64_tr_b16 v[194:195], v133 offset:0x1600
	ds_read_b64_tr_b16 v[196:197], v135 offset:0x1600
	s_waitcnt lgkmcnt(0)
	v_mfma_f32_32x32x16_bf16 v[48:63], v[128:131], v[190:193], v[48:63]
	v_mfma_f32_32x32x16_bf16 v[16:31], v[146:149], v[150:153], v[16:31]
	v_add_u32_e32 v133, 0x2000, v133
	ds_read_b64_tr_b16 v[150:151], v133 offset:0
	v_add_u32_e32 v135, 0x2000, v135
	ds_read_b64_tr_b16 v[152:153], v135 offset:0
	v_mfma_f32_32x32x16_bf16 v[0:15], v[146:149], v[182:185], v[0:15]
	ds_read_b64_tr_b16 v[182:183], v133 offset:0x200
	ds_read_b64_tr_b16 v[184:185], v135 offset:0x200
	v_mfma_f32_32x32x16_bf16 v[32:47], v[146:149], v[186:189], v[32:47]
	ds_read_b64_tr_b16 v[186:187], v133 offset:0x400
	ds_read_b64_tr_b16 v[188:189], v135 offset:0x400
	ds_read_b64_tr_b16 v[190:191], v133 offset:0x600
	ds_read_b64_tr_b16 v[192:193], v135 offset:0x600
	s_waitcnt lgkmcnt(0)
	v_mfma_f32_32x32x16_bf16 v[48:63], v[146:149], v[194:197], v[48:63]
	v_mfma_f32_32x32x16_bf16 v[96:111], v[128:131], v[150:153], v[96:111]
	ds_read_b64_tr_b16 v[150:151], v133 offset:0x1000
	ds_read_b64_tr_b16 v[152:153], v135 offset:0x1000
	v_mfma_f32_32x32x16_bf16 v[112:127], v[128:131], v[182:185], v[112:127]
	ds_read_b64_tr_b16 v[182:183], v133 offset:0x1200
	ds_read_b64_tr_b16 v[184:185], v135 offset:0x1200
	v_mfma_f32_32x32x16_bf16 v[80:95], v[128:131], v[186:189], v[80:95]
	ds_read_b64_tr_b16 v[186:187], v133 offset:0x1400
	ds_read_b64_tr_b16 v[188:189], v135 offset:0x1400
	ds_read_b64_tr_b16 v[194:195], v133 offset:0x1600
	ds_read_b64_tr_b16 v[196:197], v135 offset:0x1600
	s_waitcnt lgkmcnt(0)
	v_mfma_f32_32x32x16_bf16 v[64:79], v[128:131], v[190:193], v[64:79]
	v_mfma_f32_32x32x16_bf16 v[96:111], v[146:149], v[150:153], v[96:111]
	v_mfma_f32_32x32x16_bf16 v[112:127], v[146:149], v[182:185], v[112:127]
	v_mfma_f32_32x32x16_bf16 v[80:95], v[146:149], v[186:189], v[80:95]
	v_mfma_f32_32x32x16_bf16 v[64:79], v[146:149], v[194:197], v[64:79]
	s_waitcnt vmcnt(4) lgkmcnt(0)
	s_barrier
; #define VM_WAIT() asm volatile("s_waitcnt vmcnt(0)" ::: "memory")
; template <int DK, int DV, bool MLSTM>
; __device__ __forceinline__ void out_unit2(LAS unsigned char* lds, LAS unsigned char* ldstab, const OutArgs a, const int wv) {
;     ...
; #pragma unroll
;     for (int pc = 0; pc < 4; ++pc) {
;         VM_WAIT(); __syncthreads();
;         OUT_DMA(pc + 1);
;         const bf16x8 af0 = pa[2 * pc], af1 = pa[2 * pc + 1];
;         OUT_MMA(pc & 1);
;     }
; #pragma unroll 1
;     for (int pc = 4; pc < 4 + 2 * NCP; ++pc) {
;         VM_WAIT(); __syncthreads();
;         if (pc + 1 < 4 + 2 * NCP) OUT_DMA(pc + 1);
;         const int cq = pc - 4, dirb = cq >= NCP, cp = dirb ? cq - NCP : cq;
;         const float qs = dirb ? qsb : qsf;
;         const unsigned qa = QP + (cp >> 2) * 32768u + 512u * (cp & 3) + 8192u * rb;
;         const bf16x8 af0 = scale_frag(lds_r128(qa + rb0), qs), af1 = scale_frag(lds_r128(qa + rb1), qs);
;         OUT_MMA(pc & 1);
;     }
	s_add_u32 s40, s4, 0x30000
	s_addc_u32 s41, s5, 0
	v_lshl_add_u64 v[128:129], s[40:41], 0, v[198:199]
	v_lshl_add_u64 v[130:131], s[40:41], 0, v[200:201]
	v_lshl_add_u64 v[146:147], s[40:41], 0, v[202:203]
	v_lshl_add_u64 v[148:149], s[40:41], 0, v[204:205]
	s_add_i32 m0, s6, 0x10000
	s_nop 0
	global_load_lds_dwordx4 v[128:129], off
	s_add_i32 m0, s7, 0x10000
	s_nop 0
	global_load_lds_dwordx4 v[130:131], off
	s_add_i32 m0, s36, 0x10000
	s_nop 0
	global_load_lds_dwordx4 v[146:147], off
	s_add_i32 m0, s38, 0x10000
	s_nop 0
	global_load_lds_dwordx4 v[148:149], off
	v_add_u32_e32 v133, s13, v173
	v_add_u32_e32 v135, s13, v177
	ds_read_b128 v[128:131], v133 offset:32768
	ds_read_b128 v[146:149], v135 offset:32768
	s_waitcnt lgkmcnt(0)
	v_lshlrev_b32_e32 v135, 16, v128
	v_and_b32_e32 v137, 0xffff0000, v128
	v_mul_f32_e32 v135, v179, v135
	v_mul_f32_e32 v137, v179, v137
	v_cvt_pk_bf16_f32 v128, v135, v137
	v_lshlrev_b32_e32 v135, 16, v129
	v_and_b32_e32 v137, 0xffff0000, v129
	v_mul_f32_e32 v135, v179, v135
	v_mul_f32_e32 v137, v179, v137
	v_cvt_pk_bf16_f32 v129, v135, v137
	v_lshlrev_b32_e32 v135, 16, v130
	v_and_b32_e32 v137, 0xffff0000, v130
	v_mul_f32_e32 v135, v179, v135
	v_mul_f32_e32 v137, v179, v137
	v_cvt_pk_bf16_f32 v130, v135, v137
	v_lshlrev_b32_e32 v135, 16, v131
	v_and_b32_e32 v137, 0xffff0000, v131
	v_mul_f32_e32 v135, v179, v135
	v_mul_f32_e32 v137, v179, v137
	v_cvt_pk_bf16_f32 v131, v135, v137
	v_lshlrev_b32_e32 v135, 16, v146
	v_and_b32_e32 v137, 0xffff0000, v146
	v_mul_f32_e32 v135, v179, v135
	v_mul_f32_e32 v137, v179, v137
	v_cvt_pk_bf16_f32 v146, v135, v137
	v_lshlrev_b32_e32 v135, 16, v147
	v_and_b32_e32 v137, 0xffff0000, v147
	v_mul_f32_e32 v135, v179, v135
	v_mul_f32_e32 v137, v179, v137
	v_cvt_pk_bf16_f32 v147, v135, v137
	v_lshlrev_b32_e32 v135, 16, v148
	v_and_b32_e32 v137, 0xffff0000, v148
	v_mul_f32_e32 v135, v179, v135
	v_mul_f32_e32 v137, v179, v137
	v_cvt_pk_bf16_f32 v148, v135, v137
	v_lshlrev_b32_e32 v135, 16, v149
	v_and_b32_e32 v137, 0xffff0000, v149
	v_mul_f32_e32 v135, v179, v135
	v_mul_f32_e32 v137, v179, v137
	v_cvt_pk_bf16_f32 v149, v135, v137
	v_add_u32_e32 v133, 0x18000, v175
	ds_read_b64_tr_b16 v[150:151], v133 offset:0
	v_add_u32_e32 v135, 0x18000, v181
	ds_read_b64_tr_b16 v[152:153], v135 offset:0
	ds_read_b64_tr_b16 v[182:183], v133 offset:0x200
	ds_read_b64_tr_b16 v[184:185], v135 offset:0x200
	ds_read_b64_tr_b16 v[186:187], v133 offset:0x400
	ds_read_b64_tr_b16 v[188:189], v135 offset:0x400
	ds_read_b64_tr_b16 v[190:191], v133 offset:0x600
	ds_read_b64_tr_b16 v[192:193], v135 offset:0x600
	s_waitcnt lgkmcnt(0)
	s_nop 0
	v_mfma_f32_32x32x16_bf16 v[16:31], v[128:131], v[150:153], v[16:31]
	ds_read_b64_tr_b16 v[150:151], v133 offset:0x1000
	ds_read_b64_tr_b16 v[152:153], v135 offset:0x1000
	v_mfma_f32_32x32x16_bf16 v[0:15], v[128:131], v[182:185], v[0:15]
	ds_read_b64_tr_b16 v[182:183], v133 offset:0x1200
	ds_read_b64_tr_b16 v[184:185], v135 offset:0x1200
	v_mfma_f32_32x32x16_bf16 v[32:47], v[128:131], v[186:189], v[32:47]
	ds_read_b64_tr_b16 v[186:187], v133 offset:0x1400
	ds_read_b64_tr_b16 v[188:189], v135 offset:0x1400
	ds_read_b64_tr_b16 v[194:195], v133 offset:0x1600
	ds_read_b64_tr_b16 v[196:197], v135 offset:0x1600
	s_waitcnt lgkmcnt(0)
	v_mfma_f32_32x32x16_bf16 v[48:63], v[128:131], v[190:193], v[48:63]
	v_mfma_f32_32x32x16_bf16 v[16:31], v[146:149], v[150:153], v[16:31]
	v_add_u32_e32 v133, 0x2000, v133
	ds_read_b64_tr_b16 v[150:151], v133 offset:0
	v_add_u32_e32 v135, 0x2000, v135
	ds_read_b64_tr_b16 v[152:153], v135 offset:0
	v_mfma_f32_32x32x16_bf16 v[0:15], v[146:149], v[182:185], v[0:15]
	ds_read_b64_tr_b16 v[182:183], v133 offset:0x200
	ds_read_b64_tr_b16 v[184:185], v135 offset:0x200
	v_mfma_f32_32x32x16_bf16 v[32:47], v[146:149], v[186:189], v[32:47]
	ds_read_b64_tr_b16 v[186:187], v133 offset:0x400
	ds_read_b64_tr_b16 v[188:189], v135 offset:0x400
	ds_read_b64_tr_b16 v[190:191], v133 offset:0x600
	ds_read_b64_tr_b16 v[192:193], v135 offset:0x600
	s_waitcnt lgkmcnt(0)
	v_mfma_f32_32x32x16_bf16 v[48:63], v[146:149], v[194:197], v[48:63]
	v_mfma_f32_32x32x16_bf16 v[96:111], v[128:131], v[150:153], v[96:111]
	ds_read_b64_tr_b16 v[150:151], v133 offset:0x1000
	ds_read_b64_tr_b16 v[152:153], v135 offset:0x1000
	v_mfma_f32_32x32x16_bf16 v[112:127], v[128:131], v[182:185], v[112:127]
	ds_read_b64_tr_b16 v[182:183], v133 offset:0x1200
	ds_read_b64_tr_b16 v[184:185], v135 offset:0x1200
	v_mfma_f32_32x32x16_bf16 v[80:95], v[128:131], v[186:189], v[80:95]
	ds_read_b64_tr_b16 v[186:187], v133 offset:0x1400
	ds_read_b64_tr_b16 v[188:189], v135 offset:0x1400
	ds_read_b64_tr_b16 v[194:195], v133 offset:0x1600
	ds_read_b64_tr_b16 v[196:197], v135 offset:0x1600
	s_waitcnt lgkmcnt(0)
	v_mfma_f32_32x32x16_bf16 v[64:79], v[128:131], v[190:193], v[64:79]
	v_mfma_f32_32x32x16_bf16 v[96:111], v[146:149], v[150:153], v[96:111]
	v_mfma_f32_32x32x16_bf16 v[112:127], v[146:149], v[182:185], v[112:127]
	v_mfma_f32_32x32x16_bf16 v[80:95], v[146:149], v[186:189], v[80:95]
	v_mfma_f32_32x32x16_bf16 v[64:79], v[146:149], v[194:197], v[64:79]
	s_waitcnt vmcnt(4) lgkmcnt(0)
	s_barrier
; #define VM_WAIT() asm volatile("s_waitcnt vmcnt(0)" ::: "memory")
; template <int DK, int DV, bool MLSTM>
; __device__ __forceinline__ void out_unit2(LAS unsigned char* lds, LAS unsigned char* ldstab, const OutArgs a, const int wv) {
;     ...
; #pragma unroll
;     for (int pc = 0; pc < 4; ++pc) {
;         VM_WAIT(); __syncthreads();
;         OUT_DMA(pc + 1);
;         const bf16x8 af0 = pa[2 * pc], af1 = pa[2 * pc + 1];
;         OUT_MMA(pc & 1);
;     }
; #pragma unroll 1
;     for (int pc = 4; pc < 4 + 2 * NCP; ++pc) {
;         VM_WAIT(); __syncthreads();
;         if (pc + 1 < 4 + 2 * NCP) OUT_DMA(pc + 1);
;         const int cq = pc - 4, dirb = cq >= NCP, cp = dirb ? cq - NCP : cq;
;         const float qs = dirb ? qsb : qsf;
;         const unsigned qa = QP + (cp >> 2) * 32768u + 512u * (cp & 3) + 8192u * rb;
;         const bf16x8 af0 = scale_frag(lds_r128(qa + rb0), qs), af1 = scale_frag(lds_r128(qa + rb1), qs);
;         OUT_MMA(pc & 1);
;     }
	s_add_u32 s40, s4, 0x38000
	s_addc_u32 s41, s5, 0
	v_lshl_add_u64 v[128:129], s[40:41], 0, v[198:199]
	v_lshl_add_u64 v[130:131], s[40:41], 0, v[200:201]
	v_lshl_add_u64 v[146:147], s[40:41], 0, v[202:203]
	v_lshl_add_u64 v[148:149], s[40:41], 0, v[204:205]
	s_add_i32 m0, s6, 0x18000
	s_nop 0
	global_load_lds_dwordx4 v[128:129], off
	s_add_i32 m0, s7, 0x18000
	s_nop 0
	global_load_lds_dwordx4 v[130:131], off
	s_add_i32 m0, s36, 0x18000
	s_nop 0
	global_load_lds_dwordx4 v[146:147], off
	s_add_i32 m0, s38, 0x18000
	s_nop 0
	global_load_lds_dwordx4 v[148:149], off
	v_add_u32_e32 v133, s13, v173
	v_add_u32_e32 v135, s13, v177
	ds_read_b128 v[128:131], v133 offset:33280
	ds_read_b128 v[146:149], v135 offset:33280
	s_waitcnt lgkmcnt(0)
	v_lshlrev_b32_e32 v135, 16, v128
	v_and_b32_e32 v137, 0xffff0000, v128
	v_mul_f32_e32 v135, v179, v135
	v_mul_f32_e32 v137, v179, v137
	v_cvt_pk_bf16_f32 v128, v135, v137
	v_lshlrev_b32_e32 v135, 16, v129
	v_and_b32_e32 v137, 0xffff0000, v129
	v_mul_f32_e32 v135, v179, v135
	v_mul_f32_e32 v137, v179, v137
	v_cvt_pk_bf16_f32 v129, v135, v137
	v_lshlrev_b32_e32 v135, 16, v130
	v_and_b32_e32 v137, 0xffff0000, v130
	v_mul_f32_e32 v135, v179, v135
	v_mul_f32_e32 v137, v179, v137
	v_cvt_pk_bf16_f32 v130, v135, v137
	v_lshlrev_b32_e32 v135, 16, v131
	v_and_b32_e32 v137, 0xffff0000, v131
	v_mul_f32_e32 v135, v179, v135
	v_mul_f32_e32 v137, v179, v137
	v_cvt_pk_bf16_f32 v131, v135, v137
	v_lshlrev_b32_e32 v135, 16, v146
	v_and_b32_e32 v137, 0xffff0000, v146
	v_mul_f32_e32 v135, v179, v135
	v_mul_f32_e32 v137, v179, v137
	v_cvt_pk_bf16_f32 v146, v135, v137
	v_lshlrev_b32_e32 v135, 16, v147
	v_and_b32_e32 v137, 0xffff0000, v147
	v_mul_f32_e32 v135, v179, v135
	v_mul_f32_e32 v137, v179, v137
	v_cvt_pk_bf16_f32 v147, v135, v137
	v_lshlrev_b32_e32 v135, 16, v148
	v_and_b32_e32 v137, 0xffff0000, v148
	v_mul_f32_e32 v135, v179, v135
	v_mul_f32_e32 v137, v179, v137
	v_cvt_pk_bf16_f32 v148, v135, v137
	v_lshlrev_b32_e32 v135, 16, v149
	v_and_b32_e32 v137, 0xffff0000, v149
	v_mul_f32_e32 v135, v179, v135
	v_mul_f32_e32 v137, v179, v137
	v_cvt_pk_bf16_f32 v149, v135, v137
	v_mov_b32_e32 v133, v175
	ds_read_b64_tr_b16 v[150:151], v133 offset:0
	v_mov_b32_e32 v135, v181
	ds_read_b64_tr_b16 v[152:153], v135 offset:0
	ds_read_b64_tr_b16 v[182:183], v133 offset:0x200
	ds_read_b64_tr_b16 v[184:185], v135 offset:0x200
	ds_read_b64_tr_b16 v[186:187], v133 offset:0x400
	ds_read_b64_tr_b16 v[188:189], v135 offset:0x400
	ds_read_b64_tr_b16 v[190:191], v133 offset:0x600
	ds_read_b64_tr_b16 v[192:193], v135 offset:0x600
	s_waitcnt lgkmcnt(0)
	s_nop 0
	v_mfma_f32_32x32x16_bf16 v[16:31], v[128:131], v[150:153], v[16:31]
	ds_read_b64_tr_b16 v[150:151], v133 offset:0x1000
	ds_read_b64_tr_b16 v[152:153], v135 offset:0x1000
	v_mfma_f32_32x32x16_bf16 v[0:15], v[128:131], v[182:185], v[0:15]
	ds_read_b64_tr_b16 v[182:183], v133 offset:0x1200
	ds_read_b64_tr_b16 v[184:185], v135 offset:0x1200
	v_mfma_f32_32x32x16_bf16 v[32:47], v[128:131], v[186:189], v[32:47]
	ds_read_b64_tr_b16 v[186:187], v133 offset:0x1400
	ds_read_b64_tr_b16 v[188:189], v135 offset:0x1400
	ds_read_b64_tr_b16 v[194:195], v133 offset:0x1600
	ds_read_b64_tr_b16 v[196:197], v135 offset:0x1600
	s_waitcnt lgkmcnt(0)
	v_mfma_f32_32x32x16_bf16 v[48:63], v[128:131], v[190:193], v[48:63]
	v_mfma_f32_32x32x16_bf16 v[16:31], v[146:149], v[150:153], v[16:31]
	v_add_u32_e32 v133, 0x2000, v133
	ds_read_b64_tr_b16 v[150:151], v133 offset:0
	v_add_u32_e32 v135, 0x2000, v135
	ds_read_b64_tr_b16 v[152:153], v135 offset:0
	v_mfma_f32_32x32x16_bf16 v[0:15], v[146:149], v[182:185], v[0:15]
	ds_read_b64_tr_b16 v[182:183], v133 offset:0x200
	ds_read_b64_tr_b16 v[184:185], v135 offset:0x200
	v_mfma_f32_32x32x16_bf16 v[32:47], v[146:149], v[186:189], v[32:47]
	ds_read_b64_tr_b16 v[186:187], v133 offset:0x400
	ds_read_b64_tr_b16 v[188:189], v135 offset:0x400
	ds_read_b64_tr_b16 v[190:191], v133 offset:0x600
	ds_read_b64_tr_b16 v[192:193], v135 offset:0x600
	s_waitcnt lgkmcnt(0)
	v_mfma_f32_32x32x16_bf16 v[48:63], v[146:149], v[194:197], v[48:63]
	v_mfma_f32_32x32x16_bf16 v[96:111], v[128:131], v[150:153], v[96:111]
	ds_read_b64_tr_b16 v[150:151], v133 offset:0x1000
	ds_read_b64_tr_b16 v[152:153], v135 offset:0x1000
	v_mfma_f32_32x32x16_bf16 v[112:127], v[128:131], v[182:185], v[112:127]
	ds_read_b64_tr_b16 v[182:183], v133 offset:0x1200
	ds_read_b64_tr_b16 v[184:185], v135 offset:0x1200
	v_mfma_f32_32x32x16_bf16 v[80:95], v[128:131], v[186:189], v[80:95]
	ds_read_b64_tr_b16 v[186:187], v133 offset:0x1400
	ds_read_b64_tr_b16 v[188:189], v135 offset:0x1400
	ds_read_b64_tr_b16 v[194:195], v133 offset:0x1600
	ds_read_b64_tr_b16 v[196:197], v135 offset:0x1600
	s_waitcnt lgkmcnt(0)
	v_mfma_f32_32x32x16_bf16 v[64:79], v[128:131], v[190:193], v[64:79]
	v_mfma_f32_32x32x16_bf16 v[96:111], v[146:149], v[150:153], v[96:111]
	v_mfma_f32_32x32x16_bf16 v[112:127], v[146:149], v[182:185], v[112:127]
	v_mfma_f32_32x32x16_bf16 v[80:95], v[146:149], v[186:189], v[80:95]
	v_mfma_f32_32x32x16_bf16 v[64:79], v[146:149], v[194:197], v[64:79]
	s_waitcnt vmcnt(4) lgkmcnt(0)
	s_barrier
; #define VM_WAIT() asm volatile("s_waitcnt vmcnt(0)" ::: "memory")
; template <int DK, int DV, bool MLSTM>
; __device__ __forceinline__ void out_unit2(LAS unsigned char* lds, LAS unsigned char* ldstab, const OutArgs a, const int wv) {
;     ...
; #pragma unroll
;     for (int pc = 0; pc < 4; ++pc) {
;         VM_WAIT(); __syncthreads();
;         OUT_DMA(pc + 1);
;         const bf16x8 af0 = pa[2 * pc], af1 = pa[2 * pc + 1];
;         OUT_MMA(pc & 1);
;     }
; #pragma unroll 1
;     for (int pc = 4; pc < 4 + 2 * NCP; ++pc) {
;         VM_WAIT(); __syncthreads();
;         if (pc + 1 < 4 + 2 * NCP) OUT_DMA(pc + 1);
;         const int cq = pc - 4, dirb = cq >= NCP, cp = dirb ? cq - NCP : cq;
;         const float qs = dirb ? qsb : qsf;
;         const unsigned qa = QP + (cp >> 2) * 32768u + 512u * (cp & 3) + 8192u * rb;
;         const bf16x8 af0 = scale_frag(lds_r128(qa + rb0), qs), af1 = scale_frag(lds_r128(qa + rb1), qs);
;         OUT_MMA(pc & 1);
;     }
	s_add_u32 s40, s11, 0x0
	s_addc_u32 s41, s12, 0
	v_lshl_add_u64 v[128:129], s[40:41], 0, v[198:199]
	v_lshl_add_u64 v[130:131], s[40:41], 0, v[200:201]
	v_lshl_add_u64 v[146:147], s[40:41], 0, v[202:203]
	v_lshl_add_u64 v[148:149], s[40:41], 0, v[204:205]
	s_mov_b32 m0, s6
	s_nop 0
	global_load_lds_dwordx4 v[128:129], off
	s_mov_b32 m0, s7
	s_nop 0
	global_load_lds_dwordx4 v[130:131], off
	s_mov_b32 m0, s36
	s_nop 0
	global_load_lds_dwordx4 v[146:147], off
	s_mov_b32 m0, s38
	s_nop 0
	global_load_lds_dwordx4 v[148:149], off
	v_add_u32_e32 v133, s13, v173
	v_add_u32_e32 v135, s13, v177
	ds_read_b128 v[128:131], v133 offset:33792
	ds_read_b128 v[146:149], v135 offset:33792
	s_waitcnt lgkmcnt(0)
	v_lshlrev_b32_e32 v135, 16, v128
	v_and_b32_e32 v137, 0xffff0000, v128
	v_mul_f32_e32 v135, v179, v135
	v_mul_f32_e32 v137, v179, v137
	v_cvt_pk_bf16_f32 v128, v135, v137
	v_lshlrev_b32_e32 v135, 16, v129
	v_and_b32_e32 v137, 0xffff0000, v129
	v_mul_f32_e32 v135, v179, v135
	v_mul_f32_e32 v137, v179, v137
	v_cvt_pk_bf16_f32 v129, v135, v137
	v_lshlrev_b32_e32 v135, 16, v130
	v_and_b32_e32 v137, 0xffff0000, v130
	v_mul_f32_e32 v135, v179, v135
	v_mul_f32_e32 v137, v179, v137
	v_cvt_pk_bf16_f32 v130, v135, v137
	v_lshlrev_b32_e32 v135, 16, v131
	v_and_b32_e32 v137, 0xffff0000, v131
	v_mul_f32_e32 v135, v179, v135
	v_mul_f32_e32 v137, v179, v137
	v_cvt_pk_bf16_f32 v131, v135, v137
	v_lshlrev_b32_e32 v135, 16, v146
	v_and_b32_e32 v137, 0xffff0000, v146
	v_mul_f32_e32 v135, v179, v135
	v_mul_f32_e32 v137, v179, v137
	v_cvt_pk_bf16_f32 v146, v135, v137
	v_lshlrev_b32_e32 v135, 16, v147
	v_and_b32_e32 v137, 0xffff0000, v147
	v_mul_f32_e32 v135, v179, v135
	v_mul_f32_e32 v137, v179, v137
	v_cvt_pk_bf16_f32 v147, v135, v137
	v_lshlrev_b32_e32 v135, 16, v148
	v_and_b32_e32 v137, 0xffff0000, v148
	v_mul_f32_e32 v135, v179, v135
	v_mul_f32_e32 v137, v179, v137
	v_cvt_pk_bf16_f32 v148, v135, v137
	v_lshlrev_b32_e32 v135, 16, v149
	v_and_b32_e32 v137, 0xffff0000, v149
	v_mul_f32_e32 v135, v179, v135
	v_mul_f32_e32 v137, v179, v137
	v_cvt_pk_bf16_f32 v149, v135, v137
	v_add_u32_e32 v133, 0x10000, v175
	ds_read_b64_tr_b16 v[150:151], v133 offset:0
	v_add_u32_e32 v135, 0x10000, v181
	ds_read_b64_tr_b16 v[152:153], v135 offset:0
	ds_read_b64_tr_b16 v[182:183], v133 offset:0x200
	ds_read_b64_tr_b16 v[184:185], v135 offset:0x200
	ds_read_b64_tr_b16 v[186:187], v133 offset:0x400
	ds_read_b64_tr_b16 v[188:189], v135 offset:0x400
	ds_read_b64_tr_b16 v[190:191], v133 offset:0x600
	ds_read_b64_tr_b16 v[192:193], v135 offset:0x600
	s_waitcnt lgkmcnt(0)
	s_nop 0
	v_mfma_f32_32x32x16_bf16 v[16:31], v[128:131], v[150:153], v[16:31]
	ds_read_b64_tr_b16 v[150:151], v133 offset:0x1000
	ds_read_b64_tr_b16 v[152:153], v135 offset:0x1000
	v_mfma_f32_32x32x16_bf16 v[0:15], v[128:131], v[182:185], v[0:15]
	ds_read_b64_tr_b16 v[182:183], v133 offset:0x1200
	ds_read_b64_tr_b16 v[184:185], v135 offset:0x1200
	v_mfma_f32_32x32x16_bf16 v[32:47], v[128:131], v[186:189], v[32:47]
	ds_read_b64_tr_b16 v[186:187], v133 offset:0x1400
	ds_read_b64_tr_b16 v[188:189], v135 offset:0x1400
	ds_read_b64_tr_b16 v[194:195], v133 offset:0x1600
	ds_read_b64_tr_b16 v[196:197], v135 offset:0x1600
	s_waitcnt lgkmcnt(0)
	v_mfma_f32_32x32x16_bf16 v[48:63], v[128:131], v[190:193], v[48:63]
	v_mfma_f32_32x32x16_bf16 v[16:31], v[146:149], v[150:153], v[16:31]
	v_add_u32_e32 v133, 0x2000, v133
	ds_read_b64_tr_b16 v[150:151], v133 offset:0
	v_add_u32_e32 v135, 0x2000, v135
	ds_read_b64_tr_b16 v[152:153], v135 offset:0
	v_mfma_f32_32x32x16_bf16 v[0:15], v[146:149], v[182:185], v[0:15]
	ds_read_b64_tr_b16 v[182:183], v133 offset:0x200
	ds_read_b64_tr_b16 v[184:185], v135 offset:0x200
	v_mfma_f32_32x32x16_bf16 v[32:47], v[146:149], v[186:189], v[32:47]
	ds_read_b64_tr_b16 v[186:187], v133 offset:0x400
	ds_read_b64_tr_b16 v[188:189], v135 offset:0x400
	ds_read_b64_tr_b16 v[190:191], v133 offset:0x600
	ds_read_b64_tr_b16 v[192:193], v135 offset:0x600
	s_waitcnt lgkmcnt(0)
	v_mfma_f32_32x32x16_bf16 v[48:63], v[146:149], v[194:197], v[48:63]
	v_mfma_f32_32x32x16_bf16 v[96:111], v[128:131], v[150:153], v[96:111]
	ds_read_b64_tr_b16 v[150:151], v133 offset:0x1000
	ds_read_b64_tr_b16 v[152:153], v135 offset:0x1000
	v_mfma_f32_32x32x16_bf16 v[112:127], v[128:131], v[182:185], v[112:127]
	ds_read_b64_tr_b16 v[182:183], v133 offset:0x1200
	ds_read_b64_tr_b16 v[184:185], v135 offset:0x1200
	v_mfma_f32_32x32x16_bf16 v[80:95], v[128:131], v[186:189], v[80:95]
	ds_read_b64_tr_b16 v[186:187], v133 offset:0x1400
	ds_read_b64_tr_b16 v[188:189], v135 offset:0x1400
	ds_read_b64_tr_b16 v[194:195], v133 offset:0x1600
	ds_read_b64_tr_b16 v[196:197], v135 offset:0x1600
	s_waitcnt lgkmcnt(0)
	v_mfma_f32_32x32x16_bf16 v[64:79], v[128:131], v[190:193], v[64:79]
	v_mfma_f32_32x32x16_bf16 v[96:111], v[146:149], v[150:153], v[96:111]
	v_mfma_f32_32x32x16_bf16 v[112:127], v[146:149], v[182:185], v[112:127]
	v_mfma_f32_32x32x16_bf16 v[80:95], v[146:149], v[186:189], v[80:95]
	v_mfma_f32_32x32x16_bf16 v[64:79], v[146:149], v[194:197], v[64:79]
	s_waitcnt vmcnt(4) lgkmcnt(0)
	s_barrier
; #define VM_WAIT() asm volatile("s_waitcnt vmcnt(0)" ::: "memory")
; template <int DK, int DV, bool MLSTM>
; __device__ __forceinline__ void out_unit2(LAS unsigned char* lds, LAS unsigned char* ldstab, const OutArgs a, const int wv) {
;     ...
; #pragma unroll
;     for (int pc = 0; pc < 4; ++pc) {
;         VM_WAIT(); __syncthreads();
;         OUT_DMA(pc + 1);
;         const bf16x8 af0 = pa[2 * pc], af1 = pa[2 * pc + 1];
;         OUT_MMA(pc & 1);
;     }
; #pragma unroll 1
;     for (int pc = 4; pc < 4 + 2 * NCP; ++pc) {
;         VM_WAIT(); __syncthreads();
;         if (pc + 1 < 4 + 2 * NCP) OUT_DMA(pc + 1);
;         const int cq = pc - 4, dirb = cq >= NCP, cp = dirb ? cq - NCP : cq;
;         const float qs = dirb ? qsb : qsf;
;         const unsigned qa = QP + (cp >> 2) * 32768u + 512u * (cp & 3) + 8192u * rb;
;         const bf16x8 af0 = scale_frag(lds_r128(qa + rb0), qs), af1 = scale_frag(lds_r128(qa + rb1), qs);
;         OUT_MMA(pc & 1);
;     }
	s_add_u32 s40, s11, 0x8000
	s_addc_u32 s41, s12, 0
	v_lshl_add_u64 v[128:129], s[40:41], 0, v[198:199]
	v_lshl_add_u64 v[130:131], s[40:41], 0, v[200:201]
	v_lshl_add_u64 v[146:147], s[40:41], 0, v[202:203]
	v_lshl_add_u64 v[148:149], s[40:41], 0, v[204:205]
	s_add_i32 m0, s6, 0x10000
	s_nop 0
	global_load_lds_dwordx4 v[128:129], off
	s_add_i32 m0, s7, 0x10000
	s_nop 0
	global_load_lds_dwordx4 v[130:131], off
	s_add_i32 m0, s36, 0x10000
	s_nop 0
	global_load_lds_dwordx4 v[146:147], off
	s_add_i32 m0, s38, 0x10000
	s_nop 0
	global_load_lds_dwordx4 v[148:149], off
	v_add_u32_e32 v133, s13, v173
	v_add_u32_e32 v135, s13, v177
	ds_read_b128 v[128:131], v133 offset:34304
	ds_read_b128 v[146:149], v135 offset:34304
	s_waitcnt lgkmcnt(0)
	v_lshlrev_b32_e32 v135, 16, v128
	v_and_b32_e32 v137, 0xffff0000, v128
	v_mul_f32_e32 v135, v179, v135
	v_mul_f32_e32 v137, v179, v137
	v_cvt_pk_bf16_f32 v128, v135, v137
	v_lshlrev_b32_e32 v135, 16, v129
	v_and_b32_e32 v137, 0xffff0000, v129
	v_mul_f32_e32 v135, v179, v135
	v_mul_f32_e32 v137, v179, v137
	v_cvt_pk_bf16_f32 v129, v135, v137
	v_lshlrev_b32_e32 v135, 16, v130
	v_and_b32_e32 v137, 0xffff0000, v130
	v_mul_f32_e32 v135, v179, v135
	v_mul_f32_e32 v137, v179, v137
	v_cvt_pk_bf16_f32 v130, v135, v137
	v_lshlrev_b32_e32 v135, 16, v131
	v_and_b32_e32 v137, 0xffff0000, v131
	v_mul_f32_e32 v135, v179, v135
	v_mul_f32_e32 v137, v179, v137
	v_cvt_pk_bf16_f32 v131, v135, v137
	v_lshlrev_b32_e32 v135, 16, v146
	v_and_b32_e32 v137, 0xffff0000, v146
	v_mul_f32_e32 v135, v179, v135
	v_mul_f32_e32 v137, v179, v137
	v_cvt_pk_bf16_f32 v146, v135, v137
	v_lshlrev_b32_e32 v135, 16, v147
	v_and_b32_e32 v137, 0xffff0000, v147
	v_mul_f32_e32 v135, v179, v135
	v_mul_f32_e32 v137, v179, v137
	v_cvt_pk_bf16_f32 v147, v135, v137
	v_lshlrev_b32_e32 v135, 16, v148
	v_and_b32_e32 v137, 0xffff0000, v148
	v_mul_f32_e32 v135, v179, v135
	v_mul_f32_e32 v137, v179, v137
	v_cvt_pk_bf16_f32 v148, v135, v137
	v_lshlrev_b32_e32 v135, 16, v149
	v_and_b32_e32 v137, 0xffff0000, v149
	v_mul_f32_e32 v135, v179, v135
	v_mul_f32_e32 v137, v179, v137
	v_cvt_pk_bf16_f32 v149, v135, v137
	v_add_u32_e32 v133, 0x18000, v175
	ds_read_b64_tr_b16 v[150:151], v133 offset:0
	v_add_u32_e32 v135, 0x18000, v181
	ds_read_b64_tr_b16 v[152:153], v135 offset:0
	ds_read_b64_tr_b16 v[182:183], v133 offset:0x200
	ds_read_b64_tr_b16 v[184:185], v135 offset:0x200
	ds_read_b64_tr_b16 v[186:187], v133 offset:0x400
	ds_read_b64_tr_b16 v[188:189], v135 offset:0x400
	ds_read_b64_tr_b16 v[190:191], v133 offset:0x600
	ds_read_b64_tr_b16 v[192:193], v135 offset:0x600
	s_waitcnt lgkmcnt(0)
	s_nop 0
	v_mfma_f32_32x32x16_bf16 v[16:31], v[128:131], v[150:153], v[16:31]
	ds_read_b64_tr_b16 v[150:151], v133 offset:0x1000
	ds_read_b64_tr_b16 v[152:153], v135 offset:0x1000
	v_mfma_f32_32x32x16_bf16 v[0:15], v[128:131], v[182:185], v[0:15]
	ds_read_b64_tr_b16 v[182:183], v133 offset:0x1200
	ds_read_b64_tr_b16 v[184:185], v135 offset:0x1200
	v_mfma_f32_32x32x16_bf16 v[32:47], v[128:131], v[186:189], v[32:47]
	ds_read_b64_tr_b16 v[186:187], v133 offset:0x1400
	ds_read_b64_tr_b16 v[188:189], v135 offset:0x1400
	ds_read_b64_tr_b16 v[194:195], v133 offset:0x1600
	ds_read_b64_tr_b16 v[196:197], v135 offset:0x1600
	s_waitcnt lgkmcnt(0)
	v_mfma_f32_32x32x16_bf16 v[48:63], v[128:131], v[190:193], v[48:63]
	v_mfma_f32_32x32x16_bf16 v[16:31], v[146:149], v[150:153], v[16:31]
	v_add_u32_e32 v133, 0x2000, v133
	ds_read_b64_tr_b16 v[150:151], v133 offset:0
	v_add_u32_e32 v135, 0x2000, v135
	ds_read_b64_tr_b16 v[152:153], v135 offset:0
	v_mfma_f32_32x32x16_bf16 v[0:15], v[146:149], v[182:185], v[0:15]
	ds_read_b64_tr_b16 v[182:183], v133 offset:0x200
	ds_read_b64_tr_b16 v[184:185], v135 offset:0x200
	v_mfma_f32_32x32x16_bf16 v[32:47], v[146:149], v[186:189], v[32:47]
	ds_read_b64_tr_b16 v[186:187], v133 offset:0x400
	ds_read_b64_tr_b16 v[188:189], v135 offset:0x400
	ds_read_b64_tr_b16 v[190:191], v133 offset:0x600
	ds_read_b64_tr_b16 v[192:193], v135 offset:0x600
	s_waitcnt lgkmcnt(0)
	v_mfma_f32_32x32x16_bf16 v[48:63], v[146:149], v[194:197], v[48:63]
	v_mfma_f32_32x32x16_bf16 v[96:111], v[128:131], v[150:153], v[96:111]
	ds_read_b64_tr_b16 v[150:151], v133 offset:0x1000
	ds_read_b64_tr_b16 v[152:153], v135 offset:0x1000
	v_mfma_f32_32x32x16_bf16 v[112:127], v[128:131], v[182:185], v[112:127]
	ds_read_b64_tr_b16 v[182:183], v133 offset:0x1200
	ds_read_b64_tr_b16 v[184:185], v135 offset:0x1200
	v_mfma_f32_32x32x16_bf16 v[80:95], v[128:131], v[186:189], v[80:95]
	ds_read_b64_tr_b16 v[186:187], v133 offset:0x1400
	ds_read_b64_tr_b16 v[188:189], v135 offset:0x1400
	ds_read_b64_tr_b16 v[194:195], v133 offset:0x1600
	ds_read_b64_tr_b16 v[196:197], v135 offset:0x1600
	s_waitcnt lgkmcnt(0)
	v_mfma_f32_32x32x16_bf16 v[64:79], v[128:131], v[190:193], v[64:79]
	v_mfma_f32_32x32x16_bf16 v[96:111], v[146:149], v[150:153], v[96:111]
	v_mfma_f32_32x32x16_bf16 v[112:127], v[146:149], v[182:185], v[112:127]
	v_mfma_f32_32x32x16_bf16 v[80:95], v[146:149], v[186:189], v[80:95]
	v_mfma_f32_32x32x16_bf16 v[64:79], v[146:149], v[194:197], v[64:79]
	s_waitcnt vmcnt(4) lgkmcnt(0)
	s_barrier
; #define VM_WAIT() asm volatile("s_waitcnt vmcnt(0)" ::: "memory")
; template <int DK, int DV, bool MLSTM>
; __device__ __forceinline__ void out_unit2(LAS unsigned char* lds, LAS unsigned char* ldstab, const OutArgs a, const int wv) {
;     ...
; #pragma unroll
;     for (int pc = 0; pc < 4; ++pc) {
;         VM_WAIT(); __syncthreads();
;         OUT_DMA(pc + 1);
;         const bf16x8 af0 = pa[2 * pc], af1 = pa[2 * pc + 1];
;         OUT_MMA(pc & 1);
;     }
; #pragma unroll 1
;     for (int pc = 4; pc < 4 + 2 * NCP; ++pc) {
;         VM_WAIT(); __syncthreads();
;         if (pc + 1 < 4 + 2 * NCP) OUT_DMA(pc + 1);
;         const int cq = pc - 4, dirb = cq >= NCP, cp = dirb ? cq - NCP : cq;
;         const float qs = dirb ? qsb : qsf;
;         const unsigned qa = QP + (cp >> 2) * 32768u + 512u * (cp & 3) + 8192u * rb;
;         const bf16x8 af0 = scale_frag(lds_r128(qa + rb0), qs), af1 = scale_frag(lds_r128(qa + rb1), qs);
;         OUT_MMA(pc & 1);
;     }
	s_add_u32 s40, s11, 0x10000
	s_addc_u32 s41, s12, 0
	v_lshl_add_u64 v[128:129], s[40:41], 0, v[198:199]
	v_lshl_add_u64 v[130:131], s[40:41], 0, v[200:201]
	v_lshl_add_u64 v[146:147], s[40:41], 0, v[202:203]
	v_lshl_add_u64 v[148:149], s[40:41], 0, v[204:205]
	s_add_i32 m0, s6, 0x18000
	s_nop 0
	global_load_lds_dwordx4 v[128:129], off
	s_add_i32 m0, s7, 0x18000
	s_nop 0
	global_load_lds_dwordx4 v[130:131], off
	s_add_i32 m0, s36, 0x18000
	s_nop 0
	global_load_lds_dwordx4 v[146:147], off
	s_add_i32 m0, s38, 0x18000
	s_nop 0
	global_load_lds_dwordx4 v[148:149], off
	v_lshlrev_b32_e32 v135, 16, v236
	v_and_b32_e32 v137, 0xffff0000, v236
	v_mul_f32_e32 v135, v144, v135
	v_mul_f32_e32 v137, v144, v137
	v_cvt_pk_bf16_f32 v128, v135, v137
	v_lshlrev_b32_e32 v135, 16, v237
	v_and_b32_e32 v137, 0xffff0000, v237
	v_mul_f32_e32 v135, v144, v135
	v_mul_f32_e32 v137, v144, v137
	v_cvt_pk_bf16_f32 v129, v135, v137
	v_lshlrev_b32_e32 v135, 16, v238
	v_and_b32_e32 v137, 0xffff0000, v238
	v_mul_f32_e32 v135, v144, v135
	v_mul_f32_e32 v137, v144, v137
	v_cvt_pk_bf16_f32 v130, v135, v137
	v_lshlrev_b32_e32 v135, 16, v239
	v_and_b32_e32 v137, 0xffff0000, v239
	v_mul_f32_e32 v135, v144, v135
	v_mul_f32_e32 v137, v144, v137
	v_cvt_pk_bf16_f32 v131, v135, v137
	v_lshlrev_b32_e32 v135, 16, v240
	v_and_b32_e32 v137, 0xffff0000, v240
	v_mul_f32_e32 v135, v144, v135
	v_mul_f32_e32 v137, v144, v137
	v_cvt_pk_bf16_f32 v146, v135, v137
	v_lshlrev_b32_e32 v135, 16, v241
	v_and_b32_e32 v137, 0xffff0000, v241
	v_mul_f32_e32 v135, v144, v135
	v_mul_f32_e32 v137, v144, v137
	v_cvt_pk_bf16_f32 v147, v135, v137
	v_lshlrev_b32_e32 v135, 16, v242
	v_and_b32_e32 v137, 0xffff0000, v242
	v_mul_f32_e32 v135, v144, v135
	v_mul_f32_e32 v137, v144, v137
	v_cvt_pk_bf16_f32 v148, v135, v137
	v_lshlrev_b32_e32 v135, 16, v243
	v_and_b32_e32 v137, 0xffff0000, v243
	v_mul_f32_e32 v135, v144, v135
	v_mul_f32_e32 v137, v144, v137
	v_cvt_pk_bf16_f32 v149, v135, v137
	v_mov_b32_e32 v133, v175
	ds_read_b64_tr_b16 v[150:151], v133 offset:0
	v_mov_b32_e32 v135, v181
	ds_read_b64_tr_b16 v[152:153], v135 offset:0
	ds_read_b64_tr_b16 v[182:183], v133 offset:0x200
	ds_read_b64_tr_b16 v[184:185], v135 offset:0x200
	ds_read_b64_tr_b16 v[186:187], v133 offset:0x400
	ds_read_b64_tr_b16 v[188:189], v135 offset:0x400
	ds_read_b64_tr_b16 v[190:191], v133 offset:0x600
	ds_read_b64_tr_b16 v[192:193], v135 offset:0x600
	s_waitcnt lgkmcnt(0)
	s_nop 0
	v_mfma_f32_32x32x16_bf16 v[16:31], v[128:131], v[150:153], v[16:31]
	ds_read_b64_tr_b16 v[150:151], v133 offset:0x1000
	ds_read_b64_tr_b16 v[152:153], v135 offset:0x1000
	v_mfma_f32_32x32x16_bf16 v[0:15], v[128:131], v[182:185], v[0:15]
	ds_read_b64_tr_b16 v[182:183], v133 offset:0x1200
	ds_read_b64_tr_b16 v[184:185], v135 offset:0x1200
	v_mfma_f32_32x32x16_bf16 v[32:47], v[128:131], v[186:189], v[32:47]
	ds_read_b64_tr_b16 v[186:187], v133 offset:0x1400
	ds_read_b64_tr_b16 v[188:189], v135 offset:0x1400
	ds_read_b64_tr_b16 v[194:195], v133 offset:0x1600
	ds_read_b64_tr_b16 v[196:197], v135 offset:0x1600
	s_waitcnt lgkmcnt(0)
	v_mfma_f32_32x32x16_bf16 v[48:63], v[128:131], v[190:193], v[48:63]
	v_mfma_f32_32x32x16_bf16 v[16:31], v[146:149], v[150:153], v[16:31]
	v_add_u32_e32 v133, 0x2000, v133
	ds_read_b64_tr_b16 v[150:151], v133 offset:0
	v_add_u32_e32 v135, 0x2000, v135
	ds_read_b64_tr_b16 v[152:153], v135 offset:0
	v_mfma_f32_32x32x16_bf16 v[0:15], v[146:149], v[182:185], v[0:15]
	ds_read_b64_tr_b16 v[182:183], v133 offset:0x200
	ds_read_b64_tr_b16 v[184:185], v135 offset:0x200
	v_mfma_f32_32x32x16_bf16 v[32:47], v[146:149], v[186:189], v[32:47]
	ds_read_b64_tr_b16 v[186:187], v133 offset:0x400
	ds_read_b64_tr_b16 v[188:189], v135 offset:0x400
	ds_read_b64_tr_b16 v[190:191], v133 offset:0x600
	ds_read_b64_tr_b16 v[192:193], v135 offset:0x600
	s_waitcnt lgkmcnt(0)
	v_mfma_f32_32x32x16_bf16 v[48:63], v[146:149], v[194:197], v[48:63]
	v_mfma_f32_32x32x16_bf16 v[96:111], v[128:131], v[150:153], v[96:111]
	ds_read_b64_tr_b16 v[150:151], v133 offset:0x1000
	ds_read_b64_tr_b16 v[152:153], v135 offset:0x1000
	v_mfma_f32_32x32x16_bf16 v[112:127], v[128:131], v[182:185], v[112:127]
	ds_read_b64_tr_b16 v[182:183], v133 offset:0x1200
	ds_read_b64_tr_b16 v[184:185], v135 offset:0x1200
	v_mfma_f32_32x32x16_bf16 v[80:95], v[128:131], v[186:189], v[80:95]
	ds_read_b64_tr_b16 v[186:187], v133 offset:0x1400
	ds_read_b64_tr_b16 v[188:189], v135 offset:0x1400
	ds_read_b64_tr_b16 v[194:195], v133 offset:0x1600
	ds_read_b64_tr_b16 v[196:197], v135 offset:0x1600
	s_waitcnt lgkmcnt(0)
	v_mfma_f32_32x32x16_bf16 v[64:79], v[128:131], v[190:193], v[64:79]
	v_mfma_f32_32x32x16_bf16 v[96:111], v[146:149], v[150:153], v[96:111]
	v_mfma_f32_32x32x16_bf16 v[112:127], v[146:149], v[182:185], v[112:127]
	v_mfma_f32_32x32x16_bf16 v[80:95], v[146:149], v[186:189], v[80:95]
	v_mfma_f32_32x32x16_bf16 v[64:79], v[146:149], v[194:197], v[64:79]
	s_waitcnt vmcnt(4) lgkmcnt(0)
	s_barrier
; #define VM_WAIT() asm volatile("s_waitcnt vmcnt(0)" ::: "memory")
; template <int DK, int DV, bool MLSTM>
; __device__ __forceinline__ void out_unit2(LAS unsigned char* lds, LAS unsigned char* ldstab, const OutArgs a, const int wv) {
;     ...
; #pragma unroll
;     for (int pc = 0; pc < 4; ++pc) {
;         VM_WAIT(); __syncthreads();
;         OUT_DMA(pc + 1);
;         const bf16x8 af0 = pa[2 * pc], af1 = pa[2 * pc + 1];
;         OUT_MMA(pc & 1);
;     }
; #pragma unroll 1
;     for (int pc = 4; pc < 4 + 2 * NCP; ++pc) {
;         VM_WAIT(); __syncthreads();
;         if (pc + 1 < 4 + 2 * NCP) OUT_DMA(pc + 1);
;         const int cq = pc - 4, dirb = cq >= NCP, cp = dirb ? cq - NCP : cq;
;         const float qs = dirb ? qsb : qsf;
;         const unsigned qa = QP + (cp >> 2) * 32768u + 512u * (cp & 3) + 8192u * rb;
;         const bf16x8 af0 = scale_frag(lds_r128(qa + rb0), qs), af1 = scale_frag(lds_r128(qa + rb1), qs);
;         OUT_MMA(pc & 1);
;     }
	s_add_u32 s40, s11, 0x18000
	s_addc_u32 s41, s12, 0
	v_lshl_add_u64 v[128:129], s[40:41], 0, v[198:199]
	v_lshl_add_u64 v[130:131], s[40:41], 0, v[200:201]
	v_lshl_add_u64 v[146:147], s[40:41], 0, v[202:203]
	v_lshl_add_u64 v[148:149], s[40:41], 0, v[204:205]
	s_mov_b32 m0, s6
	s_nop 0
	global_load_lds_dwordx4 v[128:129], off
	s_mov_b32 m0, s7
	s_nop 0
	global_load_lds_dwordx4 v[130:131], off
	s_mov_b32 m0, s36
	s_nop 0
	global_load_lds_dwordx4 v[146:147], off
	s_mov_b32 m0, s38
	s_nop 0
	global_load_lds_dwordx4 v[148:149], off
	v_lshlrev_b32_e32 v135, 16, v244
	v_and_b32_e32 v137, 0xffff0000, v244
	v_mul_f32_e32 v135, v144, v135
	v_mul_f32_e32 v137, v144, v137
	v_cvt_pk_bf16_f32 v128, v135, v137
	v_lshlrev_b32_e32 v135, 16, v245
	v_and_b32_e32 v137, 0xffff0000, v245
	v_mul_f32_e32 v135, v144, v135
	v_mul_f32_e32 v137, v144, v137
	v_cvt_pk_bf16_f32 v129, v135, v137
	v_lshlrev_b32_e32 v135, 16, v246
	v_and_b32_e32 v137, 0xffff0000, v246
	v_mul_f32_e32 v135, v144, v135
	v_mul_f32_e32 v137, v144, v137
	v_cvt_pk_bf16_f32 v130, v135, v137
	v_lshlrev_b32_e32 v135, 16, v247
	v_and_b32_e32 v137, 0xffff0000, v247
	v_mul_f32_e32 v135, v144, v135
	v_mul_f32_e32 v137, v144, v137
	v_cvt_pk_bf16_f32 v131, v135, v137
	v_lshlrev_b32_e32 v135, 16, v248
	v_and_b32_e32 v137, 0xffff0000, v248
	v_mul_f32_e32 v135, v144, v135
	v_mul_f32_e32 v137, v144, v137
	v_cvt_pk_bf16_f32 v146, v135, v137
	v_lshlrev_b32_e32 v135, 16, v249
	v_and_b32_e32 v137, 0xffff0000, v249
	v_mul_f32_e32 v135, v144, v135
	v_mul_f32_e32 v137, v144, v137
	v_cvt_pk_bf16_f32 v147, v135, v137
	v_lshlrev_b32_e32 v135, 16, v250
	v_and_b32_e32 v137, 0xffff0000, v250
	v_mul_f32_e32 v135, v144, v135
	v_mul_f32_e32 v137, v144, v137
	v_cvt_pk_bf16_f32 v148, v135, v137
	v_lshlrev_b32_e32 v135, 16, v251
	v_and_b32_e32 v137, 0xffff0000, v251
	v_mul_f32_e32 v135, v144, v135
	v_mul_f32_e32 v137, v144, v137
	v_cvt_pk_bf16_f32 v149, v135, v137
	v_add_u32_e32 v133, 0x10000, v175
	ds_read_b64_tr_b16 v[150:151], v133 offset:0
	v_add_u32_e32 v135, 0x10000, v181
	ds_read_b64_tr_b16 v[152:153], v135 offset:0
	ds_read_b64_tr_b16 v[182:183], v133 offset:0x200
	ds_read_b64_tr_b16 v[184:185], v135 offset:0x200
	ds_read_b64_tr_b16 v[186:187], v133 offset:0x400
	ds_read_b64_tr_b16 v[188:189], v135 offset:0x400
	ds_read_b64_tr_b16 v[190:191], v133 offset:0x600
	ds_read_b64_tr_b16 v[192:193], v135 offset:0x600
	s_waitcnt lgkmcnt(0)
	s_nop 0
	v_mfma_f32_32x32x16_bf16 v[16:31], v[128:131], v[150:153], v[16:31]
	ds_read_b64_tr_b16 v[150:151], v133 offset:0x1000
	ds_read_b64_tr_b16 v[152:153], v135 offset:0x1000
	v_mfma_f32_32x32x16_bf16 v[0:15], v[128:131], v[182:185], v[0:15]
	ds_read_b64_tr_b16 v[182:183], v133 offset:0x1200
	ds_read_b64_tr_b16 v[184:185], v135 offset:0x1200
	v_mfma_f32_32x32x16_bf16 v[32:47], v[128:131], v[186:189], v[32:47]
	ds_read_b64_tr_b16 v[186:187], v133 offset:0x1400
	ds_read_b64_tr_b16 v[188:189], v135 offset:0x1400
	ds_read_b64_tr_b16 v[194:195], v133 offset:0x1600
	ds_read_b64_tr_b16 v[196:197], v135 offset:0x1600
	s_waitcnt lgkmcnt(0)
	v_mfma_f32_32x32x16_bf16 v[48:63], v[128:131], v[190:193], v[48:63]
	v_mfma_f32_32x32x16_bf16 v[16:31], v[146:149], v[150:153], v[16:31]
	v_add_u32_e32 v133, 0x2000, v133
	ds_read_b64_tr_b16 v[150:151], v133 offset:0
	v_add_u32_e32 v135, 0x2000, v135
	ds_read_b64_tr_b16 v[152:153], v135 offset:0
	v_mfma_f32_32x32x16_bf16 v[0:15], v[146:149], v[182:185], v[0:15]
	ds_read_b64_tr_b16 v[182:183], v133 offset:0x200
	ds_read_b64_tr_b16 v[184:185], v135 offset:0x200
	v_mfma_f32_32x32x16_bf16 v[32:47], v[146:149], v[186:189], v[32:47]
	ds_read_b64_tr_b16 v[186:187], v133 offset:0x400
	ds_read_b64_tr_b16 v[188:189], v135 offset:0x400
	ds_read_b64_tr_b16 v[190:191], v133 offset:0x600
	ds_read_b64_tr_b16 v[192:193], v135 offset:0x600
	s_waitcnt lgkmcnt(0)
	v_mfma_f32_32x32x16_bf16 v[48:63], v[146:149], v[194:197], v[48:63]
	v_mfma_f32_32x32x16_bf16 v[96:111], v[128:131], v[150:153], v[96:111]
	ds_read_b64_tr_b16 v[150:151], v133 offset:0x1000
	ds_read_b64_tr_b16 v[152:153], v135 offset:0x1000
	v_mfma_f32_32x32x16_bf16 v[112:127], v[128:131], v[182:185], v[112:127]
	ds_read_b64_tr_b16 v[182:183], v133 offset:0x1200
	ds_read_b64_tr_b16 v[184:185], v135 offset:0x1200
	v_mfma_f32_32x32x16_bf16 v[80:95], v[128:131], v[186:189], v[80:95]
	ds_read_b64_tr_b16 v[186:187], v133 offset:0x1400
	ds_read_b64_tr_b16 v[188:189], v135 offset:0x1400
	ds_read_b64_tr_b16 v[194:195], v133 offset:0x1600
	ds_read_b64_tr_b16 v[196:197], v135 offset:0x1600
	s_waitcnt lgkmcnt(0)
	v_mfma_f32_32x32x16_bf16 v[64:79], v[128:131], v[190:193], v[64:79]
	v_mfma_f32_32x32x16_bf16 v[96:111], v[146:149], v[150:153], v[96:111]
	v_mfma_f32_32x32x16_bf16 v[112:127], v[146:149], v[182:185], v[112:127]
	v_mfma_f32_32x32x16_bf16 v[80:95], v[146:149], v[186:189], v[80:95]
	v_mfma_f32_32x32x16_bf16 v[64:79], v[146:149], v[194:197], v[64:79]
	s_waitcnt vmcnt(4) lgkmcnt(0)
	s_barrier
; #define VM_WAIT() asm volatile("s_waitcnt vmcnt(0)" ::: "memory")
; template <int DK, int DV, bool MLSTM>
; __device__ __forceinline__ void out_unit2(LAS unsigned char* lds, LAS unsigned char* ldstab, const OutArgs a, const int wv) {
;     ...
; #pragma unroll
;     for (int pc = 0; pc < 4; ++pc) {
;         VM_WAIT(); __syncthreads();
;         OUT_DMA(pc + 1);
;         const bf16x8 af0 = pa[2 * pc], af1 = pa[2 * pc + 1];
;         OUT_MMA(pc & 1);
;     }
; #pragma unroll 1
;     for (int pc = 4; pc < 4 + 2 * NCP; ++pc) {
;         VM_WAIT(); __syncthreads();
;         if (pc + 1 < 4 + 2 * NCP) OUT_DMA(pc + 1);
;         const int cq = pc - 4, dirb = cq >= NCP, cp = dirb ? cq - NCP : cq;
;         const float qs = dirb ? qsb : qsf;
;         const unsigned qa = QP + (cp >> 2) * 32768u + 512u * (cp & 3) + 8192u * rb;
;         const bf16x8 af0 = scale_frag(lds_r128(qa + rb0), qs), af1 = scale_frag(lds_r128(qa + rb1), qs);
;         OUT_MMA(pc & 1);
;     }
	s_add_u32 s40, s11, 0x20000
	s_addc_u32 s41, s12, 0
	v_lshl_add_u64 v[128:129], s[40:41], 0, v[198:199]
	v_lshl_add_u64 v[130:131], s[40:41], 0, v[200:201]
	v_lshl_add_u64 v[146:147], s[40:41], 0, v[202:203]
	v_lshl_add_u64 v[148:149], s[40:41], 0, v[204:205]
	s_add_i32 m0, s6, 0x10000
	s_nop 0
	global_load_lds_dwordx4 v[128:129], off
	s_add_i32 m0, s7, 0x10000
	s_nop 0
	global_load_lds_dwordx4 v[130:131], off
	s_add_i32 m0, s36, 0x10000
	s_nop 0
	global_load_lds_dwordx4 v[146:147], off
	s_add_i32 m0, s38, 0x10000
	s_nop 0
	global_load_lds_dwordx4 v[148:149], off
	v_lshlrev_b32_e32 v135, 16, v252
	v_and_b32_e32 v137, 0xffff0000, v252
	v_mul_f32_e32 v135, v144, v135
	v_mul_f32_e32 v137, v144, v137
	v_cvt_pk_bf16_f32 v128, v135, v137
	v_lshlrev_b32_e32 v135, 16, v253
	v_and_b32_e32 v137, 0xffff0000, v253
	v_mul_f32_e32 v135, v144, v135
	v_mul_f32_e32 v137, v144, v137
	v_cvt_pk_bf16_f32 v129, v135, v137
	v_lshlrev_b32_e32 v135, 16, v254
	v_and_b32_e32 v137, 0xffff0000, v254
	v_mul_f32_e32 v135, v144, v135
	v_mul_f32_e32 v137, v144, v137
	v_cvt_pk_bf16_f32 v130, v135, v137
	v_lshlrev_b32_e32 v135, 16, v255
	v_and_b32_e32 v137, 0xffff0000, v255
	v_mul_f32_e32 v135, v144, v135
	v_mul_f32_e32 v137, v144, v137
	v_cvt_pk_bf16_f32 v131, v135, v137
	v_lshlrev_b32_e32 v135, 16, v218
	v_and_b32_e32 v137, 0xffff0000, v218
	v_mul_f32_e32 v135, v144, v135
	v_mul_f32_e32 v137, v144, v137
	v_cvt_pk_bf16_f32 v146, v135, v137
	v_lshlrev_b32_e32 v135, 16, v219
	v_and_b32_e32 v137, 0xffff0000, v219
	v_mul_f32_e32 v135, v144, v135
	v_mul_f32_e32 v137, v144, v137
	v_cvt_pk_bf16_f32 v147, v135, v137
	v_lshlrev_b32_e32 v135, 16, v220
	v_and_b32_e32 v137, 0xffff0000, v220
	v_mul_f32_e32 v135, v144, v135
	v_mul_f32_e32 v137, v144, v137
	v_cvt_pk_bf16_f32 v148, v135, v137
	v_lshlrev_b32_e32 v135, 16, v221
	v_and_b32_e32 v137, 0xffff0000, v221
	v_mul_f32_e32 v135, v144, v135
	v_mul_f32_e32 v137, v144, v137
	v_cvt_pk_bf16_f32 v149, v135, v137
	v_add_u32_e32 v133, 0x18000, v175
	ds_read_b64_tr_b16 v[150:151], v133 offset:0
	v_add_u32_e32 v135, 0x18000, v181
	ds_read_b64_tr_b16 v[152:153], v135 offset:0
	ds_read_b64_tr_b16 v[182:183], v133 offset:0x200
	ds_read_b64_tr_b16 v[184:185], v135 offset:0x200
	ds_read_b64_tr_b16 v[186:187], v133 offset:0x400
	ds_read_b64_tr_b16 v[188:189], v135 offset:0x400
	ds_read_b64_tr_b16 v[190:191], v133 offset:0x600
	ds_read_b64_tr_b16 v[192:193], v135 offset:0x600
	s_waitcnt lgkmcnt(0)
	s_nop 0
	v_mfma_f32_32x32x16_bf16 v[16:31], v[128:131], v[150:153], v[16:31]
	ds_read_b64_tr_b16 v[150:151], v133 offset:0x1000
	ds_read_b64_tr_b16 v[152:153], v135 offset:0x1000
	v_mfma_f32_32x32x16_bf16 v[0:15], v[128:131], v[182:185], v[0:15]
	ds_read_b64_tr_b16 v[182:183], v133 offset:0x1200
	ds_read_b64_tr_b16 v[184:185], v135 offset:0x1200
	v_mfma_f32_32x32x16_bf16 v[32:47], v[128:131], v[186:189], v[32:47]
	ds_read_b64_tr_b16 v[186:187], v133 offset:0x1400
	ds_read_b64_tr_b16 v[188:189], v135 offset:0x1400
	ds_read_b64_tr_b16 v[194:195], v133 offset:0x1600
	ds_read_b64_tr_b16 v[196:197], v135 offset:0x1600
	s_waitcnt lgkmcnt(0)
	v_mfma_f32_32x32x16_bf16 v[48:63], v[128:131], v[190:193], v[48:63]
	v_mfma_f32_32x32x16_bf16 v[16:31], v[146:149], v[150:153], v[16:31]
	v_add_u32_e32 v133, 0x2000, v133
	ds_read_b64_tr_b16 v[150:151], v133 offset:0
	v_add_u32_e32 v135, 0x2000, v135
	ds_read_b64_tr_b16 v[152:153], v135 offset:0
	v_mfma_f32_32x32x16_bf16 v[0:15], v[146:149], v[182:185], v[0:15]
	ds_read_b64_tr_b16 v[182:183], v133 offset:0x200
	ds_read_b64_tr_b16 v[184:185], v135 offset:0x200
	v_mfma_f32_32x32x16_bf16 v[32:47], v[146:149], v[186:189], v[32:47]
	ds_read_b64_tr_b16 v[186:187], v133 offset:0x400
	ds_read_b64_tr_b16 v[188:189], v135 offset:0x400
	ds_read_b64_tr_b16 v[190:191], v133 offset:0x600
	ds_read_b64_tr_b16 v[192:193], v135 offset:0x600
	s_waitcnt lgkmcnt(0)
	v_mfma_f32_32x32x16_bf16 v[48:63], v[146:149], v[194:197], v[48:63]
	v_mfma_f32_32x32x16_bf16 v[96:111], v[128:131], v[150:153], v[96:111]
	ds_read_b64_tr_b16 v[150:151], v133 offset:0x1000
	ds_read_b64_tr_b16 v[152:153], v135 offset:0x1000
	v_mfma_f32_32x32x16_bf16 v[112:127], v[128:131], v[182:185], v[112:127]
	ds_read_b64_tr_b16 v[182:183], v133 offset:0x1200
	ds_read_b64_tr_b16 v[184:185], v135 offset:0x1200
	v_mfma_f32_32x32x16_bf16 v[80:95], v[128:131], v[186:189], v[80:95]
	ds_read_b64_tr_b16 v[186:187], v133 offset:0x1400
	ds_read_b64_tr_b16 v[188:189], v135 offset:0x1400
	ds_read_b64_tr_b16 v[194:195], v133 offset:0x1600
	ds_read_b64_tr_b16 v[196:197], v135 offset:0x1600
	s_waitcnt lgkmcnt(0)
	v_mfma_f32_32x32x16_bf16 v[64:79], v[128:131], v[190:193], v[64:79]
	v_mfma_f32_32x32x16_bf16 v[96:111], v[146:149], v[150:153], v[96:111]
	v_mfma_f32_32x32x16_bf16 v[112:127], v[146:149], v[182:185], v[112:127]
	v_mfma_f32_32x32x16_bf16 v[80:95], v[146:149], v[186:189], v[80:95]
	v_mfma_f32_32x32x16_bf16 v[64:79], v[146:149], v[194:197], v[64:79]
	s_waitcnt vmcnt(4) lgkmcnt(0)
	s_barrier
; #define VM_WAIT() asm volatile("s_waitcnt vmcnt(0)" ::: "memory")
; template <int DK, int DV, bool MLSTM>
; __device__ __forceinline__ void out_unit2(LAS unsigned char* lds, LAS unsigned char* ldstab, const OutArgs a, const int wv) {
;     ...
; #pragma unroll
;     for (int pc = 0; pc < 4; ++pc) {
;         VM_WAIT(); __syncthreads();
;         OUT_DMA(pc + 1);
;         const bf16x8 af0 = pa[2 * pc], af1 = pa[2 * pc + 1];
;         OUT_MMA(pc & 1);
;     }
; #pragma unroll 1
;     for (int pc = 4; pc < 4 + 2 * NCP; ++pc) {
;         VM_WAIT(); __syncthreads();
;         if (pc + 1 < 4 + 2 * NCP) OUT_DMA(pc + 1);
;         const int cq = pc - 4, dirb = cq >= NCP, cp = dirb ? cq - NCP : cq;
;         const float qs = dirb ? qsb : qsf;
;         const unsigned qa = QP + (cp >> 2) * 32768u + 512u * (cp & 3) + 8192u * rb;
;         const bf16x8 af0 = scale_frag(lds_r128(qa + rb0), qs), af1 = scale_frag(lds_r128(qa + rb1), qs);
;         OUT_MMA(pc & 1);
;     }
	s_add_u32 s40, s11, 0x28000
	s_addc_u32 s41, s12, 0
	v_lshl_add_u64 v[128:129], s[40:41], 0, v[198:199]
	v_lshl_add_u64 v[130:131], s[40:41], 0, v[200:201]
	v_lshl_add_u64 v[146:147], s[40:41], 0, v[202:203]
	v_lshl_add_u64 v[148:149], s[40:41], 0, v[204:205]
	s_add_i32 m0, s6, 0x18000
	s_nop 0
	global_load_lds_dwordx4 v[128:129], off
	s_add_i32 m0, s7, 0x18000
	s_nop 0
	global_load_lds_dwordx4 v[130:131], off
	s_add_i32 m0, s36, 0x18000
	s_nop 0
	global_load_lds_dwordx4 v[146:147], off
	s_add_i32 m0, s38, 0x18000
	s_nop 0
	global_load_lds_dwordx4 v[148:149], off
	v_lshlrev_b32_e32 v135, 16, v222
	v_and_b32_e32 v137, 0xffff0000, v222
	v_mul_f32_e32 v135, v144, v135
	v_mul_f32_e32 v137, v144, v137
	v_cvt_pk_bf16_f32 v128, v135, v137
	v_lshlrev_b32_e32 v135, 16, v223
	v_and_b32_e32 v137, 0xffff0000, v223
	v_mul_f32_e32 v135, v144, v135
	v_mul_f32_e32 v137, v144, v137
	v_cvt_pk_bf16_f32 v129, v135, v137
	v_lshlrev_b32_e32 v135, 16, v224
	v_and_b32_e32 v137, 0xffff0000, v224
	v_mul_f32_e32 v135, v144, v135
	v_mul_f32_e32 v137, v144, v137
	v_cvt_pk_bf16_f32 v130, v135, v137
	v_lshlrev_b32_e32 v135, 16, v225
	v_and_b32_e32 v137, 0xffff0000, v225
	v_mul_f32_e32 v135, v144, v135
	v_mul_f32_e32 v137, v144, v137
	v_cvt_pk_bf16_f32 v131, v135, v137
	v_lshlrev_b32_e32 v135, 16, v206
	v_and_b32_e32 v137, 0xffff0000, v206
	v_mul_f32_e32 v135, v144, v135
	v_mul_f32_e32 v137, v144, v137
	v_cvt_pk_bf16_f32 v146, v135, v137
	v_lshlrev_b32_e32 v135, 16, v207
	v_and_b32_e32 v137, 0xffff0000, v207
	v_mul_f32_e32 v135, v144, v135
	v_mul_f32_e32 v137, v144, v137
	v_cvt_pk_bf16_f32 v147, v135, v137
	v_lshlrev_b32_e32 v135, 16, v208
	v_and_b32_e32 v137, 0xffff0000, v208
	v_mul_f32_e32 v135, v144, v135
	v_mul_f32_e32 v137, v144, v137
	v_cvt_pk_bf16_f32 v148, v135, v137
	v_lshlrev_b32_e32 v135, 16, v209
	v_and_b32_e32 v137, 0xffff0000, v209
	v_mul_f32_e32 v135, v144, v135
	v_mul_f32_e32 v137, v144, v137
	v_cvt_pk_bf16_f32 v149, v135, v137
	v_mov_b32_e32 v133, v175
	ds_read_b64_tr_b16 v[150:151], v133 offset:0
	v_mov_b32_e32 v135, v181
	ds_read_b64_tr_b16 v[152:153], v135 offset:0
	ds_read_b64_tr_b16 v[182:183], v133 offset:0x200
	ds_read_b64_tr_b16 v[184:185], v135 offset:0x200
	ds_read_b64_tr_b16 v[186:187], v133 offset:0x400
	ds_read_b64_tr_b16 v[188:189], v135 offset:0x400
	ds_read_b64_tr_b16 v[190:191], v133 offset:0x600
	ds_read_b64_tr_b16 v[192:193], v135 offset:0x600
	s_waitcnt lgkmcnt(0)
	s_nop 0
	v_mfma_f32_32x32x16_bf16 v[16:31], v[128:131], v[150:153], v[16:31]
	ds_read_b64_tr_b16 v[150:151], v133 offset:0x1000
	ds_read_b64_tr_b16 v[152:153], v135 offset:0x1000
	v_mfma_f32_32x32x16_bf16 v[0:15], v[128:131], v[182:185], v[0:15]
	ds_read_b64_tr_b16 v[182:183], v133 offset:0x1200
	ds_read_b64_tr_b16 v[184:185], v135 offset:0x1200
	v_mfma_f32_32x32x16_bf16 v[32:47], v[128:131], v[186:189], v[32:47]
	ds_read_b64_tr_b16 v[186:187], v133 offset:0x1400
	ds_read_b64_tr_b16 v[188:189], v135 offset:0x1400
	ds_read_b64_tr_b16 v[194:195], v133 offset:0x1600
	ds_read_b64_tr_b16 v[196:197], v135 offset:0x1600
	s_waitcnt lgkmcnt(0)
	v_mfma_f32_32x32x16_bf16 v[48:63], v[128:131], v[190:193], v[48:63]
	v_mfma_f32_32x32x16_bf16 v[16:31], v[146:149], v[150:153], v[16:31]
	v_add_u32_e32 v133, 0x2000, v133
	ds_read_b64_tr_b16 v[150:151], v133 offset:0
	v_add_u32_e32 v135, 0x2000, v135
	ds_read_b64_tr_b16 v[152:153], v135 offset:0
	v_mfma_f32_32x32x16_bf16 v[0:15], v[146:149], v[182:185], v[0:15]
	ds_read_b64_tr_b16 v[182:183], v133 offset:0x200
	ds_read_b64_tr_b16 v[184:185], v135 offset:0x200
	v_mfma_f32_32x32x16_bf16 v[32:47], v[146:149], v[186:189], v[32:47]
	ds_read_b64_tr_b16 v[186:187], v133 offset:0x400
	ds_read_b64_tr_b16 v[188:189], v135 offset:0x400
	ds_read_b64_tr_b16 v[190:191], v133 offset:0x600
	ds_read_b64_tr_b16 v[192:193], v135 offset:0x600
	s_waitcnt lgkmcnt(0)
	v_mfma_f32_32x32x16_bf16 v[48:63], v[146:149], v[194:197], v[48:63]
	v_mfma_f32_32x32x16_bf16 v[96:111], v[128:131], v[150:153], v[96:111]
	ds_read_b64_tr_b16 v[150:151], v133 offset:0x1000
	ds_read_b64_tr_b16 v[152:153], v135 offset:0x1000
	v_mfma_f32_32x32x16_bf16 v[112:127], v[128:131], v[182:185], v[112:127]
	ds_read_b64_tr_b16 v[182:183], v133 offset:0x1200
	ds_read_b64_tr_b16 v[184:185], v135 offset:0x1200
	v_mfma_f32_32x32x16_bf16 v[80:95], v[128:131], v[186:189], v[80:95]
	ds_read_b64_tr_b16 v[186:187], v133 offset:0x1400
	ds_read_b64_tr_b16 v[188:189], v135 offset:0x1400
	ds_read_b64_tr_b16 v[194:195], v133 offset:0x1600
	ds_read_b64_tr_b16 v[196:197], v135 offset:0x1600
	s_waitcnt lgkmcnt(0)
	v_mfma_f32_32x32x16_bf16 v[64:79], v[128:131], v[190:193], v[64:79]
	v_mfma_f32_32x32x16_bf16 v[96:111], v[146:149], v[150:153], v[96:111]
	v_mfma_f32_32x32x16_bf16 v[112:127], v[146:149], v[182:185], v[112:127]
	v_mfma_f32_32x32x16_bf16 v[80:95], v[146:149], v[186:189], v[80:95]
	v_mfma_f32_32x32x16_bf16 v[64:79], v[146:149], v[194:197], v[64:79]
	s_waitcnt vmcnt(4) lgkmcnt(0)
	s_barrier
; #define VM_WAIT() asm volatile("s_waitcnt vmcnt(0)" ::: "memory")
; template <int DK, int DV, bool MLSTM>
; __device__ __forceinline__ void out_unit2(LAS unsigned char* lds, LAS unsigned char* ldstab, const OutArgs a, const int wv) {
;     ...
; #pragma unroll
;     for (int pc = 0; pc < 4; ++pc) {
;         VM_WAIT(); __syncthreads();
;         OUT_DMA(pc + 1);
;         const bf16x8 af0 = pa[2 * pc], af1 = pa[2 * pc + 1];
;         OUT_MMA(pc & 1);
;     }
; #pragma unroll 1
;     for (int pc = 4; pc < 4 + 2 * NCP; ++pc) {
;         VM_WAIT(); __syncthreads();
;         if (pc + 1 < 4 + 2 * NCP) OUT_DMA(pc + 1);
;         const int cq = pc - 4, dirb = cq >= NCP, cp = dirb ? cq - NCP : cq;
;         const float qs = dirb ? qsb : qsf;
;         const unsigned qa = QP + (cp >> 2) * 32768u + 512u * (cp & 3) + 8192u * rb;
;         const bf16x8 af0 = scale_frag(lds_r128(qa + rb0), qs), af1 = scale_frag(lds_r128(qa + rb1), qs);
;         OUT_MMA(pc & 1);
;     }
	s_add_u32 s40, s11, 0x30000
	s_addc_u32 s41, s12, 0
	v_lshl_add_u64 v[128:129], s[40:41], 0, v[198:199]
	v_lshl_add_u64 v[130:131], s[40:41], 0, v[200:201]
	v_lshl_add_u64 v[146:147], s[40:41], 0, v[202:203]
	v_lshl_add_u64 v[148:149], s[40:41], 0, v[204:205]
	s_mov_b32 m0, s6
	s_nop 0
	global_load_lds_dwordx4 v[128:129], off
	s_mov_b32 m0, s7
	s_nop 0
	global_load_lds_dwordx4 v[130:131], off
	s_mov_b32 m0, s36
	s_nop 0
	global_load_lds_dwordx4 v[146:147], off
	s_mov_b32 m0, s38
	s_nop 0
	global_load_lds_dwordx4 v[148:149], off
	v_add_u32_e32 v133, s13, v173
	v_add_u32_e32 v135, s13, v177
	ds_read_b128 v[128:131], v133 offset:32768
	ds_read_b128 v[146:149], v135 offset:32768
	s_waitcnt lgkmcnt(0)
	v_lshlrev_b32_e32 v135, 16, v128
	v_and_b32_e32 v137, 0xffff0000, v128
	v_mul_f32_e32 v135, v144, v135
	v_mul_f32_e32 v137, v144, v137
	v_cvt_pk_bf16_f32 v128, v135, v137
	v_lshlrev_b32_e32 v135, 16, v129
	v_and_b32_e32 v137, 0xffff0000, v129
	v_mul_f32_e32 v135, v144, v135
	v_mul_f32_e32 v137, v144, v137
	v_cvt_pk_bf16_f32 v129, v135, v137
	v_lshlrev_b32_e32 v135, 16, v130
	v_and_b32_e32 v137, 0xffff0000, v130
	v_mul_f32_e32 v135, v144, v135
	v_mul_f32_e32 v137, v144, v137
	v_cvt_pk_bf16_f32 v130, v135, v137
	v_lshlrev_b32_e32 v135, 16, v131
	v_and_b32_e32 v137, 0xffff0000, v131
	v_mul_f32_e32 v135, v144, v135
	v_mul_f32_e32 v137, v144, v137
	v_cvt_pk_bf16_f32 v131, v135, v137
	v_lshlrev_b32_e32 v135, 16, v146
	v_and_b32_e32 v137, 0xffff0000, v146
	v_mul_f32_e32 v135, v144, v135
	v_mul_f32_e32 v137, v144, v137
	v_cvt_pk_bf16_f32 v146, v135, v137
	v_lshlrev_b32_e32 v135, 16, v147
	v_and_b32_e32 v137, 0xffff0000, v147
	v_mul_f32_e32 v135, v144, v135
	v_mul_f32_e32 v137, v144, v137
	v_cvt_pk_bf16_f32 v147, v135, v137
	v_lshlrev_b32_e32 v135, 16, v148
	v_and_b32_e32 v137, 0xffff0000, v148
	v_mul_f32_e32 v135, v144, v135
	v_mul_f32_e32 v137, v144, v137
	v_cvt_pk_bf16_f32 v148, v135, v137
	v_lshlrev_b32_e32 v135, 16, v149
	v_and_b32_e32 v137, 0xffff0000, v149
	v_mul_f32_e32 v135, v144, v135
	v_mul_f32_e32 v137, v144, v137
	v_cvt_pk_bf16_f32 v149, v135, v137
	v_add_u32_e32 v133, 0x10000, v175
	ds_read_b64_tr_b16 v[150:151], v133 offset:0
	v_add_u32_e32 v135, 0x10000, v181
	ds_read_b64_tr_b16 v[152:153], v135 offset:0
	ds_read_b64_tr_b16 v[182:183], v133 offset:0x200
	ds_read_b64_tr_b16 v[184:185], v135 offset:0x200
	ds_read_b64_tr_b16 v[186:187], v133 offset:0x400
	ds_read_b64_tr_b16 v[188:189], v135 offset:0x400
	ds_read_b64_tr_b16 v[190:191], v133 offset:0x600
	ds_read_b64_tr_b16 v[192:193], v135 offset:0x600
	s_waitcnt lgkmcnt(0)
	s_nop 0
	v_mfma_f32_32x32x16_bf16 v[16:31], v[128:131], v[150:153], v[16:31]
	ds_read_b64_tr_b16 v[150:151], v133 offset:0x1000
	ds_read_b64_tr_b16 v[152:153], v135 offset:0x1000
	v_mfma_f32_32x32x16_bf16 v[0:15], v[128:131], v[182:185], v[0:15]
	ds_read_b64_tr_b16 v[182:183], v133 offset:0x1200
	ds_read_b64_tr_b16 v[184:185], v135 offset:0x1200
	v_mfma_f32_32x32x16_bf16 v[32:47], v[128:131], v[186:189], v[32:47]
	ds_read_b64_tr_b16 v[186:187], v133 offset:0x1400
	ds_read_b64_tr_b16 v[188:189], v135 offset:0x1400
	ds_read_b64_tr_b16 v[194:195], v133 offset:0x1600
	ds_read_b64_tr_b16 v[196:197], v135 offset:0x1600
	s_waitcnt lgkmcnt(0)
	v_mfma_f32_32x32x16_bf16 v[48:63], v[128:131], v[190:193], v[48:63]
	v_mfma_f32_32x32x16_bf16 v[16:31], v[146:149], v[150:153], v[16:31]
	v_add_u32_e32 v133, 0x2000, v133
	ds_read_b64_tr_b16 v[150:151], v133 offset:0
	v_add_u32_e32 v135, 0x2000, v135
	ds_read_b64_tr_b16 v[152:153], v135 offset:0
	v_mfma_f32_32x32x16_bf16 v[0:15], v[146:149], v[182:185], v[0:15]
	ds_read_b64_tr_b16 v[182:183], v133 offset:0x200
	ds_read_b64_tr_b16 v[184:185], v135 offset:0x200
	v_mfma_f32_32x32x16_bf16 v[32:47], v[146:149], v[186:189], v[32:47]
	ds_read_b64_tr_b16 v[186:187], v133 offset:0x400
	ds_read_b64_tr_b16 v[188:189], v135 offset:0x400
	ds_read_b64_tr_b16 v[190:191], v133 offset:0x600
	ds_read_b64_tr_b16 v[192:193], v135 offset:0x600
	s_waitcnt lgkmcnt(0)
	v_mfma_f32_32x32x16_bf16 v[48:63], v[146:149], v[194:197], v[48:63]
	v_mfma_f32_32x32x16_bf16 v[96:111], v[128:131], v[150:153], v[96:111]
	ds_read_b64_tr_b16 v[150:151], v133 offset:0x1000
	ds_read_b64_tr_b16 v[152:153], v135 offset:0x1000
	v_mfma_f32_32x32x16_bf16 v[112:127], v[128:131], v[182:185], v[112:127]
	ds_read_b64_tr_b16 v[182:183], v133 offset:0x1200
	ds_read_b64_tr_b16 v[184:185], v135 offset:0x1200
	v_mfma_f32_32x32x16_bf16 v[80:95], v[128:131], v[186:189], v[80:95]
	ds_read_b64_tr_b16 v[186:187], v133 offset:0x1400
	ds_read_b64_tr_b16 v[188:189], v135 offset:0x1400
	ds_read_b64_tr_b16 v[194:195], v133 offset:0x1600
	ds_read_b64_tr_b16 v[196:197], v135 offset:0x1600
	s_waitcnt lgkmcnt(0)
	v_mfma_f32_32x32x16_bf16 v[64:79], v[128:131], v[190:193], v[64:79]
	v_mfma_f32_32x32x16_bf16 v[96:111], v[146:149], v[150:153], v[96:111]
	v_mfma_f32_32x32x16_bf16 v[112:127], v[146:149], v[182:185], v[112:127]
	v_mfma_f32_32x32x16_bf16 v[80:95], v[146:149], v[186:189], v[80:95]
	v_mfma_f32_32x32x16_bf16 v[64:79], v[146:149], v[194:197], v[64:79]
	s_waitcnt vmcnt(4) lgkmcnt(0)
	s_barrier
; #define VM_WAIT() asm volatile("s_waitcnt vmcnt(0)" ::: "memory")
; template <int DK, int DV, bool MLSTM>
; __device__ __forceinline__ void out_unit2(LAS unsigned char* lds, LAS unsigned char* ldstab, const OutArgs a, const int wv) {
;     ...
; #pragma unroll
;     for (int pc = 0; pc < 4; ++pc) {
;         VM_WAIT(); __syncthreads();
;         OUT_DMA(pc + 1);
;         const bf16x8 af0 = pa[2 * pc], af1 = pa[2 * pc + 1];
;         OUT_MMA(pc & 1);
;     }
; #pragma unroll 1
;     for (int pc = 4; pc < 4 + 2 * NCP; ++pc) {
;         VM_WAIT(); __syncthreads();
;         if (pc + 1 < 4 + 2 * NCP) OUT_DMA(pc + 1);
;         const int cq = pc - 4, dirb = cq >= NCP, cp = dirb ? cq - NCP : cq;
;         const float qs = dirb ? qsb : qsf;
;         const unsigned qa = QP + (cp >> 2) * 32768u + 512u * (cp & 3) + 8192u * rb;
;         const bf16x8 af0 = scale_frag(lds_r128(qa + rb0), qs), af1 = scale_frag(lds_r128(qa + rb1), qs);
;         OUT_MMA(pc & 1);
;     }
	s_add_u32 s40, s11, 0x38000
	s_addc_u32 s41, s12, 0
	v_lshl_add_u64 v[128:129], s[40:41], 0, v[198:199]
	v_lshl_add_u64 v[130:131], s[40:41], 0, v[200:201]
	v_lshl_add_u64 v[146:147], s[40:41], 0, v[202:203]
	v_lshl_add_u64 v[148:149], s[40:41], 0, v[204:205]
	s_add_i32 m0, s6, 0x10000
	s_nop 0
	global_load_lds_dwordx4 v[128:129], off
	s_add_i32 m0, s7, 0x10000
	s_nop 0
	global_load_lds_dwordx4 v[130:131], off
	s_add_i32 m0, s36, 0x10000
	s_nop 0
	global_load_lds_dwordx4 v[146:147], off
	s_add_i32 m0, s38, 0x10000
	s_nop 0
	global_load_lds_dwordx4 v[148:149], off
	v_add_u32_e32 v133, s13, v173
	v_add_u32_e32 v135, s13, v177
	ds_read_b128 v[128:131], v133 offset:33280
	ds_read_b128 v[146:149], v135 offset:33280
	s_waitcnt lgkmcnt(0)
	v_lshlrev_b32_e32 v135, 16, v128
	v_and_b32_e32 v137, 0xffff0000, v128
	v_mul_f32_e32 v135, v144, v135
	v_mul_f32_e32 v137, v144, v137
	v_cvt_pk_bf16_f32 v128, v135, v137
	v_lshlrev_b32_e32 v135, 16, v129
	v_and_b32_e32 v137, 0xffff0000, v129
	v_mul_f32_e32 v135, v144, v135
	v_mul_f32_e32 v137, v144, v137
	v_cvt_pk_bf16_f32 v129, v135, v137
	v_lshlrev_b32_e32 v135, 16, v130
	v_and_b32_e32 v137, 0xffff0000, v130
	v_mul_f32_e32 v135, v144, v135
	v_mul_f32_e32 v137, v144, v137
	v_cvt_pk_bf16_f32 v130, v135, v137
	v_lshlrev_b32_e32 v135, 16, v131
	v_and_b32_e32 v137, 0xffff0000, v131
	v_mul_f32_e32 v135, v144, v135
	v_mul_f32_e32 v137, v144, v137
	v_cvt_pk_bf16_f32 v131, v135, v137
	v_lshlrev_b32_e32 v135, 16, v146
	v_and_b32_e32 v137, 0xffff0000, v146
	v_mul_f32_e32 v135, v144, v135
	v_mul_f32_e32 v137, v144, v137
	v_cvt_pk_bf16_f32 v146, v135, v137
	v_lshlrev_b32_e32 v135, 16, v147
	v_and_b32_e32 v137, 0xffff0000, v147
	v_mul_f32_e32 v135, v144, v135
	v_mul_f32_e32 v137, v144, v137
	v_cvt_pk_bf16_f32 v147, v135, v137
	v_lshlrev_b32_e32 v135, 16, v148
	v_and_b32_e32 v137, 0xffff0000, v148
	v_mul_f32_e32 v135, v144, v135
	v_mul_f32_e32 v137, v144, v137
	v_cvt_pk_bf16_f32 v148, v135, v137
	v_lshlrev_b32_e32 v135, 16, v149
	v_and_b32_e32 v137, 0xffff0000, v149
	v_mul_f32_e32 v135, v144, v135
	v_mul_f32_e32 v137, v144, v137
	v_cvt_pk_bf16_f32 v149, v135, v137
	v_add_u32_e32 v133, 0x18000, v175
	ds_read_b64_tr_b16 v[150:151], v133 offset:0
	v_add_u32_e32 v135, 0x18000, v181
	ds_read_b64_tr_b16 v[152:153], v135 offset:0
	ds_read_b64_tr_b16 v[182:183], v133 offset:0x200
	ds_read_b64_tr_b16 v[184:185], v135 offset:0x200
	ds_read_b64_tr_b16 v[186:187], v133 offset:0x400
	ds_read_b64_tr_b16 v[188:189], v135 offset:0x400
	ds_read_b64_tr_b16 v[190:191], v133 offset:0x600
	ds_read_b64_tr_b16 v[192:193], v135 offset:0x600
	s_waitcnt lgkmcnt(0)
	s_nop 0
	v_mfma_f32_32x32x16_bf16 v[16:31], v[128:131], v[150:153], v[16:31]
	ds_read_b64_tr_b16 v[150:151], v133 offset:0x1000
	ds_read_b64_tr_b16 v[152:153], v135 offset:0x1000
	v_mfma_f32_32x32x16_bf16 v[0:15], v[128:131], v[182:185], v[0:15]
	ds_read_b64_tr_b16 v[182:183], v133 offset:0x1200
	ds_read_b64_tr_b16 v[184:185], v135 offset:0x1200
	v_mfma_f32_32x32x16_bf16 v[32:47], v[128:131], v[186:189], v[32:47]
	ds_read_b64_tr_b16 v[186:187], v133 offset:0x1400
	ds_read_b64_tr_b16 v[188:189], v135 offset:0x1400
	ds_read_b64_tr_b16 v[194:195], v133 offset:0x1600
	ds_read_b64_tr_b16 v[196:197], v135 offset:0x1600
	s_waitcnt lgkmcnt(0)
	v_mfma_f32_32x32x16_bf16 v[48:63], v[128:131], v[190:193], v[48:63]
	v_mfma_f32_32x32x16_bf16 v[16:31], v[146:149], v[150:153], v[16:31]
	v_add_u32_e32 v133, 0x2000, v133
	ds_read_b64_tr_b16 v[150:151], v133 offset:0
	v_add_u32_e32 v135, 0x2000, v135
	ds_read_b64_tr_b16 v[152:153], v135 offset:0
	v_mfma_f32_32x32x16_bf16 v[0:15], v[146:149], v[182:185], v[0:15]
	ds_read_b64_tr_b16 v[182:183], v133 offset:0x200
	ds_read_b64_tr_b16 v[184:185], v135 offset:0x200
	v_mfma_f32_32x32x16_bf16 v[32:47], v[146:149], v[186:189], v[32:47]
	ds_read_b64_tr_b16 v[186:187], v133 offset:0x400
	ds_read_b64_tr_b16 v[188:189], v135 offset:0x400
	ds_read_b64_tr_b16 v[190:191], v133 offset:0x600
	ds_read_b64_tr_b16 v[192:193], v135 offset:0x600
	s_waitcnt lgkmcnt(0)
	v_mfma_f32_32x32x16_bf16 v[48:63], v[146:149], v[194:197], v[48:63]
	v_mfma_f32_32x32x16_bf16 v[96:111], v[128:131], v[150:153], v[96:111]
	ds_read_b64_tr_b16 v[150:151], v133 offset:0x1000
	ds_read_b64_tr_b16 v[152:153], v135 offset:0x1000
	v_mfma_f32_32x32x16_bf16 v[112:127], v[128:131], v[182:185], v[112:127]
	ds_read_b64_tr_b16 v[182:183], v133 offset:0x1200
	ds_read_b64_tr_b16 v[184:185], v135 offset:0x1200
	v_mfma_f32_32x32x16_bf16 v[80:95], v[128:131], v[186:189], v[80:95]
	ds_read_b64_tr_b16 v[186:187], v133 offset:0x1400
	ds_read_b64_tr_b16 v[188:189], v135 offset:0x1400
	ds_read_b64_tr_b16 v[194:195], v133 offset:0x1600
	ds_read_b64_tr_b16 v[196:197], v135 offset:0x1600
	s_waitcnt lgkmcnt(0)
	v_mfma_f32_32x32x16_bf16 v[64:79], v[128:131], v[190:193], v[64:79]
	v_mfma_f32_32x32x16_bf16 v[96:111], v[146:149], v[150:153], v[96:111]
	v_mfma_f32_32x32x16_bf16 v[112:127], v[146:149], v[182:185], v[112:127]
	v_mfma_f32_32x32x16_bf16 v[80:95], v[146:149], v[186:189], v[80:95]
	v_mfma_f32_32x32x16_bf16 v[64:79], v[146:149], v[194:197], v[64:79]
	s_waitcnt vmcnt(4) lgkmcnt(0)
	s_barrier
; #define VM_WAIT() asm volatile("s_waitcnt vmcnt(0)" ::: "memory")
; template <int DK, int DV, bool MLSTM>
; __device__ __forceinline__ void out_unit2(LAS unsigned char* lds, LAS unsigned char* ldstab, const OutArgs a, const int wv) {
;     ...
; #pragma unroll
;     for (int pc = 0; pc < 4; ++pc) {
;         VM_WAIT(); __syncthreads();
;         OUT_DMA(pc + 1);
;         const bf16x8 af0 = pa[2 * pc], af1 = pa[2 * pc + 1];
;         OUT_MMA(pc & 1);
;     }
; #pragma unroll 1
;     for (int pc = 4; pc < 4 + 2 * NCP; ++pc) {
;         VM_WAIT(); __syncthreads();
;         if (pc + 1 < 4 + 2 * NCP) OUT_DMA(pc + 1);
;         const int cq = pc - 4, dirb = cq >= NCP, cp = dirb ? cq - NCP : cq;
;         const float qs = dirb ? qsb : qsf;
;         const unsigned qa = QP + (cp >> 2) * 32768u + 512u * (cp & 3) + 8192u * rb;
;         const bf16x8 af0 = scale_frag(lds_r128(qa + rb0), qs), af1 = scale_frag(lds_r128(qa + rb1), qs);
;         OUT_MMA(pc & 1);
;     }
	v_add_u32_e32 v133, s13, v173
	v_add_u32_e32 v135, s13, v177
	ds_read_b128 v[128:131], v133 offset:33792
	ds_read_b128 v[146:149], v135 offset:33792
	s_waitcnt lgkmcnt(0)
	v_lshlrev_b32_e32 v135, 16, v128
	v_and_b32_e32 v137, 0xffff0000, v128
	v_mul_f32_e32 v135, v144, v135
	v_mul_f32_e32 v137, v144, v137
	v_cvt_pk_bf16_f32 v128, v135, v137
	v_lshlrev_b32_e32 v135, 16, v129
	v_and_b32_e32 v137, 0xffff0000, v129
	v_mul_f32_e32 v135, v144, v135
	v_mul_f32_e32 v137, v144, v137
	v_cvt_pk_bf16_f32 v129, v135, v137
	v_lshlrev_b32_e32 v135, 16, v130
	v_and_b32_e32 v137, 0xffff0000, v130
	v_mul_f32_e32 v135, v144, v135
	v_mul_f32_e32 v137, v144, v137
	v_cvt_pk_bf16_f32 v130, v135, v137
	v_lshlrev_b32_e32 v135, 16, v131
	v_and_b32_e32 v137, 0xffff0000, v131
	v_mul_f32_e32 v135, v144, v135
	v_mul_f32_e32 v137, v144, v137
	v_cvt_pk_bf16_f32 v131, v135, v137
	v_lshlrev_b32_e32 v135, 16, v146
	v_and_b32_e32 v137, 0xffff0000, v146
	v_mul_f32_e32 v135, v144, v135
	v_mul_f32_e32 v137, v144, v137
	v_cvt_pk_bf16_f32 v146, v135, v137
	v_lshlrev_b32_e32 v135, 16, v147
	v_and_b32_e32 v137, 0xffff0000, v147
	v_mul_f32_e32 v135, v144, v135
	v_mul_f32_e32 v137, v144, v137
	v_cvt_pk_bf16_f32 v147, v135, v137
	v_lshlrev_b32_e32 v135, 16, v148
	v_and_b32_e32 v137, 0xffff0000, v148
	v_mul_f32_e32 v135, v144, v135
	v_mul_f32_e32 v137, v144, v137
	v_cvt_pk_bf16_f32 v148, v135, v137
	v_lshlrev_b32_e32 v135, 16, v149
	v_and_b32_e32 v137, 0xffff0000, v149
	v_mul_f32_e32 v135, v144, v135
	v_mul_f32_e32 v137, v144, v137
	v_cvt_pk_bf16_f32 v149, v135, v137
	v_mov_b32_e32 v133, v175
	ds_read_b64_tr_b16 v[150:151], v133 offset:0
	v_mov_b32_e32 v135, v181
	ds_read_b64_tr_b16 v[152:153], v135 offset:0
	ds_read_b64_tr_b16 v[182:183], v133 offset:0x200
	ds_read_b64_tr_b16 v[184:185], v135 offset:0x200
	ds_read_b64_tr_b16 v[186:187], v133 offset:0x400
	ds_read_b64_tr_b16 v[188:189], v135 offset:0x400
	ds_read_b64_tr_b16 v[190:191], v133 offset:0x600
	ds_read_b64_tr_b16 v[192:193], v135 offset:0x600
	s_waitcnt lgkmcnt(0)
	s_nop 0
	v_mfma_f32_32x32x16_bf16 v[16:31], v[128:131], v[150:153], v[16:31]
	ds_read_b64_tr_b16 v[150:151], v133 offset:0x1000
	ds_read_b64_tr_b16 v[152:153], v135 offset:0x1000
	v_mfma_f32_32x32x16_bf16 v[0:15], v[128:131], v[182:185], v[0:15]
	ds_read_b64_tr_b16 v[182:183], v133 offset:0x1200
	ds_read_b64_tr_b16 v[184:185], v135 offset:0x1200
	v_mfma_f32_32x32x16_bf16 v[32:47], v[128:131], v[186:189], v[32:47]
	ds_read_b64_tr_b16 v[186:187], v133 offset:0x1400
	ds_read_b64_tr_b16 v[188:189], v135 offset:0x1400
	ds_read_b64_tr_b16 v[194:195], v133 offset:0x1600
	ds_read_b64_tr_b16 v[196:197], v135 offset:0x1600
	s_waitcnt lgkmcnt(0)
	v_mfma_f32_32x32x16_bf16 v[48:63], v[128:131], v[190:193], v[48:63]
	v_mfma_f32_32x32x16_bf16 v[16:31], v[146:149], v[150:153], v[16:31]
	v_add_u32_e32 v133, 0x2000, v133
	ds_read_b64_tr_b16 v[150:151], v133 offset:0
	v_add_u32_e32 v135, 0x2000, v135
	ds_read_b64_tr_b16 v[152:153], v135 offset:0
	v_mfma_f32_32x32x16_bf16 v[0:15], v[146:149], v[182:185], v[0:15]
	ds_read_b64_tr_b16 v[182:183], v133 offset:0x200
	ds_read_b64_tr_b16 v[184:185], v135 offset:0x200
	v_mfma_f32_32x32x16_bf16 v[32:47], v[146:149], v[186:189], v[32:47]
	ds_read_b64_tr_b16 v[186:187], v133 offset:0x400
	ds_read_b64_tr_b16 v[188:189], v135 offset:0x400
	ds_read_b64_tr_b16 v[190:191], v133 offset:0x600
	ds_read_b64_tr_b16 v[192:193], v135 offset:0x600
	s_waitcnt lgkmcnt(0)
	v_mfma_f32_32x32x16_bf16 v[48:63], v[146:149], v[194:197], v[48:63]
	v_mfma_f32_32x32x16_bf16 v[96:111], v[128:131], v[150:153], v[96:111]
	ds_read_b64_tr_b16 v[150:151], v133 offset:0x1000
	ds_read_b64_tr_b16 v[152:153], v135 offset:0x1000
	v_mfma_f32_32x32x16_bf16 v[112:127], v[128:131], v[182:185], v[112:127]
	ds_read_b64_tr_b16 v[182:183], v133 offset:0x1200
	ds_read_b64_tr_b16 v[184:185], v135 offset:0x1200
	v_mfma_f32_32x32x16_bf16 v[80:95], v[128:131], v[186:189], v[80:95]
	ds_read_b64_tr_b16 v[186:187], v133 offset:0x1400
	ds_read_b64_tr_b16 v[188:189], v135 offset:0x1400
	ds_read_b64_tr_b16 v[194:195], v133 offset:0x1600
	ds_read_b64_tr_b16 v[196:197], v135 offset:0x1600
	s_waitcnt lgkmcnt(0)
	v_mfma_f32_32x32x16_bf16 v[64:79], v[128:131], v[190:193], v[64:79]
	v_mfma_f32_32x32x16_bf16 v[96:111], v[146:149], v[150:153], v[96:111]
	v_mfma_f32_32x32x16_bf16 v[112:127], v[146:149], v[182:185], v[112:127]
	v_mfma_f32_32x32x16_bf16 v[80:95], v[146:149], v[186:189], v[80:95]
	v_mfma_f32_32x32x16_bf16 v[64:79], v[146:149], v[194:197], v[64:79]
	s_waitcnt vmcnt(0) lgkmcnt(0)
	s_barrier
; #define VM_WAIT() asm volatile("s_waitcnt vmcnt(0)" ::: "memory")
; template <int DK, int DV, bool MLSTM>
; __device__ __forceinline__ void out_unit2(LAS unsigned char* lds, LAS unsigned char* ldstab, const OutArgs a, const int wv) {
;     ...
; #pragma unroll
;     for (int pc = 0; pc < 4; ++pc) {
;         VM_WAIT(); __syncthreads();
;         OUT_DMA(pc + 1);
;         const bf16x8 af0 = pa[2 * pc], af1 = pa[2 * pc + 1];
;         OUT_MMA(pc & 1);
;     }
; #pragma unroll 1
;     for (int pc = 4; pc < 4 + 2 * NCP; ++pc) {
;         VM_WAIT(); __syncthreads();
;         if (pc + 1 < 4 + 2 * NCP) OUT_DMA(pc + 1);
;         const int cq = pc - 4, dirb = cq >= NCP, cp = dirb ? cq - NCP : cq;
;         const float qs = dirb ? qsb : qsf;
;         const unsigned qa = QP + (cp >> 2) * 32768u + 512u * (cp & 3) + 8192u * rb;
;         const bf16x8 af0 = scale_frag(lds_r128(qa + rb0), qs), af1 = scale_frag(lds_r128(qa + rb1), qs);
;         OUT_MMA(pc & 1);
;     }
	v_add_u32_e32 v133, s13, v173
	v_add_u32_e32 v135, s13, v177
	ds_read_b128 v[128:131], v133 offset:34304
	ds_read_b128 v[146:149], v135 offset:34304
	s_waitcnt lgkmcnt(0)
	v_lshlrev_b32_e32 v135, 16, v128
	v_and_b32_e32 v137, 0xffff0000, v128
	v_mul_f32_e32 v135, v144, v135
	v_mul_f32_e32 v137, v144, v137
	v_cvt_pk_bf16_f32 v128, v135, v137
	v_lshlrev_b32_e32 v135, 16, v129
	v_and_b32_e32 v137, 0xffff0000, v129
	v_mul_f32_e32 v135, v144, v135
	v_mul_f32_e32 v137, v144, v137
	v_cvt_pk_bf16_f32 v129, v135, v137
	v_lshlrev_b32_e32 v135, 16, v130
	v_and_b32_e32 v137, 0xffff0000, v130
	v_mul_f32_e32 v135, v144, v135
	v_mul_f32_e32 v137, v144, v137
	v_cvt_pk_bf16_f32 v130, v135, v137
	v_lshlrev_b32_e32 v135, 16, v131
	v_and_b32_e32 v137, 0xffff0000, v131
	v_mul_f32_e32 v135, v144, v135
	v_mul_f32_e32 v137, v144, v137
	v_cvt_pk_bf16_f32 v131, v135, v137
	v_lshlrev_b32_e32 v135, 16, v146
	v_and_b32_e32 v137, 0xffff0000, v146
	v_mul_f32_e32 v135, v144, v135
	v_mul_f32_e32 v137, v144, v137
	v_cvt_pk_bf16_f32 v146, v135, v137
	v_lshlrev_b32_e32 v135, 16, v147
	v_and_b32_e32 v137, 0xffff0000, v147
	v_mul_f32_e32 v135, v144, v135
	v_mul_f32_e32 v137, v144, v137
	v_cvt_pk_bf16_f32 v147, v135, v137
	v_lshlrev_b32_e32 v135, 16, v148
	v_and_b32_e32 v137, 0xffff0000, v148
	v_mul_f32_e32 v135, v144, v135
	v_mul_f32_e32 v137, v144, v137
	v_cvt_pk_bf16_f32 v148, v135, v137
	v_lshlrev_b32_e32 v135, 16, v149
	v_and_b32_e32 v137, 0xffff0000, v149
	v_mul_f32_e32 v135, v144, v135
	v_mul_f32_e32 v137, v144, v137
	v_cvt_pk_bf16_f32 v149, v135, v137
	v_add_u32_e32 v133, 0x10000, v175
	ds_read_b64_tr_b16 v[150:151], v133 offset:0
	v_add_u32_e32 v135, 0x10000, v181
	ds_read_b64_tr_b16 v[152:153], v135 offset:0
	ds_read_b64_tr_b16 v[182:183], v133 offset:0x200
	ds_read_b64_tr_b16 v[184:185], v135 offset:0x200
	ds_read_b64_tr_b16 v[186:187], v133 offset:0x400
	ds_read_b64_tr_b16 v[188:189], v135 offset:0x400
	ds_read_b64_tr_b16 v[190:191], v133 offset:0x600
	ds_read_b64_tr_b16 v[192:193], v135 offset:0x600
	s_waitcnt lgkmcnt(0)
	s_nop 0
	v_mfma_f32_32x32x16_bf16 v[16:31], v[128:131], v[150:153], v[16:31]
	ds_read_b64_tr_b16 v[150:151], v133 offset:0x1000
	ds_read_b64_tr_b16 v[152:153], v135 offset:0x1000
	v_mfma_f32_32x32x16_bf16 v[0:15], v[128:131], v[182:185], v[0:15]
	ds_read_b64_tr_b16 v[182:183], v133 offset:0x1200
	ds_read_b64_tr_b16 v[184:185], v135 offset:0x1200
	v_mfma_f32_32x32x16_bf16 v[32:47], v[128:131], v[186:189], v[32:47]
	ds_read_b64_tr_b16 v[186:187], v133 offset:0x1400
	ds_read_b64_tr_b16 v[188:189], v135 offset:0x1400
	ds_read_b64_tr_b16 v[194:195], v133 offset:0x1600
	ds_read_b64_tr_b16 v[196:197], v135 offset:0x1600
	s_waitcnt lgkmcnt(0)
	v_mfma_f32_32x32x16_bf16 v[48:63], v[128:131], v[190:193], v[48:63]
	v_mfma_f32_32x32x16_bf16 v[16:31], v[146:149], v[150:153], v[16:31]
	v_add_u32_e32 v133, 0x2000, v133
	ds_read_b64_tr_b16 v[150:151], v133 offset:0
	v_add_u32_e32 v135, 0x2000, v135
	ds_read_b64_tr_b16 v[152:153], v135 offset:0
	v_mfma_f32_32x32x16_bf16 v[0:15], v[146:149], v[182:185], v[0:15]
	ds_read_b64_tr_b16 v[182:183], v133 offset:0x200
	ds_read_b64_tr_b16 v[184:185], v135 offset:0x200
	v_mfma_f32_32x32x16_bf16 v[32:47], v[146:149], v[186:189], v[32:47]
	ds_read_b64_tr_b16 v[186:187], v133 offset:0x400
	ds_read_b64_tr_b16 v[188:189], v135 offset:0x400
	ds_read_b64_tr_b16 v[190:191], v133 offset:0x600
	ds_read_b64_tr_b16 v[192:193], v135 offset:0x600
	s_waitcnt lgkmcnt(0)
	v_mfma_f32_32x32x16_bf16 v[48:63], v[146:149], v[194:197], v[48:63]
	v_mfma_f32_32x32x16_bf16 v[96:111], v[128:131], v[150:153], v[96:111]
	ds_read_b64_tr_b16 v[150:151], v133 offset:0x1000
	ds_read_b64_tr_b16 v[152:153], v135 offset:0x1000
	v_mfma_f32_32x32x16_bf16 v[112:127], v[128:131], v[182:185], v[112:127]
	ds_read_b64_tr_b16 v[182:183], v133 offset:0x1200
	ds_read_b64_tr_b16 v[184:185], v135 offset:0x1200
	v_mfma_f32_32x32x16_bf16 v[80:95], v[128:131], v[186:189], v[80:95]
	ds_read_b64_tr_b16 v[186:187], v133 offset:0x1400
	ds_read_b64_tr_b16 v[188:189], v135 offset:0x1400
	ds_read_b64_tr_b16 v[194:195], v133 offset:0x1600
	ds_read_b64_tr_b16 v[196:197], v135 offset:0x1600
	s_waitcnt lgkmcnt(0)
	v_mfma_f32_32x32x16_bf16 v[64:79], v[128:131], v[190:193], v[64:79]
	v_mfma_f32_32x32x16_bf16 v[96:111], v[146:149], v[150:153], v[96:111]
	v_mfma_f32_32x32x16_bf16 v[112:127], v[146:149], v[182:185], v[112:127]
	v_mfma_f32_32x32x16_bf16 v[80:95], v[146:149], v[186:189], v[80:95]
	v_mfma_f32_32x32x16_bf16 v[64:79], v[146:149], v[194:197], v[64:79]
